# v7 + nt cache policy on FFT-phase background conversion loads and stores
# speedup vs baseline: 1.0350x; 1.0084x over previous
; __device__ __forceinline__ unsigned cvt_pk_bf16(float lo, float hi) { unsigned r; asm volatile("v_cvt_pk_bf16_f32 %0, %1, %2" : "=v"(r) : "v"(lo), "v"(hi)); return r; }
; __device__ __forceinline__ void hy_fft_phase(LAS unsigned char* lds, int bid, int G, const bf16_t* vgT, bf16_t* zT, const float* a3, const float* wout, const float* skip, float* filt, float4* gspec) {
;     ...
;             bf16x8 bw[2];
; #pragma unroll
;             for (int ks = 0; ks < 2; ++ks) { float wv[8];
; #pragma unroll
;                 for (int q = 0; q < 8; ++q) wv[q] = wout[(size_t)(ks * 32 + kc * 8 + q) * 4096 + (col & 1) * D + (cok ? c : bid)] * (cok ? 1.f : 0.f);
;                 u32x4 w; w.x = cvt_pk_bf16(wv[0], wv[1]); w.y = cvt_pk_bf16(wv[2], wv[3]); w.z = cvt_pk_bf16(wv[4], wv[5]); w.w = cvt_pk_bf16(wv[6], wv[7]);
;                 bw[ks] = __builtin_bit_cast(bf16x8, w); }
.LBB0_377:
	v_mov_b32_e32 v14, v0
	v_readlane_b32 s0, v254, 4
	v_bfe_u32 v2, v14, 1, 3
	v_or_b32_e32 v2, s84, v2
	v_mul_lo_u32 v3, v2, s0
	v_readlane_b32 s0, v254, 19
	v_cmp_gt_i32_e32 vcc, s61, v2
	v_lshlrev_b32_e32 v4, 13, v14
	v_add_u32_e32 v16, s0, v3
	v_cndmask_b32_e32 v2, v63, v16, vcc
	v_and_b32_e32 v60, 0x2000, v4
	v_bfe_u32 v15, v14, 4, 2
	v_ashrrev_i32_e32 v3, 31, v2
	v_lshl_add_u64 v[4:5], s[4:5], 0, v[60:61]
	v_lshl_add_u64 v[2:3], v[2:3], 2, v[4:5]
	v_lshlrev_b32_e32 v60, 17, v15
	v_readlane_b32 s1, v254, 20
	v_lshl_add_u64 v[6:7], v[2:3], 0, v[60:61]
	s_movk_i32 s0, 0x4000
	v_add_co_u32_e64 v2, s[0:1], s0, v6
	v_cndmask_b32_e64 v29, 0, 1.0, vcc
	s_nop 0
	v_addc_co_u32_e64 v3, s[0:1], 0, v7, s[0:1]
	s_mov_b32 s0, 0x8000
	s_nop 0
	v_add_co_u32_e64 v4, s[0:1], s0, v6
	s_mul_i32 s28, s60, s16
	s_nop 0
	v_addc_co_u32_e64 v5, s[0:1], 0, v7, s[0:1]
	s_mov_b32 s0, 0xc000
	s_nop 0
	v_add_co_u32_e64 v8, s[0:1], s0, v6
	s_add_i32 s28, s28, s17
	s_nop 0
	v_addc_co_u32_e64 v9, s[0:1], 0, v7, s[0:1]
	v_add_co_u32_e64 v10, s[0:1], s71, v6
	s_cmp_gt_i32 s28, 0x1ffff
	s_nop 0
	v_addc_co_u32_e64 v11, s[0:1], 0, v7, s[0:1]
	v_add_co_u32_e64 v12, s[0:1], s72, v6
	s_mov_b64 s[8:9], -1
	s_nop 0
	v_addc_co_u32_e64 v13, s[0:1], 0, v7, s[0:1]
	v_add_co_u32_e64 v18, s[0:1], s73, v6
	s_nop 1
	v_addc_co_u32_e64 v19, s[0:1], 0, v7, s[0:1]
	v_add_co_u32_e64 v20, s[0:1], s74, v6
	s_nop 1
	v_addc_co_u32_e64 v21, s[0:1], 0, v7, s[0:1]
	global_load_dword v17, v[6:7], off nt
	s_nop 0
	global_load_dword v2, v[2:3], off nt
	s_nop 0
	global_load_dword v3, v[4:5], off nt
	s_nop 0
	global_load_dword v4, v[8:9], off nt
	global_load_dword v5, v[10:11], off nt
	global_load_dword v26, v[12:13], off nt
	global_load_dword v27, v[18:19], off nt
	global_load_dword v28, v[20:21], off nt
	s_mov_b32 s0, 0x80000
	v_add_co_u32_e32 v8, vcc, s0, v6
	s_mov_b32 s0, 0x84000
	s_nop 0
	v_addc_co_u32_e32 v9, vcc, 0, v7, vcc
	v_add_co_u32_e32 v10, vcc, s0, v6
	s_mov_b32 s0, 0x88000
	s_nop 0
	v_addc_co_u32_e32 v11, vcc, 0, v7, vcc
	v_add_co_u32_e32 v12, vcc, s0, v6
	s_mov_b32 s0, 0x8c000
	s_nop 0
	v_addc_co_u32_e32 v13, vcc, 0, v7, vcc
	v_add_co_u32_e32 v18, vcc, s0, v6
	s_mov_b32 s0, 0x90000
	s_nop 0
	v_addc_co_u32_e32 v19, vcc, 0, v7, vcc
	v_add_co_u32_e32 v20, vcc, s0, v6
	s_mov_b32 s0, 0x94000
	s_nop 0
	v_addc_co_u32_e32 v21, vcc, 0, v7, vcc
	v_add_co_u32_e32 v22, vcc, s0, v6
	s_mov_b32 s0, 0x98000
	s_nop 0
	v_addc_co_u32_e32 v23, vcc, 0, v7, vcc
	v_add_co_u32_e32 v24, vcc, s0, v6
	s_mov_b32 s0, 0x9c000
	s_nop 0
	v_addc_co_u32_e32 v25, vcc, 0, v7, vcc
	v_add_co_u32_e32 v6, vcc, s0, v6
	v_readlane_b32 s0, v254, 0
	s_nop 0
	v_addc_co_u32_e32 v7, vcc, 0, v7, vcc
	v_readlane_b32 s1, v254, 1
	s_waitcnt vmcnt(7)
	v_mul_f32_e32 v17, v17, v29
	s_waitcnt vmcnt(6)
	v_mul_f32_e32 v2, v2, v29
	s_waitcnt vmcnt(5)
	v_mul_f32_e32 v3, v3, v29
	s_waitcnt vmcnt(4)
	v_mul_f32_e32 v4, v4, v29
	s_waitcnt vmcnt(3)
	v_mul_f32_e32 v5, v29, v5
	s_waitcnt vmcnt(2)
	v_mul_f32_e32 v26, v29, v26
	s_waitcnt vmcnt(1)
	v_mul_f32_e32 v27, v29, v27
	s_waitcnt vmcnt(0)
	v_mul_f32_e32 v28, v29, v28
	v_cvt_pk_bf16_f32 v2, v17, v2
	v_cvt_pk_bf16_f32 v3, v3, v4
	v_cvt_pk_bf16_f32 v4, v5, v26
	v_cvt_pk_bf16_f32 v5, v27, v28
	global_load_dword v8, v[8:9], off nt
	s_nop 0
	global_load_dword v9, v[10:11], off nt
	s_nop 0
	global_load_dword v10, v[12:13], off nt
	global_load_dword v11, v[18:19], off nt
	s_nop 0
	global_load_dword v12, v[20:21], off nt
	global_load_dword v13, v[22:23], off nt
	global_load_dword v17, v[24:25], off nt
	s_nop 0
	global_load_dword v6, v[6:7], off nt
	s_waitcnt vmcnt(7)
	v_mul_f32_e32 v7, v29, v8
	s_waitcnt vmcnt(6)
	v_mul_f32_e32 v8, v29, v9
	s_waitcnt vmcnt(5)
	v_mul_f32_e32 v9, v29, v10
	s_waitcnt vmcnt(4)
	v_mul_f32_e32 v10, v29, v11
	s_waitcnt vmcnt(3)
	v_mul_f32_e32 v11, v29, v12
	s_waitcnt vmcnt(2)
	v_mul_f32_e32 v12, v29, v13
	s_waitcnt vmcnt(1)
	v_mul_f32_e32 v13, v29, v17
	s_waitcnt vmcnt(0)
	v_mul_f32_e32 v17, v29, v6
	v_cvt_pk_bf16_f32 v6, v7, v8
	v_cvt_pk_bf16_f32 v7, v9, v10
	v_cvt_pk_bf16_f32 v8, v11, v12
	v_cvt_pk_bf16_f32 v9, v13, v17
	s_barrier
	s_cbranch_scc0 .LBB0_379
	s_load_dwordx2 s[8:9], s[0:1], 0xd8
	v_mov_b32_e32 v65, v61
	s_waitcnt lgkmcnt(0)
	v_lshl_add_u64 v[10:11], s[8:9], 0, v[64:65]
	s_mov_b64 s[8:9], 0

; template <int BANK> __device__ __forceinline__ void bg_issue1(BgState& b, int wg, int NW, int lane) {
;     KP kp = kparams();
;     const float* src; int ldS; bf16_t* dst; int o2;
;     bg_decode(b.st, wg, NW, lane, kp, src, ldS, dst, o2);
;     b.dst[BANK] = dst; b.o2[BANK] = o2;
;     asm volatile("s_nop 6" ::: "memory");
; #pragma unroll
;     for (int i = 0; i < 8; ++i) { const float* p = src + (size_t)i * ldS;
;         asm volatile("global_load_dword %0, %4, off\n\tglobal_load_dword %1, %4, off offset:256\n\tglobal_load_dword %2, %4, off offset:512\n\tglobal_load_dword %3, %4, off offset:768"
;                      : "=&v"(b.r[(BANK * 8 + i) * 4 + 0]), "=&v"(b.r[(BANK * 8 + i) * 4 + 1]), "=&v"(b.r[(BANK * 8 + i) * 4 + 2]), "=&v"(b.r[(BANK * 8 + i) * 4 + 3]) : "v"(p) : "memory"); }
;     b.st += 1;
; }
; __device__ __forceinline__ void hy_fft_phase(LAS unsigned char* lds, int bid, int G, const bf16_t* vgT, bf16_t* zT, const float* a3, const float* wout, const float* skip, float* filt, float4* gspec) {
;     ...
;             const float dlo = -15.350567286626973f, dhi = -3.0701134573253946f;
;             const float delta = fabsf(dlo + (float)c * ((dhi - dlo) / (float)(D - 1)));
;             __syncthreads();
;             auto tap_load = [&](int blk, float4 (&av)[4]) {
;                 const float* ap = a3 + (size_t)(blk * 16 + col) * 64 + kc * 8;
;                 av[0] = *(const float4*)(ap); av[1] = *(const float4*)(ap + 4); av[2] = *(const float4*)(ap + 32); av[3] = *(const float4*)(ap + 36);
;             };
;             auto tap_blk = [&](int blk, const float4 (&av)[4]) {
;                 f32x4 acc = (f32x4){0.f, 0.f, 0.f, 0.f};
; #pragma unroll
;                 for (int ks = 0; ks < 2; ++ks) { const float4 a0 = av[ks * 2], a1 = av[ks * 2 + 1];
;                     u32x4 w; w.x = cvt_pk_bf16(a0.x, a0.y); w.y = cvt_pk_bf16(a0.z, a0.w); w.z = cvt_pk_bf16(a1.x, a1.y); w.w = cvt_pk_bf16(a1.z, a1.w);
;                     acc = __builtin_amdgcn_mfma_f32_16x16x32_bf16(__builtin_bit_cast(bf16x8, w), bw[ks], acc, 0, 0, 0); }
;                 const int tb = blk * 16 + kc * 4;
;                 float4 o;
;                 const float dsc = -delta * (1.f / (float)(T - 1));
;                 o.x = acc[0] * __expf((float)(tb + 0) * dsc); o.y = acc[1] * __expf((float)(tb + 1) * dsc);
.LBB0_387:
	s_nop 6
	s_lshl_b32 s12, s0, 2
	global_load_dword v120, v[10:11], off nt
	global_load_dword v110, v[10:11], off offset:256 nt
	global_load_dword v102, v[10:11], off offset:512 nt
	global_load_dword v94, v[10:11], off offset:768 nt
	v_lshl_add_u64 v[10:11], v[10:11], 0, s[12:13]
	global_load_dword v123, v[10:11], off nt
	global_load_dword v113, v[10:11], off offset:256 nt
	global_load_dword v105, v[10:11], off offset:512 nt
	global_load_dword v97, v[10:11], off offset:768 nt
	v_lshl_add_u64 v[10:11], v[10:11], 0, s[12:13]
	global_load_dword v121, v[10:11], off nt
	global_load_dword v111, v[10:11], off offset:256 nt
	global_load_dword v103, v[10:11], off offset:512 nt
	global_load_dword v95, v[10:11], off offset:768 nt
	v_lshl_add_u64 v[10:11], v[10:11], 0, s[12:13]
	global_load_dword v125, v[10:11], off nt
	global_load_dword v115, v[10:11], off offset:256 nt
	global_load_dword v107, v[10:11], off offset:512 nt
	global_load_dword v99, v[10:11], off offset:768 nt
	v_lshl_add_u64 v[10:11], v[10:11], 0, s[12:13]
	global_load_dword v122, v[10:11], off nt
	global_load_dword v112, v[10:11], off offset:256 nt
	global_load_dword v104, v[10:11], off offset:512 nt
	global_load_dword v96, v[10:11], off offset:768 nt
	v_lshl_add_u64 v[10:11], v[10:11], 0, s[12:13]
	v_cvt_f32_i32_e32 v12, v16
	global_load_dword v126, v[10:11], off nt
	global_load_dword v116, v[10:11], off offset:256 nt
	global_load_dword v108, v[10:11], off offset:512 nt
	global_load_dword v100, v[10:11], off offset:768 nt
	v_lshl_add_u64 v[10:11], v[10:11], 0, s[12:13]
	v_and_b32_e32 v128, 15, v14
	global_load_dword v124, v[10:11], off nt
	global_load_dword v114, v[10:11], off offset:256 nt
	global_load_dword v106, v[10:11], off offset:512 nt
	global_load_dword v98, v[10:11], off offset:768 nt
	v_lshl_add_u64 v[10:11], v[10:11], 0, s[12:13]
	global_load_dword v127, v[10:11], off nt
	global_load_dword v117, v[10:11], off offset:256 nt
	global_load_dword v109, v[10:11], off offset:512 nt
	global_load_dword v101, v[10:11], off offset:768 nt
	v_lshlrev_b32_e32 v60, 5, v15
	v_lshlrev_b32_e32 v10, 14, v128
	v_lshl_add_u64 v[70:71], s[2:3], 0, v[60:61]
	v_and_b32_e32 v60, 0x38000, v10
	v_and_b32_e32 v10, 1, v14
	v_fmamk_f32 v12, v12, 0x3bc49550, v118
	s_mov_b32 s0, 0xb9000400
	s_waitcnt lgkmcnt(0)
	v_cmp_eq_u32_e64 s[8:9], 1, v10
	v_ashrrev_i32_e32 v10, 2, v14
	v_lshlrev_b32_e32 v72, 2, v15
	v_mul_f32_e64 v129, |v12|, s0
	v_lshl_add_u64 v[74:75], s[10:11], 0, v[60:61]
	s_mov_b64 s[0:1], 0x4000
	v_and_b32_e32 v78, -16, v10
	s_add_i32 s12, s60, 1
	v_lshl_add_u64 v[76:77], v[74:75], 0, s[0:1]
	v_or_b32_e32 v10, v72, v78
	s_add_i32 s0, s60, 2
	v_mov_b32_e32 v73, v61
	v_or_b32_e32 v80, 0x80, v72
	v_mov_b32_e32 v81, v61
	v_or_b32_e32 v82, 0x100, v72
	v_mov_b32_e32 v83, v61
	v_or_b32_e32 v84, 0x180, v72
	v_mov_b32_e32 v85, v61
	s_mul_i32 s28, s16, s12
	s_mul_i32 s48, s68, s12
	v_sub_u32_e32 v86, 0x387d, v10
	s_mul_i32 s49, s16, s0
	s_mul_i32 s51, s68, s0
	s_mov_b32 s50, -2
	s_mov_b32 s52, s69
	s_mov_b32 s53, s17
	s_branch .LBB0_389

; __device__ __forceinline__ unsigned cvt_pk_bf16(float lo, float hi) { unsigned r; asm volatile("v_cvt_pk_bf16_f32 %0, %1, %2" : "=v"(r) : "v"(lo), "v"(hi)); return r; }
; #define BG_I(x) bg_issue1<x>(bg, bgwg, bgNW, bglane)
; __device__ __forceinline__ void hy_fft_phase(LAS unsigned char* lds, int bid, int G, const bf16_t* vgT, bf16_t* zT, const float* a3, const float* wout, const float* skip, float* filt, float4* gspec) {
;     ...
;             auto tap_load = [&](int blk, float4 (&av)[4]) {
;                 const float* ap = a3 + (size_t)(blk * 16 + col) * 64 + kc * 8;
;                 av[0] = *(const float4*)(ap); av[1] = *(const float4*)(ap + 4); av[2] = *(const float4*)(ap + 32); av[3] = *(const float4*)(ap + 36);
;             };
;             auto tap_blk = [&](int blk, const float4 (&av)[4]) {
;                 f32x4 acc = (f32x4){0.f, 0.f, 0.f, 0.f};
; #pragma unroll
;                 for (int ks = 0; ks < 2; ++ks) { const float4 a0 = av[ks * 2], a1 = av[ks * 2 + 1];
;                     u32x4 w; w.x = cvt_pk_bf16(a0.x, a0.y); w.y = cvt_pk_bf16(a0.z, a0.w); w.z = cvt_pk_bf16(a1.x, a1.y); w.w = cvt_pk_bf16(a1.z, a1.w);
;                     acc = __builtin_amdgcn_mfma_f32_16x16x32_bf16(__builtin_bit_cast(bf16x8, w), bw[ks], acc, 0, 0, 0); }
;                 const int tb = blk * 16 + kc * 4;
;                 float4 o;
;                 const float dsc = -delta * (1.f / (float)(T - 1));
;                 o.x = acc[0] * __expf((float)(tb + 0) * dsc); o.y = acc[1] * __expf((float)(tb + 1) * dsc);
;                 o.z = acc[2] * __expf((float)(tb + 2) * dsc); o.w = acc[3] * __expf((float)(tb + 3) * dsc);
;                 bf16_t* Arow = F + (size_t)(col >> 1) * FN;
;                 if ((col & 1) == 0) { u32x2 w; w.x = cvt_pk_bf16(o.x, o.y); w.y = cvt_pk_bf16(o.z, o.w); *(u32x2*)(Arow + tb) = w; }
;                 else {
;                     Arow[FN - tb - 3] = (bf16_t)(cvt_pk_bf16(o.w, 0.f) & 0xffffu);
;                     *(unsigned*)(Arow + FN - tb - 2) = cvt_pk_bf16(o.z, o.y);
;                     if (tb > 0) Arow[FN - tb] = (bf16_t)(cvt_pk_bf16(o.x, 0.f) & 0xffffu); else Arow[T] = (bf16_t)0;
;                 }
;             };
;             BG_I(0);
; #pragma unroll 1
;             for (int ob = 0; ob < 8; ob += 2) {
;                 BG_I(1);
;     ...
;                 TAP_GROUP(ob * 8); TAP_GROUP(ob * 8 + 4);
.LBB0_399:
	s_nop 6
	s_lshl_b32 s12, s42, 2
	global_load_dword v154, v[10:11], off nt
	global_load_dword v146, v[10:11], off offset:256 nt
	global_load_dword v138, v[10:11], off offset:512 nt
	global_load_dword v130, v[10:11], off offset:768 nt
	v_lshl_add_u64 v[10:11], v[10:11], 0, s[12:13]
	global_load_dword v156, v[10:11], off nt
	global_load_dword v148, v[10:11], off offset:256 nt
	global_load_dword v140, v[10:11], off offset:512 nt
	global_load_dword v132, v[10:11], off offset:768 nt
	v_lshl_add_u64 v[10:11], v[10:11], 0, s[12:13]
	global_load_dword v155, v[10:11], off nt
	global_load_dword v147, v[10:11], off offset:256 nt
	global_load_dword v139, v[10:11], off offset:512 nt
	global_load_dword v131, v[10:11], off offset:768 nt
	v_lshl_add_u64 v[10:11], v[10:11], 0, s[12:13]
	global_load_dword v158, v[10:11], off nt
	global_load_dword v150, v[10:11], off offset:256 nt
	global_load_dword v142, v[10:11], off offset:512 nt
	global_load_dword v134, v[10:11], off offset:768 nt
	v_lshl_add_u64 v[10:11], v[10:11], 0, s[12:13]
	global_load_dword v157, v[10:11], off nt
	global_load_dword v149, v[10:11], off offset:256 nt
	global_load_dword v141, v[10:11], off offset:512 nt
	global_load_dword v133, v[10:11], off offset:768 nt
	v_lshl_add_u64 v[10:11], v[10:11], 0, s[12:13]
	global_load_dword v160, v[10:11], off nt
	global_load_dword v152, v[10:11], off offset:256 nt
	global_load_dword v144, v[10:11], off offset:512 nt
	global_load_dword v136, v[10:11], off offset:768 nt
	v_lshl_add_u64 v[10:11], v[10:11], 0, s[12:13]
	v_add_u32_e32 v92, v128, v78
	global_load_dword v159, v[10:11], off nt
	global_load_dword v151, v[10:11], off offset:256 nt
	global_load_dword v143, v[10:11], off offset:512 nt
	global_load_dword v135, v[10:11], off offset:768 nt
	v_lshl_add_u64 v[10:11], v[10:11], 0, s[12:13]
	v_ashrrev_i32_e32 v93, 31, v92
	global_load_dword v161, v[10:11], off nt
	global_load_dword v153, v[10:11], off offset:256 nt
	global_load_dword v145, v[10:11], off offset:512 nt
	global_load_dword v137, v[10:11], off offset:768 nt
	v_lshlrev_b64 v[10:11], 8, v[92:93]
	v_lshl_add_u64 v[10:11], v[70:71], 0, v[10:11]
	global_load_dwordx4 v[162:165], v[10:11], off offset:16
	global_load_dwordx4 v[166:169], v[10:11], off
	global_load_dwordx4 v[170:173], v[10:11], off offset:144
	global_load_dwordx4 v[174:177], v[10:11], off offset:128
	v_add_u32_e32 v10, 0x80, v92
	v_ashrrev_i32_e32 v11, 31, v10
	v_lshlrev_b64 v[10:11], 8, v[10:11]
	v_lshl_add_u64 v[10:11], v[70:71], 0, v[10:11]
	global_load_dwordx4 v[50:53], v[10:11], off offset:16
	global_load_dwordx4 v[54:57], v[10:11], off
	global_load_dwordx4 v[42:45], v[10:11], off offset:144
	global_load_dwordx4 v[46:49], v[10:11], off offset:128
	v_add_u32_e32 v10, 0x100, v92
	v_ashrrev_i32_e32 v11, 31, v10
	v_lshlrev_b64 v[10:11], 8, v[10:11]
	v_lshl_add_u64 v[10:11], v[70:71], 0, v[10:11]
	global_load_dwordx4 v[34:37], v[10:11], off offset:16
	global_load_dwordx4 v[38:41], v[10:11], off
	global_load_dwordx4 v[26:29], v[10:11], off offset:144
	global_load_dwordx4 v[30:33], v[10:11], off offset:128
	v_add_u32_e32 v10, 0x180, v92
	v_ashrrev_i32_e32 v11, 31, v10
	v_lshlrev_b64 v[10:11], 8, v[10:11]
	v_lshl_add_u64 v[14:15], v[70:71], 0, v[10:11]
	global_load_dwordx4 v[18:21], v[14:15], off offset:16
	global_load_dwordx4 v[22:25], v[14:15], off
	global_load_dwordx4 v[10:13], v[14:15], off offset:144
	s_nop 0
	global_load_dwordx4 v[14:17], v[14:15], off offset:128
	v_add_u32_e32 v90, v72, v78
	v_add_u32_e32 v65, 1, v90
	v_add_u32_e32 v67, 2, v90
	v_add_u32_e32 v79, 3, v90
	v_cvt_f32_i32_e32 v60, v90
	v_cvt_f32_i32_e32 v65, v65
	v_cvt_f32_i32_e32 v67, v67
	v_cvt_f32_i32_e32 v79, v79
	v_mul_f32_e32 v60, v129, v60
	v_mul_f32_e32 v65, v129, v65
	v_mul_f32_e32 v67, v129, v67
	v_mul_f32_e32 v79, v129, v79
	v_mul_f32_e32 v60, 0x3fb8aa3b, v60
	v_mul_f32_e32 v65, 0x3fb8aa3b, v65
	v_mul_f32_e32 v67, 0x3fb8aa3b, v67
	v_mul_f32_e32 v79, 0x3fb8aa3b, v79
	v_exp_f32_e32 v60, v60
	v_exp_f32_e32 v65, v65
	v_exp_f32_e32 v87, v67
	v_exp_f32_e32 v79, v79
	s_waitcnt vmcnt(14)
	v_cvt_pk_bf16_f32 v166, v166, v167
	v_cvt_pk_bf16_f32 v167, v168, v169
	v_cvt_pk_bf16_f32 v168, v162, v163
	v_cvt_pk_bf16_f32 v169, v164, v165
	s_waitcnt vmcnt(12)
	v_cvt_pk_bf16_f32 v162, v174, v175
	v_cvt_pk_bf16_f32 v163, v176, v177
	v_cvt_pk_bf16_f32 v164, v170, v171
	v_cvt_pk_bf16_f32 v165, v172, v173
	v_mfma_f32_16x16x32_bf16 v[166:169], v[166:169], v[2:5], 0
	v_mfma_f32_16x16x32_bf16 v[162:165], v[162:165], v[6:9], v[166:169]
	s_nop 7
	v_mul_f32_e32 v60, v60, v162
	v_mul_f32_e32 v67, v65, v163
	v_mul_f32_e32 v65, v87, v164
	v_mul_f32_e32 v79, v79, v165
	s_and_saveexec_b64 s[42:43], s[8:9]
	s_xor_b64 s[42:43], exec, s[42:43]
	s_cbranch_execz .LBB0_405
	v_add_u32_e32 v162, 0x780, v86
	v_ashrrev_i32_e32 v163, 31, v162
	v_lshl_add_u64 v[162:163], v[162:163], 1, v[74:75]
	v_cvt_pk_bf16_f32 v79, v79, v61
	global_store_short v[162:163], v79, off
	v_add_u32_e32 v162, 0xffffc783, v86
	v_ashrrev_i32_e32 v163, 31, v162
	v_lshl_add_u64 v[162:163], v[162:163], 1, v[74:75]
	v_add_co_u32_e32 v162, vcc, 0x7000, v162
	v_cvt_pk_bf16_f32 v65, v65, v67
	s_nop 1
	v_addc_co_u32_e32 v163, vcc, 0, v163, vcc
	v_cmp_gt_i32_e32 vcc, 1, v90
	global_store_dword v[162:163], v65, off offset:4092
	s_and_saveexec_b64 s[46:47], vcc
	s_xor_b64 s[46:47], exec, s[46:47]
	s_cbranch_execz .LBB0_402
	global_store_short v[76:77], v61, off

; __device__ __forceinline__ unsigned cvt_pk_bf16(float lo, float hi) { unsigned r; asm volatile("v_cvt_pk_bf16_f32 %0, %1, %2" : "=v"(r) : "v"(lo), "v"(hi)); return r; }
; template <int BANK, int WAITN> __device__ __forceinline__ void bg_finish1(BgState& b) {
;     if (WAITN == 32) asm volatile("s_waitcnt vmcnt(32)" ::: "memory"); else asm volatile("s_waitcnt vmcnt(0)" ::: "memory");
;     asm volatile("" : BG_TIE16(BANK * 32) :: "memory");
;     asm volatile("" : BG_TIE16(BANK * 32 + 16) :: "memory");
;     bf16_t* dst = b.dst[BANK];
;     if (dst != nullptr) {
; #pragma unroll
;         for (int c = 0; c < 4; ++c) { u32x4 w;
;             w.x = cvt_pk_bf16(b.r[(BANK * 8 + 0) * 4 + c], b.r[(BANK * 8 + 1) * 4 + c]); w.y = cvt_pk_bf16(b.r[(BANK * 8 + 2) * 4 + c], b.r[(BANK * 8 + 3) * 4 + c]);
;             w.z = cvt_pk_bf16(b.r[(BANK * 8 + 4) * 4 + c], b.r[(BANK * 8 + 5) * 4 + c]); w.w = cvt_pk_bf16(b.r[(BANK * 8 + 6) * 4 + c], b.r[(BANK * 8 + 7) * 4 + c]);
;             bf16_t* dp = dst + (c & 1) * 512 + (c >> 1) * b.o2[BANK];
;             asm volatile("global_store_dwordx4 %0, %1, off\n\ts_nop 1" :: "v"(dp), "v"(w) : "memory"); }
;     }
; }
.LBB0_463:
	s_or_b64 exec, exec, s[42:43]
	s_waitcnt vmcnt(32)
	v_cmp_ne_u64_e32 vcc, 0, v[68:69]
	s_and_saveexec_b64 s[42:43], vcc
	s_xor_b64 s[42:43], exec, s[42:43]
	s_cbranch_execz .LBB0_465
	v_cvt_pk_bf16_f32 v10, v120, v123
	v_cvt_pk_bf16_f32 v11, v121, v125
	v_cvt_pk_bf16_f32 v12, v122, v126
	v_cvt_pk_bf16_f32 v13, v124, v127
	s_mov_b32 s45, s13
	global_store_dwordx4 v[68:69], v[10:13], off nt
	s_nop 1
	v_cvt_pk_bf16_f32 v10, v110, v113
	v_cvt_pk_bf16_f32 v11, v111, v115
	v_cvt_pk_bf16_f32 v12, v112, v116
	v_cvt_pk_bf16_f32 v13, v114, v117
	v_lshl_add_u64 v[14:15], v[68:69], 0, s[22:23]
	global_store_dwordx4 v[14:15], v[10:13], off nt
	s_nop 1
	v_cvt_pk_bf16_f32 v10, v102, v105
	v_cvt_pk_bf16_f32 v11, v103, v107
	v_cvt_pk_bf16_f32 v12, v104, v108
	v_cvt_pk_bf16_f32 v13, v106, v109
	s_lshl_b64 s[44:45], s[44:45], 1
	v_lshl_add_u64 v[16:17], v[68:69], 0, s[44:45]
	global_store_dwordx4 v[16:17], v[10:13], off nt
	s_nop 1
	v_cvt_pk_bf16_f32 v10, v94, v97
	v_cvt_pk_bf16_f32 v11, v95, v99
	v_cvt_pk_bf16_f32 v12, v96, v100
	v_cvt_pk_bf16_f32 v13, v98, v101
	v_lshl_add_u64 v[14:15], v[14:15], 0, s[44:45]
	global_store_dwordx4 v[14:15], v[10:13], off nt
	s_nop 1

; #define BG_I(x) bg_issue1<x>(bg, bgwg, bgNW, bglane)
; #define BG_F(y) bg_finish1<y, 32>(bg)
; __device__ __forceinline__ void hy_fft_phase(LAS unsigned char* lds, int bid, int G, const bf16_t* vgT, bf16_t* zT, const float* a3, const float* wout, const float* skip, float* filt, float4* gspec) {
;     ...
;             auto tap_load = [&](int blk, float4 (&av)[4]) {
;                 const float* ap = a3 + (size_t)(blk * 16 + col) * 64 + kc * 8;
;                 av[0] = *(const float4*)(ap); av[1] = *(const float4*)(ap + 4); av[2] = *(const float4*)(ap + 32); av[3] = *(const float4*)(ap + 36);
;             };
;             auto tap_blk = [&](int blk, const float4 (&av)[4]) {
;                 f32x4 acc = (f32x4){0.f, 0.f, 0.f, 0.f};
; #pragma unroll
;                 for (int ks = 0; ks < 2; ++ks) { const float4 a0 = av[ks * 2], a1 = av[ks * 2 + 1];
;                     u32x4 w; w.x = cvt_pk_bf16(a0.x, a0.y); w.y = cvt_pk_bf16(a0.z, a0.w); w.z = cvt_pk_bf16(a1.x, a1.y); w.w = cvt_pk_bf16(a1.z, a1.w);
;                     acc = __builtin_amdgcn_mfma_f32_16x16x32_bf16(__builtin_bit_cast(bf16x8, w), bw[ks], acc, 0, 0, 0); }
;                 const int tb = blk * 16 + kc * 4;
;                 float4 o;
;                 const float dsc = -delta * (1.f / (float)(T - 1));
;                 o.x = acc[0] * __expf((float)(tb + 0) * dsc); o.y = acc[1] * __expf((float)(tb + 1) * dsc);
;                 o.z = acc[2] * __expf((float)(tb + 2) * dsc); o.w = acc[3] * __expf((float)(tb + 3) * dsc);
;                 bf16_t* Arow = F + (size_t)(col >> 1) * FN;
;                 if ((col & 1) == 0) { u32x2 w; w.x = cvt_pk_bf16(o.x, o.y); w.y = cvt_pk_bf16(o.z, o.w); *(u32x2*)(Arow + tb) = w; }
;                 else {
;                     Arow[FN - tb - 3] = (bf16_t)(cvt_pk_bf16(o.w, 0.f) & 0xffffu);
;                     *(unsigned*)(Arow + FN - tb - 2) = cvt_pk_bf16(o.z, o.y);
;                     if (tb > 0) Arow[FN - tb] = (bf16_t)(cvt_pk_bf16(o.x, 0.f) & 0xffffu); else Arow[T] = (bf16_t)0;
;                 }
;             };
;             BG_I(0);
; #pragma unroll 1
;             for (int ob = 0; ob < 8; ob += 2) {
;                 BG_I(1);
;     ...
;                 TAP_GROUP(ob * 8); TAP_GROUP(ob * 8 + 4);
;                 BG_F(0);
;                 BG_I(0);
;                 TAP_GROUP((ob + 1) * 8); TAP_GROUP((ob + 1) * 8 + 4);
.LBB0_475:
	s_nop 6
	s_lshl_b32 s12, s42, 2
	global_load_dword v120, v[10:11], off nt
	global_load_dword v110, v[10:11], off offset:256 nt
	global_load_dword v102, v[10:11], off offset:512 nt
	global_load_dword v94, v[10:11], off offset:768 nt
	v_lshl_add_u64 v[10:11], v[10:11], 0, s[12:13]
	global_load_dword v123, v[10:11], off nt
	global_load_dword v113, v[10:11], off offset:256 nt
	global_load_dword v105, v[10:11], off offset:512 nt
	global_load_dword v97, v[10:11], off offset:768 nt
	v_lshl_add_u64 v[10:11], v[10:11], 0, s[12:13]
	global_load_dword v121, v[10:11], off nt
	global_load_dword v111, v[10:11], off offset:256 nt
	global_load_dword v103, v[10:11], off offset:512 nt
	global_load_dword v95, v[10:11], off offset:768 nt
	v_lshl_add_u64 v[10:11], v[10:11], 0, s[12:13]
	global_load_dword v125, v[10:11], off nt
	global_load_dword v115, v[10:11], off offset:256 nt
	global_load_dword v107, v[10:11], off offset:512 nt
	global_load_dword v99, v[10:11], off offset:768 nt
	v_lshl_add_u64 v[10:11], v[10:11], 0, s[12:13]
	global_load_dword v122, v[10:11], off nt
	global_load_dword v112, v[10:11], off offset:256 nt
	global_load_dword v104, v[10:11], off offset:512 nt
	global_load_dword v96, v[10:11], off offset:768 nt
	v_lshl_add_u64 v[10:11], v[10:11], 0, s[12:13]
	global_load_dword v126, v[10:11], off nt
	global_load_dword v116, v[10:11], off offset:256 nt
	global_load_dword v108, v[10:11], off offset:512 nt
	global_load_dword v100, v[10:11], off offset:768 nt
	v_lshl_add_u64 v[10:11], v[10:11], 0, s[12:13]
	global_load_dword v124, v[10:11], off nt
	global_load_dword v114, v[10:11], off offset:256 nt
	global_load_dword v106, v[10:11], off offset:512 nt
	global_load_dword v98, v[10:11], off offset:768 nt
	v_lshl_add_u64 v[10:11], v[10:11], 0, s[12:13]
	global_load_dword v127, v[10:11], off nt
	global_load_dword v117, v[10:11], off offset:256 nt
	global_load_dword v109, v[10:11], off offset:512 nt
	global_load_dword v101, v[10:11], off offset:768 nt
	v_add_u32_e32 v10, 0x400, v92
	v_ashrrev_i32_e32 v11, 31, v10
	v_lshlrev_b64 v[10:11], 8, v[10:11]
	v_lshl_add_u64 v[10:11], v[70:71], 0, v[10:11]
	global_load_dwordx4 v[162:165], v[10:11], off offset:16
	global_load_dwordx4 v[166:169], v[10:11], off
	global_load_dwordx4 v[170:173], v[10:11], off offset:144
	global_load_dwordx4 v[174:177], v[10:11], off offset:128
	v_add_u32_e32 v10, 0x480, v92
	v_ashrrev_i32_e32 v11, 31, v10
	v_lshlrev_b64 v[10:11], 8, v[10:11]
	v_lshl_add_u64 v[10:11], v[70:71], 0, v[10:11]
	global_load_dwordx4 v[50:53], v[10:11], off offset:16
	global_load_dwordx4 v[54:57], v[10:11], off
	global_load_dwordx4 v[42:45], v[10:11], off offset:144
	global_load_dwordx4 v[46:49], v[10:11], off offset:128
	v_add_u32_e32 v10, 0x500, v92
	v_ashrrev_i32_e32 v11, 31, v10
	v_lshlrev_b64 v[10:11], 8, v[10:11]
	v_lshl_add_u64 v[10:11], v[70:71], 0, v[10:11]
	global_load_dwordx4 v[34:37], v[10:11], off offset:16
	global_load_dwordx4 v[38:41], v[10:11], off
	global_load_dwordx4 v[26:29], v[10:11], off offset:144
	global_load_dwordx4 v[30:33], v[10:11], off offset:128
	v_add_u32_e32 v10, 0x580, v92
	v_ashrrev_i32_e32 v11, 31, v10
	v_lshlrev_b64 v[10:11], 8, v[10:11]
	v_lshl_add_u64 v[14:15], v[70:71], 0, v[10:11]
	global_load_dwordx4 v[18:21], v[14:15], off offset:16
	global_load_dwordx4 v[22:25], v[14:15], off
	global_load_dwordx4 v[10:13], v[14:15], off offset:144
	s_nop 0
	global_load_dwordx4 v[14:17], v[14:15], off offset:128
	v_add_u32_e32 v60, 0x400, v90
	v_add_u32_e32 v65, 0x401, v90
	v_add_u32_e32 v67, 0x402, v90
	v_add_u32_e32 v87, 0x403, v90
	v_cvt_f32_i32_e32 v91, v60
	v_cvt_f32_i32_e32 v65, v65
	v_cvt_f32_i32_e32 v67, v67
	v_cvt_f32_i32_e32 v87, v87
	v_mul_f32_e32 v91, v129, v91
	v_mul_f32_e32 v65, v129, v65
	v_mul_f32_e32 v67, v129, v67
	v_mul_f32_e32 v87, v129, v87
	v_mul_f32_e32 v91, 0x3fb8aa3b, v91
	v_mul_f32_e32 v65, 0x3fb8aa3b, v65
	v_mul_f32_e32 v67, 0x3fb8aa3b, v67
	v_mul_f32_e32 v87, 0x3fb8aa3b, v87
	v_exp_f32_e32 v91, v91
	v_exp_f32_e32 v93, v65
	v_exp_f32_e32 v67, v67
	v_exp_f32_e32 v178, v87
	s_waitcnt vmcnt(14)
	v_cvt_pk_bf16_f32 v166, v166, v167
	v_cvt_pk_bf16_f32 v167, v168, v169
	v_cvt_pk_bf16_f32 v168, v162, v163
	v_cvt_pk_bf16_f32 v169, v164, v165
	s_waitcnt vmcnt(12)
	v_cvt_pk_bf16_f32 v162, v174, v175
	v_cvt_pk_bf16_f32 v163, v176, v177
	v_cvt_pk_bf16_f32 v164, v170, v171
	v_cvt_pk_bf16_f32 v165, v172, v173
	v_mfma_f32_16x16x32_bf16 v[166:169], v[166:169], v[2:5], 0
	v_mfma_f32_16x16x32_bf16 v[162:165], v[162:165], v[6:9], v[166:169]
	s_nop 7
	v_mul_f32_e32 v65, v91, v162
	v_mul_f32_e32 v87, v93, v163
	v_mul_f32_e32 v67, v67, v164
	v_mul_f32_e32 v91, v178, v165
	s_and_saveexec_b64 s[42:43], s[8:9]
	s_xor_b64 s[42:43], exec, s[42:43]
	s_cbranch_execz .LBB0_481
	v_add_u32_e32 v162, 0x380, v86
	v_ashrrev_i32_e32 v163, 31, v162
	v_lshl_add_u64 v[162:163], v[162:163], 1, v[74:75]
	v_cvt_pk_bf16_f32 v91, v91, v61
	global_store_short v[162:163], v91, off
	v_lshl_add_u64 v[162:163], v[78:79], 0, v[72:73]
	v_lshlrev_b64 v[162:163], 1, v[162:163]
	v_cvt_pk_bf16_f32 v67, v67, v87
	v_sub_co_u32_e32 v87, vcc, v74, v162
	s_nop 1
	v_subb_co_u32_e32 v91, vcc, v75, v163, vcc
	v_add_co_u32_e32 v162, vcc, 0x7000, v87
	s_nop 1
	v_addc_co_u32_e32 v163, vcc, 0, v91, vcc
	v_cmp_gt_i32_e32 vcc, 1, v60
	global_store_dword v[162:163], v67, off offset:2044
	s_and_saveexec_b64 s[46:47], vcc
	s_xor_b64 s[46:47], exec, s[46:47]
	s_cbranch_execz .LBB0_478
	global_store_short v[76:77], v61, off

; __device__ __forceinline__ unsigned cvt_pk_bf16(float lo, float hi) { unsigned r; asm volatile("v_cvt_pk_bf16_f32 %0, %1, %2" : "=v"(r) : "v"(lo), "v"(hi)); return r; }
; template <int BANK, int WAITN> __device__ __forceinline__ void bg_finish1(BgState& b) {
;     if (WAITN == 32) asm volatile("s_waitcnt vmcnt(32)" ::: "memory"); else asm volatile("s_waitcnt vmcnt(0)" ::: "memory");
;     asm volatile("" : BG_TIE16(BANK * 32) :: "memory");
;     asm volatile("" : BG_TIE16(BANK * 32 + 16) :: "memory");
;     bf16_t* dst = b.dst[BANK];
;     if (dst != nullptr) {
; #pragma unroll
;         for (int c = 0; c < 4; ++c) { u32x4 w;
;             w.x = cvt_pk_bf16(b.r[(BANK * 8 + 0) * 4 + c], b.r[(BANK * 8 + 1) * 4 + c]); w.y = cvt_pk_bf16(b.r[(BANK * 8 + 2) * 4 + c], b.r[(BANK * 8 + 3) * 4 + c]);
;             w.z = cvt_pk_bf16(b.r[(BANK * 8 + 4) * 4 + c], b.r[(BANK * 8 + 5) * 4 + c]); w.w = cvt_pk_bf16(b.r[(BANK * 8 + 6) * 4 + c], b.r[(BANK * 8 + 7) * 4 + c]);
;             bf16_t* dp = dst + (c & 1) * 512 + (c >> 1) * b.o2[BANK];
;             asm volatile("global_store_dwordx4 %0, %1, off\n\ts_nop 1" :: "v"(dp), "v"(w) : "memory"); }
;     }
; }
.LBB0_539:
	s_or_b64 exec, exec, s[42:43]
	s_waitcnt vmcnt(32)
	v_cmp_ne_u64_e32 vcc, 0, v[88:89]
	s_and_saveexec_b64 s[42:43], vcc
	s_xor_b64 s[42:43], exec, s[42:43]
	s_cbranch_execz .LBB0_388
	v_cvt_pk_bf16_f32 v10, v154, v156
	v_cvt_pk_bf16_f32 v11, v155, v158
	v_cvt_pk_bf16_f32 v12, v157, v160
	v_cvt_pk_bf16_f32 v13, v159, v161
	v_lshl_add_u64 v[14:15], v[88:89], 0, s[22:23]
	global_store_dwordx4 v[88:89], v[10:13], off nt
	s_nop 1
	v_cvt_pk_bf16_f32 v10, v146, v148
	v_cvt_pk_bf16_f32 v11, v147, v150
	v_cvt_pk_bf16_f32 v12, v149, v152
	v_cvt_pk_bf16_f32 v13, v151, v153
	s_lshl_b32 s12, s0, 1
	global_store_dwordx4 v[14:15], v[10:13], off nt
	s_nop 1
	v_cvt_pk_bf16_f32 v10, v138, v140
	v_cvt_pk_bf16_f32 v11, v139, v142
	v_cvt_pk_bf16_f32 v12, v141, v144
	v_cvt_pk_bf16_f32 v13, v143, v145
	v_lshl_add_u64 v[16:17], v[88:89], 0, s[12:13]
	global_store_dwordx4 v[16:17], v[10:13], off nt
	s_nop 1
	v_cvt_pk_bf16_f32 v10, v130, v132
	v_cvt_pk_bf16_f32 v11, v131, v134
	v_cvt_pk_bf16_f32 v12, v133, v136
	v_cvt_pk_bf16_f32 v13, v135, v137
	v_lshl_add_u64 v[14:15], v[14:15], 0, s[12:13]
	global_store_dwordx4 v[14:15], v[10:13], off nt
	s_nop 1
	s_branch .LBB0_388

; #define LAS __attribute__((address_space(3)))
; __device__ __forceinline__ float bf_lo(unsigned w) { return __uint_as_float(w << 16); }
; __device__ __forceinline__ float bf_hi(unsigned w) { return __uint_as_float(w & 0xffff0000u); }
; #define SEG_WAIT() asm volatile("s_waitcnt vmcnt(32)\n\ts_nop 7" ::: "memory")
; #define BG_I(x) bg_issue1<x>(bg, bgwg, bgNW, bglane)
; #define BG_F(y) bg_finish1<y, 32>(bg)
; __device__ __forceinline__ void hy_fft_phase(LAS unsigned char* lds, int bid, int G, const bf16_t* vgT, bf16_t* zT, const float* a3, const float* wout, const float* skip, float* filt, float4* gspec) {
;     ...
;                 BG_I(1);
;                 SEG_WAIT(); asm volatile("" : SEG_TIE8(pa, 0), SEG_TIE8(pa, 8), SEG_TIE8(pb, 0) :: "memory");
;                 asm volatile("" : SEG_TIE8(pb, 8), "+v"(sk[0]), "+v"(sk[1]) :: "memory");
;                 const float sk1 = (tid == 0) ? sk[0] : 0.f, sk2 = (tid == 0 && has2) ? sk[1] : 0.f;
; #pragma unroll
;                 for (int i = 0; i < 16; ++i) { const int n = 2 * tid + 2 * NTHR * i;
;                     f32x4 fv = (f32x4){bf_lo(pa[i]), has2 ? bf_lo(pb[i]) : 0.f, bf_hi(pa[i]), has2 ? bf_hi(pb[i]) : 0.f};
;                     if (i == 0) { fv[0] += sk1; fv[1] += sk2; }
;                     *(LAS f32x4*)&z[PADI(n)] = fv; }
;                 BG_F(0);
.LBB0_553:
	s_nop 6
	global_load_dword v32, v[4:5], off nt
	global_load_dword v24, v[4:5], off offset:256 nt
	global_load_dword v16, v[4:5], off offset:512 nt
	global_load_dword v8, v[4:5], off offset:768 nt
	s_lshl_b32 s12, s42, 2
	v_lshl_add_u64 v[4:5], v[4:5], 0, s[12:13]
	global_load_dword v36, v[4:5], off nt
	global_load_dword v26, v[4:5], off offset:256 nt
	global_load_dword v18, v[4:5], off offset:512 nt
	global_load_dword v10, v[4:5], off offset:768 nt
	v_lshl_add_u64 v[4:5], v[4:5], 0, s[12:13]
	global_load_dword v33, v[4:5], off nt
	global_load_dword v25, v[4:5], off offset:256 nt
	global_load_dword v17, v[4:5], off offset:512 nt
	global_load_dword v9, v[4:5], off offset:768 nt
	v_lshl_add_u64 v[4:5], v[4:5], 0, s[12:13]
	global_load_dword v38, v[4:5], off nt
	global_load_dword v28, v[4:5], off offset:256 nt
	global_load_dword v20, v[4:5], off offset:512 nt
	global_load_dword v12, v[4:5], off offset:768 nt
	v_lshl_add_u64 v[4:5], v[4:5], 0, s[12:13]
	global_load_dword v37, v[4:5], off nt
	global_load_dword v27, v[4:5], off offset:256 nt
	global_load_dword v19, v[4:5], off offset:512 nt
	global_load_dword v11, v[4:5], off offset:768 nt
	v_lshl_add_u64 v[4:5], v[4:5], 0, s[12:13]
	global_load_dword v40, v[4:5], off nt
	global_load_dword v30, v[4:5], off offset:256 nt
	global_load_dword v22, v[4:5], off offset:512 nt
	global_load_dword v14, v[4:5], off offset:768 nt
	v_lshl_add_u64 v[4:5], v[4:5], 0, s[12:13]
	global_load_dword v39, v[4:5], off nt
	global_load_dword v29, v[4:5], off offset:256 nt
	global_load_dword v21, v[4:5], off offset:512 nt
	global_load_dword v13, v[4:5], off offset:768 nt
	v_lshl_add_u64 v[4:5], v[4:5], 0, s[12:13]
	global_load_dword v41, v[4:5], off nt
	global_load_dword v31, v[4:5], off offset:256 nt
	global_load_dword v23, v[4:5], off offset:512 nt
	global_load_dword v15, v[4:5], off offset:768 nt
	s_waitcnt vmcnt(32)
	s_nop 7
	v_cmp_eq_u32_e32 vcc, 0, v80
	v_lshlrev_b32_e32 v65, 16, v81
	v_lshlrev_b32_e32 v67, 16, v82
	v_cndmask_b32_e32 v4, 0, v83, vcc
	s_and_b64 vcc, s[8:9], vcc
	v_cndmask_b32_e32 v5, 0, v84, vcc
	v_and_b32_e32 v84, 0xffff0000, v81
	v_and_b32_e32 v81, 0xffff0000, v82
	v_add_f32_e32 v82, v4, v65
	v_ashrrev_i32_e32 v4, 4, v80
	v_lshlrev_b32_e32 v4, 3, v4
	v_cndmask_b32_e64 v67, 0, v67, s[8:9]
	v_lshl_add_u32 v65, v80, 4, 0
	v_and_b32_e32 v4, -16, v4
	v_lshlrev_b32_e32 v60, 1, v80
	v_cndmask_b32_e64 v85, 0, v81, s[8:9]
	v_add_f32_e32 v83, v5, v67
	v_add_u32_e32 v4, v65, v4
	ds_write_b128 v4, v[82:85]
	v_add_u32_e32 v4, 0x400, v60
	v_ashrrev_i32_e32 v4, 5, v4
	v_lshlrev_b32_e32 v5, 16, v79
	v_lshlrev_b32_e32 v4, 3, v4
	v_cndmask_b32_e64 v81, 0, v5, s[8:9]
	v_and_b32_e32 v5, 0xffff0000, v79
	v_and_b32_e32 v4, -16, v4
	v_lshlrev_b32_e32 v80, 16, v78
	v_and_b32_e32 v82, 0xffff0000, v78
	v_cndmask_b32_e64 v83, 0, v5, s[8:9]
	v_add_u32_e32 v4, v65, v4
	ds_write_b128 v4, v[80:83] offset:8192
	v_add_u32_e32 v4, 0x800, v60
	v_ashrrev_i32_e32 v4, 5, v4
	v_lshlrev_b32_e32 v5, 16, v77
	v_lshlrev_b32_e32 v4, 3, v4
	v_cndmask_b32_e64 v79, 0, v5, s[8:9]
	v_and_b32_e32 v5, 0xffff0000, v77
	v_and_b32_e32 v4, -16, v4
	v_lshlrev_b32_e32 v78, 16, v76
	v_and_b32_e32 v80, 0xffff0000, v76
	v_cndmask_b32_e64 v81, 0, v5, s[8:9]
	v_add_u32_e32 v4, v65, v4
	ds_write_b128 v4, v[78:81] offset:16384
	v_add_u32_e32 v4, 0xc00, v60
	v_ashrrev_i32_e32 v4, 5, v4
	v_lshlrev_b32_e32 v5, 16, v75
	v_lshlrev_b32_e32 v4, 3, v4
	v_cndmask_b32_e64 v77, 0, v5, s[8:9]
	v_and_b32_e32 v5, 0xffff0000, v75
	v_and_b32_e32 v4, -16, v4
	v_lshlrev_b32_e32 v76, 16, v74
	v_and_b32_e32 v78, 0xffff0000, v74
	v_cndmask_b32_e64 v79, 0, v5, s[8:9]
	v_add_u32_e32 v4, v65, v4
	ds_write_b128 v4, v[76:79] offset:24576
	v_add_u32_e32 v4, 0x1000, v60
	v_ashrrev_i32_e32 v4, 5, v4
	v_lshlrev_b32_e32 v5, 16, v73
	v_lshlrev_b32_e32 v4, 3, v4
	v_cndmask_b32_e64 v75, 0, v5, s[8:9]
	v_and_b32_e32 v5, 0xffff0000, v73
	v_and_b32_e32 v4, -16, v4
	v_lshlrev_b32_e32 v74, 16, v72
	v_and_b32_e32 v76, 0xffff0000, v72
	v_cndmask_b32_e64 v77, 0, v5, s[8:9]
	v_add_u32_e32 v4, v65, v4
	ds_write_b128 v4, v[74:77] offset:32768
	v_add_u32_e32 v4, 0x1400, v60
	v_ashrrev_i32_e32 v4, 5, v4
	v_lshlrev_b32_e32 v5, 16, v71
	v_lshlrev_b32_e32 v4, 3, v4
	v_cndmask_b32_e64 v73, 0, v5, s[8:9]
	v_and_b32_e32 v5, 0xffff0000, v71
	v_and_b32_e32 v4, -16, v4
	v_lshlrev_b32_e32 v72, 16, v70
	v_and_b32_e32 v74, 0xffff0000, v70
	v_cndmask_b32_e64 v75, 0, v5, s[8:9]
	v_add_u32_e32 v4, v65, v4
	ds_write_b128 v4, v[72:75] offset:40960
	v_add_u32_e32 v4, 0x1800, v60
	v_ashrrev_i32_e32 v4, 5, v4
	v_lshlrev_b32_e32 v5, 16, v57
	v_lshlrev_b32_e32 v4, 3, v4
	v_cndmask_b32_e64 v71, 0, v5, s[8:9]
	v_and_b32_e32 v5, 0xffff0000, v57
	v_and_b32_e32 v4, -16, v4
; #define LAS __attribute__((address_space(3)))
; __device__ __forceinline__ unsigned cvt_pk_bf16(float lo, float hi) { unsigned r; asm volatile("v_cvt_pk_bf16_f32 %0, %1, %2" : "=v"(r) : "v"(lo), "v"(hi)); return r; }
; __device__ __forceinline__ float bf_lo(unsigned w) { return __uint_as_float(w << 16); }
; __device__ __forceinline__ float bf_hi(unsigned w) { return __uint_as_float(w & 0xffff0000u); }
; #define BG_F(y) bg_finish1<y, 32>(bg)
; template <int BANK, int WAITN> __device__ __forceinline__ void bg_finish1(BgState& b) {
;     if (WAITN == 32) asm volatile("s_waitcnt vmcnt(32)" ::: "memory"); else asm volatile("s_waitcnt vmcnt(0)" ::: "memory");
;     asm volatile("" : BG_TIE16(BANK * 32) :: "memory");
;     asm volatile("" : BG_TIE16(BANK * 32 + 16) :: "memory");
;     bf16_t* dst = b.dst[BANK];
;     if (dst != nullptr) {
; #pragma unroll
;         for (int c = 0; c < 4; ++c) { u32x4 w;
;             w.x = cvt_pk_bf16(b.r[(BANK * 8 + 0) * 4 + c], b.r[(BANK * 8 + 1) * 4 + c]); w.y = cvt_pk_bf16(b.r[(BANK * 8 + 2) * 4 + c], b.r[(BANK * 8 + 3) * 4 + c]);
;             w.z = cvt_pk_bf16(b.r[(BANK * 8 + 4) * 4 + c], b.r[(BANK * 8 + 5) * 4 + c]); w.w = cvt_pk_bf16(b.r[(BANK * 8 + 6) * 4 + c], b.r[(BANK * 8 + 7) * 4 + c]);
;             bf16_t* dp = dst + (c & 1) * 512 + (c >> 1) * b.o2[BANK];
;             asm volatile("global_store_dwordx4 %0, %1, off\n\ts_nop 1" :: "v"(dp), "v"(w) : "memory"); }
;     }
; }
; __device__ __forceinline__ void hy_fft_phase(LAS unsigned char* lds, int bid, int G, const bf16_t* vgT, bf16_t* zT, const float* a3, const float* wout, const float* skip, float* filt, float4* gspec) {
;     ...
;                 const float sk1 = (tid == 0) ? sk[0] : 0.f, sk2 = (tid == 0 && has2) ? sk[1] : 0.f;
; #pragma unroll
;                 for (int i = 0; i < 16; ++i) { const int n = 2 * tid + 2 * NTHR * i;
;                     f32x4 fv = (f32x4){bf_lo(pa[i]), has2 ? bf_lo(pb[i]) : 0.f, bf_hi(pa[i]), has2 ? bf_hi(pb[i]) : 0.f};
;                     if (i == 0) { fv[0] += sk1; fv[1] += sk2; }
;                     *(LAS f32x4*)&z[PADI(n)] = fv; }
;                 BG_F(0);
	v_lshlrev_b32_e32 v70, 16, v56
	v_and_b32_e32 v72, 0xffff0000, v56
	v_cndmask_b32_e64 v73, 0, v5, s[8:9]
	v_add_u32_e32 v4, v65, v4
	ds_write_b128 v4, v[70:73] offset:49152
	v_add_u32_e32 v4, 0x1c00, v60
	v_ashrrev_i32_e32 v4, 5, v4
	v_lshlrev_b32_e32 v5, 16, v55
	v_lshlrev_b32_e32 v4, 3, v4
	v_cndmask_b32_e64 v71, 0, v5, s[8:9]
	v_and_b32_e32 v5, 0xffff0000, v55
	v_and_b32_e32 v4, -16, v4
	v_lshlrev_b32_e32 v70, 16, v54
	v_and_b32_e32 v72, 0xffff0000, v54
	v_cndmask_b32_e64 v73, 0, v5, s[8:9]
	v_add_u32_e32 v4, v65, v4
	ds_write_b128 v4, v[70:73] offset:57344
	v_add_u32_e32 v4, 0x2000, v60
	v_ashrrev_i32_e32 v4, 5, v4
	v_lshlrev_b32_e32 v5, 16, v53
	v_lshlrev_b32_e32 v4, 3, v4
	v_cndmask_b32_e64 v55, 0, v5, s[8:9]
	v_and_b32_e32 v5, 0xffff0000, v53
	v_and_b32_e32 v4, -16, v4
	v_lshlrev_b32_e32 v54, 16, v52
	v_and_b32_e32 v56, 0xffff0000, v52
	v_cndmask_b32_e64 v57, 0, v5, s[8:9]
	v_add3_u32 v4, v65, v4, s71
	ds_write_b128 v4, v[54:57]
	v_add_u32_e32 v4, 0x2400, v60
	v_ashrrev_i32_e32 v4, 5, v4
	v_lshlrev_b32_e32 v5, 16, v51
	v_lshlrev_b32_e32 v4, 3, v4
	v_cndmask_b32_e64 v53, 0, v5, s[8:9]
	v_and_b32_e32 v5, 0xffff0000, v51
	v_and_b32_e32 v4, -16, v4
	v_lshlrev_b32_e32 v52, 16, v50
	v_and_b32_e32 v54, 0xffff0000, v50
	v_cndmask_b32_e64 v55, 0, v5, s[8:9]
	v_add3_u32 v4, v65, v4, s76
	ds_write_b128 v4, v[52:55]
	v_add_u32_e32 v4, 0x2800, v60
	v_ashrrev_i32_e32 v4, 5, v4
	v_lshlrev_b32_e32 v5, 16, v49
	v_lshlrev_b32_e32 v4, 3, v4
	v_cndmask_b32_e64 v51, 0, v5, s[8:9]
	v_and_b32_e32 v5, 0xffff0000, v49
	v_and_b32_e32 v4, -16, v4
	v_lshlrev_b32_e32 v50, 16, v48
	v_and_b32_e32 v52, 0xffff0000, v48
	v_cndmask_b32_e64 v53, 0, v5, s[8:9]
	v_add3_u32 v4, v65, v4, s72
	ds_write_b128 v4, v[50:53]
	v_add_u32_e32 v4, 0x2c00, v60
	v_ashrrev_i32_e32 v4, 5, v4
	v_lshlrev_b32_e32 v5, 16, v47
	v_lshlrev_b32_e32 v4, 3, v4
	v_cndmask_b32_e64 v49, 0, v5, s[8:9]
	v_and_b32_e32 v5, 0xffff0000, v47
	v_and_b32_e32 v4, -16, v4
	v_lshlrev_b32_e32 v48, 16, v46
	v_and_b32_e32 v50, 0xffff0000, v46
	v_cndmask_b32_e64 v51, 0, v5, s[8:9]
	v_add3_u32 v4, v65, v4, s77
	ds_write_b128 v4, v[48:51]
	v_add_u32_e32 v4, 0x3000, v60
	v_ashrrev_i32_e32 v4, 5, v4
	v_lshlrev_b32_e32 v5, 16, v45
	v_lshlrev_b32_e32 v4, 3, v4
	v_cndmask_b32_e64 v47, 0, v5, s[8:9]
	v_and_b32_e32 v5, 0xffff0000, v45
	v_and_b32_e32 v4, -16, v4
	v_lshlrev_b32_e32 v46, 16, v44
	v_and_b32_e32 v48, 0xffff0000, v44
	v_cndmask_b32_e64 v49, 0, v5, s[8:9]
	v_add3_u32 v4, v65, v4, s73
	ds_write_b128 v4, v[46:49]
	v_add_u32_e32 v4, 0x3400, v60
	v_ashrrev_i32_e32 v4, 5, v4
	v_lshlrev_b32_e32 v5, 16, v43
	v_lshlrev_b32_e32 v4, 3, v4
	v_cndmask_b32_e64 v45, 0, v5, s[8:9]
	v_and_b32_e32 v5, 0xffff0000, v43
	v_and_b32_e32 v4, -16, v4
	v_lshlrev_b32_e32 v44, 16, v42
	v_and_b32_e32 v46, 0xffff0000, v42
	v_cndmask_b32_e64 v47, 0, v5, s[8:9]
	v_add3_u32 v4, v65, v4, s78
	ds_write_b128 v4, v[44:47]
	v_add_u32_e32 v4, 0x3800, v60
	v_lshlrev_b32_e32 v42, 16, v34
	v_and_b32_e32 v44, 0xffff0000, v34
	v_ashrrev_i32_e32 v4, 5, v4
	v_add_u32_e32 v34, 0x3c00, v60
	v_lshlrev_b32_e32 v5, 16, v35
	v_lshlrev_b32_e32 v4, 3, v4
	v_ashrrev_i32_e32 v34, 5, v34
	v_cndmask_b32_e64 v43, 0, v5, s[8:9]
	v_and_b32_e32 v5, 0xffff0000, v35
	v_and_b32_e32 v4, -16, v4
	v_lshlrev_b32_e32 v34, 3, v34
	v_cndmask_b32_e64 v45, 0, v5, s[8:9]
	v_add3_u32 v4, v65, v4, s74
	v_lshlrev_b32_e32 v5, 16, v7
	v_and_b32_e32 v7, 0xffff0000, v7
	v_and_b32_e32 v34, -16, v34
	ds_write_b128 v4, v[42:45]
	v_lshlrev_b32_e32 v4, 16, v6
	v_cndmask_b32_e64 v5, 0, v5, s[8:9]
	v_and_b32_e32 v6, 0xffff0000, v6
	v_cndmask_b32_e64 v7, 0, v7, s[8:9]
	v_add3_u32 v34, v65, v34, s80
	ds_write_b128 v34, v[4:7]
	s_waitcnt vmcnt(32)
	v_cmp_ne_u64_e32 vcc, 0, v[68:69]
	s_and_saveexec_b64 s[42:43], vcc
	s_cbranch_execz .LBB0_555
	v_cvt_pk_bf16_f32 v4, v120, v123
	v_cvt_pk_bf16_f32 v5, v121, v125
	v_cvt_pk_bf16_f32 v6, v122, v126
	v_cvt_pk_bf16_f32 v7, v124, v127
	s_mov_b32 s45, s13
	global_store_dwordx4 v[68:69], v[4:7], off nt
	s_nop 1
	v_cvt_pk_bf16_f32 v4, v110, v113
	v_cvt_pk_bf16_f32 v5, v111, v115
	v_cvt_pk_bf16_f32 v6, v112, v116
	v_cvt_pk_bf16_f32 v7, v114, v117
	v_lshl_add_u64 v[34:35], v[68:69], 0, s[22:23]
	global_store_dwordx4 v[34:35], v[4:7], off nt
	s_nop 1
	v_cvt_pk_bf16_f32 v4, v102, v105
	v_cvt_pk_bf16_f32 v5, v103, v107
	v_cvt_pk_bf16_f32 v6, v104, v108
	v_cvt_pk_bf16_f32 v7, v106, v109
	s_lshl_b64 s[44:45], s[44:45], 1
	v_lshl_add_u64 v[42:43], v[68:69], 0, s[44:45]
	global_store_dwordx4 v[42:43], v[4:7], off nt
	s_nop 1
	v_cvt_pk_bf16_f32 v4, v94, v97
	v_cvt_pk_bf16_f32 v5, v95, v99
	v_cvt_pk_bf16_f32 v6, v96, v100
	v_cvt_pk_bf16_f32 v7, v98, v101
	v_lshl_add_u64 v[34:35], v[34:35], 0, s[44:45]
	global_store_dwordx4 v[34:35], v[4:7], off nt
	s_nop 1

; __device__ __forceinline__ KP kparams() { KP q = (KP)__builtin_amdgcn_kernarg_segment_ptr(); asm volatile("" : "+s"(q)); return q; }
; FFT_HD cf2 cmul(cf2 a, cf2 b) { return mk2(a.x * b.x - a.y * b.y, a.x * b.y + a.y * b.x); }
; FFT_HD cf2 cmulc(cf2 a, cf2 b) { return mk2(a.x * b.x + a.y * b.y, a.y * b.x - a.x * b.y); }
; template <int BANK> __device__ __forceinline__ void bg_issue1(BgState& b, int wg, int NW, int lane) {
;     KP kp = kparams();
;     const float* src; int ldS; bf16_t* dst; int o2;
;     bg_decode(b.st, wg, NW, lane, kp, src, ldS, dst, o2);
;     b.dst[BANK] = dst; b.o2[BANK] = o2;
;     asm volatile("s_nop 6" ::: "memory");
; #pragma unroll
;     for (int i = 0; i < 8; ++i) { const float* p = src + (size_t)i * ldS;
;         asm volatile("global_load_dword %0, %4, off\n\tglobal_load_dword %1, %4, off offset:256\n\tglobal_load_dword %2, %4, off offset:512\n\tglobal_load_dword %3, %4, off offset:768"
;                      : "=&v"(b.r[(BANK * 8 + i) * 4 + 0]), "=&v"(b.r[(BANK * 8 + i) * 4 + 1]), "=&v"(b.r[(BANK * 8 + i) * 4 + 2]), "=&v"(b.r[(BANK * 8 + i) * 4 + 3]) : "v"(p) : "memory"); }
;     b.st += 1;
; }
; template <bool INV, int lS, class ZP> FFT_HD void fft_r16_pass(ZP z, int tid) {
;     ...
;     } else {
; #pragma unroll 1
;         for (int it = 0; it < 2; ++it) {
;             const int w = tid + 512 * it;
;             const int blk = w >> lS, p = w & (S - 1), pb = PADI((blk << (lS + 4)) + p);
;             fft_gen_tw((float)p * inv, tw);
;             cf2 x[16];
; #pragma unroll
;             for (int j = 0; j < 16; ++j) x[j] = z[pb + j * STEP];
;             if (INV) {
; #pragma unroll
;                 for (int j = 1; j < 16; ++j) x[j] = cmulc(x[j], tw[j]);
;             }
;             dft16<INV>(x);
;             if (!INV) {
; #pragma unroll
;                 for (int j = 1; j < 16; ++j) x[j] = cmul(x[j], tw[j]);
;             }
; #pragma unroll
;             for (int j = 0; j < 16; ++j) z[pb + j * STEP] = x[j];
;         }
.LBB0_565:
	s_nop 6
	global_load_dword v144, v[4:5], off nt
	global_load_dword v136, v[4:5], off offset:256 nt
	global_load_dword v128, v[4:5], off offset:512 nt
	global_load_dword v120, v[4:5], off offset:768 nt
	s_lshl_b32 s12, s44, 2
	v_lshl_add_u64 v[4:5], v[4:5], 0, s[12:13]
	global_load_dword v146, v[4:5], off nt
	global_load_dword v138, v[4:5], off offset:256 nt
	global_load_dword v130, v[4:5], off offset:512 nt
	global_load_dword v122, v[4:5], off offset:768 nt
	v_lshl_add_u64 v[4:5], v[4:5], 0, s[12:13]
	global_load_dword v145, v[4:5], off nt
	global_load_dword v137, v[4:5], off offset:256 nt
	global_load_dword v129, v[4:5], off offset:512 nt
	global_load_dword v121, v[4:5], off offset:768 nt
	v_lshl_add_u64 v[4:5], v[4:5], 0, s[12:13]
	global_load_dword v148, v[4:5], off nt
	global_load_dword v140, v[4:5], off offset:256 nt
	global_load_dword v132, v[4:5], off offset:512 nt
	global_load_dword v124, v[4:5], off offset:768 nt
	v_lshl_add_u64 v[4:5], v[4:5], 0, s[12:13]
	global_load_dword v147, v[4:5], off nt
	global_load_dword v139, v[4:5], off offset:256 nt
	global_load_dword v131, v[4:5], off offset:512 nt
	global_load_dword v123, v[4:5], off offset:768 nt
	v_lshl_add_u64 v[4:5], v[4:5], 0, s[12:13]
	global_load_dword v150, v[4:5], off nt
	global_load_dword v142, v[4:5], off offset:256 nt
	global_load_dword v134, v[4:5], off offset:512 nt
	global_load_dword v126, v[4:5], off offset:768 nt
	v_lshl_add_u64 v[4:5], v[4:5], 0, s[12:13]
	global_load_dword v149, v[4:5], off nt
	global_load_dword v141, v[4:5], off offset:256 nt
	global_load_dword v133, v[4:5], off offset:512 nt
	global_load_dword v125, v[4:5], off offset:768 nt
	v_lshl_add_u64 v[4:5], v[4:5], 0, s[12:13]
	global_load_dword v151, v[4:5], off nt
	global_load_dword v143, v[4:5], off offset:256 nt
	global_load_dword v135, v[4:5], off offset:512 nt
	global_load_dword v127, v[4:5], off offset:768 nt
	s_mov_b32 s1, 0
	s_mov_b64 s[44:45], -1
.LBB0_566:
	v_add_u32_e32 v4, s1, v57
	v_and_b32_e32 v5, 0x3ff, v4
	v_lshlrev_b32_e32 v4, 4, v4
	v_and_or_b32 v4, v4, s81, v5
	v_cvt_f32_u32_e32 v5, v5
	v_ashrrev_i32_e32 v6, 5, v4
	v_lshlrev_b32_e32 v6, 3, v6
	v_lshlrev_b32_e32 v4, 3, v4
	v_and_b32_e32 v6, 0xfffff0f0, v6
	v_mul_f32_e32 v7, 0x38800000, v5
	v_add3_u32 v65, 0, v6, v4
	v_sin_f32_e32 v5, v7
	v_cos_f32_e32 v4, v7
	v_add_u32_e32 v67, 0x10800, v65
	ds_read_b64 v[6:7], v65
	ds_read_b64 v[42:43], v65 offset:8448
	ds_read_b64 v[44:45], v65 offset:16896
	ds_read_b64 v[46:47], v65 offset:25344
	ds_read_b64 v[48:49], v65 offset:33792
	ds_read_b64 v[50:51], v65 offset:42240
	ds_read_b64 v[52:53], v65 offset:50688
	ds_read_b64 v[54:55], v65 offset:59136
	v_add_u32_e32 v168, 0x12900, v65
	v_add_u32_e32 v169, 0x14a00, v65
	v_add_u32_e32 v170, 0x16b00, v65
	v_add_u32_e32 v171, 0x18c00, v65
	v_add_u32_e32 v172, 0x1ad00, v65
	v_add_u32_e32 v173, 0x1ce00, v65
	v_add_u32_e32 v174, 0x1ef00, v65
	ds_read_b64 v[68:69], v67
	ds_read_b64 v[70:71], v168
	ds_read_b64 v[72:73], v169
	ds_read_b64 v[74:75], v170
	ds_read_b64 v[76:77], v171
	ds_read_b64 v[78:79], v172
	ds_read_b64 v[80:81], v173
	ds_read_b64 v[82:83], v174
	v_pk_mul_f32 v[84:85], v[4:5], v[4:5]
	v_mul_f32_e64 v86, v4, -v5
	v_mov_b32_e32 v87, v84
	v_mov_b32_e32 v84, v86
	s_waitcnt lgkmcnt(10)
	v_pk_mov_b32 v[90:91], v[42:43], v[50:51] op_sel:[1,0]
	v_mov_b32_e32 v92, v42
	v_mov_b32_e32 v93, v51
	s_waitcnt lgkmcnt(9)
	v_pk_mov_b32 v[94:95], v[44:45], v[52:53] op_sel:[1,0]
	v_mov_b32_e32 v96, v44
	v_mov_b32_e32 v97, v53
	s_waitcnt lgkmcnt(8)
	v_pk_mov_b32 v[98:99], v[46:47], v[54:55] op_sel:[1,0]
	v_mov_b32_e32 v100, v46
	v_mov_b32_e32 v101, v55
	v_pk_add_f32 v[102:103], v[86:87], v[84:85]
	v_pk_add_f32 v[84:85], v[86:87], v[84:85] neg_lo:[0,1] neg_hi:[0,1]
	s_waitcnt lgkmcnt(2)
	v_pk_mov_b32 v[86:87], v[70:71], v[78:79] op_sel:[1,0]
	v_mov_b32_e32 v104, v70
	v_mov_b32_e32 v105, v79
	s_waitcnt lgkmcnt(1)
	v_pk_mov_b32 v[106:107], v[72:73], v[80:81] op_sel:[1,0]
	v_mov_b32_e32 v108, v72
	v_mov_b32_e32 v109, v81
	s_waitcnt lgkmcnt(0)
	v_pk_mov_b32 v[110:111], v[74:75], v[82:83] op_sel:[1,0]
	v_mov_b32_e32 v112, v74
	v_mov_b32_e32 v113, v83
	v_pk_add_f32 v[114:115], v[6:7], v[68:69]
	v_pk_add_f32 v[116:117], v[48:49], v[76:77]
	v_pk_add_f32 v[42:43], v[42:43], v[70:71]
	v_pk_add_f32 v[50:51], v[50:51], v[78:79]
	v_pk_add_f32 v[44:45], v[44:45], v[72:73]
	v_pk_add_f32 v[52:53], v[52:53], v[80:81]
	v_pk_add_f32 v[46:47], v[46:47], v[74:75]
	v_pk_add_f32 v[54:55], v[54:55], v[82:83]
	v_pk_add_f32 v[48:49], v[48:49], v[76:77] neg_lo:[0,1] neg_hi:[0,1]
	v_mov_b32_e32 v88, v5
	v_mov_b32_e32 v89, v4
	v_pk_add_f32 v[6:7], v[6:7], v[68:69] neg_lo:[0,1] neg_hi:[0,1]
	v_mov_b32_e32 v68, v102
	v_mov_b32_e32 v69, v85
	v_pk_add_f32 v[72:73], v[90:91], v[86:87] neg_lo:[0,1] neg_hi:[0,1]
	v_pk_add_f32 v[74:75], v[92:93], v[104:105] neg_lo:[0,1] neg_hi:[0,1]
	v_pk_add_f32 v[76:77], v[94:95], v[106:107] neg_lo:[0,1] neg_hi:[0,1]
	v_pk_add_f32 v[78:79], v[96:97], v[108:109] neg_lo:[0,1] neg_hi:[0,1]
	v_pk_add_f32 v[80:81], v[98:99], v[110:111] neg_lo:[0,1] neg_hi:[0,1]
	v_pk_add_f32 v[82:83], v[100:101], v[112:113] neg_lo:[0,1] neg_hi:[0,1]
	v_pk_add_f32 v[86:87], v[114:115], v[116:117]
	v_pk_add_f32 v[90:91], v[42:43], v[50:51]
	v_pk_add_f32 v[92:93], v[44:45], v[52:53]
	v_pk_add_f32 v[94:95], v[46:47], v[54:55]
	v_pk_mov_b32 v[96:97], v[48:49], v[48:49] op_sel:[1,0]
	v_pk_add_f32 v[44:45], v[44:45], v[52:53] neg_lo:[0,1] neg_hi:[0,1]
	v_mov_b32_e32 v52, v46
	v_mov_b32_e32 v53, v43
	v_mov_b32_e32 v104, v54
	v_mov_b32_e32 v105, v51
	v_mov_b32_e32 v106, v42
	v_mov_b32_e32 v107, v46
	v_mov_b32_e32 v108, v50
	v_mov_b32_e32 v109, v54
	v_mov_b32_e32 v110, v43
; FFT_HD cf2 mk2(float x, float y) { return (cf2){x, y}; }
; FFT_HD void fft_sincos(float frac, float& s, float& c) { s = __builtin_amdgcn_sinf(frac); c = __builtin_amdgcn_cosf(frac); }
; FFT_HD cf2 cmul(cf2 a, cf2 b) { return mk2(a.x * b.x - a.y * b.y, a.x * b.y + a.y * b.x); }
; FFT_HD cf2 cadd(cf2 a, cf2 b) { return mk2(a.x + b.x, a.y + b.y); }
; FFT_HD cf2 csub(cf2 a, cf2 b) { return mk2(a.x - b.x, a.y - b.y); }
; template <bool INV> FFT_HD void dft4(cf2& a, cf2& b, cf2& c, cf2& d) {
;     const cf2 s0 = cadd(a, c), s1 = csub(a, c), s2 = cadd(b, d), s3 = csub(b, d);
;     a = cadd(s0, s2); c = csub(s0, s2);
;     const cf2 r = INV ? mk2(-s3.y, s3.x) : mk2(s3.y, -s3.x);
;     b = cadd(s1, r); d = csub(s1, r);
; }
; template <bool INV> FFT_HD void dft16(cf2 (&x)[16]) {
;     const float C1 = 0.9238795325112867f, S1 = 0.3826834323650898f, H = 0.7071067811865476f;
; #pragma unroll
;     for (int b = 0; b < 4; ++b) dft4<INV>(x[b], x[4 + b], x[8 + b], x[12 + b]);
;     const float s = INV ? -1.f : 1.f;
;     x[4 + 1] = cmul(x[4 + 1], mk2(C1, -s * S1)); x[8 + 1] = cmul(x[8 + 1], mk2(H, -s * H));   x[12 + 1] = cmul(x[12 + 1], mk2(S1, -s * C1));
;     x[4 + 2] = cmul(x[4 + 2], mk2(H, -s * H));   x[8 + 2] = cmul(x[8 + 2], mk2(0.f, -s));     x[12 + 2] = cmul(x[12 + 2], mk2(-H, -s * H));
;     x[4 + 3] = cmul(x[4 + 3], mk2(S1, -s * C1)); x[8 + 3] = cmul(x[8 + 3], mk2(-H, -s * H));  x[12 + 3] = cmul(x[12 + 3], mk2(-C1, s * S1));
; #pragma unroll
;     for (int c = 0; c < 4; ++c) dft4<INV>(x[4 * c], x[4 * c + 1], x[4 * c + 2], x[4 * c + 3]);
; #pragma unroll
;     for (int c = 0; c < 4; ++c)
; #pragma unroll
;         for (int d = c + 1; d < 4; ++d) { const cf2 t = x[4 * c + d]; x[4 * c + d] = x[4 * d + c]; x[4 * d + c] = t; }
; }
; FFT_HD void fft_gen_tw(float frac, cf2 (&tw)[16]) {
;     float sn, cs; fft_sincos(frac, sn, cs);
;     tw[1] = mk2(cs, -sn);
;     tw[2] = cmul(tw[1], tw[1]); tw[3] = cmul(tw[2], tw[1]); tw[4] = cmul(tw[2], tw[2]); tw[5] = cmul(tw[4], tw[1]); tw[6] = cmul(tw[4], tw[2]); tw[7] = cmul(tw[4], tw[3]);
;     tw[8] = cmul(tw[4], tw[4]);
; #pragma unroll
;     for (int j = 9; j < 16; ++j) tw[j] = cmul(tw[8], tw[j - 8]);
; }
	v_mov_b32_e32 v111, v47
	v_mov_b32_e32 v112, v51
	v_mov_b32_e32 v113, v55
	v_pk_mov_b32 v[42:43], v[46:47], v[42:43] op_sel:[1,0]
	v_pk_mov_b32 v[46:47], v[54:55], v[50:51] op_sel:[1,0]
	s_mov_b32 s50, s27
	s_mov_b32 s51, s26
	s_mov_b32 s52, s25
	s_mov_b32 s53, s24
	v_pk_add_f32 v[98:99], v[6:7], v[48:49] op_sel:[0,1] op_sel_hi:[1,0]
	v_pk_add_f32 v[48:49], v[6:7], v[48:49] op_sel:[0,1] op_sel_hi:[1,0] neg_lo:[0,1] neg_hi:[0,1]
	v_pk_add_f32 v[100:101], v[114:115], v[116:117] neg_lo:[0,1] neg_hi:[0,1]
	v_pk_mul_f32 v[50:51], v[88:89], v[68:69]
	v_pk_mul_f32 v[54:55], v[4:5], v[68:69]
	v_pk_mul_f32 v[114:115], v[68:69], v[68:69]
	v_pk_mul_f32 v[116:117], v[84:85], v[68:69] op_sel:[1,0] op_sel_hi:[0,1]
	v_add_f32_e32 v7, v78, v79
	v_sub_f32_e32 v97, v76, v77
	v_mov_b32_e32 v152, v82
	v_mov_b32_e32 v153, v80
	v_mov_b32_e32 v154, v83
	v_mov_b32_e32 v155, v81
	v_pk_add_f32 v[156:157], v[86:87], v[92:93]
	v_pk_add_f32 v[162:163], v[74:75], v[74:75] op_sel:[0,1] op_sel_hi:[0,1]
	v_pk_add_f32 v[164:165], v[72:73], v[72:73] op_sel:[0,1] op_sel_hi:[0,1] neg_lo:[0,1] neg_hi:[0,1]
	v_pk_add_f32 v[82:83], v[82:83], v[82:83] op_sel:[0,1] op_sel_hi:[0,1]
	v_pk_add_f32 v[52:53], v[52:53], v[104:105] neg_lo:[0,1] neg_hi:[0,1]
	v_pk_add_f32 v[104:105], v[106:107], v[108:109] neg_lo:[0,1] neg_hi:[0,1]
	v_pk_add_f32 v[106:107], v[110:111], v[112:113] neg_lo:[0,1] neg_hi:[0,1]
	v_pk_add_f32 v[42:43], v[42:43], v[46:47] neg_lo:[0,1] neg_hi:[0,1]
	v_pk_fma_f32 v[46:47], v[44:45], 0, v[44:45] op_sel:[0,0,1] op_sel_hi:[1,0,0]
	v_pk_fma_f32 v[44:45], v[44:45], 0, v[44:45] op_sel:[0,0,1] op_sel_hi:[1,0,0] neg_lo:[0,0,1] neg_hi:[0,0,1]
	v_mov_b32_e32 v108, v74
	v_mov_b32_e32 v109, v78
	v_mov_b32_e32 v78, v75
	v_mov_b32_e32 v74, v72
	v_mov_b32_e32 v75, v76
	v_mov_b32_e32 v76, v73
	v_pk_add_f32 v[72:73], v[86:87], v[92:93] neg_lo:[0,1] neg_hi:[0,1]
	v_pk_add_f32 v[86:87], v[90:91], v[94:95] neg_lo:[0,1] neg_hi:[0,1]
	s_mov_b32 s58, s26
	s_mov_b32 s59, s24
	v_pk_add_f32 v[158:159], v[90:91], v[94:95]
	v_pk_add_f32 v[80:81], v[80:81], v[80:81] op_sel:[0,1] op_sel_hi:[0,1] neg_lo:[0,1] neg_hi:[0,1]
	v_pk_mov_b32 v[90:91], v[114:115], v[116:117] op_sel:[1,0]
	v_mov_b32_e32 v115, v116
	v_mov_b32_e32 v92, v54
	v_mov_b32_e32 v93, v51
	v_pk_mov_b32 v[50:51], v[54:55], v[50:51] op_sel:[1,0]
	v_mul_f32_e32 v7, 0x3f3504f3, v7
	v_pk_add_f32 v[54:55], v[152:153], v[154:155] neg_lo:[0,1] neg_hi:[0,1]
	v_pk_add_f32 v[94:95], v[152:153], v[154:155]
	v_pk_mul_f32 v[112:113], v[162:163], s[26:27]
	v_pk_mul_f32 v[82:83], v[82:83], s[50:51]
	v_mov_b32_e32 v47, v45
	v_pk_mul_f32 v[44:45], v[106:107], s[52:53]
	v_pk_mul_f32 v[42:43], v[42:43], s[24:25]
	v_pk_add_f32 v[78:79], v[108:109], v[78:79] neg_lo:[0,1] neg_hi:[0,1]
	v_pk_add_f32 v[74:75], v[74:75], v[76:77]
	v_pk_add_f32 v[76:77], v[72:73], v[86:87] op_sel:[0,1] op_sel_hi:[1,0]
	v_pk_add_f32 v[72:73], v[72:73], v[86:87] op_sel:[0,1] op_sel_hi:[1,0] neg_lo:[0,1] neg_hi:[0,1]
	s_mov_b32 s56, s27
	s_mov_b32 s57, s24
	s_mov_b32 s28, s25
	v_pk_add_f32 v[110:111], v[156:157], v[158:159]
	v_pk_add_f32 v[86:87], v[156:157], v[158:159] neg_lo:[0,1] neg_hi:[0,1]
	v_pk_add_f32 v[106:107], v[90:91], v[114:115] neg_lo:[0,1] neg_hi:[0,1]
	v_pk_add_f32 v[90:91], v[90:91], v[114:115]
	v_pk_add_f32 v[108:109], v[92:93], v[50:51] neg_lo:[0,1] neg_hi:[0,1]
	v_pk_add_f32 v[50:51], v[92:93], v[50:51]
	v_mov_b32_e32 v55, v95
	v_mul_f32_e32 v60, 0x3ec3ef15, v95
	v_mul_f32_e32 v158, 0x3ec3ef15, v54
	v_mul_f32_e32 v159, 0x3f6c835e, v95
	v_pk_fma_f32 v[92:93], v[164:165], s[50:51], v[112:113]
	v_pk_fma_f32 v[94:95], v[164:165], s[50:51], v[112:113] neg_lo:[0,0,1] neg_hi:[0,0,1]
	v_fma_f32 v114, v97, s25, -v7
	v_pk_fma_f32 v[116:117], v[80:81], s[26:27], v[82:83]
	v_pk_fma_f32 v[80:81], v[80:81], s[26:27], v[82:83] neg_lo:[0,0,1] neg_hi:[0,0,1]
	v_pk_fma_f32 v[42:43], v[52:53], s[24:25], v[42:43] neg_lo:[0,0,1] neg_hi:[0,0,1]
	v_pk_fma_f32 v[44:45], v[104:105], s[52:53], v[44:45]
	v_pk_mov_b32 v[82:83], v[78:79], v[74:75] op_sel:[1,0]
	v_pk_mul_f32 v[104:105], v[74:75], s[58:59]
	v_pk_mov_b32 v[74:75], v[74:75], v[78:79] op_sel:[1,0]
	v_pk_mov_b32 v[154:155], v[72:73], v[76:77] op_sel:[1,0]
	s_mov_b32 s54, s24
	s_mov_b32 s55, s27
	v_mov_b32_e32 v56, v5
	v_pk_mov_b32 v[70:71], v[84:85], v[102:103] op_sel:[1,0]
	v_mov_b32_e32 v160, v98
	v_mov_b32_e32 v161, v49
	v_fmamk_f32 v112, v97, 0x3f3504f3, v7
	v_pk_add_f32 v[52:53], v[100:101], v[46:47]
	v_mov_b32_e32 v152, v76
	v_mov_b32_e32 v153, v73
	v_pk_add_f32 v[46:47], v[100:101], v[46:47] neg_lo:[0,1] neg_hi:[0,1]
	v_mov_b32_e32 v100, v106
	v_mov_b32_e32 v101, v91
	v_pk_fma_f32 v[54:55], v[54:55], s[30:31], v[60:61] op_sel_hi:[1,1,0] neg_lo:[0,0,1] neg_hi:[0,0,1]
	v_mov_b32_e32 v94, v92
	v_mov_b32_e32 v115, v114
	v_mov_b32_e32 v113, v114
	v_mov_b32_e32 v80, v116
	v_pk_mov_b32 v[48:49], v[48:49], v[92:93] op_sel:[1,0]
	v_pk_add_f32 v[92:93], v[44:45], v[42:43]
	v_pk_mul_f32 v[74:75], v[74:75], s[28:29]
	v_pk_fma_f32 v[78:79], v[78:79], s[56:57], v[104:105]
	v_mov_b32_e32 v7, v158
	v_mov_b32_e32 v97, v159
	v_pk_mov_b32 v[104:105], v[90:91], v[106:107] op_sel:[1,0]
	v_pk_mul_f32 v[154:155], v[90:91], v[154:155] op_sel:[1,0]
	v_pk_mov_b32 v[158:159], v[42:43], v[44:45] op_sel:[1,0]
	v_pk_mov_b32 v[42:43], v[44:45], v[42:43] op_sel:[1,0]
	v_pk_mov_b32 v[156:157], v[50:51], v[108:109] op_sel:[1,0]
	v_pk_mul_f32 v[44:45], v[70:71], v[100:101]
	v_pk_mul_f32 v[70:71], v[68:69], v[100:101]
	v_pk_mul_f32 v[164:165], v[100:101], v[100:101]
	v_pk_mul_f32 v[90:91], v[100:101], v[90:91] op_sel:[0,1] op_sel_hi:[1,0]
	v_pk_add_f32 v[160:161], v[160:161], v[112:113]
	v_pk_add_f32 v[166:167], v[94:95], v[80:81]
; FFT_HD cf2 mk2(float x, float y) { return (cf2){x, y}; }
; FFT_HD cf2 cmul(cf2 a, cf2 b) { return mk2(a.x * b.x - a.y * b.y, a.x * b.y + a.y * b.x); }
; template <bool INV> FFT_HD void dft16(cf2 (&x)[16]) {
;     const float C1 = 0.9238795325112867f, S1 = 0.3826834323650898f, H = 0.7071067811865476f;
; #pragma unroll
;     for (int b = 0; b < 4; ++b) dft4<INV>(x[b], x[4 + b], x[8 + b], x[12 + b]);
;     const float s = INV ? -1.f : 1.f;
;     x[4 + 1] = cmul(x[4 + 1], mk2(C1, -s * S1)); x[8 + 1] = cmul(x[8 + 1], mk2(H, -s * H));   x[12 + 1] = cmul(x[12 + 1], mk2(S1, -s * C1));
;     x[4 + 2] = cmul(x[4 + 2], mk2(H, -s * H));   x[8 + 2] = cmul(x[8 + 2], mk2(0.f, -s));     x[12 + 2] = cmul(x[12 + 2], mk2(-H, -s * H));
;     x[4 + 3] = cmul(x[4 + 3], mk2(S1, -s * C1)); x[8 + 3] = cmul(x[8 + 3], mk2(-H, -s * H));  x[12 + 3] = cmul(x[12 + 3], mk2(-C1, s * S1));
; #pragma unroll
;     for (int c = 0; c < 4; ++c) dft4<INV>(x[4 * c], x[4 * c + 1], x[4 * c + 2], x[4 * c + 3]);
; #pragma unroll
;     for (int c = 0; c < 4; ++c)
; #pragma unroll
;         for (int d = c + 1; d < 4; ++d) { const cf2 t = x[4 * c + d]; x[4 * c + d] = x[4 * d + c]; x[4 * d + c] = t; }
; }
; template <bool INV, int lS, class ZP> FFT_HD void fft_r16_pass(ZP z, int tid) {
;     ...
;             if (!INV) {
; #pragma unroll
;                 for (int j = 1; j < 16; ++j) x[j] = cmul(x[j], tw[j]);
;             }
; #pragma unroll
;             for (int j = 0; j < 16; ++j) z[pb + j * STEP] = x[j];
	v_pk_mov_b32 v[114:115], v[114:115], v[116:117] op_sel:[1,0]
	v_mov_b32_e32 v94, v98
	v_mov_b32_e32 v113, v81
	v_pk_add_f32 v[80:81], v[52:53], v[92:93]
	v_pk_fma_f32 v[74:75], v[82:83], s[54:55], v[74:75]
	v_pk_add_f32 v[6:7], v[6:7], v[96:97] neg_lo:[0,1] neg_hi:[0,1]
	v_mov_b32_e32 v98, v54
	v_pk_fma_f32 v[82:83], v[106:107], v[76:77], v[154:155] neg_lo:[0,0,1] neg_hi:[0,0,1]
	v_pk_fma_f32 v[96:97], v[106:107], v[152:153], v[154:155] op_sel_hi:[0,1,1]
	v_pk_mul_f32 v[104:105], v[56:57], v[104:105] op_sel_hi:[0,1]
	v_pk_add_f32 v[42:43], v[158:159], v[42:43] neg_lo:[0,1] neg_hi:[0,1]
	ds_write_b64 v65, v[110:111]
	v_mov_b32_e32 v110, v108
	v_mov_b32_e32 v111, v51
	v_pk_mul_f32 v[156:157], v[100:101], v[156:157]
	v_pk_add_f32 v[52:53], v[52:53], v[92:93] neg_lo:[0,1] neg_hi:[0,1]
	v_mov_b32_e32 v91, v164
	v_mov_b32_e32 v164, v90
	v_pk_add_f32 v[48:49], v[48:49], v[114:115] neg_lo:[0,1] neg_hi:[0,1]
	v_pk_add_f32 v[92:93], v[94:95], v[112:113] neg_lo:[0,1] neg_hi:[0,1]
	v_pk_add_f32 v[94:95], v[160:161], v[166:167]
	v_pk_mul_f32 v[102:103], v[102:103], v[80:81] op_sel:[0,1] op_sel_hi:[0,0]
	v_pk_add_f32 v[106:107], v[74:75], v[6:7]
	v_pk_add_f32 v[112:113], v[78:79], v[98:99]
	v_mov_b32_e32 v83, v97
	v_pk_fma_f32 v[96:97], v[4:5], v[100:101], v[104:105] op_sel_hi:[0,1,1]
	v_pk_fma_f32 v[104:105], v[4:5], v[100:101], v[104:105] op_sel_hi:[0,1,1] neg_lo:[0,0,1] neg_hi:[0,0,1]
	v_pk_add_f32 v[114:115], v[46:47], v[42:43]
	v_pk_add_f32 v[42:43], v[46:47], v[42:43] neg_lo:[0,1] neg_hi:[0,1]
	v_pk_add_f32 v[46:47], v[70:71], v[70:71] op_sel:[0,1] op_sel_hi:[0,1]
	v_pk_mov_b32 v[70:71], v[74:75], v[78:79] op_sel:[1,0]
	v_pk_mov_b32 v[54:55], v[6:7], v[54:55] op_sel:[1,0]
	v_mov_b32_e32 v7, v99
	v_mov_b32_e32 v75, v79
	v_pk_mul_f32 v[162:163], v[100:101], v[110:111]
	v_pk_add_f32 v[98:99], v[156:157], v[156:157] op_sel:[0,1] op_sel_hi:[0,1] neg_lo:[0,1] neg_hi:[0,1]
	v_pk_add_f32 v[116:117], v[160:161], v[166:167] neg_lo:[0,1] neg_hi:[0,1]
	v_pk_add_f32 v[152:153], v[90:91], v[164:165]
	v_pk_add_f32 v[90:91], v[90:91], v[164:165] neg_lo:[0,1] neg_hi:[0,1]
	v_pk_mul_f32 v[154:155], v[56:57], v[94:95] op_sel_hi:[0,1]
	v_pk_fma_f32 v[156:157], v[84:85], v[80:81], v[102:103] op_sel:[1,0,0] neg_lo:[0,0,1] neg_hi:[0,0,1]
	v_pk_fma_f32 v[80:81], v[84:85], v[80:81], v[102:103] op_sel:[1,0,0]
	v_pk_add_f32 v[84:85], v[112:113], v[106:107]
	v_mov_b32_e32 v102, v96
	v_mov_b32_e32 v103, v105
	v_pk_mov_b32 v[104:105], v[104:105], v[96:97] op_sel:[1,0]
	v_pk_add_f32 v[160:161], v[48:49], v[48:49] op_sel:[0,1] op_sel_hi:[0,1] neg_lo:[0,1] neg_hi:[0,1]
	v_pk_mov_b32 v[164:165], v[42:43], v[114:115] op_sel:[1,0]
	v_pk_add_f32 v[54:55], v[70:71], v[54:55] neg_lo:[0,1] neg_hi:[0,1]
	v_pk_add_f32 v[6:7], v[6:7], v[74:75] neg_lo:[0,1] neg_hi:[0,1]
	v_mov_b32_e32 v70, v106
	v_mov_b32_e32 v71, v113
	v_mov_b32_e32 v113, v107
	v_pk_add_f32 v[44:45], v[44:45], v[44:45] op_sel:[0,1] op_sel_hi:[0,1] neg_lo:[0,1] neg_hi:[0,1]
	v_pk_add_f32 v[78:79], v[162:163], v[162:163] op_sel:[0,1] op_sel_hi:[0,1]
	v_pk_add_f32 v[158:159], v[92:93], v[92:93] op_sel:[0,1] op_sel_hi:[0,1]
	v_mov_b32_e32 v162, v114
	v_mov_b32_e32 v163, v43
	v_pk_add_f32 v[74:75], v[92:93], v[92:93] op_sel:[0,1] op_sel_hi:[0,1] neg_lo:[0,1] neg_hi:[0,1]
	ds_write_b64 v65, v[82:83] offset:33792
	v_mov_b32_e32 v82, v152
	v_mov_b32_e32 v83, v91
	v_pk_mov_b32 v[92:93], v[90:91], v[152:153] op_sel:[1,0]
	v_pk_fma_f32 v[106:107], v[4:5], v[94:95], v[154:155] op_sel:[0,0,1] op_sel_hi:[1,1,0]
	v_pk_fma_f32 v[94:95], v[4:5], v[94:95], v[154:155] op_sel:[0,0,1] op_sel_hi:[0,1,0] neg_lo:[0,0,1] neg_hi:[0,0,1]
	v_mov_b32_e32 v157, v81
	v_pk_mul_f32 v[80:81], v[108:109], v[84:85] op_sel:[0,1] op_sel_hi:[0,0]
	v_pk_mul_f32 v[104:105], v[104:105], v[160:161]
	v_pk_mul_f32 v[108:109], v[46:47], v[164:165]
	v_pk_add_f32 v[154:155], v[6:7], v[54:55]
	v_pk_add_f32 v[6:7], v[6:7], v[54:55] neg_lo:[0,1] neg_hi:[0,1]
	v_pk_mul_f32 v[54:55], v[152:153], v[86:87] op_sel_hi:[0,1]
	v_pk_add_f32 v[70:71], v[70:71], v[112:113] neg_lo:[0,1] neg_hi:[0,1]
	v_pk_mul_f32 v[112:113], v[100:101], v[152:153] op_sel_hi:[1,0]
	v_pk_mul_f32 v[152:153], v[152:153], v[102:103] op_sel_hi:[0,1]
	v_pk_mul_f32 v[4:5], v[4:5], v[82:83]
	v_pk_mul_f32 v[160:161], v[68:69], v[82:83]
	v_pk_mul_f32 v[68:69], v[68:69], v[92:93]
	v_pk_mul_f32 v[164:165], v[110:111], v[82:83]
	v_pk_mul_f32 v[92:93], v[110:111], v[92:93]
	v_mov_b32_e32 v107, v95
	v_pk_fma_f32 v[94:95], v[50:51], v[84:85], v[80:81] op_sel:[1,0,0] neg_lo:[0,0,1] neg_hi:[0,0,1]
	v_pk_fma_f32 v[50:51], v[50:51], v[84:85], v[80:81] op_sel:[1,0,0]
	v_pk_fma_f32 v[80:81], v[96:97], v[158:159], v[104:105] neg_lo:[0,0,1] neg_hi:[0,0,1]
	v_pk_fma_f32 v[84:85], v[102:103], v[158:159], v[104:105]
	v_pk_fma_f32 v[96:97], v[44:45], v[114:115], v[108:109] neg_lo:[0,0,1] neg_hi:[0,0,1]
	v_pk_fma_f32 v[104:105], v[44:45], v[162:163], v[108:109]
	v_pk_mov_b32 v[110:111], v[6:7], v[154:155] op_sel:[1,0]
	v_pk_fma_f32 v[158:159], v[90:91], v[86:87], v[54:55] op_sel:[1,0,1] op_sel_hi:[1,1,0] neg_lo:[0,0,1] neg_hi:[0,0,1]
	v_pk_fma_f32 v[54:55], v[90:91], v[86:87], v[54:55] op_sel:[1,0,1] op_sel_hi:[1,1,0]
	v_pk_fma_f32 v[86:87], v[100:101], v[90:91], v[112:113] op_sel:[0,1,1] op_sel_hi:[1,1,0] neg_lo:[0,0,1] neg_hi:[0,0,1]
	v_pk_fma_f32 v[100:101], v[100:101], v[90:91], v[112:113] op_sel:[0,1,1] op_sel_hi:[1,1,0]
; __device__ __forceinline__ unsigned cvt_pk_bf16(float lo, float hi) { unsigned r; asm volatile("v_cvt_pk_bf16_f32 %0, %1, %2" : "=v"(r) : "v"(lo), "v"(hi)); return r; }
; FFT_HD cf2 cmul(cf2 a, cf2 b) { return mk2(a.x * b.x - a.y * b.y, a.x * b.y + a.y * b.x); }
; template <int BANK, int WAITN> __device__ __forceinline__ void bg_finish1(BgState& b) {
;     if (WAITN == 32) asm volatile("s_waitcnt vmcnt(32)" ::: "memory"); else asm volatile("s_waitcnt vmcnt(0)" ::: "memory");
;     asm volatile("" : BG_TIE16(BANK * 32) :: "memory");
;     asm volatile("" : BG_TIE16(BANK * 32 + 16) :: "memory");
;     bf16_t* dst = b.dst[BANK];
;     if (dst != nullptr) {
; #pragma unroll
;         for (int c = 0; c < 4; ++c) { u32x4 w;
;             w.x = cvt_pk_bf16(b.r[(BANK * 8 + 0) * 4 + c], b.r[(BANK * 8 + 1) * 4 + c]); w.y = cvt_pk_bf16(b.r[(BANK * 8 + 2) * 4 + c], b.r[(BANK * 8 + 3) * 4 + c]);
;             w.z = cvt_pk_bf16(b.r[(BANK * 8 + 4) * 4 + c], b.r[(BANK * 8 + 5) * 4 + c]); w.w = cvt_pk_bf16(b.r[(BANK * 8 + 6) * 4 + c], b.r[(BANK * 8 + 7) * 4 + c]);
;             bf16_t* dp = dst + (c & 1) * 512 + (c >> 1) * b.o2[BANK];
;             asm volatile("global_store_dwordx4 %0, %1, off\n\ts_nop 1" :: "v"(dp), "v"(w) : "memory"); }
;     }
; }
; template <bool INV, int lS, class ZP> FFT_HD void fft_r16_pass(ZP z, int tid) {
;     ...
;             if (!INV) {
; #pragma unroll
;                 for (int j = 1; j < 16; ++j) x[j] = cmul(x[j], tw[j]);
;             }
; #pragma unroll
;             for (int j = 0; j < 16; ++j) z[pb + j * STEP] = x[j];
;         }
	v_pk_fma_f32 v[112:113], v[90:91], v[102:103], v[152:153] op_sel:[1,0,1] op_sel_hi:[1,1,0] neg_lo:[0,0,1] neg_hi:[0,0,1]
	v_pk_fma_f32 v[90:91], v[90:91], v[102:103], v[152:153] op_sel:[1,0,1] op_sel_hi:[1,1,0]
	v_pk_mul_f32 v[44:45], v[82:83], v[44:45]
	v_pk_mul_f32 v[102:103], v[82:83], v[98:99]
	v_pk_add_f32 v[48:49], v[48:49], v[48:49] op_sel:[0,1] op_sel_hi:[0,1]
	v_pk_mul_f32 v[88:89], v[88:89], v[82:83]
	v_mov_b32_e32 v108, v154
	v_mov_b32_e32 v109, v7
	v_mov_b32_e32 v95, v51
	v_mov_b32_e32 v97, v105
	v_pk_mul_f32 v[50:51], v[78:79], v[110:111]
	v_pk_add_f32 v[4:5], v[4:5], v[4:5] op_sel:[0,1] op_sel_hi:[0,1] neg_lo:[0,1] neg_hi:[0,1]
	v_mov_b32_e32 v105, v101
	v_pk_mov_b32 v[100:101], v[100:101], v[86:87] op_sel:[1,0]
	v_mov_b32_e32 v111, v91
	v_pk_mov_b32 v[90:91], v[90:91], v[112:113] op_sel:[1,0]
	v_pk_fma_f32 v[152:153], v[82:83], v[46:47], v[44:45] op_sel:[0,0,1] op_sel_hi:[1,1,0] neg_lo:[1,0,0] neg_hi:[1,0,0]
	v_pk_fma_f32 v[44:45], v[82:83], v[46:47], v[44:45] op_sel:[0,0,1] op_sel_hi:[1,1,0]
	v_pk_fma_f32 v[46:47], v[82:83], v[78:79], v[102:103] op_sel:[0,0,1] op_sel_hi:[1,1,0] neg_lo:[1,0,0] neg_hi:[1,0,0]
	v_pk_fma_f32 v[78:79], v[82:83], v[78:79], v[102:103] op_sel:[0,0,1] op_sel_hi:[1,1,0]
	v_mov_b32_e32 v81, v85
	v_mov_b32_e32 v159, v55
	v_pk_add_f32 v[54:55], v[88:89], v[88:89] op_sel:[1,0] op_sel_hi:[1,0]
	v_pk_add_f32 v[68:69], v[68:69], v[68:69] op_sel:[0,1] op_sel_hi:[0,1]
	v_pk_add_f32 v[88:89], v[92:93], v[92:93] op_sel:[0,1] op_sel_hi:[0,1]
	v_mov_b32_e32 v104, v86
	v_mov_b32_e32 v110, v112
	v_pk_fma_f32 v[82:83], v[98:99], v[154:155], v[50:51] neg_lo:[0,0,1] neg_hi:[0,0,1]
	v_pk_fma_f32 v[50:51], v[98:99], v[108:109], v[50:51]
	v_pk_mul_f32 v[4:5], v[4:5], v[116:117] op_sel:[0,1] op_sel_hi:[1,0]
	v_pk_mul_f32 v[76:77], v[100:101], v[76:77] op_sel:[0,1]
	v_pk_mul_f32 v[48:49], v[90:91], v[48:49]
	v_mov_b32_e32 v91, v45
	v_pk_mov_b32 v[44:45], v[44:45], v[152:153] op_sel:[1,0]
	v_mov_b32_e32 v99, v79
	v_pk_mov_b32 v[78:79], v[78:79], v[46:47] op_sel:[1,0]
	ds_write_b64 v65, v[156:157] offset:16896
	v_pk_add_f32 v[84:85], v[160:161], v[160:161] op_sel:[1,0] op_sel_hi:[1,0] neg_lo:[0,1] neg_hi:[0,1]
	v_pk_add_f32 v[92:93], v[164:165], v[164:165] op_sel:[1,0] op_sel_hi:[1,0] neg_lo:[0,1] neg_hi:[0,1]
	ds_write_b64 v65, v[106:107] offset:8448
	v_pk_mul_f32 v[68:69], v[68:69], v[52:53] op_sel:[0,1] op_sel_hi:[1,0]
	v_pk_mul_f32 v[88:89], v[88:89], v[70:71] op_sel:[0,1] op_sel_hi:[1,0]
	v_mov_b32_e32 v90, v152
	v_mov_b32_e32 v98, v46
	ds_write_b64 v65, v[94:95] offset:25344
	ds_write_b64 v65, v[80:81] offset:42240
	ds_write_b64 v65, v[96:97] offset:50688
	ds_write_b64 v67, v[158:159]
	v_mov_b32_e32 v83, v51
	v_pk_fma_f32 v[50:51], v[54:55], v[116:117], v[4:5] neg_lo:[0,0,1] neg_hi:[0,0,1]
	v_pk_fma_f32 v[4:5], v[54:55], v[116:117], v[4:5]
	v_pk_fma_f32 v[80:81], v[86:87], v[72:73], v[76:77] neg_lo:[0,0,1] neg_hi:[0,0,1]
	v_pk_fma_f32 v[72:73], v[104:105], v[72:73], v[76:77] op_sel_hi:[1,0,1]
	v_pk_fma_f32 v[76:77], v[112:113], v[74:75], v[48:49] neg_lo:[0,0,1] neg_hi:[0,0,1]
	v_pk_fma_f32 v[48:49], v[110:111], v[74:75], v[48:49]
	v_pk_mul_f32 v[44:45], v[44:45], v[114:115] op_sel:[0,1]
	v_pk_mul_f32 v[74:75], v[78:79], v[154:155] op_sel:[0,1]
	s_movk_i32 s1, 0x200
	s_and_b64 vcc, exec, s[44:45]
	s_mov_b64 s[44:45], 0
	v_pk_fma_f32 v[54:55], v[84:85], v[52:53], v[68:69] neg_lo:[0,0,1] neg_hi:[0,0,1]
	v_pk_fma_f32 v[52:53], v[84:85], v[52:53], v[68:69]
	v_pk_fma_f32 v[68:69], v[92:93], v[70:71], v[88:89] neg_lo:[0,0,1] neg_hi:[0,0,1]
	v_pk_fma_f32 v[70:71], v[92:93], v[70:71], v[88:89]
	v_mov_b32_e32 v51, v5
	v_pk_fma_f32 v[4:5], v[152:153], v[42:43], v[44:45] neg_lo:[0,0,1] neg_hi:[0,0,1]
	v_pk_fma_f32 v[42:43], v[90:91], v[42:43], v[44:45] op_sel_hi:[1,0,1]
	v_pk_fma_f32 v[44:45], v[46:47], v[6:7], v[74:75] neg_lo:[0,0,1] neg_hi:[0,0,1]
	v_pk_fma_f32 v[6:7], v[98:99], v[6:7], v[74:75] op_sel_hi:[1,0,1]
	v_mov_b32_e32 v55, v53
	v_mov_b32_e32 v69, v71
	v_mov_b32_e32 v81, v73
	v_mov_b32_e32 v77, v49
	ds_write_b64 v65, v[82:83] offset:59136
	v_mov_b32_e32 v5, v43
	v_mov_b32_e32 v45, v7
	ds_write_b64 v168, v[50:51]
	ds_write_b64 v169, v[54:55]
	ds_write_b64 v170, v[68:69]
	ds_write_b64 v171, v[80:81]
	ds_write_b64 v172, v[76:77]
	ds_write_b64 v173, v[4:5]
	ds_write_b64 v174, v[44:45]
	s_cbranch_vccnz .LBB0_566
	s_waitcnt lgkmcnt(0)
	s_barrier
	s_waitcnt vmcnt(32)
	v_cmp_ne_u64_e32 vcc, 0, v[2:3]
	s_and_saveexec_b64 s[44:45], vcc
	s_cbranch_execz .LBB0_569
	v_cvt_pk_bf16_f32 v4, v32, v36
	v_cvt_pk_bf16_f32 v5, v33, v38
	v_cvt_pk_bf16_f32 v6, v37, v40
	v_cvt_pk_bf16_f32 v7, v39, v41
	s_lshl_b32 s12, s48, 1
	global_store_dwordx4 v[2:3], v[4:7], off nt
	s_nop 1
	v_cvt_pk_bf16_f32 v4, v24, v26
	v_cvt_pk_bf16_f32 v5, v25, v28
	v_cvt_pk_bf16_f32 v6, v27, v30
	v_cvt_pk_bf16_f32 v7, v29, v31
	v_lshl_add_u64 v[24:25], v[2:3], 0, s[22:23]
	global_store_dwordx4 v[24:25], v[4:7], off nt
	s_nop 1
	v_cvt_pk_bf16_f32 v4, v16, v18
	v_cvt_pk_bf16_f32 v5, v17, v20
	v_cvt_pk_bf16_f32 v6, v19, v22
	v_cvt_pk_bf16_f32 v7, v21, v23
	v_lshl_add_u64 v[2:3], v[2:3], 0, s[12:13]
	global_store_dwordx4 v[2:3], v[4:7], off nt
	s_nop 1
	v_cvt_pk_bf16_f32 v2, v8, v10
	v_cvt_pk_bf16_f32 v3, v9, v12
	v_cvt_pk_bf16_f32 v4, v11, v14
	v_cvt_pk_bf16_f32 v5, v13, v15
	v_lshl_add_u64 v[6:7], v[24:25], 0, s[12:13]
	global_store_dwordx4 v[6:7], v[2:5], off nt
	s_nop 1

; __device__ __forceinline__ KP kparams() { KP q = (KP)__builtin_amdgcn_kernarg_segment_ptr(); asm volatile("" : "+s"(q)); return q; }
; template <int BANK> __device__ __forceinline__ void bg_issue1(BgState& b, int wg, int NW, int lane) {
;     KP kp = kparams();
;     const float* src; int ldS; bf16_t* dst; int o2;
;     bg_decode(b.st, wg, NW, lane, kp, src, ldS, dst, o2);
;     b.dst[BANK] = dst; b.o2[BANK] = o2;
;     asm volatile("s_nop 6" ::: "memory");
; #pragma unroll
;     for (int i = 0; i < 8; ++i) { const float* p = src + (size_t)i * ldS;
;         asm volatile("global_load_dword %0, %4, off\n\tglobal_load_dword %1, %4, off offset:256\n\tglobal_load_dword %2, %4, off offset:512\n\tglobal_load_dword %3, %4, off offset:768"
;                      : "=&v"(b.r[(BANK * 8 + i) * 4 + 0]), "=&v"(b.r[(BANK * 8 + i) * 4 + 1]), "=&v"(b.r[(BANK * 8 + i) * 4 + 2]), "=&v"(b.r[(BANK * 8 + i) * 4 + 3]) : "v"(p) : "memory"); }
;     b.st += 1;
; }
; template <bool INV, int lS, class ZP> FFT_HD void fft_r16_pass(ZP z, int tid) {
;     constexpr int S = 1 << lS, STEP = (S >= 64) ? S + S / 32 : S;
;     constexpr float inv = 1.0f / (float)(16 * S);
;     cf2 tw[16];
;     if (lS != 10) {
;         fft_gen_tw((float)(tid & (S - 1)) * inv, tw);
;         const int w0 = tid, w1 = tid + 512;
;         const int pb0 = PADI(((w0 >> lS) << (lS + 4)) + (w0 & (S - 1))), pb1 = PADI(((w1 >> lS) << (lS + 4)) + (w1 & (S - 1)));
;         cf2 x[16], y[16];
; #pragma unroll
;         for (int j = 0; j < 16; ++j) x[j] = z[pb0 + j * STEP];
; #pragma unroll
;         for (int j = 0; j < 16; ++j) y[j] = z[pb1 + j * STEP];
.LBB0_579:
	s_nop 6
	s_lshl_b32 s12, s48, 2
	global_load_dword v176, v[2:3], off nt
	global_load_dword v168, v[2:3], off offset:256 nt
	global_load_dword v160, v[2:3], off offset:512 nt
	global_load_dword v152, v[2:3], off offset:768 nt
	v_lshl_add_u64 v[2:3], v[2:3], 0, s[12:13]
	v_and_b32_e32 v14, 63, v57
	global_load_dword v178, v[2:3], off nt
	global_load_dword v170, v[2:3], off offset:256 nt
	global_load_dword v162, v[2:3], off offset:512 nt
	global_load_dword v154, v[2:3], off offset:768 nt
	v_lshl_add_u64 v[2:3], v[2:3], 0, s[12:13]
	v_cvt_f32_ubyte0_e32 v4, v14
	global_load_dword v177, v[2:3], off nt
	global_load_dword v169, v[2:3], off offset:256 nt
	global_load_dword v161, v[2:3], off offset:512 nt
	global_load_dword v153, v[2:3], off offset:768 nt
	v_lshl_add_u64 v[2:3], v[2:3], 0, s[12:13]
	v_mul_f32_e32 v4, 0x3a800000, v4
	global_load_dword v180, v[2:3], off nt
	global_load_dword v172, v[2:3], off offset:256 nt
	global_load_dword v164, v[2:3], off offset:512 nt
	global_load_dword v156, v[2:3], off offset:768 nt
	v_lshl_add_u64 v[2:3], v[2:3], 0, s[12:13]
	v_sin_f32_e32 v39, v4
	v_cos_f32_e32 v38, v4
	global_load_dword v179, v[2:3], off nt
	global_load_dword v171, v[2:3], off offset:256 nt
	global_load_dword v163, v[2:3], off offset:512 nt
	global_load_dword v155, v[2:3], off offset:768 nt
	v_lshl_add_u64 v[2:3], v[2:3], 0, s[12:13]
	global_load_dword v181, v[2:3], off nt
	global_load_dword v173, v[2:3], off offset:256 nt
	global_load_dword v165, v[2:3], off offset:512 nt
	global_load_dword v157, v[2:3], off offset:768 nt
	v_lshl_add_u64 v[2:3], v[2:3], 0, s[12:13]
	global_load_dword v182, v[2:3], off nt
	global_load_dword v174, v[2:3], off offset:256 nt
	global_load_dword v166, v[2:3], off offset:512 nt
	global_load_dword v158, v[2:3], off offset:768 nt
	v_lshl_add_u64 v[2:3], v[2:3], 0, s[12:13]
	global_load_dword v183, v[2:3], off nt
	global_load_dword v175, v[2:3], off offset:256 nt
	global_load_dword v167, v[2:3], off offset:512 nt
	global_load_dword v159, v[2:3], off offset:768 nt
	v_pk_mul_f32 v[2:3], v[38:39], v[38:39]
	v_mul_f32_e64 v4, v38, -v39
	v_mov_b32_e32 v5, v2
	v_mov_b32_e32 v2, v4
	v_pk_add_f32 v[202:203], v[4:5], v[2:3]
	v_pk_add_f32 v[204:205], v[4:5], v[2:3] neg_lo:[0,1] neg_hi:[0,1]
	v_mov_b32_e32 v46, v202
	v_mov_b32_e32 v47, v205
	v_pk_mul_f32 v[8:9], v[46:47], v[46:47]
	v_pk_mul_f32 v[10:11], v[204:205], v[46:47] op_sel:[1,0] op_sel_hi:[0,1]
	v_mov_b32_e32 v2, v39
	v_mov_b32_e32 v3, v38
	v_pk_mov_b32 v[12:13], v[8:9], v[10:11] op_sel:[1,0]
	v_mov_b32_e32 v9, v10
	v_pk_mul_f32 v[4:5], v[2:3], v[46:47]
	v_pk_mul_f32 v[6:7], v[38:39], v[46:47]
	v_pk_add_f32 v[48:49], v[12:13], v[8:9] neg_lo:[0,1] neg_hi:[0,1]
	v_pk_add_f32 v[68:69], v[12:13], v[8:9]
	v_mov_b32_e32 v50, v48
	v_mov_b32_e32 v51, v69
	v_mov_b32_e32 v8, v6
	v_mov_b32_e32 v9, v5
	v_pk_mov_b32 v[4:5], v[6:7], v[4:5] op_sel:[1,0]
	v_pk_mul_f32 v[6:7], v[50:51], v[68:69] op_sel:[0,1] op_sel_hi:[1,0]
	v_pk_add_f32 v[72:73], v[8:9], v[4:5] neg_lo:[0,1] neg_hi:[0,1]
	v_pk_add_f32 v[70:71], v[8:9], v[4:5]
	v_pk_mul_f32 v[4:5], v[50:51], v[50:51]
	v_lshlrev_b32_e32 v184, 4, v57
	v_mov_b32_e32 v7, v4
	v_mov_b32_e32 v4, v6
	v_pk_add_f32 v[76:77], v[6:7], v[4:5]
	v_pk_add_f32 v[74:75], v[6:7], v[4:5] neg_lo:[0,1] neg_hi:[0,1]
	v_mov_b32_e32 v54, v76
	v_mov_b32_e32 v55, v75
	v_pk_mul_f32 v[86:87], v[2:3], v[54:55]
	v_and_b32_e32 v2, 0xfffffc00, v184
	v_lshlrev_b32_e32 v4, 3, v2
	v_lshlrev_b32_e32 v5, 3, v14
	v_add_u32_e32 v3, 0x2000, v2
	v_add3_u32 v4, 0, v4, v5
	v_ashrrev_i32_e32 v2, 2, v2
	v_add_u32_e32 v238, v4, v2
	v_add_u32_e32 v239, 0x800, v238
	v_add_u32_e32 v240, 0x1000, v238
	v_add_u32_e32 v241, 0x1800, v238
	ds_read2_b64 v[98:101], v238 offset1:66
	ds_read2_b64 v[102:105], v238 offset0:132 offset1:198
	ds_read2_b64 v[106:109], v239 offset0:8 offset1:74
	ds_read2_b64 v[110:113], v239 offset0:140 offset1:206
	ds_read2_b64 v[114:117], v240 offset0:16 offset1:82
	ds_read2_b64 v[186:189], v240 offset0:148 offset1:214
	ds_read2_b64 v[190:193], v241 offset0:24 offset1:90
	ds_read2_b64 v[198:201], v241 offset0:156 offset1:222
	s_mov_b32 s48, s27
	s_waitcnt lgkmcnt(5)
	v_pk_mov_b32 v[206:207], v[100:101], v[108:109] op_sel:[1,0]
	s_waitcnt lgkmcnt(3)
	v_mov_b32_e32 v210, v116
	s_waitcnt lgkmcnt(1)
	v_pk_mov_b32 v[208:209], v[116:117], v[192:193] op_sel:[1,0]
	v_mov_b32_e32 v211, v193
	v_pk_add_f32 v[206:207], v[206:207], v[208:209] neg_lo:[0,1] neg_hi:[0,1]
	v_mov_b32_e32 v208, v100
	v_mov_b32_e32 v209, v109
	v_pk_add_f32 v[208:209], v[208:209], v[210:211] neg_lo:[0,1] neg_hi:[0,1]
	v_pk_mov_b32 v[210:211], v[102:103], v[110:111] op_sel:[1,0]
	s_waitcnt lgkmcnt(0)
; FFT_HD cf2 mk2(float x, float y) { return (cf2){x, y}; }
; FFT_HD cf2 cmul(cf2 a, cf2 b) { return mk2(a.x * b.x - a.y * b.y, a.x * b.y + a.y * b.x); }
; FFT_HD cf2 cadd(cf2 a, cf2 b) { return mk2(a.x + b.x, a.y + b.y); }
; FFT_HD cf2 csub(cf2 a, cf2 b) { return mk2(a.x - b.x, a.y - b.y); }
; template <bool INV> FFT_HD void dft4(cf2& a, cf2& b, cf2& c, cf2& d) {
;     const cf2 s0 = cadd(a, c), s1 = csub(a, c), s2 = cadd(b, d), s3 = csub(b, d);
;     a = cadd(s0, s2); c = csub(s0, s2);
;     const cf2 r = INV ? mk2(-s3.y, s3.x) : mk2(s3.y, -s3.x);
;     b = cadd(s1, r); d = csub(s1, r);
; }
; template <bool INV> FFT_HD void dft16(cf2 (&x)[16]) {
;     const float C1 = 0.9238795325112867f, S1 = 0.3826834323650898f, H = 0.7071067811865476f;
; #pragma unroll
;     for (int b = 0; b < 4; ++b) dft4<INV>(x[b], x[4 + b], x[8 + b], x[12 + b]);
;     const float s = INV ? -1.f : 1.f;
;     x[4 + 1] = cmul(x[4 + 1], mk2(C1, -s * S1)); x[8 + 1] = cmul(x[8 + 1], mk2(H, -s * H));   x[12 + 1] = cmul(x[12 + 1], mk2(S1, -s * C1));
;     x[4 + 2] = cmul(x[4 + 2], mk2(H, -s * H));   x[8 + 2] = cmul(x[8 + 2], mk2(0.f, -s));     x[12 + 2] = cmul(x[12 + 2], mk2(-H, -s * H));
;     x[4 + 3] = cmul(x[4 + 3], mk2(S1, -s * C1)); x[8 + 3] = cmul(x[8 + 3], mk2(-H, -s * H));  x[12 + 3] = cmul(x[12 + 3], mk2(-C1, s * S1));
; #pragma unroll
;     for (int c = 0; c < 4; ++c) dft4<INV>(x[4 * c], x[4 * c + 1], x[4 * c + 2], x[4 * c + 3]);
; #pragma unroll
;     for (int c = 0; c < 4; ++c)
; #pragma unroll
;         for (int d = c + 1; d < 4; ++d) { const cf2 t = x[4 * c + d]; x[4 * c + d] = x[4 * d + c]; x[4 * d + c] = t; }
; }
	v_pk_mov_b32 v[212:213], v[186:187], v[198:199] op_sel:[1,0]
	v_mov_b32_e32 v214, v186
	v_pk_add_f32 v[210:211], v[210:211], v[212:213] neg_lo:[0,1] neg_hi:[0,1]
	v_mov_b32_e32 v212, v102
	v_mov_b32_e32 v213, v111
	v_mov_b32_e32 v215, v199
	v_pk_add_f32 v[212:213], v[212:213], v[214:215] neg_lo:[0,1] neg_hi:[0,1]
	v_pk_mov_b32 v[214:215], v[104:105], v[112:113] op_sel:[1,0]
	v_pk_mov_b32 v[216:217], v[188:189], v[200:201] op_sel:[1,0]
	v_mov_b32_e32 v218, v188
	v_pk_add_f32 v[214:215], v[214:215], v[216:217] neg_lo:[0,1] neg_hi:[0,1]
	v_mov_b32_e32 v216, v104
	v_mov_b32_e32 v217, v113
	v_mov_b32_e32 v219, v201
	v_pk_add_f32 v[216:217], v[216:217], v[218:219] neg_lo:[0,1] neg_hi:[0,1]
	v_mov_b32_e32 v219, v214
	v_mov_b32_e32 v218, v216
	v_mov_b32_e32 v220, v217
	v_mov_b32_e32 v221, v215
	v_add_f32_e32 v56, v212, v213
	v_pk_add_f32 v[222:223], v[218:219], v[220:221] neg_lo:[0,1] neg_hi:[0,1]
	v_pk_add_f32 v[218:219], v[218:219], v[220:221]
	v_mul_f32_e32 v235, 0x3f3504f3, v56
	v_mov_b32_e32 v223, v219
	v_mul_f32_e32 v56, 0x3ec3ef15, v219
	v_pk_add_f32 v[228:229], v[208:209], v[208:209] op_sel:[0,1] op_sel_hi:[0,1]
	s_mov_b32 s49, s26
	v_pk_add_f32 v[216:217], v[216:217], v[216:217] op_sel:[0,1] op_sel_hi:[0,1]
	v_sub_f32_e32 v234, v210, v211
	v_pk_fma_f32 v[220:221], v[222:223], s[30:31], v[56:57] op_sel_hi:[1,1,0] neg_lo:[0,0,1] neg_hi:[0,0,1]
	v_mul_f32_e32 v242, 0x3ec3ef15, v222
	v_mul_f32_e32 v243, 0x3f6c835e, v219
	v_pk_add_f32 v[218:219], v[98:99], v[114:115]
	v_pk_add_f32 v[222:223], v[106:107], v[190:191]
	v_pk_add_f32 v[98:99], v[98:99], v[114:115] neg_lo:[0,1] neg_hi:[0,1]
	v_pk_add_f32 v[106:107], v[106:107], v[190:191] neg_lo:[0,1] neg_hi:[0,1]
	v_pk_mul_f32 v[228:229], v[228:229], s[26:27]
	v_pk_add_f32 v[230:231], v[206:207], v[206:207] op_sel:[0,1] op_sel_hi:[0,1] neg_lo:[0,1] neg_hi:[0,1]
	v_pk_mul_f32 v[216:217], v[216:217], s[48:49]
	v_pk_add_f32 v[214:215], v[214:215], v[214:215] op_sel:[0,1] op_sel_hi:[0,1] neg_lo:[0,1] neg_hi:[0,1]
	v_pk_mov_b32 v[114:115], v[106:107], v[106:107] op_sel:[1,0]
	v_pk_add_f32 v[190:191], v[98:99], v[106:107] op_sel:[0,1] op_sel_hi:[1,0]
	v_pk_add_f32 v[106:107], v[98:99], v[106:107] op_sel:[0,1] op_sel_hi:[1,0] neg_lo:[0,1] neg_hi:[0,1]
	v_pk_fma_f32 v[232:233], v[230:231], s[48:49], v[228:229]
	v_pk_fma_f32 v[228:229], v[230:231], s[48:49], v[228:229] neg_lo:[0,0,1] neg_hi:[0,0,1]
	v_fmamk_f32 v230, v234, 0x3f3504f3, v235
	v_fma_f32 v234, v234, s25, -v235
	v_pk_fma_f32 v[236:237], v[214:215], s[26:27], v[216:217]
	v_pk_fma_f32 v[214:215], v[214:215], s[26:27], v[216:217] neg_lo:[0,0,1] neg_hi:[0,0,1]
	v_mov_b32_e32 v226, v190
	v_mov_b32_e32 v227, v107
	v_mov_b32_e32 v228, v232
	v_mov_b32_e32 v235, v234
	v_mov_b32_e32 v231, v234
	v_mov_b32_e32 v214, v236
	v_pk_add_f32 v[216:217], v[226:227], v[230:231]
	v_pk_add_f32 v[226:227], v[228:229], v[214:215]
	v_pk_mov_b32 v[106:107], v[106:107], v[232:233] op_sel:[1,0]
	v_pk_mov_b32 v[232:233], v[234:235], v[236:237] op_sel:[1,0]
	v_mov_b32_e32 v228, v190
	v_pk_add_f32 v[232:233], v[106:107], v[232:233] neg_lo:[0,1] neg_hi:[0,1]
	v_mov_b32_e32 v231, v215
	v_pk_add_f32 v[106:107], v[216:217], v[226:227]
	v_mov_b32_e32 v56, v39
	v_pk_add_f32 v[214:215], v[228:229], v[230:231] neg_lo:[0,1] neg_hi:[0,1]
	v_pk_mul_f32 v[228:229], v[56:57], v[106:107] op_sel_hi:[0,1]
	v_pk_add_f32 v[100:101], v[100:101], v[116:117]
	v_pk_add_f32 v[108:109], v[108:109], v[192:193]
	v_pk_add_f32 v[102:103], v[102:103], v[186:187]
	v_pk_add_f32 v[186:187], v[110:111], v[198:199]
	v_pk_add_f32 v[104:105], v[104:105], v[188:189]
	v_pk_add_f32 v[112:113], v[112:113], v[200:201]
	v_pk_fma_f32 v[230:231], v[38:39], v[106:107], v[228:229] op_sel:[0,0,1] op_sel_hi:[1,1,0]
	v_pk_fma_f32 v[106:107], v[38:39], v[106:107], v[228:229] op_sel:[0,0,1] op_sel_hi:[0,1,0] neg_lo:[0,0,1] neg_hi:[0,0,1]
	v_pk_add_f32 v[224:225], v[218:219], v[222:223]
	v_pk_add_f32 v[192:193], v[102:103], v[186:187]
	v_mov_b32_e32 v231, v107
	v_pk_add_f32 v[106:107], v[218:219], v[222:223] neg_lo:[0,1] neg_hi:[0,1]
	v_pk_add_f32 v[102:103], v[102:103], v[186:187] neg_lo:[0,1] neg_hi:[0,1]
	v_mov_b32_e32 v186, v104
	v_mov_b32_e32 v187, v101
	v_mov_b32_e32 v218, v112
	v_mov_b32_e32 v219, v109
	v_pk_add_f32 v[186:187], v[186:187], v[218:219] neg_lo:[0,1] neg_hi:[0,1]
	v_mov_b32_e32 v218, v100
	v_mov_b32_e32 v219, v104
	v_mov_b32_e32 v222, v108
	v_mov_b32_e32 v223, v112
	v_pk_add_f32 v[116:117], v[100:101], v[108:109]
	v_pk_add_f32 v[188:189], v[104:105], v[112:113]
	v_pk_add_f32 v[218:219], v[218:219], v[222:223] neg_lo:[0,1] neg_hi:[0,1]
	v_mov_b32_e32 v222, v101
	v_mov_b32_e32 v223, v105
	v_mov_b32_e32 v228, v109
	v_mov_b32_e32 v229, v113
	v_pk_mov_b32 v[100:101], v[104:105], v[100:101] op_sel:[1,0]
	v_pk_mov_b32 v[104:105], v[112:113], v[108:109] op_sel:[1,0]
	v_pk_add_f32 v[222:223], v[222:223], v[228:229] neg_lo:[0,1] neg_hi:[0,1]
	v_pk_add_f32 v[100:101], v[100:101], v[104:105] neg_lo:[0,1] neg_hi:[0,1]
	v_pk_fma_f32 v[104:105], v[102:103], 0, v[102:103] op_sel:[0,0,1] op_sel_hi:[1,0,0]
	v_pk_fma_f32 v[102:103], v[102:103], 0, v[102:103] op_sel:[0,0,1] op_sel_hi:[1,0,0] neg_lo:[0,0,1] neg_hi:[0,0,1]
	s_mov_b32 s50, s25
	s_mov_b32 s51, s24
	v_mov_b32_e32 v105, v103
	v_pk_mul_f32 v[102:103], v[222:223], s[50:51]
	v_pk_mul_f32 v[100:101], v[100:101], s[24:25]
	v_pk_fma_f32 v[102:103], v[218:219], s[50:51], v[102:103]
	v_pk_fma_f32 v[100:101], v[186:187], s[24:25], v[100:101] neg_lo:[0,0,1] neg_hi:[0,0,1]
	v_pk_add_f32 v[108:109], v[106:107], v[104:105]
	v_pk_add_f32 v[186:187], v[102:103], v[100:101]
	v_pk_mov_b32 v[44:45], v[204:205], v[202:203] op_sel:[1,0]
	v_pk_add_f32 v[112:113], v[108:109], v[186:187]
; template <bool INV> FFT_HD void dft16(cf2 (&x)[16]) {
;     const float C1 = 0.9238795325112867f, S1 = 0.3826834323650898f, H = 0.7071067811865476f;
; #pragma unroll
;     for (int b = 0; b < 4; ++b) dft4<INV>(x[b], x[4 + b], x[8 + b], x[12 + b]);
;     const float s = INV ? -1.f : 1.f;
;     x[4 + 1] = cmul(x[4 + 1], mk2(C1, -s * S1)); x[8 + 1] = cmul(x[8 + 1], mk2(H, -s * H));   x[12 + 1] = cmul(x[12 + 1], mk2(S1, -s * C1));
;     x[4 + 2] = cmul(x[4 + 2], mk2(H, -s * H));   x[8 + 2] = cmul(x[8 + 2], mk2(0.f, -s));     x[12 + 2] = cmul(x[12 + 2], mk2(-H, -s * H));
;     x[4 + 3] = cmul(x[4 + 3], mk2(S1, -s * C1)); x[8 + 3] = cmul(x[8 + 3], mk2(-H, -s * H));  x[12 + 3] = cmul(x[12 + 3], mk2(-C1, s * S1));
; #pragma unroll
;     for (int c = 0; c < 4; ++c) dft4<INV>(x[4 * c], x[4 * c + 1], x[4 * c + 2], x[4 * c + 3]);
; #pragma unroll
;     for (int c = 0; c < 4; ++c)
; #pragma unroll
;         for (int d = c + 1; d < 4; ++d) { const cf2 t = x[4 * c + d]; x[4 * c + d] = x[4 * d + c]; x[4 * d + c] = t; }
; }
; FFT_HD void fft_gen_tw(float frac, cf2 (&tw)[16]) {
;     float sn, cs; fft_sincos(frac, sn, cs);
;     tw[1] = mk2(cs, -sn);
;     tw[2] = cmul(tw[1], tw[1]); tw[3] = cmul(tw[2], tw[1]); tw[4] = cmul(tw[2], tw[2]); tw[5] = cmul(tw[4], tw[1]); tw[6] = cmul(tw[4], tw[2]); tw[7] = cmul(tw[4], tw[3]);
;     tw[8] = cmul(tw[4], tw[4]);
; #pragma unroll
;     for (int j = 9; j < 16; ++j) tw[j] = cmul(tw[8], tw[j - 8]);
; }
; template <bool INV, int lS, class ZP> FFT_HD void fft_r16_pass(ZP z, int tid) {
;     constexpr int S = 1 << lS, STEP = (S >= 64) ? S + S / 32 : S;
;     constexpr float inv = 1.0f / (float)(16 * S);
;     cf2 tw[16];
;     if (lS != 10) {
;         fft_gen_tw((float)(tid & (S - 1)) * inv, tw);
;         const int w0 = tid, w1 = tid + 512;
;         const int pb0 = PADI(((w0 >> lS) << (lS + 4)) + (w0 & (S - 1))), pb1 = PADI(((w1 >> lS) << (lS + 4)) + (w1 & (S - 1)));
;         cf2 x[16], y[16];
; #pragma unroll
;         for (int j = 0; j < 16; ++j) x[j] = z[pb0 + j * STEP];
; #pragma unroll
;         for (int j = 0; j < 16; ++j) y[j] = z[pb1 + j * STEP];
;         if (INV) {
; #pragma unroll
;             for (int j = 1; j < 16; ++j) x[j] = cmulc(x[j], tw[j]);
;         }
;         dft16<INV>(x);
;         if (!INV) {
; #pragma unroll
;             for (int j = 1; j < 16; ++j) x[j] = cmul(x[j], tw[j]);
;         }
	s_mov_b32 s56, s26
	v_pk_mul_f32 v[202:203], v[202:203], v[112:113] op_sel:[0,1] op_sel_hi:[0,0]
	v_pk_fma_f32 v[218:219], v[204:205], v[112:113], v[202:203] op_sel:[1,0,0] neg_lo:[0,0,1] neg_hi:[0,0,1]
	v_pk_fma_f32 v[112:113], v[204:205], v[112:113], v[202:203] op_sel:[1,0,0]
	v_mov_b32_e32 v202, v206
	v_mov_b32_e32 v219, v113
	v_mov_b32_e32 v112, v208
	v_mov_b32_e32 v113, v212
	v_mov_b32_e32 v212, v209
	v_mov_b32_e32 v203, v210
	v_mov_b32_e32 v210, v207
	v_pk_add_f32 v[112:113], v[112:113], v[212:213] neg_lo:[0,1] neg_hi:[0,1]
	v_pk_add_f32 v[202:203], v[202:203], v[210:211]
	s_mov_b32 s57, s24
	v_pk_mov_b32 v[204:205], v[112:113], v[202:203] op_sel:[1,0]
	v_pk_mul_f32 v[206:207], v[202:203], s[56:57]
	v_pk_mov_b32 v[202:203], v[202:203], v[112:113] op_sel:[1,0]
	s_mov_b32 s28, s25
	s_mov_b32 s52, s27
	s_mov_b32 s53, s24
	s_mov_b32 s54, s24
	s_mov_b32 s55, s27
	v_pk_mul_f32 v[202:203], v[202:203], s[28:29]
	v_mov_b32_e32 v99, v242
	v_mov_b32_e32 v115, v243
	v_pk_fma_f32 v[202:203], v[204:205], s[54:55], v[202:203]
	v_pk_fma_f32 v[204:205], v[112:113], s[52:53], v[206:207]
	v_pk_add_f32 v[98:99], v[98:99], v[114:115] neg_lo:[0,1] neg_hi:[0,1]
	v_mov_b32_e32 v190, v220
	v_pk_add_f32 v[206:207], v[202:203], v[98:99]
	v_pk_add_f32 v[208:209], v[204:205], v[190:191]
	v_mov_b32_e32 v42, v72
	v_pk_add_f32 v[112:113], v[208:209], v[206:207]
	v_pk_mov_b32 v[40:41], v[70:71], v[72:73] op_sel:[1,0]
	v_pk_mul_f32 v[72:73], v[72:73], v[112:113] op_sel:[0,1] op_sel_hi:[0,0]
	v_mov_b32_e32 v43, v71
	v_pk_fma_f32 v[210:211], v[70:71], v[112:113], v[72:73] op_sel:[1,0,0] neg_lo:[0,0,1] neg_hi:[0,0,1]
	v_pk_fma_f32 v[70:71], v[70:71], v[112:113], v[72:73] op_sel:[1,0,0]
	v_pk_add_f32 v[72:73], v[116:117], v[188:189] neg_lo:[0,1] neg_hi:[0,1]
	v_mov_b32_e32 v211, v71
	v_pk_add_f32 v[70:71], v[224:225], v[192:193] neg_lo:[0,1] neg_hi:[0,1]
	v_pk_add_f32 v[198:199], v[224:225], v[192:193]
	v_pk_add_f32 v[200:201], v[116:117], v[188:189]
	v_pk_add_f32 v[188:189], v[70:71], v[72:73] op_sel:[0,1] op_sel_hi:[1,0]
	v_pk_add_f32 v[192:193], v[70:71], v[72:73] op_sel:[0,1] op_sel_hi:[1,0] neg_lo:[0,1] neg_hi:[0,1]
	v_mov_b32_e32 v70, v188
	v_pk_mov_b32 v[72:73], v[192:193], v[188:189] op_sel:[1,0]
	v_mov_b32_e32 v71, v193
	v_pk_mov_b32 v[112:113], v[68:69], v[48:49] op_sel:[1,0]
	v_pk_mul_f32 v[68:69], v[68:69], v[72:73] op_sel:[1,0]
	v_pk_add_f32 v[116:117], v[232:233], v[232:233] op_sel:[0,1] op_sel_hi:[0,1] neg_lo:[0,1] neg_hi:[0,1]
	v_pk_fma_f32 v[212:213], v[48:49], v[188:189], v[68:69] neg_lo:[0,0,1] neg_hi:[0,0,1]
	v_pk_fma_f32 v[68:69], v[48:49], v[70:71], v[68:69] op_sel_hi:[0,1,1]
	v_pk_mul_f32 v[70:71], v[56:57], v[112:113] op_sel_hi:[0,1]
	v_mov_b32_e32 v213, v69
	v_pk_fma_f32 v[68:69], v[38:39], v[50:51], v[70:71] op_sel_hi:[0,1,1]
	v_pk_fma_f32 v[72:73], v[38:39], v[50:51], v[70:71] op_sel_hi:[0,1,1] neg_lo:[0,0,1] neg_hi:[0,0,1]
	v_mov_b32_e32 v71, v73
	v_pk_mov_b32 v[72:73], v[72:73], v[68:69] op_sel:[1,0]
	v_pk_add_f32 v[104:105], v[106:107], v[104:105] neg_lo:[0,1] neg_hi:[0,1]
	v_pk_mov_b32 v[106:107], v[100:101], v[102:103] op_sel:[1,0]
	v_pk_mov_b32 v[100:101], v[102:103], v[100:101] op_sel:[1,0]
	v_mov_b32_e32 v70, v68
	v_pk_add_f32 v[114:115], v[214:215], v[214:215] op_sel:[0,1] op_sel_hi:[0,1]
	v_pk_mul_f32 v[116:117], v[72:73], v[116:117]
	v_pk_add_f32 v[100:101], v[106:107], v[100:101] neg_lo:[0,1] neg_hi:[0,1]
	v_pk_mul_f32 v[96:97], v[46:47], v[50:51]
	v_pk_fma_f32 v[222:223], v[68:69], v[114:115], v[116:117] neg_lo:[0,0,1] neg_hi:[0,0,1]
	v_pk_fma_f32 v[114:115], v[70:71], v[114:115], v[116:117]
	v_pk_add_f32 v[102:103], v[104:105], v[100:101]
	v_pk_add_f32 v[100:101], v[104:105], v[100:101] neg_lo:[0,1] neg_hi:[0,1]
	v_pk_mul_f32 v[94:95], v[44:45], v[50:51]
	v_mov_b32_e32 v223, v115
	v_pk_add_f32 v[114:115], v[96:97], v[96:97] op_sel:[0,1] op_sel_hi:[0,1]
	v_pk_mov_b32 v[96:97], v[100:101], v[102:103] op_sel:[1,0]
	v_mov_b32_e32 v104, v102
	v_mov_b32_e32 v105, v101
	v_pk_mul_f32 v[96:97], v[114:115], v[96:97]
	v_pk_add_f32 v[116:117], v[94:95], v[94:95] op_sel:[0,1] op_sel_hi:[0,1] neg_lo:[0,1] neg_hi:[0,1]
	v_pk_fma_f32 v[224:225], v[116:117], v[102:103], v[96:97] neg_lo:[0,0,1] neg_hi:[0,0,1]
	v_pk_fma_f32 v[94:95], v[116:117], v[104:105], v[96:97]
	v_pk_mov_b32 v[96:97], v[98:99], v[220:221] op_sel:[1,0]
	v_mov_b32_e32 v225, v95
	v_pk_mov_b32 v[94:95], v[202:203], v[204:205] op_sel:[1,0]
	v_mov_b32_e32 v99, v191
	v_mov_b32_e32 v203, v205
	v_pk_add_f32 v[94:95], v[94:95], v[96:97] neg_lo:[0,1] neg_hi:[0,1]
	v_pk_add_f32 v[96:97], v[98:99], v[202:203] neg_lo:[0,1] neg_hi:[0,1]
	v_pk_mul_f32 v[92:93], v[50:51], v[42:43]
	v_pk_add_f32 v[190:191], v[96:97], v[94:95]
	v_pk_add_f32 v[202:203], v[96:97], v[94:95] neg_lo:[0,1] neg_hi:[0,1]
	v_pk_mul_f32 v[84:85], v[50:51], v[40:41]
	v_pk_add_f32 v[104:105], v[92:93], v[92:93] op_sel:[0,1] op_sel_hi:[0,1]
	v_pk_mov_b32 v[92:93], v[202:203], v[190:191] op_sel:[1,0]
	v_mov_b32_e32 v94, v190
	v_mov_b32_e32 v95, v203
	v_pk_mul_f32 v[92:93], v[104:105], v[92:93]
	v_pk_add_f32 v[106:107], v[84:85], v[84:85] op_sel:[0,1] op_sel_hi:[0,1] neg_lo:[0,1] neg_hi:[0,1]
	v_pk_fma_f32 v[204:205], v[106:107], v[190:191], v[92:93] neg_lo:[0,0,1] neg_hi:[0,0,1]
	v_pk_fma_f32 v[84:85], v[106:107], v[94:95], v[92:93]
	v_pk_mul_f32 v[90:91], v[38:39], v[54:55]
	v_mov_b32_e32 v205, v85
	v_pk_add_f32 v[84:85], v[198:199], v[200:201] neg_lo:[0,1] neg_hi:[0,1]
	v_pk_add_f32 v[110:111], v[198:199], v[200:201]
	v_pk_mul_f32 v[92:93], v[76:77], v[84:85] op_sel_hi:[0,1]
	v_pk_fma_f32 v[198:199], v[74:75], v[84:85], v[92:93] op_sel:[1,0,1] op_sel_hi:[1,1,0] neg_lo:[0,0,1] neg_hi:[0,0,1]
; FFT_HD cf2 mk2(float x, float y) { return (cf2){x, y}; }
; FFT_HD void fft_sincos(float frac, float& s, float& c) { s = __builtin_amdgcn_sinf(frac); c = __builtin_amdgcn_cosf(frac); }
; FFT_HD cf2 cmul(cf2 a, cf2 b) { return mk2(a.x * b.x - a.y * b.y, a.x * b.y + a.y * b.x); }
; FFT_HD cf2 cmulc(cf2 a, cf2 b) { return mk2(a.x * b.x + a.y * b.y, a.y * b.x - a.x * b.y); }
; FFT_HD void fft_gen_tw(float frac, cf2 (&tw)[16]) {
;     float sn, cs; fft_sincos(frac, sn, cs);
;     tw[1] = mk2(cs, -sn);
;     tw[2] = cmul(tw[1], tw[1]); tw[3] = cmul(tw[2], tw[1]); tw[4] = cmul(tw[2], tw[2]); tw[5] = cmul(tw[4], tw[1]); tw[6] = cmul(tw[4], tw[2]); tw[7] = cmul(tw[4], tw[3]);
;     tw[8] = cmul(tw[4], tw[4]);
; #pragma unroll
;     for (int j = 9; j < 16; ++j) tw[j] = cmul(tw[8], tw[j - 8]);
; }
; template <bool INV, int lS, class ZP> FFT_HD void fft_r16_pass(ZP z, int tid) {
;     constexpr int S = 1 << lS, STEP = (S >= 64) ? S + S / 32 : S;
;     constexpr float inv = 1.0f / (float)(16 * S);
;     cf2 tw[16];
;     if (lS != 10) {
;         fft_gen_tw((float)(tid & (S - 1)) * inv, tw);
;         const int w0 = tid, w1 = tid + 512;
;         const int pb0 = PADI(((w0 >> lS) << (lS + 4)) + (w0 & (S - 1))), pb1 = PADI(((w1 >> lS) << (lS + 4)) + (w1 & (S - 1)));
;         cf2 x[16], y[16];
; #pragma unroll
;         for (int j = 0; j < 16; ++j) x[j] = z[pb0 + j * STEP];
; #pragma unroll
;         for (int j = 0; j < 16; ++j) y[j] = z[pb1 + j * STEP];
;         if (INV) {
; #pragma unroll
;             for (int j = 1; j < 16; ++j) x[j] = cmulc(x[j], tw[j]);
;         }
;         dft16<INV>(x);
;         if (!INV) {
; #pragma unroll
;             for (int j = 1; j < 16; ++j) x[j] = cmul(x[j], tw[j]);
;         }
; #pragma unroll
;         for (int j = 0; j < 16; ++j) z[pb0 + j * STEP] = x[j];
;         if (INV) {
; #pragma unroll
;             for (int j = 1; j < 16; ++j) y[j] = cmulc(y[j], tw[j]);
;         }
;         dft16<INV>(y);
;         if (!INV) {
; #pragma unroll
;             for (int j = 1; j < 16; ++j) y[j] = cmul(y[j], tw[j]);
;         }
	v_pk_fma_f32 v[84:85], v[74:75], v[84:85], v[92:93] op_sel:[1,0,1] op_sel_hi:[1,1,0]
	v_pk_add_f32 v[92:93], v[216:217], v[226:227] neg_lo:[0,1] neg_hi:[0,1]
	v_mov_b32_e32 v199, v85
	v_pk_add_f32 v[84:85], v[90:91], v[90:91] op_sel:[0,1] op_sel_hi:[0,1] neg_lo:[0,1] neg_hi:[0,1]
	v_pk_mov_b32 v[52:53], v[74:75], v[76:77] op_sel:[1,0]
	v_pk_mul_f32 v[90:91], v[84:85], v[92:93]
	v_pk_add_f32 v[86:87], v[86:87], v[86:87] op_sel:[1,0] op_sel_hi:[1,0]
	v_pk_mul_f32 v[88:89], v[46:47], v[52:53]
	v_pk_fma_f32 v[200:201], v[86:87], v[92:93], v[90:91] op_sel:[0,0,1] op_sel_hi:[1,1,0] neg_lo:[0,0,1] neg_hi:[0,0,1]
	v_pk_fma_f32 v[90:91], v[86:87], v[92:93], v[90:91] op_sel:[0,0,1] op_sel_hi:[1,1,0]
	v_pk_mul_f32 v[82:83], v[46:47], v[54:55]
	v_mov_b32_e32 v201, v91
	v_pk_add_f32 v[90:91], v[108:109], v[186:187] neg_lo:[0,1] neg_hi:[0,1]
	v_pk_add_f32 v[186:187], v[88:89], v[88:89] op_sel:[0,1] op_sel_hi:[0,1]
	v_pk_mul_f32 v[88:89], v[186:187], v[90:91]
	v_pk_add_f32 v[216:217], v[82:83], v[82:83] op_sel:[1,0] op_sel_hi:[1,0] neg_lo:[0,1] neg_hi:[0,1]
	v_pk_mul_f32 v[80:81], v[42:43], v[52:53]
	v_pk_fma_f32 v[220:221], v[216:217], v[90:91], v[88:89] op_sel:[0,0,1] op_sel_hi:[1,1,0] neg_lo:[0,0,1] neg_hi:[0,0,1]
	v_pk_fma_f32 v[82:83], v[216:217], v[90:91], v[88:89] op_sel:[0,0,1] op_sel_hi:[1,1,0]
	v_pk_mul_f32 v[78:79], v[42:43], v[54:55]
	v_mov_b32_e32 v221, v83
	v_mov_b32_e32 v82, v206
	v_mov_b32_e32 v83, v209
	v_mov_b32_e32 v209, v207
	v_pk_add_f32 v[82:83], v[82:83], v[208:209] neg_lo:[0,1] neg_hi:[0,1]
	v_pk_add_f32 v[80:81], v[80:81], v[80:81] op_sel:[0,1] op_sel_hi:[0,1]
	v_pk_mul_f32 v[88:89], v[80:81], v[82:83]
	v_pk_add_f32 v[78:79], v[78:79], v[78:79] op_sel:[1,0] op_sel_hi:[1,0] neg_lo:[0,1] neg_hi:[0,1]
	v_pk_add_f32 v[96:97], v[232:233], v[232:233] op_sel:[0,1] op_sel_hi:[0,1]
	v_pk_fma_f32 v[206:207], v[78:79], v[82:83], v[88:89] op_sel:[0,0,1] op_sel_hi:[1,1,0] neg_lo:[0,0,1] neg_hi:[0,0,1]
	v_pk_fma_f32 v[82:83], v[78:79], v[82:83], v[88:89] op_sel:[0,0,1] op_sel_hi:[1,1,0]
	v_pk_mul_f32 v[88:89], v[50:51], v[76:77] op_sel_hi:[1,0]
	v_mov_b32_e32 v207, v83
	v_pk_fma_f32 v[82:83], v[50:51], v[74:75], v[88:89] op_sel:[0,1,1] op_sel_hi:[1,1,0] neg_lo:[0,0,1] neg_hi:[0,0,1]
	v_pk_fma_f32 v[90:91], v[50:51], v[74:75], v[88:89] op_sel:[0,1,1] op_sel_hi:[1,1,0]
	v_mov_b32_e32 v88, v82
	v_mov_b32_e32 v89, v91
	v_pk_mov_b32 v[90:91], v[90:91], v[82:83] op_sel:[1,0]
	v_pk_add_f32 v[94:95], v[214:215], v[214:215] op_sel:[0,1] op_sel_hi:[0,1] neg_lo:[0,1] neg_hi:[0,1]
	v_pk_mul_f32 v[92:93], v[90:91], v[188:189] op_sel:[0,1]
	v_ashrrev_i32_e32 v2, 2, v3
	v_pk_fma_f32 v[188:189], v[82:83], v[192:193], v[92:93] neg_lo:[0,0,1] neg_hi:[0,0,1]
	v_pk_fma_f32 v[92:93], v[88:89], v[192:193], v[92:93] op_sel_hi:[1,0,1]
	v_add3_u32 v60, v4, v2, s71
	v_mov_b32_e32 v189, v93
	v_pk_mul_f32 v[92:93], v[76:77], v[70:71] op_sel_hi:[0,1]
	v_pk_fma_f32 v[76:77], v[74:75], v[70:71], v[92:93] op_sel:[1,0,1] op_sel_hi:[1,1,0] neg_lo:[0,0,1] neg_hi:[0,0,1]
	v_pk_fma_f32 v[92:93], v[74:75], v[70:71], v[92:93] op_sel:[1,0,1] op_sel_hi:[1,1,0]
	v_mov_b32_e32 v74, v76
	v_mov_b32_e32 v75, v93
	v_pk_mov_b32 v[92:93], v[92:93], v[76:77] op_sel:[1,0]
	v_add_u32_e32 v65, 0x800, v60
	v_pk_mul_f32 v[96:97], v[92:93], v[96:97]
	v_add_u32_e32 v67, 0x1000, v60
	v_pk_fma_f32 v[192:193], v[76:77], v[94:95], v[96:97] neg_lo:[0,0,1] neg_hi:[0,0,1]
	v_pk_fma_f32 v[94:95], v[74:75], v[94:95], v[96:97]
	v_pk_mul_f32 v[96:97], v[54:55], v[116:117]
	v_mov_b32_e32 v193, v95
	v_pk_fma_f32 v[94:95], v[54:55], v[114:115], v[96:97] op_sel:[0,0,1] op_sel_hi:[1,1,0] neg_lo:[1,0,0] neg_hi:[1,0,0]
	v_pk_fma_f32 v[98:99], v[54:55], v[114:115], v[96:97] op_sel:[0,0,1] op_sel_hi:[1,1,0]
	v_mov_b32_e32 v96, v94
	v_mov_b32_e32 v97, v99
	v_pk_mov_b32 v[98:99], v[98:99], v[94:95] op_sel:[1,0]
	v_add_u32_e32 v185, 0x1800, v60
	v_pk_mul_f32 v[102:103], v[98:99], v[102:103] op_sel:[0,1]
	ds_read2_b64 v[2:5], v60 offset1:66
	ds_read2_b64 v[18:21], v60 offset0:132 offset1:198
	v_pk_fma_f32 v[208:209], v[94:95], v[100:101], v[102:103] neg_lo:[0,0,1] neg_hi:[0,0,1]
	v_pk_fma_f32 v[100:101], v[96:97], v[100:101], v[102:103] op_sel_hi:[1,0,1]
	v_pk_mul_f32 v[102:103], v[54:55], v[106:107]
	ds_read2_b64 v[6:9], v65 offset0:8 offset1:74
	ds_read2_b64 v[22:25], v65 offset0:140 offset1:206
	ds_read2_b64 v[10:13], v67 offset0:16 offset1:82
	ds_read2_b64 v[26:29], v67 offset0:148 offset1:214
	ds_read2_b64 v[14:17], v185 offset0:24 offset1:90
	ds_read2_b64 v[30:33], v185 offset0:156 offset1:222
	v_mov_b32_e32 v209, v101
	v_pk_fma_f32 v[100:101], v[54:55], v[104:105], v[102:103] op_sel:[0,0,1] op_sel_hi:[1,1,0] neg_lo:[1,0,0] neg_hi:[1,0,0]
	v_pk_fma_f32 v[108:109], v[54:55], v[104:105], v[102:103] op_sel:[0,0,1] op_sel_hi:[1,1,0]
	v_mov_b32_e32 v102, v100
	v_mov_b32_e32 v103, v109
	v_pk_mov_b32 v[108:109], v[108:109], v[100:101] op_sel:[1,0]
	v_cmp_ne_u64_e32 vcc, 0, v[34:35]
	v_pk_mul_f32 v[190:191], v[108:109], v[190:191] op_sel:[0,1]
	s_nop 0
	v_pk_fma_f32 v[214:215], v[100:101], v[202:203], v[190:191] neg_lo:[0,0,1] neg_hi:[0,0,1]
	v_pk_fma_f32 v[190:191], v[102:103], v[202:203], v[190:191] op_sel_hi:[1,0,1]
	s_waitcnt lgkmcnt(1)
; FFT_HD cf2 cmul(cf2 a, cf2 b) { return mk2(a.x * b.x - a.y * b.y, a.x * b.y + a.y * b.x); }
; FFT_HD cf2 cmulc(cf2 a, cf2 b) { return mk2(a.x * b.x + a.y * b.y, a.y * b.x - a.x * b.y); }
; template <bool INV, int lS, class ZP> FFT_HD void fft_r16_pass(ZP z, int tid) {
;     ...
; #pragma unroll
;         for (int j = 0; j < 16; ++j) z[pb0 + j * STEP] = x[j];
;         if (INV) {
; #pragma unroll
;             for (int j = 1; j < 16; ++j) y[j] = cmulc(y[j], tw[j]);
;         }
;         dft16<INV>(y);
;         if (!INV) {
; #pragma unroll
;             for (int j = 1; j < 16; ++j) y[j] = cmul(y[j], tw[j]);
;         }
; #pragma unroll
;         for (int j = 0; j < 16; ++j) z[pb1 + j * STEP] = y[j];
	v_pk_add_f32 v[202:203], v[6:7], v[14:15]
	v_mov_b32_e32 v215, v191
	ds_write2_b64 v238, v[110:111], v[230:231] offset1:66
	ds_write2_b64 v238, v[218:219], v[210:211] offset0:132 offset1:198
	ds_write2_b64 v239, v[212:213], v[222:223] offset0:8 offset1:74
	ds_write2_b64 v239, v[224:225], v[204:205] offset0:140 offset1:206
	ds_write2_b64 v240, v[198:199], v[200:201] offset0:16 offset1:82
	ds_write2_b64 v240, v[220:221], v[206:207] offset0:148 offset1:214
	ds_write2_b64 v241, v[188:189], v[192:193] offset0:24 offset1:90
	ds_write2_b64 v241, v[208:209], v[214:215] offset0:156 offset1:222
	v_pk_mov_b32 v[110:111], v[4:5], v[8:9] op_sel:[1,0]
	v_pk_mov_b32 v[188:189], v[12:13], v[16:17] op_sel:[1,0]
	v_mov_b32_e32 v190, v12
	v_pk_add_f32 v[110:111], v[110:111], v[188:189] neg_lo:[0,1] neg_hi:[0,1]
	v_mov_b32_e32 v188, v4
	v_mov_b32_e32 v189, v9
	v_mov_b32_e32 v191, v17
	v_pk_add_f32 v[188:189], v[188:189], v[190:191] neg_lo:[0,1] neg_hi:[0,1]
	v_pk_mov_b32 v[190:191], v[18:19], v[22:23] op_sel:[1,0]
	s_waitcnt lgkmcnt(8)
	v_pk_mov_b32 v[192:193], v[26:27], v[30:31] op_sel:[1,0]
	v_pk_mov_b32 v[206:207], v[20:21], v[4:5] op_sel:[1,0]
	v_pk_mov_b32 v[208:209], v[28:29], v[12:13] op_sel:[1,0]
	v_pk_add_f32 v[190:191], v[190:191], v[192:193] neg_lo:[0,1] neg_hi:[0,1]
	v_mov_b32_e32 v192, v18
	v_mov_b32_e32 v193, v23
	v_mov_b32_e32 v198, v26
	v_mov_b32_e32 v199, v31
	v_pk_add_f32 v[206:207], v[206:207], v[208:209]
	v_mov_b32_e32 v208, v4
	v_mov_b32_e32 v209, v20
	v_mov_b32_e32 v210, v12
	v_mov_b32_e32 v211, v28
	v_pk_add_f32 v[192:193], v[192:193], v[198:199] neg_lo:[0,1] neg_hi:[0,1]
	v_pk_add_f32 v[208:209], v[208:209], v[210:211]
	v_pk_mov_b32 v[210:211], v[24:25], v[8:9] op_sel:[1,0]
	v_pk_mov_b32 v[212:213], v[32:33], v[16:17] op_sel:[1,0]
	v_add_f32_e32 v39, v192, v193
	v_sub_f32_e32 v218, v190, v191
	v_sub_f32_e32 v219, v192, v193
	v_add_f32_e32 v200, v190, v191
	v_pk_mov_b32 v[190:191], v[20:21], v[24:25] op_sel:[1,0]
	v_pk_mov_b32 v[192:193], v[28:29], v[32:33] op_sel:[1,0]
	v_pk_add_f32 v[210:211], v[210:211], v[212:213]
	v_mov_b32_e32 v212, v8
	v_mov_b32_e32 v213, v24
	v_mov_b32_e32 v214, v16
	v_mov_b32_e32 v215, v32
	v_mov_b32_e32 v4, v20
	v_mov_b32_e32 v12, v28
	v_mov_b32_e32 v8, v24
	v_mov_b32_e32 v16, v32
	v_pk_add_f32 v[190:191], v[190:191], v[192:193] neg_lo:[0,1] neg_hi:[0,1]
	v_mov_b32_e32 v192, v20
	v_mov_b32_e32 v198, v28
	v_pk_add_f32 v[212:213], v[212:213], v[214:215]
	v_pk_add_f32 v[214:215], v[4:5], v[12:13]
	v_mov_b32_e32 v20, v5
	v_mov_b32_e32 v28, v13
	v_pk_add_f32 v[12:13], v[8:9], v[16:17]
	v_mov_b32_e32 v24, v9
	v_mov_b32_e32 v32, v17
	v_pk_add_f32 v[16:17], v[18:19], v[26:27]
	v_pk_add_f32 v[18:19], v[22:23], v[30:31]
	v_pk_add_f32 v[4:5], v[20:21], v[28:29]
	v_pk_add_f32 v[8:9], v[24:25], v[32:33]
	v_pk_add_f32 v[20:21], v[16:17], v[18:19] neg_lo:[0,1] neg_hi:[0,1]
	v_mov_b32_e32 v193, v25
	v_pk_add_f32 v[24:25], v[4:5], v[8:9] neg_lo:[0,1] neg_hi:[0,1]
	v_pk_add_f32 v[26:27], v[206:207], v[210:211] neg_lo:[0,1] neg_hi:[0,1]
	v_pk_fma_f32 v[28:29], v[20:21], 0, v[20:21] op_sel:[0,0,1] op_sel_hi:[1,0,0]
	v_pk_fma_f32 v[20:21], v[20:21], 0, v[20:21] op_sel:[0,0,1] op_sel_hi:[1,0,0] neg_lo:[0,0,1] neg_hi:[0,0,1]
	v_mov_b32_e32 v199, v33
	v_pk_add_f32 v[12:13], v[214:215], v[12:13] neg_lo:[0,1] neg_hi:[0,1]
	v_mov_b32_e32 v29, v21
	v_pk_mul_f32 v[20:21], v[24:25], s[50:51]
	v_pk_mul_f32 v[24:25], v[26:27], s[24:25]
	v_pk_add_f32 v[192:193], v[192:193], v[198:199] neg_lo:[0,1] neg_hi:[0,1]
	v_mul_f32_e32 v199, 0xbf3504f3, v200
	v_pk_add_f32 v[200:201], v[2:3], v[10:11]
	v_pk_add_f32 v[22:23], v[208:209], v[212:213] neg_lo:[0,1] neg_hi:[0,1]
	v_pk_fma_f32 v[12:13], v[12:13], s[24:25], v[24:25] neg_lo:[0,0,1] neg_hi:[0,0,1]
	v_mov_b32_e32 v24, v208
	v_mov_b32_e32 v25, v4
	v_mov_b32_e32 v26, v212
	v_mov_b32_e32 v27, v8
	v_mov_b32_e32 v4, v209
	v_mov_b32_e32 v8, v213
	v_pk_fma_f32 v[20:21], v[22:23], s[50:51], v[20:21]
	v_pk_add_f32 v[22:23], v[200:201], v[202:203]
	v_pk_add_f32 v[24:25], v[24:25], v[26:27]
	v_pk_add_f32 v[16:17], v[16:17], v[18:19]
	v_pk_add_f32 v[4:5], v[4:5], v[8:9]
	v_pk_add_f32 v[204:205], v[200:201], v[202:203] neg_lo:[0,1] neg_hi:[0,1]
	v_pk_add_f32 v[8:9], v[22:23], v[16:17]
	v_pk_add_f32 v[18:19], v[24:25], v[4:5]
	v_pk_mov_b32 v[26:27], v[22:23], v[24:25] op_sel:[1,0]
	v_pk_mov_b32 v[30:31], v[16:17], v[4:5] op_sel:[1,0]
	v_mov_b32_e32 v23, v25
	v_mov_b32_e32 v17, v5
	v_pk_add_f32 v[4:5], v[22:23], v[16:17] neg_lo:[0,1] neg_hi:[0,1]
	v_pk_add_f32 v[16:17], v[8:9], v[18:19]
	v_pk_add_f32 v[8:9], v[8:9], v[18:19] neg_lo:[0,1] neg_hi:[0,1]
	v_pk_add_f32 v[18:19], v[204:205], v[28:29]
	v_pk_add_f32 v[22:23], v[20:21], v[12:13]
	v_pk_add_f32 v[26:27], v[26:27], v[30:31] neg_lo:[0,1] neg_hi:[0,1]
	v_pk_add_f32 v[24:25], v[18:19], v[22:23]
	v_pk_add_f32 v[18:19], v[18:19], v[22:23] neg_lo:[0,1] neg_hi:[0,1]
	v_pk_mul_f32 v[22:23], v[46:47], v[24:25] op_sel:[0,1]
	v_pk_add_f32 v[2:3], v[2:3], v[10:11] neg_lo:[0,1] neg_hi:[0,1]
	v_pk_fma_f32 v[30:31], v[44:45], v[24:25], v[22:23] neg_lo:[0,0,1] neg_hi:[0,0,1]
	v_pk_fma_f32 v[22:23], v[44:45], v[24:25], v[22:23] op_sel_hi:[1,0,1]
	v_pk_add_f32 v[24:25], v[26:27], v[26:27] op_sel:[0,1] op_sel_hi:[0,1] neg_lo:[0,1] neg_hi:[0,1]
	v_mov_b32_e32 v31, v23
	v_pk_add_f32 v[22:23], v[4:5], v[4:5] op_sel:[0,1] op_sel_hi:[0,1]
	v_pk_mul_f32 v[24:25], v[112:113], v[24:25]
	v_pk_add_f32 v[10:11], v[188:189], v[188:189] op_sel:[0,1] op_sel_hi:[0,1] neg_lo:[0,1] neg_hi:[0,1]
	v_pk_fma_f32 v[32:33], v[48:49], v[22:23], v[24:25] neg_lo:[0,0,1] neg_hi:[0,0,1]
	v_pk_fma_f32 v[22:23], v[50:51], v[22:23], v[24:25]
	v_pk_mov_b32 v[24:25], v[12:13], v[20:21] op_sel:[1,0]
; FFT_HD cf2 mk2(float x, float y) { return (cf2){x, y}; }
; FFT_HD cf2 cmul(cf2 a, cf2 b) { return mk2(a.x * b.x - a.y * b.y, a.x * b.y + a.y * b.x); }
; FFT_HD cf2 cadd(cf2 a, cf2 b) { return mk2(a.x + b.x, a.y + b.y); }
; FFT_HD cf2 csub(cf2 a, cf2 b) { return mk2(a.x - b.x, a.y - b.y); }
; template <bool INV> FFT_HD void dft4(cf2& a, cf2& b, cf2& c, cf2& d) {
;     const cf2 s0 = cadd(a, c), s1 = csub(a, c), s2 = cadd(b, d), s3 = csub(b, d);
;     a = cadd(s0, s2); c = csub(s0, s2);
;     const cf2 r = INV ? mk2(-s3.y, s3.x) : mk2(s3.y, -s3.x);
;     b = cadd(s1, r); d = csub(s1, r);
; }
; template <bool INV> FFT_HD void dft16(cf2 (&x)[16]) {
;     const float C1 = 0.9238795325112867f, S1 = 0.3826834323650898f, H = 0.7071067811865476f;
; #pragma unroll
;     for (int b = 0; b < 4; ++b) dft4<INV>(x[b], x[4 + b], x[8 + b], x[12 + b]);
;     const float s = INV ? -1.f : 1.f;
;     x[4 + 1] = cmul(x[4 + 1], mk2(C1, -s * S1)); x[8 + 1] = cmul(x[8 + 1], mk2(H, -s * H));   x[12 + 1] = cmul(x[12 + 1], mk2(S1, -s * C1));
;     x[4 + 2] = cmul(x[4 + 2], mk2(H, -s * H));   x[8 + 2] = cmul(x[8 + 2], mk2(0.f, -s));     x[12 + 2] = cmul(x[12 + 2], mk2(-H, -s * H));
;     x[4 + 3] = cmul(x[4 + 3], mk2(S1, -s * C1)); x[8 + 3] = cmul(x[8 + 3], mk2(-H, -s * H));  x[12 + 3] = cmul(x[12 + 3], mk2(-C1, s * S1));
; #pragma unroll
;     for (int c = 0; c < 4; ++c) dft4<INV>(x[4 * c], x[4 * c + 1], x[4 * c + 2], x[4 * c + 3]);
; #pragma unroll
;     for (int c = 0; c < 4; ++c)
; #pragma unroll
;         for (int d = c + 1; d < 4; ++d) { const cf2 t = x[4 * c + d]; x[4 * c + d] = x[4 * d + c]; x[4 * d + c] = t; }
; }
; template <bool INV, int lS, class ZP> FFT_HD void fft_r16_pass(ZP z, int tid) {
;     ...
;         dft16<INV>(y);
;         if (!INV) {
; #pragma unroll
;             for (int j = 1; j < 16; ++j) y[j] = cmul(y[j], tw[j]);
;         }
	v_pk_mov_b32 v[12:13], v[20:21], v[12:13] op_sel:[1,0]
	v_mov_b32_e32 v33, v23
	v_pk_add_f32 v[22:23], v[204:205], v[28:29] neg_lo:[0,1] neg_hi:[0,1]
	v_pk_add_f32 v[12:13], v[24:25], v[12:13] neg_lo:[0,1] neg_hi:[0,1]
	v_pk_add_f32 v[6:7], v[6:7], v[14:15] neg_lo:[0,1] neg_hi:[0,1]
	v_pk_add_f32 v[20:21], v[22:23], v[12:13]
	v_pk_add_f32 v[12:13], v[22:23], v[12:13] neg_lo:[0,1] neg_hi:[0,1]
	v_mov_b32_e32 v22, v20
	v_pk_mov_b32 v[24:25], v[12:13], v[20:21] op_sel:[1,0]
	v_mov_b32_e32 v23, v13
	v_pk_mul_f32 v[24:25], v[114:115], v[24:25]
	v_pk_mul_f32 v[10:11], v[10:11], s[48:49]
	v_pk_fma_f32 v[28:29], v[116:117], v[20:21], v[24:25] neg_lo:[0,0,1] neg_hi:[0,0,1]
	v_pk_fma_f32 v[22:23], v[116:117], v[22:23], v[24:25]
	v_pk_add_f32 v[14:15], v[110:111], v[110:111] op_sel:[0,1] op_sel_hi:[0,1]
	v_mov_b32_e32 v29, v23
	v_pk_mul_f32 v[22:23], v[54:55], v[8:9] op_sel:[0,1]
	v_mul_f32_e32 v198, 0xbf3504f3, v219
	v_pk_fma_f32 v[24:25], v[52:53], v[8:9], v[22:23] neg_lo:[0,0,1] neg_hi:[0,0,1]
	v_pk_fma_f32 v[8:9], v[52:53], v[8:9], v[22:23] op_sel_hi:[1,0,1]
	v_sub_f32_e32 v198, v198, v199
	v_mov_b32_e32 v25, v9
	v_pk_mul_f32 v[8:9], v[186:187], v[18:19]
	v_fmac_f32_e32 v199, 0xbf3504f3, v219
	v_pk_fma_f32 v[22:23], v[216:217], v[18:19], v[8:9] op_sel:[0,0,1] op_sel_hi:[1,1,0] neg_lo:[0,0,1] neg_hi:[0,0,1]
	v_pk_fma_f32 v[8:9], v[216:217], v[18:19], v[8:9] op_sel:[0,0,1] op_sel_hi:[1,1,0]
	v_pk_fma_f32 v[18:19], v[14:15], s[26:27], v[10:11]
	v_pk_fma_f32 v[10:11], v[14:15], s[26:27], v[10:11] neg_lo:[0,0,1] neg_hi:[0,0,1]
	v_pk_add_f32 v[14:15], v[190:191], v[190:191] op_sel:[0,1] op_sel_hi:[0,1]
	v_mov_b32_e32 v23, v9
	v_pk_add_f32 v[8:9], v[2:3], v[6:7] op_sel:[0,1] op_sel_hi:[1,0] neg_lo:[0,1] neg_hi:[0,1]
	v_pk_add_f32 v[2:3], v[2:3], v[6:7] op_sel:[0,1] op_sel_hi:[1,0]
	v_mov_b32_e32 v19, v11
	v_pk_add_f32 v[10:11], v[192:193], v[192:193] op_sel:[0,1] op_sel_hi:[0,1] neg_lo:[0,1] neg_hi:[0,1]
	v_pk_mul_f32 v[14:15], v[14:15], s[48:49]
	v_mov_b32_e32 v6, v8
	v_mov_b32_e32 v7, v3
	v_pk_fma_f32 v[10:11], v[10:11], s[30:31], v[14:15] neg_lo:[0,0,1] neg_hi:[0,0,1]
	v_pk_add_f32 v[14:15], v[6:7], v[198:199]
	v_pk_add_f32 v[44:45], v[18:19], v[10:11]
	v_pk_add_f32 v[6:7], v[6:7], v[198:199] neg_lo:[0,1] neg_hi:[0,1]
	v_pk_add_f32 v[46:47], v[14:15], v[44:45]
	v_pk_add_f32 v[10:11], v[18:19], v[10:11] neg_lo:[0,1] neg_hi:[0,1]
	v_pk_mul_f32 v[42:43], v[42:43], v[46:47] op_sel:[0,1]
	v_pk_add_f32 v[14:15], v[14:15], v[44:45] neg_lo:[0,1] neg_hi:[0,1]
	v_pk_fma_f32 v[44:45], v[40:41], v[46:47], v[42:43] neg_lo:[0,0,1] neg_hi:[0,0,1]
	v_pk_fma_f32 v[40:41], v[40:41], v[46:47], v[42:43] op_sel_hi:[1,0,1]
	v_pk_add_f32 v[18:19], v[6:7], v[10:11] op_sel:[0,1] op_sel_hi:[1,0]
	v_pk_add_f32 v[6:7], v[6:7], v[10:11] op_sel:[0,1] op_sel_hi:[1,0] neg_lo:[0,1] neg_hi:[0,1]
	v_mov_b32_e32 v45, v41
	v_pk_mov_b32 v[40:41], v[6:7], v[18:19] op_sel:[1,0]
	v_mov_b32_e32 v10, v18
	v_mov_b32_e32 v11, v7
	v_pk_mul_f32 v[40:41], v[104:105], v[40:41]
	v_pk_add_f32 v[50:51], v[192:193], v[192:193] op_sel:[0,1] op_sel_hi:[0,1]
	v_pk_fma_f32 v[42:43], v[106:107], v[18:19], v[40:41] neg_lo:[0,0,1] neg_hi:[0,0,1]
	v_pk_fma_f32 v[10:11], v[106:107], v[10:11], v[40:41]
	v_mul_f32_e32 v39, 0x3f3504f3, v39
	v_mov_b32_e32 v43, v11
	v_pk_add_f32 v[10:11], v[188:189], v[188:189] op_sel:[0,1] op_sel_hi:[0,1]
	v_pk_mul_f32 v[10:11], v[10:11], s[26:27]
	v_pk_add_f32 v[40:41], v[110:111], v[110:111] op_sel:[0,1] op_sel_hi:[0,1] neg_lo:[0,1] neg_hi:[0,1]
	v_pk_mul_f32 v[50:51], v[50:51], s[48:49]
	v_pk_add_f32 v[52:53], v[190:191], v[190:191] op_sel:[0,1] op_sel_hi:[0,1] neg_lo:[0,1] neg_hi:[0,1]
	v_pk_fma_f32 v[46:47], v[40:41], s[48:49], v[10:11]
	v_pk_fma_f32 v[10:11], v[40:41], s[48:49], v[10:11] neg_lo:[0,0,1] neg_hi:[0,0,1]
	v_fma_f32 v48, v218, s25, -v39
	v_pk_fma_f32 v[54:55], v[52:53], s[26:27], v[50:51]
	v_pk_fma_f32 v[50:51], v[52:53], s[26:27], v[50:51] neg_lo:[0,0,1] neg_hi:[0,0,1]
	v_mov_b32_e32 v10, v46
	v_fmamk_f32 v40, v218, 0x3f3504f3, v39
	v_mov_b32_e32 v41, v48
	v_mov_b32_e32 v50, v54
	v_mov_b32_e32 v3, v9
	v_mov_b32_e32 v49, v48
	v_pk_add_f32 v[52:53], v[10:11], v[50:51]
	v_pk_add_f32 v[104:105], v[2:3], v[40:41]
	v_mov_b32_e32 v3, v11
	v_mov_b32_e32 v41, v51
	v_pk_add_f32 v[2:3], v[2:3], v[40:41] neg_lo:[0,1] neg_hi:[0,1]
; __device__ __forceinline__ unsigned cvt_pk_bf16(float lo, float hi) { unsigned r; asm volatile("v_cvt_pk_bf16_f32 %0, %1, %2" : "=v"(r) : "v"(lo), "v"(hi)); return r; }
; FFT_HD cf2 cmul(cf2 a, cf2 b) { return mk2(a.x * b.x - a.y * b.y, a.x * b.y + a.y * b.x); }
; template <int BANK, int WAITN> __device__ __forceinline__ void bg_finish1(BgState& b) {
;     if (WAITN == 32) asm volatile("s_waitcnt vmcnt(32)" ::: "memory"); else asm volatile("s_waitcnt vmcnt(0)" ::: "memory");
;     asm volatile("" : BG_TIE16(BANK * 32) :: "memory");
;     asm volatile("" : BG_TIE16(BANK * 32 + 16) :: "memory");
;     bf16_t* dst = b.dst[BANK];
;     if (dst != nullptr) {
; #pragma unroll
;         for (int c = 0; c < 4; ++c) { u32x4 w;
;             w.x = cvt_pk_bf16(b.r[(BANK * 8 + 0) * 4 + c], b.r[(BANK * 8 + 1) * 4 + c]); w.y = cvt_pk_bf16(b.r[(BANK * 8 + 2) * 4 + c], b.r[(BANK * 8 + 3) * 4 + c]);
;             w.z = cvt_pk_bf16(b.r[(BANK * 8 + 4) * 4 + c], b.r[(BANK * 8 + 5) * 4 + c]); w.w = cvt_pk_bf16(b.r[(BANK * 8 + 6) * 4 + c], b.r[(BANK * 8 + 7) * 4 + c]);
;             bf16_t* dp = dst + (c & 1) * 512 + (c >> 1) * b.o2[BANK];
;             asm volatile("global_store_dwordx4 %0, %1, off\n\ts_nop 1" :: "v"(dp), "v"(w) : "memory"); }
;     }
; }
; template <bool INV, int lS, class ZP> FFT_HD void fft_r16_pass(ZP z, int tid) {
;     ...
;         dft16<INV>(y);
;         if (!INV) {
; #pragma unroll
;             for (int j = 1; j < 16; ++j) y[j] = cmul(y[j], tw[j]);
;         }
; #pragma unroll
;         for (int j = 0; j < 16; ++j) z[pb1 + j * STEP] = y[j];
	v_pk_mov_b32 v[8:9], v[8:9], v[46:47] op_sel:[1,0]
	v_pk_mov_b32 v[10:11], v[48:49], v[54:55] op_sel:[1,0]
	v_pk_add_f32 v[40:41], v[104:105], v[52:53]
	v_pk_add_f32 v[8:9], v[8:9], v[10:11] neg_lo:[0,1] neg_hi:[0,1]
	v_pk_mul_f32 v[46:47], v[56:57], v[40:41] op_sel_hi:[0,1]
	v_pk_fma_f32 v[48:49], v[38:39], v[40:41], v[46:47] op_sel:[0,0,1] op_sel_hi:[1,1,0]
	v_pk_fma_f32 v[38:39], v[38:39], v[40:41], v[46:47] op_sel:[0,0,1] op_sel_hi:[0,1,0] neg_lo:[0,0,1] neg_hi:[0,0,1]
	v_pk_add_f32 v[40:41], v[8:9], v[8:9] op_sel:[0,1] op_sel_hi:[0,1] neg_lo:[0,1] neg_hi:[0,1]
	v_mov_b32_e32 v49, v39
	v_pk_add_f32 v[38:39], v[2:3], v[2:3] op_sel:[0,1] op_sel_hi:[0,1]
	v_pk_mul_f32 v[40:41], v[72:73], v[40:41]
	v_pk_add_f32 v[10:11], v[104:105], v[52:53] neg_lo:[0,1] neg_hi:[0,1]
	v_pk_fma_f32 v[46:47], v[68:69], v[38:39], v[40:41] neg_lo:[0,0,1] neg_hi:[0,0,1]
	v_pk_fma_f32 v[38:39], v[70:71], v[38:39], v[40:41]
	v_pk_add_f32 v[4:5], v[4:5], v[4:5] op_sel:[0,1] op_sel_hi:[0,1] neg_lo:[0,1] neg_hi:[0,1]
	v_mov_b32_e32 v47, v39
	v_pk_mul_f32 v[38:39], v[84:85], v[10:11]
	v_pk_add_f32 v[2:3], v[2:3], v[2:3] op_sel:[0,1] op_sel_hi:[0,1] neg_lo:[0,1] neg_hi:[0,1]
	v_pk_fma_f32 v[40:41], v[86:87], v[10:11], v[38:39] op_sel:[0,0,1] op_sel_hi:[1,1,0] neg_lo:[0,0,1] neg_hi:[0,0,1]
	v_pk_fma_f32 v[10:11], v[86:87], v[10:11], v[38:39] op_sel:[0,0,1] op_sel_hi:[1,1,0]
	s_nop 0
	v_mov_b32_e32 v41, v11
	v_pk_mul_f32 v[10:11], v[80:81], v[14:15]
	s_nop 0
	v_pk_fma_f32 v[38:39], v[78:79], v[14:15], v[10:11] op_sel:[0,0,1] op_sel_hi:[1,1,0] neg_lo:[0,0,1] neg_hi:[0,0,1]
	v_pk_fma_f32 v[10:11], v[78:79], v[14:15], v[10:11] op_sel:[0,0,1] op_sel_hi:[1,1,0]
	s_nop 0
	v_mov_b32_e32 v39, v11
	v_pk_add_f32 v[10:11], v[26:27], v[26:27] op_sel:[0,1] op_sel_hi:[0,1]
	v_pk_mul_f32 v[10:11], v[90:91], v[10:11]
	s_nop 0
	v_pk_fma_f32 v[14:15], v[82:83], v[4:5], v[10:11] neg_lo:[0,0,1] neg_hi:[0,0,1]
	v_pk_fma_f32 v[4:5], v[88:89], v[4:5], v[10:11]
	s_nop 0
	v_mov_b32_e32 v15, v5
	v_pk_add_f32 v[4:5], v[8:9], v[8:9] op_sel:[0,1] op_sel_hi:[0,1]
	v_pk_mul_f32 v[4:5], v[92:93], v[4:5]
	s_nop 0
	v_pk_fma_f32 v[8:9], v[76:77], v[2:3], v[4:5] neg_lo:[0,0,1] neg_hi:[0,0,1]
	v_pk_fma_f32 v[2:3], v[74:75], v[2:3], v[4:5]
	s_nop 0
	v_mov_b32_e32 v9, v3
	v_pk_mul_f32 v[2:3], v[98:99], v[20:21] op_sel:[0,1]
	s_nop 0
	v_pk_fma_f32 v[4:5], v[94:95], v[12:13], v[2:3] neg_lo:[0,0,1] neg_hi:[0,0,1]
	v_pk_fma_f32 v[2:3], v[96:97], v[12:13], v[2:3] op_sel_hi:[1,0,1]
	s_nop 0
	v_mov_b32_e32 v5, v3
	v_pk_mul_f32 v[2:3], v[108:109], v[18:19] op_sel:[0,1]
	s_nop 0
	v_pk_fma_f32 v[10:11], v[100:101], v[6:7], v[2:3] neg_lo:[0,0,1] neg_hi:[0,0,1]
	v_pk_fma_f32 v[2:3], v[102:103], v[6:7], v[2:3] op_sel_hi:[1,0,1]
	s_nop 0
	v_mov_b32_e32 v11, v3
	ds_write2_b64 v60, v[16:17], v[48:49] offset1:66
	ds_write2_b64 v60, v[30:31], v[44:45] offset0:132 offset1:198
	ds_write2_b64 v65, v[32:33], v[46:47] offset0:8 offset1:74
	ds_write2_b64 v65, v[28:29], v[42:43] offset0:140 offset1:206
	ds_write2_b64 v67, v[24:25], v[40:41] offset0:16 offset1:82
	ds_write2_b64 v67, v[22:23], v[38:39] offset0:148 offset1:214
	ds_write2_b64 v185, v[14:15], v[8:9] offset0:24 offset1:90
	ds_write2_b64 v185, v[4:5], v[10:11] offset0:156 offset1:222
	s_waitcnt lgkmcnt(0)
	s_barrier
	s_waitcnt vmcnt(32)
	s_and_saveexec_b64 s[48:49], vcc
	s_cbranch_execz .LBB0_581
	v_cvt_pk_bf16_f32 v2, v144, v146
	v_cvt_pk_bf16_f32 v3, v145, v148
	v_cvt_pk_bf16_f32 v4, v147, v150
	v_cvt_pk_bf16_f32 v5, v149, v151
	v_lshl_add_u64 v[6:7], v[34:35], 0, s[22:23]
	global_store_dwordx4 v[34:35], v[2:5], off nt
	s_nop 1
	v_cvt_pk_bf16_f32 v2, v136, v138
	v_cvt_pk_bf16_f32 v3, v137, v140
	v_cvt_pk_bf16_f32 v4, v139, v142
	v_cvt_pk_bf16_f32 v5, v141, v143
	s_lshl_b32 s12, s42, 1
	global_store_dwordx4 v[6:7], v[2:5], off nt
	s_nop 1
	v_cvt_pk_bf16_f32 v2, v128, v130
	v_cvt_pk_bf16_f32 v3, v129, v132
	v_cvt_pk_bf16_f32 v4, v131, v134
	v_cvt_pk_bf16_f32 v5, v133, v135
	v_lshl_add_u64 v[8:9], v[34:35], 0, s[12:13]
	global_store_dwordx4 v[8:9], v[2:5], off nt
	s_nop 1
	v_cvt_pk_bf16_f32 v2, v120, v122
	v_cvt_pk_bf16_f32 v3, v121, v124
	v_cvt_pk_bf16_f32 v4, v123, v126
	v_cvt_pk_bf16_f32 v5, v125, v127
	v_lshl_add_u64 v[6:7], v[6:7], 0, s[12:13]
	global_store_dwordx4 v[6:7], v[2:5], off nt
	s_nop 1

; __device__ __forceinline__ KP kparams() { KP q = (KP)__builtin_amdgcn_kernarg_segment_ptr(); asm volatile("" : "+s"(q)); return q; }
; template <int BANK> __device__ __forceinline__ void bg_issue1(BgState& b, int wg, int NW, int lane) {
;     KP kp = kparams();
;     const float* src; int ldS; bf16_t* dst; int o2;
;     bg_decode(b.st, wg, NW, lane, kp, src, ldS, dst, o2);
;     b.dst[BANK] = dst; b.o2[BANK] = o2;
;     asm volatile("s_nop 6" ::: "memory");
; #pragma unroll
;     for (int i = 0; i < 8; ++i) { const float* p = src + (size_t)i * ldS;
;         asm volatile("global_load_dword %0, %4, off\n\tglobal_load_dword %1, %4, off offset:256\n\tglobal_load_dword %2, %4, off offset:512\n\tglobal_load_dword %3, %4, off offset:768"
;                      : "=&v"(b.r[(BANK * 8 + i) * 4 + 0]), "=&v"(b.r[(BANK * 8 + i) * 4 + 1]), "=&v"(b.r[(BANK * 8 + i) * 4 + 2]), "=&v"(b.r[(BANK * 8 + i) * 4 + 3]) : "v"(p) : "memory"); }
;     b.st += 1;
; }
; template <bool INV, int lS, class ZP> FFT_HD void fft_r16_pass(ZP z, int tid) {
;     constexpr int S = 1 << lS, STEP = (S >= 64) ? S + S / 32 : S;
;     constexpr float inv = 1.0f / (float)(16 * S);
;     cf2 tw[16];
;     if (lS != 10) {
;         fft_gen_tw((float)(tid & (S - 1)) * inv, tw);
;         const int w0 = tid, w1 = tid + 512;
;         const int pb0 = PADI(((w0 >> lS) << (lS + 4)) + (w0 & (S - 1))), pb1 = PADI(((w1 >> lS) << (lS + 4)) + (w1 & (S - 1)));
;         cf2 x[16], y[16];
; #pragma unroll
;         for (int j = 0; j < 16; ++j) x[j] = z[pb0 + j * STEP];
; #pragma unroll
;         for (int j = 0; j < 16; ++j) y[j] = z[pb1 + j * STEP];
.LBB0_591:
	s_nop 6
	s_lshl_b32 s12, s48, 2
	global_load_dword v144, v[2:3], off nt
	global_load_dword v136, v[2:3], off offset:256 nt
	global_load_dword v128, v[2:3], off offset:512 nt
	global_load_dword v120, v[2:3], off offset:768 nt
	v_lshl_add_u64 v[2:3], v[2:3], 0, s[12:13]
	v_and_b32_e32 v14, 3, v57
	global_load_dword v146, v[2:3], off nt
	global_load_dword v138, v[2:3], off offset:256 nt
	global_load_dword v130, v[2:3], off offset:512 nt
	global_load_dword v122, v[2:3], off offset:768 nt
	v_lshl_add_u64 v[2:3], v[2:3], 0, s[12:13]
	v_cvt_f32_ubyte0_e32 v4, v14
	global_load_dword v145, v[2:3], off nt
	global_load_dword v137, v[2:3], off offset:256 nt
	global_load_dword v129, v[2:3], off offset:512 nt
	global_load_dword v121, v[2:3], off offset:768 nt
	v_lshl_add_u64 v[2:3], v[2:3], 0, s[12:13]
	v_mul_f32_e32 v4, 0x3c800000, v4
	global_load_dword v148, v[2:3], off nt
	global_load_dword v140, v[2:3], off offset:256 nt
	global_load_dword v132, v[2:3], off offset:512 nt
	global_load_dword v124, v[2:3], off offset:768 nt
	v_lshl_add_u64 v[2:3], v[2:3], 0, s[12:13]
	v_sin_f32_e32 v39, v4
	v_cos_f32_e32 v38, v4
	global_load_dword v147, v[2:3], off nt
	global_load_dword v139, v[2:3], off offset:256 nt
	global_load_dword v131, v[2:3], off offset:512 nt
	global_load_dword v123, v[2:3], off offset:768 nt
	v_lshl_add_u64 v[2:3], v[2:3], 0, s[12:13]
	global_load_dword v149, v[2:3], off nt
	global_load_dword v141, v[2:3], off offset:256 nt
	global_load_dword v133, v[2:3], off offset:512 nt
	global_load_dword v125, v[2:3], off offset:768 nt
	v_lshl_add_u64 v[2:3], v[2:3], 0, s[12:13]
	global_load_dword v150, v[2:3], off nt
	global_load_dword v142, v[2:3], off offset:256 nt
	global_load_dword v134, v[2:3], off offset:512 nt
	global_load_dword v126, v[2:3], off offset:768 nt
	v_lshl_add_u64 v[2:3], v[2:3], 0, s[12:13]
	global_load_dword v151, v[2:3], off nt
	global_load_dword v143, v[2:3], off offset:256 nt
	global_load_dword v135, v[2:3], off offset:512 nt
	global_load_dword v127, v[2:3], off offset:768 nt
	v_pk_mul_f32 v[2:3], v[38:39], v[38:39]
	v_mul_f32_e64 v4, v38, -v39
	v_mov_b32_e32 v5, v2
	v_mov_b32_e32 v2, v4
	v_pk_add_f32 v[192:193], v[4:5], v[2:3]
	v_pk_add_f32 v[202:203], v[4:5], v[2:3] neg_lo:[0,1] neg_hi:[0,1]
	v_mov_b32_e32 v46, v192
	v_mov_b32_e32 v47, v203
	v_pk_mul_f32 v[8:9], v[46:47], v[46:47]
	v_pk_mul_f32 v[10:11], v[202:203], v[46:47] op_sel:[1,0] op_sel_hi:[0,1]
	v_mov_b32_e32 v2, v39
	v_mov_b32_e32 v3, v38
	v_pk_mov_b32 v[12:13], v[8:9], v[10:11] op_sel:[1,0]
	v_mov_b32_e32 v9, v10
	v_pk_mul_f32 v[4:5], v[2:3], v[46:47]
	v_pk_mul_f32 v[6:7], v[38:39], v[46:47]
	v_pk_add_f32 v[48:49], v[12:13], v[8:9] neg_lo:[0,1] neg_hi:[0,1]
	v_pk_add_f32 v[68:69], v[12:13], v[8:9]
	v_mov_b32_e32 v50, v48
	v_mov_b32_e32 v51, v69
	v_mov_b32_e32 v8, v6
	v_mov_b32_e32 v9, v5
	v_pk_mov_b32 v[4:5], v[6:7], v[4:5] op_sel:[1,0]
	v_pk_mul_f32 v[6:7], v[50:51], v[68:69] op_sel:[0,1] op_sel_hi:[1,0]
	v_pk_add_f32 v[72:73], v[8:9], v[4:5] neg_lo:[0,1] neg_hi:[0,1]
	v_pk_add_f32 v[70:71], v[8:9], v[4:5]
	v_pk_mul_f32 v[4:5], v[50:51], v[50:51]
	s_mov_b32 s48, s27
	v_mov_b32_e32 v7, v4
	v_mov_b32_e32 v4, v6
	v_pk_add_f32 v[76:77], v[6:7], v[4:5]
	v_pk_add_f32 v[74:75], v[6:7], v[4:5] neg_lo:[0,1] neg_hi:[0,1]
	v_mov_b32_e32 v54, v76
	v_mov_b32_e32 v55, v75
	v_pk_mul_f32 v[84:85], v[2:3], v[54:55]
	v_and_b32_e32 v2, 0xffffffc0, v184
	v_ashrrev_i32_e32 v3, 5, v184
	v_add_u32_e32 v4, 0x2000, v2
	v_lshlrev_b32_e32 v2, 3, v2
	v_lshlrev_b32_e32 v5, 3, v14
	v_lshlrev_b32_e32 v3, 3, v3
	v_add3_u32 v2, 0, v2, v5
	v_and_b32_e32 v3, -16, v3
	v_add_u32_e32 v65, v2, v3
	ds_read2_b64 v[98:101], v65 offset1:4
	ds_read2_b64 v[102:105], v65 offset0:8 offset1:12
	ds_read2_b64 v[106:109], v65 offset0:16 offset1:20
	ds_read2_b64 v[110:113], v65 offset0:24 offset1:28
	ds_read2_b64 v[114:117], v65 offset0:32 offset1:36
	ds_read2_b64 v[184:187], v65 offset0:40 offset1:44
	ds_read2_b64 v[188:191], v65 offset0:48 offset1:52
	ds_read2_b64 v[198:201], v65 offset0:56 offset1:60
	s_waitcnt lgkmcnt(5)
	v_pk_mov_b32 v[204:205], v[100:101], v[108:109] op_sel:[1,0]
	s_waitcnt lgkmcnt(3)
	v_mov_b32_e32 v208, v116
	s_waitcnt lgkmcnt(2)
	v_mov_b32_e32 v212, v184
	s_waitcnt lgkmcnt(1)
	v_pk_mov_b32 v[206:207], v[116:117], v[190:191] op_sel:[1,0]
	v_mov_b32_e32 v209, v191
	v_pk_add_f32 v[204:205], v[204:205], v[206:207] neg_lo:[0,1] neg_hi:[0,1]
	v_mov_b32_e32 v206, v100
	v_mov_b32_e32 v207, v109
	v_pk_add_f32 v[206:207], v[206:207], v[208:209] neg_lo:[0,1] neg_hi:[0,1]
	v_pk_mov_b32 v[208:209], v[102:103], v[110:111] op_sel:[1,0]
	s_waitcnt lgkmcnt(0)
; FFT_HD cf2 mk2(float x, float y) { return (cf2){x, y}; }
; FFT_HD cf2 cmul(cf2 a, cf2 b) { return mk2(a.x * b.x - a.y * b.y, a.x * b.y + a.y * b.x); }
; FFT_HD cf2 cadd(cf2 a, cf2 b) { return mk2(a.x + b.x, a.y + b.y); }
; FFT_HD cf2 csub(cf2 a, cf2 b) { return mk2(a.x - b.x, a.y - b.y); }
; template <bool INV> FFT_HD void dft4(cf2& a, cf2& b, cf2& c, cf2& d) {
;     const cf2 s0 = cadd(a, c), s1 = csub(a, c), s2 = cadd(b, d), s3 = csub(b, d);
;     a = cadd(s0, s2); c = csub(s0, s2);
;     const cf2 r = INV ? mk2(-s3.y, s3.x) : mk2(s3.y, -s3.x);
;     b = cadd(s1, r); d = csub(s1, r);
; }
; template <bool INV> FFT_HD void dft16(cf2 (&x)[16]) {
;     const float C1 = 0.9238795325112867f, S1 = 0.3826834323650898f, H = 0.7071067811865476f;
; #pragma unroll
;     for (int b = 0; b < 4; ++b) dft4<INV>(x[b], x[4 + b], x[8 + b], x[12 + b]);
;     const float s = INV ? -1.f : 1.f;
;     x[4 + 1] = cmul(x[4 + 1], mk2(C1, -s * S1)); x[8 + 1] = cmul(x[8 + 1], mk2(H, -s * H));   x[12 + 1] = cmul(x[12 + 1], mk2(S1, -s * C1));
;     x[4 + 2] = cmul(x[4 + 2], mk2(H, -s * H));   x[8 + 2] = cmul(x[8 + 2], mk2(0.f, -s));     x[12 + 2] = cmul(x[12 + 2], mk2(-H, -s * H));
;     x[4 + 3] = cmul(x[4 + 3], mk2(S1, -s * C1)); x[8 + 3] = cmul(x[8 + 3], mk2(-H, -s * H));  x[12 + 3] = cmul(x[12 + 3], mk2(-C1, s * S1));
; #pragma unroll
;     for (int c = 0; c < 4; ++c) dft4<INV>(x[4 * c], x[4 * c + 1], x[4 * c + 2], x[4 * c + 3]);
; #pragma unroll
;     for (int c = 0; c < 4; ++c)
; #pragma unroll
;         for (int d = c + 1; d < 4; ++d) { const cf2 t = x[4 * c + d]; x[4 * c + d] = x[4 * d + c]; x[4 * d + c] = t; }
; }
; template <bool INV, int lS, class ZP> FFT_HD void fft_r16_pass(ZP z, int tid) {
;     ...
;         if (!INV) {
; #pragma unroll
;             for (int j = 1; j < 16; ++j) x[j] = cmul(x[j], tw[j]);
;         }
	v_pk_mov_b32 v[210:211], v[184:185], v[198:199] op_sel:[1,0]
	v_mov_b32_e32 v213, v199
	v_pk_add_f32 v[208:209], v[208:209], v[210:211] neg_lo:[0,1] neg_hi:[0,1]
	v_mov_b32_e32 v210, v102
	v_mov_b32_e32 v211, v111
	v_pk_add_f32 v[210:211], v[210:211], v[212:213] neg_lo:[0,1] neg_hi:[0,1]
	v_pk_mov_b32 v[212:213], v[104:105], v[112:113] op_sel:[1,0]
	v_pk_mov_b32 v[214:215], v[186:187], v[200:201] op_sel:[1,0]
	v_mov_b32_e32 v216, v186
	v_pk_add_f32 v[212:213], v[212:213], v[214:215] neg_lo:[0,1] neg_hi:[0,1]
	v_mov_b32_e32 v214, v104
	v_mov_b32_e32 v215, v113
	v_mov_b32_e32 v217, v201
	v_pk_add_f32 v[214:215], v[214:215], v[216:217] neg_lo:[0,1] neg_hi:[0,1]
	v_mov_b32_e32 v217, v212
	v_mov_b32_e32 v216, v214
	v_mov_b32_e32 v218, v215
	v_mov_b32_e32 v219, v213
	v_add_f32_e32 v56, v210, v211
	v_pk_add_f32 v[220:221], v[216:217], v[218:219] neg_lo:[0,1] neg_hi:[0,1]
	v_pk_add_f32 v[216:217], v[216:217], v[218:219]
	v_mul_f32_e32 v232, 0x3f3504f3, v56
	v_mov_b32_e32 v221, v217
	v_mul_f32_e32 v56, 0x3ec3ef15, v217
	v_pk_add_f32 v[226:227], v[206:207], v[206:207] op_sel:[0,1] op_sel_hi:[0,1]
	s_mov_b32 s49, s26
	v_pk_add_f32 v[214:215], v[214:215], v[214:215] op_sel:[0,1] op_sel_hi:[0,1]
	v_sub_f32_e32 v67, v208, v209
	v_pk_fma_f32 v[218:219], v[220:221], s[30:31], v[56:57] op_sel_hi:[1,1,0] neg_lo:[0,0,1] neg_hi:[0,0,1]
	v_mul_f32_e32 v236, 0x3ec3ef15, v220
	v_mul_f32_e32 v237, 0x3f6c835e, v217
	v_pk_add_f32 v[216:217], v[98:99], v[114:115]
	v_pk_add_f32 v[220:221], v[106:107], v[188:189]
	v_pk_add_f32 v[98:99], v[98:99], v[114:115] neg_lo:[0,1] neg_hi:[0,1]
	v_pk_add_f32 v[106:107], v[106:107], v[188:189] neg_lo:[0,1] neg_hi:[0,1]
	v_pk_mul_f32 v[226:227], v[226:227], s[26:27]
	v_pk_add_f32 v[228:229], v[204:205], v[204:205] op_sel:[0,1] op_sel_hi:[0,1] neg_lo:[0,1] neg_hi:[0,1]
	v_pk_mul_f32 v[214:215], v[214:215], s[48:49]
	v_pk_add_f32 v[212:213], v[212:213], v[212:213] op_sel:[0,1] op_sel_hi:[0,1] neg_lo:[0,1] neg_hi:[0,1]
	v_pk_mov_b32 v[114:115], v[106:107], v[106:107] op_sel:[1,0]
	v_pk_add_f32 v[188:189], v[98:99], v[106:107] op_sel:[0,1] op_sel_hi:[1,0]
	v_pk_add_f32 v[106:107], v[98:99], v[106:107] op_sel:[0,1] op_sel_hi:[1,0] neg_lo:[0,1] neg_hi:[0,1]
	v_pk_fma_f32 v[230:231], v[228:229], s[48:49], v[226:227]
	v_pk_fma_f32 v[226:227], v[228:229], s[48:49], v[226:227] neg_lo:[0,0,1] neg_hi:[0,0,1]
	v_fmamk_f32 v228, v67, 0x3f3504f3, v232
	v_fma_f32 v232, v67, s25, -v232
	v_pk_fma_f32 v[234:235], v[212:213], s[26:27], v[214:215]
	v_pk_fma_f32 v[212:213], v[212:213], s[26:27], v[214:215] neg_lo:[0,0,1] neg_hi:[0,0,1]
	v_mov_b32_e32 v224, v188
	v_mov_b32_e32 v225, v107
	v_mov_b32_e32 v226, v230
	v_mov_b32_e32 v233, v232
	v_mov_b32_e32 v229, v232
	v_mov_b32_e32 v212, v234
	v_pk_add_f32 v[214:215], v[224:225], v[228:229]
	v_pk_add_f32 v[224:225], v[226:227], v[212:213]
	v_pk_mov_b32 v[106:107], v[106:107], v[230:231] op_sel:[1,0]
	v_pk_mov_b32 v[230:231], v[232:233], v[234:235] op_sel:[1,0]
	v_mov_b32_e32 v226, v188
	v_pk_add_f32 v[230:231], v[106:107], v[230:231] neg_lo:[0,1] neg_hi:[0,1]
	v_mov_b32_e32 v229, v213
	v_pk_add_f32 v[106:107], v[214:215], v[224:225]
	v_mov_b32_e32 v56, v39
	v_pk_add_f32 v[212:213], v[226:227], v[228:229] neg_lo:[0,1] neg_hi:[0,1]
	v_pk_mul_f32 v[226:227], v[56:57], v[106:107] op_sel_hi:[0,1]
	v_pk_add_f32 v[100:101], v[100:101], v[116:117]
	v_pk_add_f32 v[108:109], v[108:109], v[190:191]
	v_pk_add_f32 v[102:103], v[102:103], v[184:185]
	v_pk_add_f32 v[184:185], v[110:111], v[198:199]
	v_pk_add_f32 v[104:105], v[104:105], v[186:187]
	v_pk_add_f32 v[112:113], v[112:113], v[200:201]
	v_pk_fma_f32 v[228:229], v[38:39], v[106:107], v[226:227] op_sel:[0,0,1] op_sel_hi:[1,1,0]
	v_pk_fma_f32 v[106:107], v[38:39], v[106:107], v[226:227] op_sel:[0,0,1] op_sel_hi:[0,1,0] neg_lo:[0,0,1] neg_hi:[0,0,1]
	v_pk_add_f32 v[222:223], v[216:217], v[220:221]
	v_pk_add_f32 v[190:191], v[102:103], v[184:185]
	v_mov_b32_e32 v229, v107
	v_pk_add_f32 v[106:107], v[216:217], v[220:221] neg_lo:[0,1] neg_hi:[0,1]
	v_pk_add_f32 v[102:103], v[102:103], v[184:185] neg_lo:[0,1] neg_hi:[0,1]
	v_mov_b32_e32 v184, v104
	v_mov_b32_e32 v185, v101
	v_mov_b32_e32 v216, v112
	v_mov_b32_e32 v217, v109
	v_pk_add_f32 v[184:185], v[184:185], v[216:217] neg_lo:[0,1] neg_hi:[0,1]
	v_mov_b32_e32 v216, v100
	v_mov_b32_e32 v217, v104
	v_mov_b32_e32 v220, v108
	v_mov_b32_e32 v221, v112
	v_pk_add_f32 v[116:117], v[100:101], v[108:109]
	v_pk_add_f32 v[186:187], v[104:105], v[112:113]
	v_pk_add_f32 v[216:217], v[216:217], v[220:221] neg_lo:[0,1] neg_hi:[0,1]
	v_mov_b32_e32 v220, v101
	v_mov_b32_e32 v221, v105
	v_mov_b32_e32 v226, v109
	v_mov_b32_e32 v227, v113
	v_pk_mov_b32 v[100:101], v[104:105], v[100:101] op_sel:[1,0]
	v_pk_mov_b32 v[104:105], v[112:113], v[108:109] op_sel:[1,0]
	v_pk_add_f32 v[220:221], v[220:221], v[226:227] neg_lo:[0,1] neg_hi:[0,1]
	v_pk_add_f32 v[100:101], v[100:101], v[104:105] neg_lo:[0,1] neg_hi:[0,1]
	v_pk_fma_f32 v[104:105], v[102:103], 0, v[102:103] op_sel:[0,0,1] op_sel_hi:[1,0,0]
	v_pk_fma_f32 v[102:103], v[102:103], 0, v[102:103] op_sel:[0,0,1] op_sel_hi:[1,0,0] neg_lo:[0,0,1] neg_hi:[0,0,1]
	s_mov_b32 s50, s25
	s_mov_b32 s51, s24
	v_mov_b32_e32 v105, v103
	v_pk_mul_f32 v[102:103], v[220:221], s[50:51]
	v_pk_mul_f32 v[100:101], v[100:101], s[24:25]
	v_pk_fma_f32 v[102:103], v[216:217], s[50:51], v[102:103]
	v_pk_fma_f32 v[100:101], v[184:185], s[24:25], v[100:101] neg_lo:[0,0,1] neg_hi:[0,0,1]
	v_pk_add_f32 v[108:109], v[106:107], v[104:105]
	v_pk_add_f32 v[184:185], v[102:103], v[100:101]
	v_pk_mov_b32 v[44:45], v[202:203], v[192:193] op_sel:[1,0]
	v_pk_add_f32 v[112:113], v[108:109], v[184:185]
	s_mov_b32 s56, s26
; FFT_HD cf2 mk2(float x, float y) { return (cf2){x, y}; }
; FFT_HD cf2 cmul(cf2 a, cf2 b) { return mk2(a.x * b.x - a.y * b.y, a.x * b.y + a.y * b.x); }
; FFT_HD cf2 cadd(cf2 a, cf2 b) { return mk2(a.x + b.x, a.y + b.y); }
; FFT_HD cf2 csub(cf2 a, cf2 b) { return mk2(a.x - b.x, a.y - b.y); }
; template <bool INV> FFT_HD void dft4(cf2& a, cf2& b, cf2& c, cf2& d) {
;     const cf2 s0 = cadd(a, c), s1 = csub(a, c), s2 = cadd(b, d), s3 = csub(b, d);
;     a = cadd(s0, s2); c = csub(s0, s2);
;     const cf2 r = INV ? mk2(-s3.y, s3.x) : mk2(s3.y, -s3.x);
;     b = cadd(s1, r); d = csub(s1, r);
; }
; template <bool INV> FFT_HD void dft16(cf2 (&x)[16]) {
;     const float C1 = 0.9238795325112867f, S1 = 0.3826834323650898f, H = 0.7071067811865476f;
; #pragma unroll
;     for (int b = 0; b < 4; ++b) dft4<INV>(x[b], x[4 + b], x[8 + b], x[12 + b]);
;     const float s = INV ? -1.f : 1.f;
;     x[4 + 1] = cmul(x[4 + 1], mk2(C1, -s * S1)); x[8 + 1] = cmul(x[8 + 1], mk2(H, -s * H));   x[12 + 1] = cmul(x[12 + 1], mk2(S1, -s * C1));
;     x[4 + 2] = cmul(x[4 + 2], mk2(H, -s * H));   x[8 + 2] = cmul(x[8 + 2], mk2(0.f, -s));     x[12 + 2] = cmul(x[12 + 2], mk2(-H, -s * H));
;     x[4 + 3] = cmul(x[4 + 3], mk2(S1, -s * C1)); x[8 + 3] = cmul(x[8 + 3], mk2(-H, -s * H));  x[12 + 3] = cmul(x[12 + 3], mk2(-C1, s * S1));
; #pragma unroll
;     for (int c = 0; c < 4; ++c) dft4<INV>(x[4 * c], x[4 * c + 1], x[4 * c + 2], x[4 * c + 3]);
; #pragma unroll
;     for (int c = 0; c < 4; ++c)
; #pragma unroll
;         for (int d = c + 1; d < 4; ++d) { const cf2 t = x[4 * c + d]; x[4 * c + d] = x[4 * d + c]; x[4 * d + c] = t; }
; }
; template <bool INV, int lS, class ZP> FFT_HD void fft_r16_pass(ZP z, int tid) {
;     ...
;         if (!INV) {
; #pragma unroll
;             for (int j = 1; j < 16; ++j) x[j] = cmul(x[j], tw[j]);
;         }
	v_pk_mul_f32 v[192:193], v[192:193], v[112:113] op_sel:[0,1] op_sel_hi:[0,0]
	v_pk_fma_f32 v[216:217], v[202:203], v[112:113], v[192:193] op_sel:[1,0,0] neg_lo:[0,0,1] neg_hi:[0,0,1]
	v_pk_fma_f32 v[112:113], v[202:203], v[112:113], v[192:193] op_sel:[1,0,0]
	v_mov_b32_e32 v192, v204
	v_mov_b32_e32 v217, v113
	v_mov_b32_e32 v112, v206
	v_mov_b32_e32 v113, v210
	v_mov_b32_e32 v210, v207
	v_mov_b32_e32 v193, v208
	v_mov_b32_e32 v208, v205
	v_pk_add_f32 v[112:113], v[112:113], v[210:211] neg_lo:[0,1] neg_hi:[0,1]
	v_pk_add_f32 v[192:193], v[192:193], v[208:209]
	s_mov_b32 s57, s24
	v_pk_mov_b32 v[202:203], v[112:113], v[192:193] op_sel:[1,0]
	v_pk_mul_f32 v[204:205], v[192:193], s[56:57]
	v_pk_mov_b32 v[192:193], v[192:193], v[112:113] op_sel:[1,0]
	s_mov_b32 s28, s25
	s_mov_b32 s52, s27
	s_mov_b32 s53, s24
	s_mov_b32 s54, s24
	s_mov_b32 s55, s27
	v_pk_mul_f32 v[192:193], v[192:193], s[28:29]
	v_mov_b32_e32 v99, v236
	v_mov_b32_e32 v115, v237
	v_pk_fma_f32 v[192:193], v[202:203], s[54:55], v[192:193]
	v_pk_fma_f32 v[202:203], v[112:113], s[52:53], v[204:205]
	v_pk_add_f32 v[98:99], v[98:99], v[114:115] neg_lo:[0,1] neg_hi:[0,1]
	v_mov_b32_e32 v188, v218
	v_pk_add_f32 v[204:205], v[192:193], v[98:99]
	v_pk_add_f32 v[206:207], v[202:203], v[188:189]
	v_mov_b32_e32 v42, v72
	v_pk_add_f32 v[112:113], v[206:207], v[204:205]
	v_pk_mov_b32 v[40:41], v[70:71], v[72:73] op_sel:[1,0]
	v_pk_mul_f32 v[72:73], v[72:73], v[112:113] op_sel:[0,1] op_sel_hi:[0,0]
	v_mov_b32_e32 v43, v71
	v_pk_fma_f32 v[208:209], v[70:71], v[112:113], v[72:73] op_sel:[1,0,0] neg_lo:[0,0,1] neg_hi:[0,0,1]
	v_pk_fma_f32 v[70:71], v[70:71], v[112:113], v[72:73] op_sel:[1,0,0]
	v_pk_add_f32 v[72:73], v[116:117], v[186:187] neg_lo:[0,1] neg_hi:[0,1]
	v_mov_b32_e32 v209, v71
	v_pk_add_f32 v[70:71], v[222:223], v[190:191] neg_lo:[0,1] neg_hi:[0,1]
	v_pk_add_f32 v[198:199], v[222:223], v[190:191]
	v_pk_add_f32 v[200:201], v[116:117], v[186:187]
	v_pk_add_f32 v[186:187], v[70:71], v[72:73] op_sel:[0,1] op_sel_hi:[1,0]
	v_pk_add_f32 v[190:191], v[70:71], v[72:73] op_sel:[0,1] op_sel_hi:[1,0] neg_lo:[0,1] neg_hi:[0,1]
	v_mov_b32_e32 v70, v186
	v_pk_mov_b32 v[72:73], v[190:191], v[186:187] op_sel:[1,0]
	v_mov_b32_e32 v71, v191
	v_pk_mov_b32 v[112:113], v[68:69], v[48:49] op_sel:[1,0]
	v_pk_mul_f32 v[68:69], v[68:69], v[72:73] op_sel:[1,0]
	v_pk_add_f32 v[116:117], v[230:231], v[230:231] op_sel:[0,1] op_sel_hi:[0,1] neg_lo:[0,1] neg_hi:[0,1]
	v_pk_fma_f32 v[210:211], v[48:49], v[186:187], v[68:69] neg_lo:[0,0,1] neg_hi:[0,0,1]
	v_pk_fma_f32 v[68:69], v[48:49], v[70:71], v[68:69] op_sel_hi:[0,1,1]
	v_pk_mul_f32 v[70:71], v[56:57], v[112:113] op_sel_hi:[0,1]
	v_mov_b32_e32 v211, v69
	v_pk_fma_f32 v[68:69], v[38:39], v[50:51], v[70:71] op_sel_hi:[0,1,1]
	v_pk_fma_f32 v[72:73], v[38:39], v[50:51], v[70:71] op_sel_hi:[0,1,1] neg_lo:[0,0,1] neg_hi:[0,0,1]
	v_mov_b32_e32 v71, v73
	v_pk_mov_b32 v[72:73], v[72:73], v[68:69] op_sel:[1,0]
	v_pk_add_f32 v[104:105], v[106:107], v[104:105] neg_lo:[0,1] neg_hi:[0,1]
	v_pk_mov_b32 v[106:107], v[100:101], v[102:103] op_sel:[1,0]
	v_pk_mov_b32 v[100:101], v[102:103], v[100:101] op_sel:[1,0]
	v_mov_b32_e32 v70, v68
	v_pk_add_f32 v[114:115], v[212:213], v[212:213] op_sel:[0,1] op_sel_hi:[0,1]
	v_pk_mul_f32 v[116:117], v[72:73], v[116:117]
	v_pk_add_f32 v[100:101], v[106:107], v[100:101] neg_lo:[0,1] neg_hi:[0,1]
	v_pk_mul_f32 v[96:97], v[46:47], v[50:51]
	v_pk_fma_f32 v[220:221], v[68:69], v[114:115], v[116:117] neg_lo:[0,0,1] neg_hi:[0,0,1]
	v_pk_fma_f32 v[114:115], v[70:71], v[114:115], v[116:117]
	v_pk_add_f32 v[102:103], v[104:105], v[100:101]
	v_pk_add_f32 v[100:101], v[104:105], v[100:101] neg_lo:[0,1] neg_hi:[0,1]
	v_pk_mul_f32 v[94:95], v[44:45], v[50:51]
	v_mov_b32_e32 v221, v115
	v_pk_add_f32 v[114:115], v[96:97], v[96:97] op_sel:[0,1] op_sel_hi:[0,1]
	v_pk_mov_b32 v[96:97], v[100:101], v[102:103] op_sel:[1,0]
	v_mov_b32_e32 v104, v102
	v_mov_b32_e32 v105, v101
	v_pk_mul_f32 v[96:97], v[114:115], v[96:97]
	v_pk_add_f32 v[116:117], v[94:95], v[94:95] op_sel:[0,1] op_sel_hi:[0,1] neg_lo:[0,1] neg_hi:[0,1]
	v_pk_fma_f32 v[222:223], v[116:117], v[102:103], v[96:97] neg_lo:[0,0,1] neg_hi:[0,0,1]
	v_pk_fma_f32 v[94:95], v[116:117], v[104:105], v[96:97]
	v_pk_mov_b32 v[96:97], v[98:99], v[218:219] op_sel:[1,0]
	v_mov_b32_e32 v223, v95
	v_pk_mov_b32 v[94:95], v[192:193], v[202:203] op_sel:[1,0]
	v_mov_b32_e32 v99, v189
	v_mov_b32_e32 v193, v203
	v_pk_add_f32 v[94:95], v[94:95], v[96:97] neg_lo:[0,1] neg_hi:[0,1]
	v_pk_add_f32 v[96:97], v[98:99], v[192:193] neg_lo:[0,1] neg_hi:[0,1]
	v_pk_mul_f32 v[92:93], v[50:51], v[42:43]
	v_pk_add_f32 v[188:189], v[96:97], v[94:95]
	v_pk_add_f32 v[192:193], v[96:97], v[94:95] neg_lo:[0,1] neg_hi:[0,1]
	v_pk_mul_f32 v[82:83], v[50:51], v[40:41]
	v_pk_add_f32 v[104:105], v[92:93], v[92:93] op_sel:[0,1] op_sel_hi:[0,1]
	v_pk_mov_b32 v[92:93], v[192:193], v[188:189] op_sel:[1,0]
	v_mov_b32_e32 v94, v188
	v_mov_b32_e32 v95, v193
	v_pk_mul_f32 v[92:93], v[104:105], v[92:93]
	v_pk_add_f32 v[106:107], v[82:83], v[82:83] op_sel:[0,1] op_sel_hi:[0,1] neg_lo:[0,1] neg_hi:[0,1]
	v_pk_fma_f32 v[202:203], v[106:107], v[188:189], v[92:93] neg_lo:[0,0,1] neg_hi:[0,0,1]
	v_pk_fma_f32 v[82:83], v[106:107], v[94:95], v[92:93]
	v_pk_mul_f32 v[90:91], v[38:39], v[54:55]
	v_mov_b32_e32 v203, v83
	v_pk_add_f32 v[82:83], v[198:199], v[200:201] neg_lo:[0,1] neg_hi:[0,1]
	v_pk_add_f32 v[110:111], v[198:199], v[200:201]
	v_pk_mul_f32 v[92:93], v[76:77], v[82:83] op_sel_hi:[0,1]
	v_pk_fma_f32 v[198:199], v[74:75], v[82:83], v[92:93] op_sel:[1,0,1] op_sel_hi:[1,1,0] neg_lo:[0,0,1] neg_hi:[0,0,1]
	v_pk_fma_f32 v[82:83], v[74:75], v[82:83], v[92:93] op_sel:[1,0,1] op_sel_hi:[1,1,0]
; FFT_HD cf2 cmul(cf2 a, cf2 b) { return mk2(a.x * b.x - a.y * b.y, a.x * b.y + a.y * b.x); }
; FFT_HD cf2 cmulc(cf2 a, cf2 b) { return mk2(a.x * b.x + a.y * b.y, a.y * b.x - a.x * b.y); }
; template <bool INV, int lS, class ZP> FFT_HD void fft_r16_pass(ZP z, int tid) {
;     ...
; #pragma unroll
;         for (int j = 0; j < 16; ++j) x[j] = z[pb0 + j * STEP];
; #pragma unroll
;         for (int j = 0; j < 16; ++j) y[j] = z[pb1 + j * STEP];
;         if (INV) {
; #pragma unroll
;             for (int j = 1; j < 16; ++j) x[j] = cmulc(x[j], tw[j]);
;         }
;         dft16<INV>(x);
;         if (!INV) {
; #pragma unroll
;             for (int j = 1; j < 16; ++j) x[j] = cmul(x[j], tw[j]);
;         }
; #pragma unroll
;         for (int j = 0; j < 16; ++j) z[pb0 + j * STEP] = x[j];
;         if (INV) {
; #pragma unroll
;             for (int j = 1; j < 16; ++j) y[j] = cmulc(y[j], tw[j]);
;         }
;         dft16<INV>(y);
	v_pk_add_f32 v[92:93], v[214:215], v[224:225] neg_lo:[0,1] neg_hi:[0,1]
	v_mov_b32_e32 v199, v83
	v_pk_add_f32 v[82:83], v[90:91], v[90:91] op_sel:[0,1] op_sel_hi:[0,1] neg_lo:[0,1] neg_hi:[0,1]
	v_pk_mov_b32 v[52:53], v[74:75], v[76:77] op_sel:[1,0]
	v_pk_mul_f32 v[90:91], v[82:83], v[92:93]
	v_pk_add_f32 v[84:85], v[84:85], v[84:85] op_sel:[1,0] op_sel_hi:[1,0]
	v_pk_mul_f32 v[88:89], v[46:47], v[52:53]
	v_pk_fma_f32 v[200:201], v[84:85], v[92:93], v[90:91] op_sel:[0,0,1] op_sel_hi:[1,1,0] neg_lo:[0,0,1] neg_hi:[0,0,1]
	v_pk_fma_f32 v[90:91], v[84:85], v[92:93], v[90:91] op_sel:[0,0,1] op_sel_hi:[1,1,0]
	v_pk_mul_f32 v[86:87], v[46:47], v[54:55]
	v_mov_b32_e32 v201, v91
	v_pk_add_f32 v[90:91], v[108:109], v[184:185] neg_lo:[0,1] neg_hi:[0,1]
	v_pk_add_f32 v[184:185], v[88:89], v[88:89] op_sel:[0,1] op_sel_hi:[0,1]
	v_pk_mul_f32 v[88:89], v[184:185], v[90:91]
	v_pk_add_f32 v[214:215], v[86:87], v[86:87] op_sel:[1,0] op_sel_hi:[1,0] neg_lo:[0,1] neg_hi:[0,1]
	v_pk_mul_f32 v[80:81], v[42:43], v[52:53]
	v_pk_fma_f32 v[218:219], v[214:215], v[90:91], v[88:89] op_sel:[0,0,1] op_sel_hi:[1,1,0] neg_lo:[0,0,1] neg_hi:[0,0,1]
	v_pk_fma_f32 v[86:87], v[214:215], v[90:91], v[88:89] op_sel:[0,0,1] op_sel_hi:[1,1,0]
	v_pk_mul_f32 v[78:79], v[42:43], v[54:55]
	v_mov_b32_e32 v219, v87
	v_mov_b32_e32 v86, v204
	v_mov_b32_e32 v87, v207
	v_mov_b32_e32 v207, v205
	v_pk_add_f32 v[86:87], v[86:87], v[206:207] neg_lo:[0,1] neg_hi:[0,1]
	v_pk_add_f32 v[80:81], v[80:81], v[80:81] op_sel:[0,1] op_sel_hi:[0,1]
	v_pk_mul_f32 v[88:89], v[80:81], v[86:87]
	v_pk_add_f32 v[78:79], v[78:79], v[78:79] op_sel:[1,0] op_sel_hi:[1,0] neg_lo:[0,1] neg_hi:[0,1]
	v_pk_add_f32 v[96:97], v[230:231], v[230:231] op_sel:[0,1] op_sel_hi:[0,1]
	v_pk_fma_f32 v[204:205], v[78:79], v[86:87], v[88:89] op_sel:[0,0,1] op_sel_hi:[1,1,0] neg_lo:[0,0,1] neg_hi:[0,0,1]
	v_pk_fma_f32 v[86:87], v[78:79], v[86:87], v[88:89] op_sel:[0,0,1] op_sel_hi:[1,1,0]
	v_pk_mul_f32 v[88:89], v[50:51], v[76:77] op_sel_hi:[1,0]
	v_mov_b32_e32 v205, v87
	v_pk_fma_f32 v[86:87], v[50:51], v[74:75], v[88:89] op_sel:[0,1,1] op_sel_hi:[1,1,0] neg_lo:[0,0,1] neg_hi:[0,0,1]
	v_pk_fma_f32 v[90:91], v[50:51], v[74:75], v[88:89] op_sel:[0,1,1] op_sel_hi:[1,1,0]
	v_mov_b32_e32 v88, v86
	v_mov_b32_e32 v89, v91
	v_pk_mov_b32 v[90:91], v[90:91], v[86:87] op_sel:[1,0]
	v_pk_add_f32 v[94:95], v[212:213], v[212:213] op_sel:[0,1] op_sel_hi:[0,1] neg_lo:[0,1] neg_hi:[0,1]
	v_pk_mul_f32 v[92:93], v[90:91], v[186:187] op_sel:[0,1]
	v_ashrrev_i32_e32 v3, 2, v4
	v_pk_fma_f32 v[186:187], v[86:87], v[190:191], v[92:93] neg_lo:[0,0,1] neg_hi:[0,0,1]
	v_pk_fma_f32 v[92:93], v[88:89], v[190:191], v[92:93] op_sel_hi:[1,0,1]
	v_add3_u32 v60, v2, v3, s71
	v_mov_b32_e32 v187, v93
	v_pk_mul_f32 v[92:93], v[76:77], v[70:71] op_sel_hi:[0,1]
	v_pk_fma_f32 v[76:77], v[74:75], v[70:71], v[92:93] op_sel:[1,0,1] op_sel_hi:[1,1,0] neg_lo:[0,0,1] neg_hi:[0,0,1]
	v_pk_fma_f32 v[92:93], v[74:75], v[70:71], v[92:93] op_sel:[1,0,1] op_sel_hi:[1,1,0]
	v_mov_b32_e32 v74, v76
	v_mov_b32_e32 v75, v93
	v_pk_mov_b32 v[92:93], v[92:93], v[76:77] op_sel:[1,0]
	ds_read2_b64 v[2:5], v60 offset1:4
	ds_read2_b64 v[18:21], v60 offset0:8 offset1:12
	ds_read2_b64 v[6:9], v60 offset0:16 offset1:20
	ds_read2_b64 v[22:25], v60 offset0:24 offset1:28
	ds_read2_b64 v[10:13], v60 offset0:32 offset1:36
	ds_read2_b64 v[26:29], v60 offset0:40 offset1:44
	ds_read2_b64 v[14:17], v60 offset0:48 offset1:52
	ds_read2_b64 v[30:33], v60 offset0:56 offset1:60
	v_pk_mul_f32 v[96:97], v[92:93], v[96:97]
	v_cmp_ne_u64_e32 vcc, 0, v[36:37]
	v_pk_fma_f32 v[190:191], v[76:77], v[94:95], v[96:97] neg_lo:[0,0,1] neg_hi:[0,0,1]
	v_pk_fma_f32 v[94:95], v[74:75], v[94:95], v[96:97]
	v_pk_mul_f32 v[96:97], v[54:55], v[116:117]
	v_mov_b32_e32 v191, v95
	v_pk_fma_f32 v[94:95], v[54:55], v[114:115], v[96:97] op_sel:[0,0,1] op_sel_hi:[1,1,0] neg_lo:[1,0,0] neg_hi:[1,0,0]
	v_pk_fma_f32 v[98:99], v[54:55], v[114:115], v[96:97] op_sel:[0,0,1] op_sel_hi:[1,1,0]
	v_mov_b32_e32 v96, v94
	v_mov_b32_e32 v97, v99
	v_pk_mov_b32 v[98:99], v[98:99], v[94:95] op_sel:[1,0]
	s_nop 0
	v_pk_mul_f32 v[102:103], v[98:99], v[102:103] op_sel:[0,1]
	s_nop 0
	v_pk_fma_f32 v[206:207], v[94:95], v[100:101], v[102:103] neg_lo:[0,0,1] neg_hi:[0,0,1]
	v_pk_fma_f32 v[100:101], v[96:97], v[100:101], v[102:103] op_sel_hi:[1,0,1]
	v_pk_mul_f32 v[102:103], v[54:55], v[106:107]
	v_mov_b32_e32 v207, v101
	v_pk_fma_f32 v[100:101], v[54:55], v[104:105], v[102:103] op_sel:[0,0,1] op_sel_hi:[1,1,0] neg_lo:[1,0,0] neg_hi:[1,0,0]
	v_pk_fma_f32 v[108:109], v[54:55], v[104:105], v[102:103] op_sel:[0,0,1] op_sel_hi:[1,1,0]
	v_mov_b32_e32 v102, v100
	v_mov_b32_e32 v103, v109
	v_pk_mov_b32 v[108:109], v[108:109], v[100:101] op_sel:[1,0]
	s_nop 0
	v_pk_mul_f32 v[188:189], v[108:109], v[188:189] op_sel:[0,1]
	s_nop 0
	v_pk_fma_f32 v[212:213], v[100:101], v[192:193], v[188:189] neg_lo:[0,0,1] neg_hi:[0,0,1]
	v_pk_fma_f32 v[188:189], v[102:103], v[192:193], v[188:189] op_sel_hi:[1,0,1]
	s_waitcnt lgkmcnt(2)
	v_mov_b32_e32 v192, v26
	v_mov_b32_e32 v213, v189
	ds_write2_b64 v65, v[110:111], v[228:229] offset1:4
	ds_write2_b64 v65, v[216:217], v[208:209] offset0:8 offset1:12
	ds_write2_b64 v65, v[210:211], v[220:221] offset0:16 offset1:20
	ds_write2_b64 v65, v[222:223], v[202:203] offset0:24 offset1:28
	ds_write2_b64 v65, v[198:199], v[200:201] offset0:32 offset1:36
	ds_write2_b64 v65, v[218:219], v[204:205] offset0:40 offset1:44
	ds_write2_b64 v65, v[186:187], v[190:191] offset0:48 offset1:52
	ds_write2_b64 v65, v[206:207], v[212:213] offset0:56 offset1:60
	v_pk_mov_b32 v[110:111], v[4:5], v[8:9] op_sel:[1,0]
	s_waitcnt lgkmcnt(9)
; FFT_HD cf2 mk2(float x, float y) { return (cf2){x, y}; }
; FFT_HD cf2 cmul(cf2 a, cf2 b) { return mk2(a.x * b.x - a.y * b.y, a.x * b.y + a.y * b.x); }
; FFT_HD cf2 cadd(cf2 a, cf2 b) { return mk2(a.x + b.x, a.y + b.y); }
; FFT_HD cf2 csub(cf2 a, cf2 b) { return mk2(a.x - b.x, a.y - b.y); }
; template <bool INV> FFT_HD void dft4(cf2& a, cf2& b, cf2& c, cf2& d) {
;     const cf2 s0 = cadd(a, c), s1 = csub(a, c), s2 = cadd(b, d), s3 = csub(b, d);
;     a = cadd(s0, s2); c = csub(s0, s2);
;     const cf2 r = INV ? mk2(-s3.y, s3.x) : mk2(s3.y, -s3.x);
;     b = cadd(s1, r); d = csub(s1, r);
; }
; template <bool INV> FFT_HD void dft16(cf2 (&x)[16]) {
;     const float C1 = 0.9238795325112867f, S1 = 0.3826834323650898f, H = 0.7071067811865476f;
; #pragma unroll
;     for (int b = 0; b < 4; ++b) dft4<INV>(x[b], x[4 + b], x[8 + b], x[12 + b]);
;     const float s = INV ? -1.f : 1.f;
;     x[4 + 1] = cmul(x[4 + 1], mk2(C1, -s * S1)); x[8 + 1] = cmul(x[8 + 1], mk2(H, -s * H));   x[12 + 1] = cmul(x[12 + 1], mk2(S1, -s * C1));
;     x[4 + 2] = cmul(x[4 + 2], mk2(H, -s * H));   x[8 + 2] = cmul(x[8 + 2], mk2(0.f, -s));     x[12 + 2] = cmul(x[12 + 2], mk2(-H, -s * H));
;     x[4 + 3] = cmul(x[4 + 3], mk2(S1, -s * C1)); x[8 + 3] = cmul(x[8 + 3], mk2(-H, -s * H));  x[12 + 3] = cmul(x[12 + 3], mk2(-C1, s * S1));
; #pragma unroll
;     for (int c = 0; c < 4; ++c) dft4<INV>(x[4 * c], x[4 * c + 1], x[4 * c + 2], x[4 * c + 3]);
; #pragma unroll
;     for (int c = 0; c < 4; ++c)
; #pragma unroll
;         for (int d = c + 1; d < 4; ++d) { const cf2 t = x[4 * c + d]; x[4 * c + d] = x[4 * d + c]; x[4 * d + c] = t; }
; }
	v_pk_mov_b32 v[186:187], v[12:13], v[16:17] op_sel:[1,0]
	v_mov_b32_e32 v188, v12
	v_pk_add_f32 v[110:111], v[110:111], v[186:187] neg_lo:[0,1] neg_hi:[0,1]
	v_mov_b32_e32 v186, v4
	v_mov_b32_e32 v187, v9
	v_mov_b32_e32 v189, v17
	v_pk_add_f32 v[186:187], v[186:187], v[188:189] neg_lo:[0,1] neg_hi:[0,1]
	v_pk_mov_b32 v[188:189], v[18:19], v[22:23] op_sel:[1,0]
	s_waitcnt lgkmcnt(8)
	v_pk_mov_b32 v[190:191], v[26:27], v[30:31] op_sel:[1,0]
	v_pk_mov_b32 v[204:205], v[20:21], v[4:5] op_sel:[1,0]
	v_pk_mov_b32 v[206:207], v[28:29], v[12:13] op_sel:[1,0]
	v_pk_add_f32 v[188:189], v[188:189], v[190:191] neg_lo:[0,1] neg_hi:[0,1]
	v_mov_b32_e32 v190, v18
	v_mov_b32_e32 v191, v23
	v_mov_b32_e32 v193, v31
	v_pk_add_f32 v[204:205], v[204:205], v[206:207]
	v_mov_b32_e32 v206, v4
	v_mov_b32_e32 v207, v20
	v_mov_b32_e32 v208, v12
	v_mov_b32_e32 v209, v28
	v_pk_add_f32 v[190:191], v[190:191], v[192:193] neg_lo:[0,1] neg_hi:[0,1]
	v_pk_add_f32 v[206:207], v[206:207], v[208:209]
	v_pk_mov_b32 v[208:209], v[24:25], v[8:9] op_sel:[1,0]
	v_pk_mov_b32 v[210:211], v[32:33], v[16:17] op_sel:[1,0]
	v_add_f32_e32 v39, v190, v191
	v_sub_f32_e32 v65, v188, v189
	v_sub_f32_e32 v67, v190, v191
	v_add_f32_e32 v198, v188, v189
	v_pk_mov_b32 v[188:189], v[20:21], v[24:25] op_sel:[1,0]
	v_pk_mov_b32 v[190:191], v[28:29], v[32:33] op_sel:[1,0]
	v_pk_add_f32 v[208:209], v[208:209], v[210:211]
	v_mov_b32_e32 v210, v8
	v_mov_b32_e32 v211, v24
	v_mov_b32_e32 v212, v16
	v_mov_b32_e32 v213, v32
	v_mov_b32_e32 v4, v20
	v_mov_b32_e32 v12, v28
	v_mov_b32_e32 v8, v24
	v_mov_b32_e32 v16, v32
	v_pk_add_f32 v[188:189], v[188:189], v[190:191] neg_lo:[0,1] neg_hi:[0,1]
	v_mov_b32_e32 v190, v20
	v_mov_b32_e32 v192, v28
	v_pk_add_f32 v[210:211], v[210:211], v[212:213]
	v_pk_add_f32 v[212:213], v[4:5], v[12:13]
	v_mov_b32_e32 v20, v5
	v_mov_b32_e32 v28, v13
	v_pk_add_f32 v[12:13], v[8:9], v[16:17]
	v_mov_b32_e32 v24, v9
	v_mov_b32_e32 v32, v17
	v_pk_add_f32 v[16:17], v[18:19], v[26:27]
	v_pk_add_f32 v[18:19], v[22:23], v[30:31]
	v_pk_add_f32 v[4:5], v[20:21], v[28:29]
	v_pk_add_f32 v[8:9], v[24:25], v[32:33]
	v_pk_add_f32 v[20:21], v[16:17], v[18:19] neg_lo:[0,1] neg_hi:[0,1]
	v_mov_b32_e32 v191, v25
	v_pk_add_f32 v[24:25], v[4:5], v[8:9] neg_lo:[0,1] neg_hi:[0,1]
	v_pk_add_f32 v[26:27], v[204:205], v[208:209] neg_lo:[0,1] neg_hi:[0,1]
	v_pk_fma_f32 v[28:29], v[20:21], 0, v[20:21] op_sel:[0,0,1] op_sel_hi:[1,0,0]
	v_pk_fma_f32 v[20:21], v[20:21], 0, v[20:21] op_sel:[0,0,1] op_sel_hi:[1,0,0] neg_lo:[0,0,1] neg_hi:[0,0,1]
	v_mov_b32_e32 v193, v33
	v_pk_add_f32 v[12:13], v[212:213], v[12:13] neg_lo:[0,1] neg_hi:[0,1]
	v_mov_b32_e32 v29, v21
	v_pk_mul_f32 v[20:21], v[24:25], s[50:51]
	v_pk_mul_f32 v[24:25], v[26:27], s[24:25]
	v_pk_add_f32 v[190:191], v[190:191], v[192:193] neg_lo:[0,1] neg_hi:[0,1]
	v_mul_f32_e32 v193, 0xbf3504f3, v198
	v_pk_add_f32 v[198:199], v[2:3], v[10:11]
	v_pk_add_f32 v[200:201], v[6:7], v[14:15]
	v_pk_add_f32 v[22:23], v[206:207], v[210:211] neg_lo:[0,1] neg_hi:[0,1]
	v_pk_fma_f32 v[12:13], v[12:13], s[24:25], v[24:25] neg_lo:[0,0,1] neg_hi:[0,0,1]
	v_mov_b32_e32 v24, v206
	v_mov_b32_e32 v25, v4
	v_mov_b32_e32 v26, v210
	v_mov_b32_e32 v27, v8
	v_mov_b32_e32 v4, v207
	v_mov_b32_e32 v8, v211
	v_pk_fma_f32 v[20:21], v[22:23], s[50:51], v[20:21]
	v_pk_add_f32 v[22:23], v[198:199], v[200:201]
	v_pk_add_f32 v[24:25], v[24:25], v[26:27]
	v_pk_add_f32 v[16:17], v[16:17], v[18:19]
	v_pk_add_f32 v[4:5], v[4:5], v[8:9]
	v_pk_add_f32 v[202:203], v[198:199], v[200:201] neg_lo:[0,1] neg_hi:[0,1]
	v_pk_add_f32 v[8:9], v[22:23], v[16:17]
	v_pk_add_f32 v[18:19], v[24:25], v[4:5]
	v_pk_mov_b32 v[26:27], v[22:23], v[24:25] op_sel:[1,0]
	v_pk_mov_b32 v[30:31], v[16:17], v[4:5] op_sel:[1,0]
	v_mov_b32_e32 v23, v25
	v_mov_b32_e32 v17, v5
	v_pk_add_f32 v[4:5], v[22:23], v[16:17] neg_lo:[0,1] neg_hi:[0,1]
	v_pk_add_f32 v[16:17], v[8:9], v[18:19]
	v_pk_add_f32 v[8:9], v[8:9], v[18:19] neg_lo:[0,1] neg_hi:[0,1]
	v_pk_add_f32 v[18:19], v[202:203], v[28:29]
	v_pk_add_f32 v[22:23], v[20:21], v[12:13]
	v_pk_add_f32 v[26:27], v[26:27], v[30:31] neg_lo:[0,1] neg_hi:[0,1]
	v_pk_add_f32 v[24:25], v[18:19], v[22:23]
	v_pk_add_f32 v[18:19], v[18:19], v[22:23] neg_lo:[0,1] neg_hi:[0,1]
	v_pk_mul_f32 v[22:23], v[46:47], v[24:25] op_sel:[0,1]
	v_pk_add_f32 v[2:3], v[2:3], v[10:11] neg_lo:[0,1] neg_hi:[0,1]
	v_pk_fma_f32 v[30:31], v[44:45], v[24:25], v[22:23] neg_lo:[0,0,1] neg_hi:[0,0,1]
	v_pk_fma_f32 v[22:23], v[44:45], v[24:25], v[22:23] op_sel_hi:[1,0,1]
	v_pk_add_f32 v[24:25], v[26:27], v[26:27] op_sel:[0,1] op_sel_hi:[0,1] neg_lo:[0,1] neg_hi:[0,1]
	v_mov_b32_e32 v31, v23
	v_pk_add_f32 v[22:23], v[4:5], v[4:5] op_sel:[0,1] op_sel_hi:[0,1]
	v_pk_mul_f32 v[24:25], v[112:113], v[24:25]
	v_pk_add_f32 v[10:11], v[186:187], v[186:187] op_sel:[0,1] op_sel_hi:[0,1] neg_lo:[0,1] neg_hi:[0,1]
	v_pk_fma_f32 v[32:33], v[48:49], v[22:23], v[24:25] neg_lo:[0,0,1] neg_hi:[0,0,1]
	v_pk_fma_f32 v[22:23], v[50:51], v[22:23], v[24:25]
	v_pk_mov_b32 v[24:25], v[12:13], v[20:21] op_sel:[1,0]
	v_pk_mov_b32 v[12:13], v[20:21], v[12:13] op_sel:[1,0]
	v_mov_b32_e32 v33, v23
	v_pk_add_f32 v[22:23], v[202:203], v[28:29] neg_lo:[0,1] neg_hi:[0,1]
	v_pk_add_f32 v[12:13], v[24:25], v[12:13] neg_lo:[0,1] neg_hi:[0,1]
	v_pk_add_f32 v[6:7], v[6:7], v[14:15] neg_lo:[0,1] neg_hi:[0,1]
	v_pk_add_f32 v[20:21], v[22:23], v[12:13]
	v_pk_add_f32 v[12:13], v[22:23], v[12:13] neg_lo:[0,1] neg_hi:[0,1]
	v_mov_b32_e32 v22, v20
	v_pk_mov_b32 v[24:25], v[12:13], v[20:21] op_sel:[1,0]
	v_mov_b32_e32 v23, v13
	v_pk_mul_f32 v[24:25], v[114:115], v[24:25]
	v_pk_mul_f32 v[10:11], v[10:11], s[48:49]
	v_pk_fma_f32 v[28:29], v[116:117], v[20:21], v[24:25] neg_lo:[0,0,1] neg_hi:[0,0,1]
; FFT_HD cf2 mk2(float x, float y) { return (cf2){x, y}; }
; FFT_HD cf2 cmul(cf2 a, cf2 b) { return mk2(a.x * b.x - a.y * b.y, a.x * b.y + a.y * b.x); }
; template <bool INV> FFT_HD void dft16(cf2 (&x)[16]) {
;     const float C1 = 0.9238795325112867f, S1 = 0.3826834323650898f, H = 0.7071067811865476f;
; #pragma unroll
;     for (int b = 0; b < 4; ++b) dft4<INV>(x[b], x[4 + b], x[8 + b], x[12 + b]);
;     const float s = INV ? -1.f : 1.f;
;     x[4 + 1] = cmul(x[4 + 1], mk2(C1, -s * S1)); x[8 + 1] = cmul(x[8 + 1], mk2(H, -s * H));   x[12 + 1] = cmul(x[12 + 1], mk2(S1, -s * C1));
;     x[4 + 2] = cmul(x[4 + 2], mk2(H, -s * H));   x[8 + 2] = cmul(x[8 + 2], mk2(0.f, -s));     x[12 + 2] = cmul(x[12 + 2], mk2(-H, -s * H));
;     x[4 + 3] = cmul(x[4 + 3], mk2(S1, -s * C1)); x[8 + 3] = cmul(x[8 + 3], mk2(-H, -s * H));  x[12 + 3] = cmul(x[12 + 3], mk2(-C1, s * S1));
; #pragma unroll
;     for (int c = 0; c < 4; ++c) dft4<INV>(x[4 * c], x[4 * c + 1], x[4 * c + 2], x[4 * c + 3]);
; #pragma unroll
;     for (int c = 0; c < 4; ++c)
; #pragma unroll
;         for (int d = c + 1; d < 4; ++d) { const cf2 t = x[4 * c + d]; x[4 * c + d] = x[4 * d + c]; x[4 * d + c] = t; }
; }
; template <bool INV, int lS, class ZP> FFT_HD void fft_r16_pass(ZP z, int tid) {
;     ...
;         if (!INV) {
; #pragma unroll
;             for (int j = 1; j < 16; ++j) y[j] = cmul(y[j], tw[j]);
;         }
; #pragma unroll
;         for (int j = 0; j < 16; ++j) z[pb1 + j * STEP] = y[j];
	v_pk_fma_f32 v[22:23], v[116:117], v[22:23], v[24:25]
	v_pk_add_f32 v[14:15], v[110:111], v[110:111] op_sel:[0,1] op_sel_hi:[0,1]
	v_mov_b32_e32 v29, v23
	v_pk_mul_f32 v[22:23], v[54:55], v[8:9] op_sel:[0,1]
	v_mul_f32_e32 v192, 0xbf3504f3, v67
	v_pk_fma_f32 v[24:25], v[52:53], v[8:9], v[22:23] neg_lo:[0,0,1] neg_hi:[0,0,1]
	v_pk_fma_f32 v[8:9], v[52:53], v[8:9], v[22:23] op_sel_hi:[1,0,1]
	v_sub_f32_e32 v192, v192, v193
	v_mov_b32_e32 v25, v9
	v_pk_mul_f32 v[8:9], v[184:185], v[18:19]
	v_fmac_f32_e32 v193, 0xbf3504f3, v67
	v_pk_fma_f32 v[22:23], v[214:215], v[18:19], v[8:9] op_sel:[0,0,1] op_sel_hi:[1,1,0] neg_lo:[0,0,1] neg_hi:[0,0,1]
	v_pk_fma_f32 v[8:9], v[214:215], v[18:19], v[8:9] op_sel:[0,0,1] op_sel_hi:[1,1,0]
	v_pk_fma_f32 v[18:19], v[14:15], s[26:27], v[10:11]
	v_pk_fma_f32 v[10:11], v[14:15], s[26:27], v[10:11] neg_lo:[0,0,1] neg_hi:[0,0,1]
	v_pk_add_f32 v[14:15], v[188:189], v[188:189] op_sel:[0,1] op_sel_hi:[0,1]
	v_mov_b32_e32 v23, v9
	v_pk_add_f32 v[8:9], v[2:3], v[6:7] op_sel:[0,1] op_sel_hi:[1,0] neg_lo:[0,1] neg_hi:[0,1]
	v_pk_add_f32 v[2:3], v[2:3], v[6:7] op_sel:[0,1] op_sel_hi:[1,0]
	v_mov_b32_e32 v19, v11
	v_pk_add_f32 v[10:11], v[190:191], v[190:191] op_sel:[0,1] op_sel_hi:[0,1] neg_lo:[0,1] neg_hi:[0,1]
	v_pk_mul_f32 v[14:15], v[14:15], s[48:49]
	v_mov_b32_e32 v6, v8
	v_mov_b32_e32 v7, v3
	v_pk_fma_f32 v[10:11], v[10:11], s[30:31], v[14:15] neg_lo:[0,0,1] neg_hi:[0,0,1]
	v_pk_add_f32 v[14:15], v[6:7], v[192:193]
	v_pk_add_f32 v[44:45], v[18:19], v[10:11]
	v_pk_add_f32 v[6:7], v[6:7], v[192:193] neg_lo:[0,1] neg_hi:[0,1]
	v_pk_add_f32 v[46:47], v[14:15], v[44:45]
	v_pk_add_f32 v[10:11], v[18:19], v[10:11] neg_lo:[0,1] neg_hi:[0,1]
	v_pk_mul_f32 v[42:43], v[42:43], v[46:47] op_sel:[0,1]
	v_pk_add_f32 v[14:15], v[14:15], v[44:45] neg_lo:[0,1] neg_hi:[0,1]
	v_pk_fma_f32 v[44:45], v[40:41], v[46:47], v[42:43] neg_lo:[0,0,1] neg_hi:[0,0,1]
	v_pk_fma_f32 v[40:41], v[40:41], v[46:47], v[42:43] op_sel_hi:[1,0,1]
	v_pk_add_f32 v[18:19], v[6:7], v[10:11] op_sel:[0,1] op_sel_hi:[1,0]
	v_pk_add_f32 v[6:7], v[6:7], v[10:11] op_sel:[0,1] op_sel_hi:[1,0] neg_lo:[0,1] neg_hi:[0,1]
	v_mov_b32_e32 v45, v41
	v_pk_mov_b32 v[40:41], v[6:7], v[18:19] op_sel:[1,0]
	v_mov_b32_e32 v10, v18
	v_mov_b32_e32 v11, v7
	v_pk_mul_f32 v[40:41], v[104:105], v[40:41]
	v_pk_add_f32 v[50:51], v[190:191], v[190:191] op_sel:[0,1] op_sel_hi:[0,1]
	v_pk_fma_f32 v[42:43], v[106:107], v[18:19], v[40:41] neg_lo:[0,0,1] neg_hi:[0,0,1]
	v_pk_fma_f32 v[10:11], v[106:107], v[10:11], v[40:41]
	v_mul_f32_e32 v39, 0x3f3504f3, v39
	v_mov_b32_e32 v43, v11
	v_pk_add_f32 v[10:11], v[186:187], v[186:187] op_sel:[0,1] op_sel_hi:[0,1]
	v_pk_mul_f32 v[10:11], v[10:11], s[26:27]
	v_pk_add_f32 v[40:41], v[110:111], v[110:111] op_sel:[0,1] op_sel_hi:[0,1] neg_lo:[0,1] neg_hi:[0,1]
	v_pk_mul_f32 v[50:51], v[50:51], s[48:49]
	v_pk_add_f32 v[52:53], v[188:189], v[188:189] op_sel:[0,1] op_sel_hi:[0,1] neg_lo:[0,1] neg_hi:[0,1]
	v_pk_fma_f32 v[46:47], v[40:41], s[48:49], v[10:11]
	v_pk_fma_f32 v[10:11], v[40:41], s[48:49], v[10:11] neg_lo:[0,0,1] neg_hi:[0,0,1]
	v_fma_f32 v48, v65, s25, -v39
	v_pk_fma_f32 v[54:55], v[52:53], s[26:27], v[50:51]
	v_pk_fma_f32 v[50:51], v[52:53], s[26:27], v[50:51] neg_lo:[0,0,1] neg_hi:[0,0,1]
	v_mov_b32_e32 v10, v46
	v_fmamk_f32 v40, v65, 0x3f3504f3, v39
	v_mov_b32_e32 v41, v48
	v_mov_b32_e32 v50, v54
	v_mov_b32_e32 v3, v9
	v_mov_b32_e32 v49, v48
	v_pk_add_f32 v[52:53], v[10:11], v[50:51]
	v_pk_add_f32 v[104:105], v[2:3], v[40:41]
	v_mov_b32_e32 v3, v11
	v_mov_b32_e32 v41, v51
	v_pk_add_f32 v[2:3], v[2:3], v[40:41] neg_lo:[0,1] neg_hi:[0,1]
	v_pk_mov_b32 v[8:9], v[8:9], v[46:47] op_sel:[1,0]
	v_pk_mov_b32 v[10:11], v[48:49], v[54:55] op_sel:[1,0]
	v_pk_add_f32 v[40:41], v[104:105], v[52:53]
	v_pk_add_f32 v[8:9], v[8:9], v[10:11] neg_lo:[0,1] neg_hi:[0,1]
	v_pk_mul_f32 v[46:47], v[56:57], v[40:41] op_sel_hi:[0,1]
	v_pk_fma_f32 v[48:49], v[38:39], v[40:41], v[46:47] op_sel:[0,0,1] op_sel_hi:[1,1,0]
	v_pk_fma_f32 v[38:39], v[38:39], v[40:41], v[46:47] op_sel:[0,0,1] op_sel_hi:[0,1,0] neg_lo:[0,0,1] neg_hi:[0,0,1]
	v_pk_add_f32 v[40:41], v[8:9], v[8:9] op_sel:[0,1] op_sel_hi:[0,1] neg_lo:[0,1] neg_hi:[0,1]
	v_mov_b32_e32 v49, v39
	v_pk_add_f32 v[38:39], v[2:3], v[2:3] op_sel:[0,1] op_sel_hi:[0,1]
	v_pk_mul_f32 v[40:41], v[72:73], v[40:41]
	v_pk_add_f32 v[10:11], v[104:105], v[52:53] neg_lo:[0,1] neg_hi:[0,1]
	v_pk_fma_f32 v[46:47], v[68:69], v[38:39], v[40:41] neg_lo:[0,0,1] neg_hi:[0,0,1]
	v_pk_fma_f32 v[38:39], v[70:71], v[38:39], v[40:41]
	v_pk_add_f32 v[4:5], v[4:5], v[4:5] op_sel:[0,1] op_sel_hi:[0,1] neg_lo:[0,1] neg_hi:[0,1]
	v_mov_b32_e32 v47, v39
	v_pk_mul_f32 v[38:39], v[82:83], v[10:11]
	v_pk_add_f32 v[2:3], v[2:3], v[2:3] op_sel:[0,1] op_sel_hi:[0,1] neg_lo:[0,1] neg_hi:[0,1]
	v_pk_fma_f32 v[40:41], v[84:85], v[10:11], v[38:39] op_sel:[0,0,1] op_sel_hi:[1,1,0] neg_lo:[0,0,1] neg_hi:[0,0,1]
	v_pk_fma_f32 v[10:11], v[84:85], v[10:11], v[38:39] op_sel:[0,0,1] op_sel_hi:[1,1,0]
	s_nop 0
	v_mov_b32_e32 v41, v11
	v_pk_mul_f32 v[10:11], v[80:81], v[14:15]
	s_nop 0
	v_pk_fma_f32 v[38:39], v[78:79], v[14:15], v[10:11] op_sel:[0,0,1] op_sel_hi:[1,1,0] neg_lo:[0,0,1] neg_hi:[0,0,1]
	v_pk_fma_f32 v[10:11], v[78:79], v[14:15], v[10:11] op_sel:[0,0,1] op_sel_hi:[1,1,0]
	s_nop 0
	v_mov_b32_e32 v39, v11
	v_pk_add_f32 v[10:11], v[26:27], v[26:27] op_sel:[0,1] op_sel_hi:[0,1]
	v_pk_mul_f32 v[10:11], v[90:91], v[10:11]
	s_nop 0
	v_pk_fma_f32 v[14:15], v[86:87], v[4:5], v[10:11] neg_lo:[0,0,1] neg_hi:[0,0,1]
	v_pk_fma_f32 v[4:5], v[88:89], v[4:5], v[10:11]
	s_nop 0
	v_mov_b32_e32 v15, v5
	v_pk_add_f32 v[4:5], v[8:9], v[8:9] op_sel:[0,1] op_sel_hi:[0,1]
	v_pk_mul_f32 v[4:5], v[92:93], v[4:5]
	s_nop 0
	v_pk_fma_f32 v[8:9], v[76:77], v[2:3], v[4:5] neg_lo:[0,0,1] neg_hi:[0,0,1]
	v_pk_fma_f32 v[2:3], v[74:75], v[2:3], v[4:5]
	s_nop 0
	v_mov_b32_e32 v9, v3
	v_pk_mul_f32 v[2:3], v[98:99], v[20:21] op_sel:[0,1]
	s_nop 0
	v_pk_fma_f32 v[4:5], v[94:95], v[12:13], v[2:3] neg_lo:[0,0,1] neg_hi:[0,0,1]
	v_pk_fma_f32 v[2:3], v[96:97], v[12:13], v[2:3] op_sel_hi:[1,0,1]
	s_nop 0
	v_mov_b32_e32 v5, v3
	v_pk_mul_f32 v[2:3], v[108:109], v[18:19] op_sel:[0,1]
	s_nop 0
	v_pk_fma_f32 v[10:11], v[100:101], v[6:7], v[2:3] neg_lo:[0,0,1] neg_hi:[0,0,1]
	v_pk_fma_f32 v[2:3], v[102:103], v[6:7], v[2:3] op_sel_hi:[1,0,1]
	s_nop 0
	v_mov_b32_e32 v11, v3
	ds_write2_b64 v60, v[16:17], v[48:49] offset1:4
	ds_write2_b64 v60, v[30:31], v[44:45] offset0:8 offset1:12
	ds_write2_b64 v60, v[32:33], v[46:47] offset0:16 offset1:20
	ds_write2_b64 v60, v[28:29], v[42:43] offset0:24 offset1:28
	ds_write2_b64 v60, v[24:25], v[40:41] offset0:32 offset1:36
	ds_write2_b64 v60, v[22:23], v[38:39] offset0:40 offset1:44
	ds_write2_b64 v60, v[14:15], v[8:9] offset0:48 offset1:52
	ds_write2_b64 v60, v[4:5], v[10:11] offset0:56 offset1:60
	s_waitcnt lgkmcnt(0)
	s_barrier
; __device__ __forceinline__ unsigned cvt_pk_bf16(float lo, float hi) { unsigned r; asm volatile("v_cvt_pk_bf16_f32 %0, %1, %2" : "=v"(r) : "v"(lo), "v"(hi)); return r; }
; template <int BANK, int WAITN> __device__ __forceinline__ void bg_finish1(BgState& b) {
;     if (WAITN == 32) asm volatile("s_waitcnt vmcnt(32)" ::: "memory"); else asm volatile("s_waitcnt vmcnt(0)" ::: "memory");
;     asm volatile("" : BG_TIE16(BANK * 32) :: "memory");
;     asm volatile("" : BG_TIE16(BANK * 32 + 16) :: "memory");
;     bf16_t* dst = b.dst[BANK];
;     if (dst != nullptr) {
; #pragma unroll
;         for (int c = 0; c < 4; ++c) { u32x4 w;
;             w.x = cvt_pk_bf16(b.r[(BANK * 8 + 0) * 4 + c], b.r[(BANK * 8 + 1) * 4 + c]); w.y = cvt_pk_bf16(b.r[(BANK * 8 + 2) * 4 + c], b.r[(BANK * 8 + 3) * 4 + c]);
;             w.z = cvt_pk_bf16(b.r[(BANK * 8 + 4) * 4 + c], b.r[(BANK * 8 + 5) * 4 + c]); w.w = cvt_pk_bf16(b.r[(BANK * 8 + 6) * 4 + c], b.r[(BANK * 8 + 7) * 4 + c]);
;             bf16_t* dp = dst + (c & 1) * 512 + (c >> 1) * b.o2[BANK];
;             asm volatile("global_store_dwordx4 %0, %1, off\n\ts_nop 1" :: "v"(dp), "v"(w) : "memory"); }
;     }
; }
	s_waitcnt vmcnt(32)
	s_and_saveexec_b64 s[48:49], vcc
	s_cbranch_execz .LBB0_593
	v_cvt_pk_bf16_f32 v2, v176, v178
	v_cvt_pk_bf16_f32 v3, v177, v180
	v_cvt_pk_bf16_f32 v4, v179, v181
	v_cvt_pk_bf16_f32 v5, v182, v183
	v_lshl_add_u64 v[6:7], v[36:37], 0, s[22:23]
	global_store_dwordx4 v[36:37], v[2:5], off nt
	s_nop 1
	v_cvt_pk_bf16_f32 v2, v168, v170
	v_cvt_pk_bf16_f32 v3, v169, v172
	v_cvt_pk_bf16_f32 v4, v171, v173
	v_cvt_pk_bf16_f32 v5, v174, v175
	s_lshl_b32 s12, s44, 1
	global_store_dwordx4 v[6:7], v[2:5], off nt
	s_nop 1
	v_cvt_pk_bf16_f32 v2, v160, v162
	v_cvt_pk_bf16_f32 v3, v161, v164
	v_cvt_pk_bf16_f32 v4, v163, v165
	v_cvt_pk_bf16_f32 v5, v166, v167
	v_lshl_add_u64 v[8:9], v[36:37], 0, s[12:13]
	global_store_dwordx4 v[8:9], v[2:5], off nt
	s_nop 1
	v_cvt_pk_bf16_f32 v2, v152, v154
	v_cvt_pk_bf16_f32 v3, v153, v156
	v_cvt_pk_bf16_f32 v4, v155, v157
	v_cvt_pk_bf16_f32 v5, v158, v159
	v_lshl_add_u64 v[6:7], v[6:7], 0, s[12:13]
	global_store_dwordx4 v[6:7], v[2:5], off nt
	s_nop 1

; __device__ __forceinline__ KP kparams() { KP q = (KP)__builtin_amdgcn_kernarg_segment_ptr(); asm volatile("" : "+s"(q)); return q; }
; template <int BANK> __device__ __forceinline__ void bg_issue1(BgState& b, int wg, int NW, int lane) {
;     KP kp = kparams();
;     const float* src; int ldS; bf16_t* dst; int o2;
;     bg_decode(b.st, wg, NW, lane, kp, src, ldS, dst, o2);
;     b.dst[BANK] = dst; b.o2[BANK] = o2;
;     asm volatile("s_nop 6" ::: "memory");
; #pragma unroll
;     for (int i = 0; i < 8; ++i) { const float* p = src + (size_t)i * ldS;
;         asm volatile("global_load_dword %0, %4, off\n\tglobal_load_dword %1, %4, off offset:256\n\tglobal_load_dword %2, %4, off offset:512\n\tglobal_load_dword %3, %4, off offset:768"
;                      : "=&v"(b.r[(BANK * 8 + i) * 4 + 0]), "=&v"(b.r[(BANK * 8 + i) * 4 + 1]), "=&v"(b.r[(BANK * 8 + i) * 4 + 2]), "=&v"(b.r[(BANK * 8 + i) * 4 + 3]) : "v"(p) : "memory"); }
;     b.st += 1;
; }
; template <bool INV, class ZP> FFT_HD void fft_r4_pass(ZP z, int tid, int nthr) {
;     for (int w = tid; w < FN / 4; w += nthr) {
;         const int base = PADI(4 * w);
;         cf2 a = z[base], b = z[base + 1], c = z[base + 2], d = z[base + 3];
;         dft4<INV>(a, b, c, d);
;         z[base] = a; z[base + 1] = b; z[base + 2] = c; z[base + 3] = d;
;     }
.LBB0_603:
	s_nop 6
	global_load_dword v77, v[4:5], off nt
	global_load_dword v69, v[4:5], off offset:256 nt
	global_load_dword v50, v[4:5], off offset:512 nt
	global_load_dword v42, v[4:5], off offset:768 nt
	s_lshl_b32 s12, s44, 2
	v_lshl_add_u64 v[4:5], v[4:5], 0, s[12:13]
	global_load_dword v79, v[4:5], off nt
	global_load_dword v71, v[4:5], off offset:256 nt
	global_load_dword v52, v[4:5], off offset:512 nt
	global_load_dword v44, v[4:5], off offset:768 nt
	v_lshl_add_u64 v[4:5], v[4:5], 0, s[12:13]
	global_load_dword v78, v[4:5], off nt
	global_load_dword v70, v[4:5], off offset:256 nt
	global_load_dword v51, v[4:5], off offset:512 nt
	global_load_dword v43, v[4:5], off offset:768 nt
	v_lshl_add_u64 v[4:5], v[4:5], 0, s[12:13]
	global_load_dword v81, v[4:5], off nt
	global_load_dword v73, v[4:5], off offset:256 nt
	global_load_dword v54, v[4:5], off offset:512 nt
	global_load_dword v46, v[4:5], off offset:768 nt
	v_lshl_add_u64 v[4:5], v[4:5], 0, s[12:13]
	global_load_dword v80, v[4:5], off nt
	global_load_dword v72, v[4:5], off offset:256 nt
	global_load_dword v53, v[4:5], off offset:512 nt
	global_load_dword v45, v[4:5], off offset:768 nt
	v_lshl_add_u64 v[4:5], v[4:5], 0, s[12:13]
	global_load_dword v83, v[4:5], off nt
	global_load_dword v75, v[4:5], off offset:256 nt
	global_load_dword v56, v[4:5], off offset:512 nt
	global_load_dword v48, v[4:5], off offset:768 nt
	v_lshl_add_u64 v[4:5], v[4:5], 0, s[12:13]
	global_load_dword v82, v[4:5], off nt
	global_load_dword v74, v[4:5], off offset:256 nt
	global_load_dword v55, v[4:5], off offset:512 nt
	global_load_dword v47, v[4:5], off offset:768 nt
	v_lshl_add_u64 v[4:5], v[4:5], 0, s[12:13]
	global_load_dword v84, v[4:5], off nt
	global_load_dword v76, v[4:5], off offset:256 nt
	global_load_dword v68, v[4:5], off offset:512 nt
	global_load_dword v49, v[4:5], off offset:768 nt
	v_cmp_gt_i32_e32 vcc, s75, v57
	s_and_saveexec_b64 s[44:45], vcc
	s_cbranch_execz .LBB0_606
	v_lshl_add_u32 v4, v57, 5, 0
	s_mov_b64 s[50:51], 0

; __device__ __forceinline__ unsigned cvt_pk_bf16(float lo, float hi) { unsigned r; asm volatile("v_cvt_pk_bf16_f32 %0, %1, %2" : "=v"(r) : "v"(lo), "v"(hi)); return r; }
; template <int BANK, int WAITN> __device__ __forceinline__ void bg_finish1(BgState& b) {
;     if (WAITN == 32) asm volatile("s_waitcnt vmcnt(32)" ::: "memory"); else asm volatile("s_waitcnt vmcnt(0)" ::: "memory");
;     asm volatile("" : BG_TIE16(BANK * 32) :: "memory");
;     asm volatile("" : BG_TIE16(BANK * 32 + 16) :: "memory");
;     bf16_t* dst = b.dst[BANK];
;     if (dst != nullptr) {
; #pragma unroll
;         for (int c = 0; c < 4; ++c) { u32x4 w;
;             w.x = cvt_pk_bf16(b.r[(BANK * 8 + 0) * 4 + c], b.r[(BANK * 8 + 1) * 4 + c]); w.y = cvt_pk_bf16(b.r[(BANK * 8 + 2) * 4 + c], b.r[(BANK * 8 + 3) * 4 + c]);
;             w.z = cvt_pk_bf16(b.r[(BANK * 8 + 4) * 4 + c], b.r[(BANK * 8 + 5) * 4 + c]); w.w = cvt_pk_bf16(b.r[(BANK * 8 + 6) * 4 + c], b.r[(BANK * 8 + 7) * 4 + c]);
;             bf16_t* dp = dst + (c & 1) * 512 + (c >> 1) * b.o2[BANK];
;             asm volatile("global_store_dwordx4 %0, %1, off\n\ts_nop 1" :: "v"(dp), "v"(w) : "memory"); }
;     }
; }
.LBB0_606:
	s_or_b64 exec, exec, s[44:45]
	s_waitcnt lgkmcnt(0)
	s_barrier
	s_waitcnt vmcnt(32)
	v_cmp_ne_u64_e32 vcc, 0, v[34:35]
	s_and_saveexec_b64 s[44:45], vcc
	s_cbranch_execz .LBB0_608
	v_cvt_pk_bf16_f32 v4, v144, v146
	v_cvt_pk_bf16_f32 v5, v145, v148
	v_cvt_pk_bf16_f32 v6, v147, v149
	v_cvt_pk_bf16_f32 v7, v150, v151
	v_lshl_add_u64 v[8:9], v[34:35], 0, s[22:23]
	global_store_dwordx4 v[34:35], v[4:7], off nt
	s_nop 1
	v_cvt_pk_bf16_f32 v4, v136, v138
	v_cvt_pk_bf16_f32 v5, v137, v140
	v_cvt_pk_bf16_f32 v6, v139, v141
	v_cvt_pk_bf16_f32 v7, v142, v143
	s_lshl_b32 s12, s42, 1
	global_store_dwordx4 v[8:9], v[4:7], off nt
	s_nop 1
	v_cvt_pk_bf16_f32 v4, v128, v130
	v_cvt_pk_bf16_f32 v5, v129, v132
	v_cvt_pk_bf16_f32 v6, v131, v133
	v_cvt_pk_bf16_f32 v7, v134, v135
	v_lshl_add_u64 v[10:11], v[34:35], 0, s[12:13]
	global_store_dwordx4 v[10:11], v[4:7], off nt
	s_nop 1
	v_cvt_pk_bf16_f32 v4, v120, v122
	v_cvt_pk_bf16_f32 v5, v121, v124
	v_cvt_pk_bf16_f32 v6, v123, v125
	v_cvt_pk_bf16_f32 v7, v126, v127
	v_lshl_add_u64 v[8:9], v[8:9], 0, s[12:13]
	global_store_dwordx4 v[8:9], v[4:7], off nt
	s_nop 1

; __device__ __forceinline__ KP kparams() { KP q = (KP)__builtin_amdgcn_kernarg_segment_ptr(); asm volatile("" : "+s"(q)); return q; }
; __device__ __forceinline__ unsigned cvt_pk_bf16(float lo, float hi) { unsigned r; asm volatile("v_cvt_pk_bf16_f32 %0, %1, %2" : "=v"(r) : "v"(lo), "v"(hi)); return r; }
; FFT_HD int fpos(int k) { return ((k & 15) << 10) + (((k >> 4) & 15) << 6) + (((k >> 8) & 15) << 2) + (k >> 12); }
; #define BG_I(x) bg_issue1<x>(bg, bgwg, bgNW, bglane)
; template <int BANK> __device__ __forceinline__ void bg_issue1(BgState& b, int wg, int NW, int lane) {
;     KP kp = kparams();
;     const float* src; int ldS; bf16_t* dst; int o2;
;     bg_decode(b.st, wg, NW, lane, kp, src, ldS, dst, o2);
;     b.dst[BANK] = dst; b.o2[BANK] = o2;
;     asm volatile("s_nop 6" ::: "memory");
; #pragma unroll
;     for (int i = 0; i < 8; ++i) { const float* p = src + (size_t)i * ldS;
;         asm volatile("global_load_dword %0, %4, off\n\tglobal_load_dword %1, %4, off offset:256\n\tglobal_load_dword %2, %4, off offset:512\n\tglobal_load_dword %3, %4, off offset:768"
;                      : "=&v"(b.r[(BANK * 8 + i) * 4 + 0]), "=&v"(b.r[(BANK * 8 + i) * 4 + 1]), "=&v"(b.r[(BANK * 8 + i) * 4 + 2]), "=&v"(b.r[(BANK * 8 + i) * 4 + 3]) : "v"(p) : "memory"); }
;     b.st += 1;
; }
; __device__ __forceinline__ void hy_fft_phase(LAS unsigned char* lds, int bid, int G, const bf16_t* vgT, bf16_t* zT, const float* a3, const float* wout, const float* skip, float* filt, float4* gspec) {
;     ...
;             BG_I(0);
; #pragma unroll 4
;             for (int k = tid; k <= FN / 2; k += NTHR) {
;                 const cf2 zk = z[PADI(fpos(k))], zm = z[PADI(fpos((FN - k) & (FN - 1)))];
;                 u32x2 g; g.x = cvt_pk_bf16(0.5f * (zk.x + zm.x), 0.5f * (zk.y - zm.y)); g.y = cvt_pk_bf16(0.5f * (zk.y + zm.y), -0.5f * (zk.x - zm.x)); GS[k] = g;
;             }
.LBB0_618:
	s_nop 6
	global_load_dword v34, v[8:9], off nt
	global_load_dword v26, v[8:9], off offset:256 nt
	global_load_dword v18, v[8:9], off offset:512 nt
	global_load_dword v10, v[8:9], off offset:768 nt
	s_lshl_b32 s12, s42, 2
	v_lshl_add_u64 v[8:9], v[8:9], 0, s[12:13]
	global_load_dword v36, v[8:9], off nt
	global_load_dword v28, v[8:9], off offset:256 nt
	global_load_dword v20, v[8:9], off offset:512 nt
	global_load_dword v12, v[8:9], off offset:768 nt
	v_lshl_add_u64 v[8:9], v[8:9], 0, s[12:13]
	global_load_dword v35, v[8:9], off nt
	global_load_dword v27, v[8:9], off offset:256 nt
	global_load_dword v19, v[8:9], off offset:512 nt
	global_load_dword v11, v[8:9], off offset:768 nt
	v_lshl_add_u64 v[8:9], v[8:9], 0, s[12:13]
	global_load_dword v38, v[8:9], off nt
	global_load_dword v30, v[8:9], off offset:256 nt
	global_load_dword v22, v[8:9], off offset:512 nt
	global_load_dword v14, v[8:9], off offset:768 nt
	v_lshl_add_u64 v[8:9], v[8:9], 0, s[12:13]
	global_load_dword v37, v[8:9], off nt
	global_load_dword v29, v[8:9], off offset:256 nt
	global_load_dword v21, v[8:9], off offset:512 nt
	global_load_dword v13, v[8:9], off offset:768 nt
	v_lshl_add_u64 v[8:9], v[8:9], 0, s[12:13]
	global_load_dword v40, v[8:9], off nt
	global_load_dword v32, v[8:9], off offset:256 nt
	global_load_dword v24, v[8:9], off offset:512 nt
	global_load_dword v16, v[8:9], off offset:768 nt
	v_lshl_add_u64 v[8:9], v[8:9], 0, s[12:13]
	global_load_dword v39, v[8:9], off nt
	global_load_dword v31, v[8:9], off offset:256 nt
	global_load_dword v23, v[8:9], off offset:512 nt
	global_load_dword v15, v[8:9], off offset:768 nt
	v_lshl_add_u64 v[8:9], v[8:9], 0, s[12:13]
	global_load_dword v41, v[8:9], off nt
	global_load_dword v33, v[8:9], off offset:256 nt
	global_load_dword v25, v[8:9], off offset:512 nt
	global_load_dword v17, v[8:9], off offset:768 nt
	s_movk_i32 s1, 0x2001
	v_cmp_gt_i32_e32 vcc, s1, v6
	s_and_saveexec_b64 s[42:43], vcc
	s_cbranch_execz .LBB0_621
	v_ashrrev_i32_e32 v7, 31, v6
	v_lshl_add_u64 v[8:9], v[6:7], 3, s[20:21]
	v_sub_u32_e32 v7, 0, v6
	v_lshlrev_b32_e32 v57, 2, v6
	v_lshlrev_b32_e32 v60, 10, v6
	s_mov_b64 s[50:51], 0

; __device__ __forceinline__ unsigned cvt_pk_bf16(float lo, float hi) { unsigned r; asm volatile("v_cvt_pk_bf16_f32 %0, %1, %2" : "=v"(r) : "v"(lo), "v"(hi)); return r; }
; template <int BANK, int WAITN> __device__ __forceinline__ void bg_finish1(BgState& b) {
;     if (WAITN == 32) asm volatile("s_waitcnt vmcnt(32)" ::: "memory"); else asm volatile("s_waitcnt vmcnt(0)" ::: "memory");
;     asm volatile("" : BG_TIE16(BANK * 32) :: "memory");
;     asm volatile("" : BG_TIE16(BANK * 32 + 16) :: "memory");
;     bf16_t* dst = b.dst[BANK];
;     if (dst != nullptr) {
; #pragma unroll
;         for (int c = 0; c < 4; ++c) { u32x4 w;
;             w.x = cvt_pk_bf16(b.r[(BANK * 8 + 0) * 4 + c], b.r[(BANK * 8 + 1) * 4 + c]); w.y = cvt_pk_bf16(b.r[(BANK * 8 + 2) * 4 + c], b.r[(BANK * 8 + 3) * 4 + c]);
;             w.z = cvt_pk_bf16(b.r[(BANK * 8 + 4) * 4 + c], b.r[(BANK * 8 + 5) * 4 + c]); w.w = cvt_pk_bf16(b.r[(BANK * 8 + 6) * 4 + c], b.r[(BANK * 8 + 7) * 4 + c]);
;             bf16_t* dp = dst + (c & 1) * 512 + (c >> 1) * b.o2[BANK];
;             asm volatile("global_store_dwordx4 %0, %1, off\n\ts_nop 1" :: "v"(dp), "v"(w) : "memory"); }
;     }
; }
.LBB0_621:
	s_or_b64 exec, exec, s[42:43]
	s_waitcnt vmcnt(32)
	v_cmp_ne_u64_e32 vcc, 0, v[2:3]
	s_and_saveexec_b64 s[42:43], vcc
	s_cbranch_execz .LBB0_623
	v_cvt_pk_bf16_f32 v6, v77, v79
	v_cvt_pk_bf16_f32 v7, v78, v81
	v_cvt_pk_bf16_f32 v8, v80, v83
	v_cvt_pk_bf16_f32 v9, v82, v84
	s_lshl_b32 s12, s48, 1
	global_store_dwordx4 v[2:3], v[6:9], off nt
	s_nop 1
	v_cvt_pk_bf16_f32 v6, v69, v71
	v_cvt_pk_bf16_f32 v7, v70, v73
	v_cvt_pk_bf16_f32 v8, v72, v75
	v_cvt_pk_bf16_f32 v9, v74, v76
	v_lshl_add_u64 v[70:71], v[2:3], 0, s[22:23]
	global_store_dwordx4 v[70:71], v[6:9], off nt
	s_nop 1
	v_cvt_pk_bf16_f32 v6, v50, v52
	v_cvt_pk_bf16_f32 v7, v51, v54
	v_cvt_pk_bf16_f32 v8, v53, v56
	v_cvt_pk_bf16_f32 v9, v55, v68
	v_lshl_add_u64 v[2:3], v[2:3], 0, s[12:13]
	global_store_dwordx4 v[2:3], v[6:9], off nt
	s_nop 1
	v_cvt_pk_bf16_f32 v6, v42, v44
	v_cvt_pk_bf16_f32 v7, v43, v46
	v_cvt_pk_bf16_f32 v8, v45, v48
	v_cvt_pk_bf16_f32 v9, v47, v49
	v_lshl_add_u64 v[2:3], v[70:71], 0, s[12:13]
	global_store_dwordx4 v[2:3], v[6:9], off nt
	s_nop 1

; #define LAS __attribute__((address_space(3)))
; __device__ __forceinline__ int tid_fresh() { int t = threadIdx.x; asm volatile("" : "+v"(t)); return t; }
; __device__ __forceinline__ float bf_lo(unsigned w) { return __uint_as_float(w << 16); }
; __device__ __forceinline__ float bf_hi(unsigned w) { return __uint_as_float(w & 0xffff0000u); }
; #define SEG_LD32(dst, off, base) asm volatile("global_load_dword %0, %1, %2" : "=v"(dst) : "v"(off), "s"(base) : "memory")
; #define SEG_WAIT() asm volatile("s_waitcnt vmcnt(32)\n\ts_nop 7" ::: "memory")
; #define BG_I(x) bg_issue1<x>(bg, bgwg, bgNW, bglane)
; #define BG_F(y) bg_finish1<y, 32>(bg)
; __device__ __forceinline__ void hy_fft_phase(LAS unsigned char* lds, int bid, int G, const bf16_t* vgT, bf16_t* zT, const float* a3, const float* wout, const float* skip, float* filt, float4* gspec) {
;     ...
;             tid = tid_fresh();
;             {   unsigned pa[8], pb[8];
; #pragma unroll
;                 for (int i = 0; i < 8; ++i) { const unsigned off = 4u * tid + 2048u * i; SEG_LD32(pa[i], off, v1); SEG_LD32(pb[i], off, v2); }
;                 BG_I(1);
;                 SEG_WAIT(); asm volatile("" : SEG_TIE8(pa, 0), SEG_TIE8(pb, 0) :: "memory");
; #pragma unroll
;                 for (int i = 0; i < 8; ++i) { const int n = 2 * tid + 2 * NTHR * i;
;                     *(LAS f32x4*)&z[PADI(n)] = (f32x4){bf_lo(pa[i]), has2 ? bf_lo(pb[i]) : 0.f, bf_hi(pa[i]), has2 ? bf_hi(pb[i]) : 0.f};
;                     *(LAS f32x4*)&z[PADI(T + n)] = (f32x4){0.f, 0.f, 0.f, 0.f}; }
;                 BG_F(0);
;             }
.LBB0_633:
	s_nop 6
	global_load_dword v175, v[6:7], off nt
	global_load_dword v167, v[6:7], off offset:256 nt
	global_load_dword v159, v[6:7], off offset:512 nt
	global_load_dword v116, v[6:7], off offset:768 nt
	s_lshl_b32 s12, s50, 2
	v_lshl_add_u64 v[6:7], v[6:7], 0, s[12:13]
	global_load_dword v177, v[6:7], off nt
	global_load_dword v169, v[6:7], off offset:256 nt
	global_load_dword v161, v[6:7], off offset:512 nt
	global_load_dword v153, v[6:7], off offset:768 nt
	v_lshl_add_u64 v[6:7], v[6:7], 0, s[12:13]
	global_load_dword v176, v[6:7], off nt
	global_load_dword v168, v[6:7], off offset:256 nt
	global_load_dword v160, v[6:7], off offset:512 nt
	global_load_dword v117, v[6:7], off offset:768 nt
	v_lshl_add_u64 v[6:7], v[6:7], 0, s[12:13]
	global_load_dword v179, v[6:7], off nt
	global_load_dword v171, v[6:7], off offset:256 nt
	global_load_dword v163, v[6:7], off offset:512 nt
	global_load_dword v155, v[6:7], off offset:768 nt
	v_lshl_add_u64 v[6:7], v[6:7], 0, s[12:13]
	global_load_dword v178, v[6:7], off nt
	global_load_dword v170, v[6:7], off offset:256 nt
	global_load_dword v162, v[6:7], off offset:512 nt
	global_load_dword v154, v[6:7], off offset:768 nt
	v_lshl_add_u64 v[6:7], v[6:7], 0, s[12:13]
	global_load_dword v181, v[6:7], off nt
	global_load_dword v173, v[6:7], off offset:256 nt
	global_load_dword v165, v[6:7], off offset:512 nt
	global_load_dword v157, v[6:7], off offset:768 nt
	v_lshl_add_u64 v[6:7], v[6:7], 0, s[12:13]
	global_load_dword v180, v[6:7], off nt
	global_load_dword v172, v[6:7], off offset:256 nt
	global_load_dword v164, v[6:7], off offset:512 nt
	global_load_dword v156, v[6:7], off offset:768 nt
	v_lshl_add_u64 v[6:7], v[6:7], 0, s[12:13]
	global_load_dword v182, v[6:7], off nt
	global_load_dword v174, v[6:7], off offset:256 nt
	global_load_dword v166, v[6:7], off offset:512 nt
	global_load_dword v158, v[6:7], off offset:768 nt
	s_waitcnt vmcnt(32)
	s_nop 7
	v_lshl_add_u32 v65, v54, 4, 0
	v_lshlrev_b32_e32 v6, 16, v56
	v_cndmask_b32_e64 v69, 0, v6, s[8:9]
	v_and_b32_e32 v6, 0xffff0000, v56
	v_cndmask_b32_e64 v71, 0, v6, s[8:9]
	v_ashrrev_i32_e32 v6, 4, v54
	v_lshlrev_b32_e32 v6, 3, v6
	v_and_b32_e32 v6, -16, v6
	v_lshlrev_b32_e32 v60, 1, v54
	v_lshlrev_b32_e32 v68, 16, v55
	v_and_b32_e32 v70, 0xffff0000, v55
	v_add_u32_e32 v6, v65, v6
	ds_write_b128 v6, v[68:71]
	v_add_u32_e32 v6, 0x2000, v60
	v_ashrrev_i32_e32 v6, 5, v6
	v_lshlrev_b32_e32 v6, 3, v6
	v_and_b32_e32 v6, -16, v6
	v_add3_u32 v6, v65, v6, s71
	ds_write_b128 v6, v[194:197]
	v_add_u32_e32 v6, 0x400, v60
	v_ashrrev_i32_e32 v6, 5, v6
	v_lshlrev_b32_e32 v7, 16, v53
	v_lshlrev_b32_e32 v6, 3, v6
	v_cndmask_b32_e64 v55, 0, v7, s[8:9]
	v_and_b32_e32 v7, 0xffff0000, v53
	v_and_b32_e32 v6, -16, v6
	v_lshlrev_b32_e32 v54, 16, v52
	v_and_b32_e32 v56, 0xffff0000, v52
	v_cndmask_b32_e64 v57, 0, v7, s[8:9]
	v_add_u32_e32 v6, v65, v6
	ds_write_b128 v6, v[54:57] offset:8192
	v_add_u32_e32 v6, 0x2400, v60
	v_ashrrev_i32_e32 v6, 5, v6
	v_lshlrev_b32_e32 v6, 3, v6
	v_and_b32_e32 v6, -16, v6
	v_add3_u32 v6, v65, v6, s76
	ds_write_b128 v6, v[194:197]
	v_add_u32_e32 v6, 0x800, v60
	v_ashrrev_i32_e32 v6, 5, v6
	v_lshlrev_b32_e32 v7, 16, v51
	v_lshlrev_b32_e32 v6, 3, v6
	v_cndmask_b32_e64 v53, 0, v7, s[8:9]
	v_and_b32_e32 v7, 0xffff0000, v51
	v_and_b32_e32 v6, -16, v6
	v_lshlrev_b32_e32 v52, 16, v50
	v_and_b32_e32 v54, 0xffff0000, v50
	v_cndmask_b32_e64 v55, 0, v7, s[8:9]
	v_add_u32_e32 v6, v65, v6
	ds_write_b128 v6, v[52:55] offset:16384
	v_add_u32_e32 v6, 0x2800, v60
	v_ashrrev_i32_e32 v6, 5, v6
	v_lshlrev_b32_e32 v6, 3, v6
	v_and_b32_e32 v6, -16, v6
	v_add3_u32 v6, v65, v6, s72
	ds_write_b128 v6, v[194:197]
	v_add_u32_e32 v6, 0xc00, v60
	v_ashrrev_i32_e32 v6, 5, v6
	v_lshlrev_b32_e32 v7, 16, v49
	v_lshlrev_b32_e32 v6, 3, v6
	v_cndmask_b32_e64 v51, 0, v7, s[8:9]
	v_and_b32_e32 v7, 0xffff0000, v49
	v_and_b32_e32 v6, -16, v6
	v_lshlrev_b32_e32 v50, 16, v48
	v_and_b32_e32 v52, 0xffff0000, v48
	v_cndmask_b32_e64 v53, 0, v7, s[8:9]
	v_add_u32_e32 v6, v65, v6
	ds_write_b128 v6, v[50:53] offset:24576
	v_add_u32_e32 v6, 0x2c00, v60
	v_ashrrev_i32_e32 v6, 5, v6
	v_lshlrev_b32_e32 v6, 3, v6
	v_and_b32_e32 v6, -16, v6
	v_add3_u32 v6, v65, v6, s77
	ds_write_b128 v6, v[194:197]
	v_add_u32_e32 v6, 0x1000, v60
	v_ashrrev_i32_e32 v6, 5, v6
	v_lshlrev_b32_e32 v7, 16, v47
	v_lshlrev_b32_e32 v6, 3, v6
	v_cndmask_b32_e64 v49, 0, v7, s[8:9]
	v_and_b32_e32 v7, 0xffff0000, v47
	v_and_b32_e32 v6, -16, v6
	v_lshlrev_b32_e32 v48, 16, v46
	v_and_b32_e32 v50, 0xffff0000, v46
	v_cndmask_b32_e64 v51, 0, v7, s[8:9]
	v_add_u32_e32 v6, v65, v6
	ds_write_b128 v6, v[48:51] offset:32768
	v_add_u32_e32 v6, 0x3000, v60
	v_ashrrev_i32_e32 v6, 5, v6
	v_lshlrev_b32_e32 v6, 3, v6
	v_and_b32_e32 v6, -16, v6
	v_add3_u32 v6, v65, v6, s73
	ds_write_b128 v6, v[194:197]
	v_add_u32_e32 v6, 0x1400, v60
	v_ashrrev_i32_e32 v6, 5, v6
	v_lshlrev_b32_e32 v7, 16, v45
	v_lshlrev_b32_e32 v6, 3, v6
	v_cndmask_b32_e64 v47, 0, v7, s[8:9]
	v_and_b32_e32 v7, 0xffff0000, v45
	v_and_b32_e32 v6, -16, v6
	v_lshlrev_b32_e32 v46, 16, v44
	v_and_b32_e32 v48, 0xffff0000, v44
	v_cndmask_b32_e64 v49, 0, v7, s[8:9]
	v_add_u32_e32 v6, v65, v6
	ds_write_b128 v6, v[46:49] offset:40960
	v_add_u32_e32 v6, 0x3400, v60
	v_ashrrev_i32_e32 v6, 5, v6
	v_lshlrev_b32_e32 v6, 3, v6
	v_and_b32_e32 v6, -16, v6
	v_add3_u32 v6, v65, v6, s78
	ds_write_b128 v6, v[194:197]
	v_add_u32_e32 v6, 0x1800, v60
	v_ashrrev_i32_e32 v6, 5, v6
	v_lshlrev_b32_e32 v7, 16, v43
	v_lshlrev_b32_e32 v6, 3, v6
	v_cndmask_b32_e64 v45, 0, v7, s[8:9]
	v_and_b32_e32 v7, 0xffff0000, v43
	v_and_b32_e32 v6, -16, v6
	v_lshlrev_b32_e32 v44, 16, v42
	v_and_b32_e32 v46, 0xffff0000, v42
	v_cndmask_b32_e64 v47, 0, v7, s[8:9]
	v_add_u32_e32 v6, v65, v6
	ds_write_b128 v6, v[44:47] offset:49152
	v_add_u32_e32 v6, 0x3800, v60
	v_ashrrev_i32_e32 v6, 5, v6
	v_add_u32_e32 v42, 0x1c00, v60
	v_lshlrev_b32_e32 v6, 3, v6
	v_ashrrev_i32_e32 v42, 5, v42
	v_and_b32_e32 v6, -16, v6
	v_lshlrev_b32_e32 v42, 3, v42
	v_add3_u32 v6, v65, v6, s74
	v_lshlrev_b32_e32 v7, 16, v9
	v_and_b32_e32 v9, 0xffff0000, v9
	v_and_b32_e32 v42, -16, v42
	ds_write_b128 v6, v[194:197]
	v_lshlrev_b32_e32 v6, 16, v8
	v_cndmask_b32_e64 v7, 0, v7, s[8:9]
	v_and_b32_e32 v8, 0xffff0000, v8
	v_cndmask_b32_e64 v9, 0, v9, s[8:9]
	v_add_u32_e32 v42, v65, v42
	ds_write_b128 v42, v[6:9] offset:57344
	v_add_u32_e32 v6, 0x3c00, v60
	v_ashrrev_i32_e32 v6, 5, v6
	v_lshlrev_b32_e32 v6, 3, v6
	v_and_b32_e32 v6, -16, v6
	v_add3_u32 v6, v65, v6, s80
	ds_write_b128 v6, v[194:197]
	s_waitcnt vmcnt(32)
	s_lshl_b64 s[42:43], s[0:1], 13
	s_lshl_b64 s[0:1], s[46:47], 13
	v_cmp_ne_u64_e32 vcc, 0, v[4:5]
	s_and_saveexec_b64 s[46:47], vcc
	s_cbranch_execz .LBB0_635
; __device__ __forceinline__ unsigned cvt_pk_bf16(float lo, float hi) { unsigned r; asm volatile("v_cvt_pk_bf16_f32 %0, %1, %2" : "=v"(r) : "v"(lo), "v"(hi)); return r; }
; template <int BANK, int WAITN> __device__ __forceinline__ void bg_finish1(BgState& b) {
;     if (WAITN == 32) asm volatile("s_waitcnt vmcnt(32)" ::: "memory"); else asm volatile("s_waitcnt vmcnt(0)" ::: "memory");
;     asm volatile("" : BG_TIE16(BANK * 32) :: "memory");
;     asm volatile("" : BG_TIE16(BANK * 32 + 16) :: "memory");
;     bf16_t* dst = b.dst[BANK];
;     if (dst != nullptr) {
; #pragma unroll
;         for (int c = 0; c < 4; ++c) { u32x4 w;
;             w.x = cvt_pk_bf16(b.r[(BANK * 8 + 0) * 4 + c], b.r[(BANK * 8 + 1) * 4 + c]); w.y = cvt_pk_bf16(b.r[(BANK * 8 + 2) * 4 + c], b.r[(BANK * 8 + 3) * 4 + c]);
;             w.z = cvt_pk_bf16(b.r[(BANK * 8 + 4) * 4 + c], b.r[(BANK * 8 + 5) * 4 + c]); w.w = cvt_pk_bf16(b.r[(BANK * 8 + 6) * 4 + c], b.r[(BANK * 8 + 7) * 4 + c]);
;             bf16_t* dp = dst + (c & 1) * 512 + (c >> 1) * b.o2[BANK];
;             asm volatile("global_store_dwordx4 %0, %1, off\n\ts_nop 1" :: "v"(dp), "v"(w) : "memory"); }
;     }
; }
	v_cvt_pk_bf16_f32 v6, v34, v36
	v_cvt_pk_bf16_f32 v7, v35, v38
	v_cvt_pk_bf16_f32 v8, v37, v40
	v_cvt_pk_bf16_f32 v9, v39, v41
	s_lshl_b32 s12, s44, 1
	global_store_dwordx4 v[4:5], v[6:9], off nt
	s_nop 1
	v_cvt_pk_bf16_f32 v6, v26, v28
	v_cvt_pk_bf16_f32 v7, v27, v30
	v_cvt_pk_bf16_f32 v8, v29, v32
	v_cvt_pk_bf16_f32 v9, v31, v33
	v_lshl_add_u64 v[26:27], v[4:5], 0, s[22:23]
	global_store_dwordx4 v[26:27], v[6:9], off nt
	s_nop 1
	v_cvt_pk_bf16_f32 v6, v18, v20
	v_cvt_pk_bf16_f32 v7, v19, v22
	v_cvt_pk_bf16_f32 v8, v21, v24
	v_cvt_pk_bf16_f32 v9, v23, v25
	v_lshl_add_u64 v[4:5], v[4:5], 0, s[12:13]
	global_store_dwordx4 v[4:5], v[6:9], off nt
	s_nop 1
	v_cvt_pk_bf16_f32 v4, v10, v12
	v_cvt_pk_bf16_f32 v5, v11, v14
	v_cvt_pk_bf16_f32 v6, v13, v16
	v_cvt_pk_bf16_f32 v7, v15, v17
	v_lshl_add_u64 v[8:9], v[26:27], 0, s[12:13]
	global_store_dwordx4 v[8:9], v[4:7], off nt
	s_nop 1

; __device__ __forceinline__ KP kparams() { KP q = (KP)__builtin_amdgcn_kernarg_segment_ptr(); asm volatile("" : "+s"(q)); return q; }
; FFT_HD cf2 mk2(float x, float y) { return (cf2){x, y}; }
; FFT_HD void fft_sincos(float frac, float& s, float& c) { s = __builtin_amdgcn_sinf(frac); c = __builtin_amdgcn_cosf(frac); }
; FFT_HD cf2 cmul(cf2 a, cf2 b) { return mk2(a.x * b.x - a.y * b.y, a.x * b.y + a.y * b.x); }
; template <int BANK> __device__ __forceinline__ void bg_issue1(BgState& b, int wg, int NW, int lane) {
;     KP kp = kparams();
;     const float* src; int ldS; bf16_t* dst; int o2;
;     bg_decode(b.st, wg, NW, lane, kp, src, ldS, dst, o2);
;     b.dst[BANK] = dst; b.o2[BANK] = o2;
;     asm volatile("s_nop 6" ::: "memory");
; #pragma unroll
;     for (int i = 0; i < 8; ++i) { const float* p = src + (size_t)i * ldS;
;         asm volatile("global_load_dword %0, %4, off\n\tglobal_load_dword %1, %4, off offset:256\n\tglobal_load_dword %2, %4, off offset:512\n\tglobal_load_dword %3, %4, off offset:768"
;                      : "=&v"(b.r[(BANK * 8 + i) * 4 + 0]), "=&v"(b.r[(BANK * 8 + i) * 4 + 1]), "=&v"(b.r[(BANK * 8 + i) * 4 + 2]), "=&v"(b.r[(BANK * 8 + i) * 4 + 3]) : "v"(p) : "memory"); }
;     b.st += 1;
; }
; FFT_HD void fft_gen_tw(float frac, cf2 (&tw)[16]) {
;     float sn, cs; fft_sincos(frac, sn, cs);
;     tw[1] = mk2(cs, -sn);
;     tw[2] = cmul(tw[1], tw[1]); tw[3] = cmul(tw[2], tw[1]); tw[4] = cmul(tw[2], tw[2]); tw[5] = cmul(tw[4], tw[1]); tw[6] = cmul(tw[4], tw[2]); tw[7] = cmul(tw[4], tw[3]);
;     tw[8] = cmul(tw[4], tw[4]);
; #pragma unroll
;     for (int j = 9; j < 16; ++j) tw[j] = cmul(tw[8], tw[j - 8]);
; }
; template <bool INV, int lS, class ZP> FFT_HD void fft_r16_pass(ZP z, int tid) {
;     ...
; #pragma unroll 1
;         for (int it = 0; it < 2; ++it) {
;             const int w = tid + 512 * it;
;             const int blk = w >> lS, p = w & (S - 1), pb = PADI((blk << (lS + 4)) + p);
;             fft_gen_tw((float)p * inv, tw);
;             cf2 x[16];
; #pragma unroll
;             for (int j = 0; j < 16; ++j) x[j] = z[pb + j * STEP];
.LBB0_645:
	s_nop 6
	global_load_dword v145, v[4:5], off nt
	global_load_dword v137, v[4:5], off offset:256 nt
	global_load_dword v129, v[4:5], off offset:512 nt
	global_load_dword v121, v[4:5], off offset:768 nt
	s_lshl_b32 s12, s46, 2
	v_lshl_add_u64 v[4:5], v[4:5], 0, s[12:13]
	global_load_dword v147, v[4:5], off nt
	global_load_dword v139, v[4:5], off offset:256 nt
	global_load_dword v131, v[4:5], off offset:512 nt
	global_load_dword v123, v[4:5], off offset:768 nt
	v_lshl_add_u64 v[4:5], v[4:5], 0, s[12:13]
	global_load_dword v146, v[4:5], off nt
	global_load_dword v138, v[4:5], off offset:256 nt
	global_load_dword v130, v[4:5], off offset:512 nt
	global_load_dword v122, v[4:5], off offset:768 nt
	v_lshl_add_u64 v[4:5], v[4:5], 0, s[12:13]
	global_load_dword v149, v[4:5], off nt
	global_load_dword v141, v[4:5], off offset:256 nt
	global_load_dword v133, v[4:5], off offset:512 nt
	global_load_dword v125, v[4:5], off offset:768 nt
	v_lshl_add_u64 v[4:5], v[4:5], 0, s[12:13]
	global_load_dword v148, v[4:5], off nt
	global_load_dword v140, v[4:5], off offset:256 nt
	global_load_dword v132, v[4:5], off offset:512 nt
	global_load_dword v124, v[4:5], off offset:768 nt
	v_lshl_add_u64 v[4:5], v[4:5], 0, s[12:13]
	global_load_dword v151, v[4:5], off nt
	global_load_dword v143, v[4:5], off offset:256 nt
	global_load_dword v135, v[4:5], off offset:512 nt
	global_load_dword v127, v[4:5], off offset:768 nt
	v_lshl_add_u64 v[4:5], v[4:5], 0, s[12:13]
	global_load_dword v150, v[4:5], off nt
	global_load_dword v142, v[4:5], off offset:256 nt
	global_load_dword v134, v[4:5], off offset:512 nt
	global_load_dword v126, v[4:5], off offset:768 nt
	v_lshl_add_u64 v[4:5], v[4:5], 0, s[12:13]
	global_load_dword v152, v[4:5], off nt
	global_load_dword v144, v[4:5], off offset:256 nt
	global_load_dword v136, v[4:5], off offset:512 nt
	global_load_dword v128, v[4:5], off offset:768 nt
	s_mov_b32 s12, 0
	s_mov_b64 s[46:47], -1
.LBB0_646:
	v_add_u32_e32 v4, s12, v120
	v_and_b32_e32 v5, 0x3ff, v4
	v_lshlrev_b32_e32 v4, 4, v4
	v_and_or_b32 v48, v4, s81, v5
	v_cvt_f32_u32_e32 v4, v5
	v_ashrrev_i32_e32 v49, 5, v48
	s_mov_b32 s50, s27
	s_mov_b32 s51, s26
	v_mul_f32_e32 v4, 0x38800000, v4
	v_sin_f32_e32 v29, v4
	v_cos_f32_e32 v28, v4
	s_mov_b32 s54, s26
	s_mov_b32 s55, s24
	v_mov_b32_e32 v14, v29
	v_pk_mul_f32 v[4:5], v[28:29], v[28:29]
	v_mul_f32_e64 v6, v28, -v29
	v_mov_b32_e32 v7, v4
	v_mov_b32_e32 v4, v6
	v_pk_add_f32 v[74:75], v[6:7], v[4:5]
	v_pk_add_f32 v[72:73], v[6:7], v[4:5] neg_lo:[0,1] neg_hi:[0,1]
	v_mov_b32_e32 v12, v74
	v_mov_b32_e32 v13, v73
	v_pk_mul_f32 v[6:7], v[12:13], v[12:13]
	v_pk_mul_f32 v[16:17], v[72:73], v[12:13] op_sel:[1,0] op_sel_hi:[0,1]
	v_pk_mov_b32 v[18:19], v[6:7], v[16:17] op_sel:[1,0]
	v_mov_b32_e32 v7, v16
	v_mov_b32_e32 v15, v28
	v_pk_add_f32 v[38:39], v[18:19], v[6:7] neg_lo:[0,1] neg_hi:[0,1]
	v_pk_add_f32 v[40:41], v[18:19], v[6:7]
	v_pk_mov_b32 v[4:5], v[72:73], v[74:75] op_sel:[1,0]
	v_pk_mul_f32 v[8:9], v[14:15], v[12:13]
	v_pk_mul_f32 v[10:11], v[28:29], v[12:13]
	v_mov_b32_e32 v6, v38
	v_mov_b32_e32 v7, v41
	v_pk_mul_f32 v[30:31], v[4:5], v[6:7]
	v_mov_b32_e32 v4, v10
	v_mov_b32_e32 v5, v9
	v_pk_mov_b32 v[8:9], v[10:11], v[8:9] op_sel:[1,0]
	v_pk_mul_f32 v[32:33], v[12:13], v[6:7]
	v_pk_add_f32 v[44:45], v[4:5], v[8:9] neg_lo:[0,1] neg_hi:[0,1]
	v_pk_add_f32 v[42:43], v[4:5], v[8:9]
	v_pk_mul_f32 v[8:9], v[6:7], v[40:41] op_sel:[0,1] op_sel_hi:[1,0]
	v_pk_mov_b32 v[4:5], v[42:43], v[44:45] op_sel:[1,0]
	v_mov_b32_e32 v36, v44
	v_pk_mul_f32 v[22:23], v[6:7], v[4:5]
	v_pk_mul_f32 v[4:5], v[6:7], v[6:7]
	v_mov_b32_e32 v37, v43
	v_mov_b32_e32 v9, v4
	v_mov_b32_e32 v4, v8
	v_pk_add_f32 v[10:11], v[8:9], v[4:5]
	v_pk_add_f32 v[8:9], v[8:9], v[4:5] neg_lo:[0,1] neg_hi:[0,1]
	v_mov_b32_e32 v4, v10
	v_mov_b32_e32 v5, v9
	v_pk_mov_b32 v[46:47], v[8:9], v[10:11] op_sel:[1,0]
	v_pk_mul_f32 v[26:27], v[6:7], v[36:37]
	v_pk_mul_f32 v[20:21], v[14:15], v[4:5]
	v_pk_mul_f32 v[16:17], v[12:13], v[4:5]
	v_pk_mul_f32 v[18:19], v[12:13], v[46:47]
	v_pk_mul_f32 v[12:13], v[36:37], v[4:5]
	v_pk_mul_f32 v[14:15], v[36:37], v[46:47]
	v_lshlrev_b32_e32 v36, 3, v49
	v_and_b32_e32 v36, 0xfffff0f0, v36
	v_lshlrev_b32_e32 v37, 3, v48
	v_add3_u32 v65, 0, v36, v37
	v_add_u32_e32 v67, 0x10800, v65
	v_add_u32_e32 v183, 0x12900, v65
	v_add_u32_e32 v186, 0x18c00, v65
	v_add_u32_e32 v187, 0x1ad00, v65
	ds_read_b64 v[52:53], v65
	ds_read_b64 v[36:37], v65 offset:8448
	ds_read_b64 v[46:47], v65 offset:16896
	ds_read_b64 v[50:51], v65 offset:25344
	ds_read_b64 v[78:79], v65 offset:33792
	ds_read_b64 v[56:57], v65 offset:42240
	ds_read_b64 v[68:69], v65 offset:50688
	ds_read_b64 v[70:71], v65 offset:59136
	ds_read_b64 v[76:77], v67
	ds_read_b64 v[88:89], v183
	ds_read_b64 v[108:109], v186
	ds_read_b64 v[90:91], v187
	v_add_u32_e32 v184, 0x14a00, v65
	v_add_u32_e32 v188, 0x1ce00, v65
	ds_read_b64 v[92:93], v184
	ds_read_b64 v[104:105], v188
	v_add_u32_e32 v185, 0x16b00, v65
	v_add_u32_e32 v189, 0x1ef00, v65
	ds_read_b64 v[94:95], v185
	ds_read_b64 v[110:111], v189
	s_waitcnt lgkmcnt(10)
	v_pk_mov_b32 v[48:49], v[36:37], v[56:57] op_sel:[1,0]
	s_waitcnt lgkmcnt(4)
	v_pk_mov_b32 v[54:55], v[88:89], v[90:91] op_sel:[1,0]
	v_pk_add_f32 v[100:101], v[78:79], v[108:109]
	v_pk_add_f32 v[80:81], v[48:49], v[54:55] neg_lo:[0,1] neg_hi:[0,1]
	v_mov_b32_e32 v48, v36
	v_mov_b32_e32 v49, v57
	v_mov_b32_e32 v54, v88
	v_mov_b32_e32 v55, v91
	v_pk_add_f32 v[84:85], v[48:49], v[54:55] neg_lo:[0,1] neg_hi:[0,1]
	v_pk_mov_b32 v[48:49], v[46:47], v[68:69] op_sel:[1,0]
	s_waitcnt lgkmcnt(2)
; FFT_HD cf2 mk2(float x, float y) { return (cf2){x, y}; }
; FFT_HD cf2 cmul(cf2 a, cf2 b) { return mk2(a.x * b.x - a.y * b.y, a.x * b.y + a.y * b.x); }
; FFT_HD cf2 cadd(cf2 a, cf2 b) { return mk2(a.x + b.x, a.y + b.y); }
; FFT_HD cf2 csub(cf2 a, cf2 b) { return mk2(a.x - b.x, a.y - b.y); }
; template <bool INV> FFT_HD void dft4(cf2& a, cf2& b, cf2& c, cf2& d) {
;     const cf2 s0 = cadd(a, c), s1 = csub(a, c), s2 = cadd(b, d), s3 = csub(b, d);
;     a = cadd(s0, s2); c = csub(s0, s2);
;     const cf2 r = INV ? mk2(-s3.y, s3.x) : mk2(s3.y, -s3.x);
;     b = cadd(s1, r); d = csub(s1, r);
; }
; template <bool INV> FFT_HD void dft16(cf2 (&x)[16]) {
;     const float C1 = 0.9238795325112867f, S1 = 0.3826834323650898f, H = 0.7071067811865476f;
; #pragma unroll
;     for (int b = 0; b < 4; ++b) dft4<INV>(x[b], x[4 + b], x[8 + b], x[12 + b]);
;     const float s = INV ? -1.f : 1.f;
;     x[4 + 1] = cmul(x[4 + 1], mk2(C1, -s * S1)); x[8 + 1] = cmul(x[8 + 1], mk2(H, -s * H));   x[12 + 1] = cmul(x[12 + 1], mk2(S1, -s * C1));
;     x[4 + 2] = cmul(x[4 + 2], mk2(H, -s * H));   x[8 + 2] = cmul(x[8 + 2], mk2(0.f, -s));     x[12 + 2] = cmul(x[12 + 2], mk2(-H, -s * H));
;     x[4 + 3] = cmul(x[4 + 3], mk2(S1, -s * C1)); x[8 + 3] = cmul(x[8 + 3], mk2(-H, -s * H));  x[12 + 3] = cmul(x[12 + 3], mk2(-C1, s * S1));
; #pragma unroll
;     for (int c = 0; c < 4; ++c) dft4<INV>(x[4 * c], x[4 * c + 1], x[4 * c + 2], x[4 * c + 3]);
; #pragma unroll
;     for (int c = 0; c < 4; ++c)
; #pragma unroll
;         for (int d = c + 1; d < 4; ++d) { const cf2 t = x[4 * c + d]; x[4 * c + d] = x[4 * d + c]; x[4 * d + c] = t; }
; }
	v_pk_mov_b32 v[54:55], v[92:93], v[104:105] op_sel:[1,0]
	v_pk_add_f32 v[112:113], v[84:85], v[84:85] op_sel:[0,1] op_sel_hi:[0,1]
	v_pk_add_f32 v[82:83], v[48:49], v[54:55] neg_lo:[0,1] neg_hi:[0,1]
	v_mov_b32_e32 v48, v46
	v_mov_b32_e32 v49, v69
	v_mov_b32_e32 v54, v92
	v_mov_b32_e32 v55, v105
	v_pk_add_f32 v[86:87], v[48:49], v[54:55] neg_lo:[0,1] neg_hi:[0,1]
	v_pk_mov_b32 v[48:49], v[50:51], v[70:71] op_sel:[1,0]
	s_waitcnt lgkmcnt(0)
	v_pk_mov_b32 v[54:55], v[94:95], v[110:111] op_sel:[1,0]
	v_add_f32_e32 v98, v86, v87
	v_pk_add_f32 v[96:97], v[48:49], v[54:55] neg_lo:[0,1] neg_hi:[0,1]
	v_mov_b32_e32 v48, v50
	v_mov_b32_e32 v49, v71
	v_mov_b32_e32 v54, v94
	v_mov_b32_e32 v55, v111
	v_pk_add_f32 v[106:107], v[48:49], v[54:55] neg_lo:[0,1] neg_hi:[0,1]
	v_mov_b32_e32 v49, v96
	v_mov_b32_e32 v48, v106
	v_mov_b32_e32 v54, v107
	v_mov_b32_e32 v55, v97
	v_mul_f32_e32 v192, 0x3f3504f3, v98
	v_pk_add_f32 v[98:99], v[48:49], v[54:55] neg_lo:[0,1] neg_hi:[0,1]
	v_pk_add_f32 v[54:55], v[48:49], v[54:55]
	v_pk_add_f32 v[106:107], v[106:107], v[106:107] op_sel:[0,1] op_sel_hi:[0,1]
	v_mov_b32_e32 v99, v55
	v_mul_f32_e32 v48, 0x3ec3ef15, v55
	v_sub_f32_e32 v60, v82, v83
	v_pk_fma_f32 v[48:49], v[98:99], s[30:31], v[48:49] op_sel_hi:[1,1,0] neg_lo:[0,0,1] neg_hi:[0,0,1]
	v_mul_f32_e32 v190, 0x3ec3ef15, v98
	v_pk_add_f32 v[98:99], v[52:53], v[76:77]
	v_pk_add_f32 v[76:77], v[52:53], v[76:77] neg_lo:[0,1] neg_hi:[0,1]
	v_pk_add_f32 v[108:109], v[78:79], v[108:109] neg_lo:[0,1] neg_hi:[0,1]
	v_pk_mul_f32 v[112:113], v[112:113], s[26:27]
	v_pk_add_f32 v[114:115], v[80:81], v[80:81] op_sel:[0,1] op_sel_hi:[0,1] neg_lo:[0,1] neg_hi:[0,1]
	v_pk_mul_f32 v[106:107], v[106:107], s[50:51]
	v_pk_add_f32 v[96:97], v[96:97], v[96:97] op_sel:[0,1] op_sel_hi:[0,1] neg_lo:[0,1] neg_hi:[0,1]
	v_pk_mov_b32 v[78:79], v[108:109], v[108:109] op_sel:[1,0]
	v_pk_add_f32 v[52:53], v[76:77], v[108:109] op_sel:[0,1] op_sel_hi:[1,0]
	v_pk_add_f32 v[108:109], v[76:77], v[108:109] op_sel:[0,1] op_sel_hi:[1,0] neg_lo:[0,1] neg_hi:[0,1]
	v_pk_fma_f32 v[198:199], v[114:115], s[50:51], v[112:113]
	v_pk_fma_f32 v[114:115], v[114:115], s[50:51], v[112:113] neg_lo:[0,0,1] neg_hi:[0,0,1]
	v_fmamk_f32 v200, v60, 0x3f3504f3, v192
	v_fma_f32 v192, v60, s25, -v192
	v_pk_fma_f32 v[202:203], v[96:97], s[26:27], v[106:107]
	v_pk_fma_f32 v[96:97], v[96:97], s[26:27], v[106:107] neg_lo:[0,0,1] neg_hi:[0,0,1]
	v_pk_add_f32 v[102:103], v[46:47], v[92:93]
	v_pk_add_f32 v[92:93], v[50:51], v[94:95]
	v_pk_add_f32 v[94:95], v[70:71], v[110:111]
	v_mov_b32_e32 v110, v52
	v_mov_b32_e32 v111, v109
	v_mov_b32_e32 v114, v198
	v_mov_b32_e32 v193, v192
	v_mov_b32_e32 v201, v192
	v_mov_b32_e32 v96, v202
	v_pk_add_f32 v[110:111], v[110:111], v[200:201]
	v_pk_add_f32 v[112:113], v[114:115], v[96:97]
	v_pk_mov_b32 v[106:107], v[108:109], v[198:199] op_sel:[1,0]
	v_pk_mov_b32 v[108:109], v[192:193], v[202:203] op_sel:[1,0]
	v_mov_b32_e32 v114, v52
	v_mov_b32_e32 v201, v97
	v_pk_add_f32 v[106:107], v[106:107], v[108:109] neg_lo:[0,1] neg_hi:[0,1]
	v_pk_add_f32 v[108:109], v[114:115], v[200:201] neg_lo:[0,1] neg_hi:[0,1]
	v_pk_add_f32 v[114:115], v[110:111], v[112:113]
	v_mov_b32_e32 v60, v29
	v_pk_add_f32 v[88:89], v[36:37], v[88:89]
	v_pk_add_f32 v[90:91], v[56:57], v[90:91]
	v_pk_add_f32 v[104:105], v[68:69], v[104:105]
	v_pk_mul_f32 v[192:193], v[60:61], v[114:115] op_sel_hi:[0,1]
	v_mul_f32_e32 v191, 0x3f6c835e, v55
	v_pk_add_f32 v[54:55], v[98:99], v[100:101]
	v_pk_add_f32 v[68:69], v[102:103], v[104:105]
	v_pk_fma_f32 v[96:97], v[28:29], v[114:115], v[192:193] op_sel:[0,0,1] op_sel_hi:[1,1,0]
	v_pk_fma_f32 v[114:115], v[28:29], v[114:115], v[192:193] op_sel:[0,0,1] op_sel_hi:[0,1,0] neg_lo:[0,0,1] neg_hi:[0,0,1]
	v_pk_add_f32 v[98:99], v[98:99], v[100:101] neg_lo:[0,1] neg_hi:[0,1]
	v_pk_add_f32 v[100:101], v[102:103], v[104:105] neg_lo:[0,1] neg_hi:[0,1]
	v_mov_b32_e32 v102, v92
	v_mov_b32_e32 v103, v89
	v_mov_b32_e32 v104, v94
	v_mov_b32_e32 v105, v91
	v_mov_b32_e32 v97, v115
	v_pk_add_f32 v[102:103], v[102:103], v[104:105] neg_lo:[0,1] neg_hi:[0,1]
	v_mov_b32_e32 v104, v88
	v_mov_b32_e32 v105, v92
	v_mov_b32_e32 v114, v90
	v_mov_b32_e32 v115, v94
	v_pk_add_f32 v[56:57], v[88:89], v[90:91]
	v_pk_add_f32 v[104:105], v[104:105], v[114:115] neg_lo:[0,1] neg_hi:[0,1]
	v_mov_b32_e32 v114, v89
	v_mov_b32_e32 v115, v93
	v_mov_b32_e32 v192, v91
	v_mov_b32_e32 v193, v95
	v_pk_mov_b32 v[88:89], v[92:93], v[88:89] op_sel:[1,0]
	v_pk_mov_b32 v[90:91], v[94:95], v[90:91] op_sel:[1,0]
	v_pk_add_f32 v[70:71], v[92:93], v[94:95]
	v_pk_add_f32 v[114:115], v[114:115], v[192:193] neg_lo:[0,1] neg_hi:[0,1]
	v_pk_add_f32 v[90:91], v[88:89], v[90:91] neg_lo:[0,1] neg_hi:[0,1]
	v_pk_fma_f32 v[88:89], v[100:101], 0, v[100:101] op_sel:[0,0,1] op_sel_hi:[1,0,0]
	v_pk_fma_f32 v[92:93], v[100:101], 0, v[100:101] op_sel:[0,0,1] op_sel_hi:[1,0,0] neg_lo:[0,0,1] neg_hi:[0,0,1]
	s_mov_b32 s50, s25
	s_mov_b32 s51, s24
	v_mov_b32_e32 v89, v93
	v_pk_mul_f32 v[92:93], v[114:115], s[50:51]
	v_pk_mul_f32 v[90:91], v[90:91], s[24:25]
	v_pk_fma_f32 v[92:93], v[104:105], s[50:51], v[92:93]
	v_pk_fma_f32 v[90:91], v[102:103], s[24:25], v[90:91] neg_lo:[0,0,1] neg_hi:[0,0,1]
	v_pk_add_f32 v[94:95], v[98:99], v[88:89]
	v_pk_add_f32 v[100:101], v[92:93], v[90:91]
	s_mov_b32 s28, s25
	v_pk_add_f32 v[102:103], v[94:95], v[100:101]
	s_mov_b32 s50, s27
	v_pk_mul_f32 v[104:105], v[74:75], v[102:103] op_sel:[0,1] op_sel_hi:[0,0]
	v_pk_fma_f32 v[74:75], v[72:73], v[102:103], v[104:105] op_sel:[1,0,0] neg_lo:[0,0,1] neg_hi:[0,0,1]
	v_pk_fma_f32 v[72:73], v[72:73], v[102:103], v[104:105] op_sel:[1,0,0]
	s_mov_b32 s52, s24
	v_mov_b32_e32 v75, v73
; FFT_HD cf2 mk2(float x, float y) { return (cf2){x, y}; }
; FFT_HD cf2 cmul(cf2 a, cf2 b) { return mk2(a.x * b.x - a.y * b.y, a.x * b.y + a.y * b.x); }
; template <bool INV> FFT_HD void dft16(cf2 (&x)[16]) {
;     const float C1 = 0.9238795325112867f, S1 = 0.3826834323650898f, H = 0.7071067811865476f;
; #pragma unroll
;     for (int b = 0; b < 4; ++b) dft4<INV>(x[b], x[4 + b], x[8 + b], x[12 + b]);
;     const float s = INV ? -1.f : 1.f;
;     x[4 + 1] = cmul(x[4 + 1], mk2(C1, -s * S1)); x[8 + 1] = cmul(x[8 + 1], mk2(H, -s * H));   x[12 + 1] = cmul(x[12 + 1], mk2(S1, -s * C1));
;     x[4 + 2] = cmul(x[4 + 2], mk2(H, -s * H));   x[8 + 2] = cmul(x[8 + 2], mk2(0.f, -s));     x[12 + 2] = cmul(x[12 + 2], mk2(-H, -s * H));
;     x[4 + 3] = cmul(x[4 + 3], mk2(S1, -s * C1)); x[8 + 3] = cmul(x[8 + 3], mk2(-H, -s * H));  x[12 + 3] = cmul(x[12 + 3], mk2(-C1, s * S1));
; #pragma unroll
;     for (int c = 0; c < 4; ++c) dft4<INV>(x[4 * c], x[4 * c + 1], x[4 * c + 2], x[4 * c + 3]);
; #pragma unroll
;     for (int c = 0; c < 4; ++c)
; #pragma unroll
;         for (int d = c + 1; d < 4; ++d) { const cf2 t = x[4 * c + d]; x[4 * c + d] = x[4 * d + c]; x[4 * d + c] = t; }
; }
; template <bool INV, int lS, class ZP> FFT_HD void fft_r16_pass(ZP z, int tid) {
;     ...
;             if (!INV) {
; #pragma unroll
;                 for (int j = 1; j < 16; ++j) x[j] = cmul(x[j], tw[j]);
;             }
	v_mov_b32_e32 v72, v84
	v_mov_b32_e32 v73, v86
	v_mov_b32_e32 v86, v85
	v_mov_b32_e32 v84, v80
	v_mov_b32_e32 v85, v82
	v_mov_b32_e32 v82, v81
	v_pk_add_f32 v[72:73], v[72:73], v[86:87] neg_lo:[0,1] neg_hi:[0,1]
	v_pk_add_f32 v[80:81], v[84:85], v[82:83]
	s_mov_b32 s53, s27
	v_pk_mov_b32 v[82:83], v[72:73], v[80:81] op_sel:[1,0]
	v_pk_mul_f32 v[84:85], v[80:81], s[54:55]
	v_pk_mov_b32 v[80:81], v[80:81], v[72:73] op_sel:[1,0]
	v_mov_b32_e32 v77, v190
	v_pk_mul_f32 v[80:81], v[80:81], s[28:29]
	v_mov_b32_e32 v79, v191
	v_pk_fma_f32 v[80:81], v[82:83], s[52:53], v[80:81]
	v_pk_fma_f32 v[72:73], v[72:73], s[50:51], v[84:85]
	v_pk_add_f32 v[76:77], v[76:77], v[78:79] neg_lo:[0,1] neg_hi:[0,1]
	v_mov_b32_e32 v52, v48
	v_pk_add_f32 v[78:79], v[80:81], v[76:77]
	v_pk_add_f32 v[82:83], v[72:73], v[52:53]
	v_pk_add_f32 v[46:47], v[54:55], v[68:69]
	v_pk_add_f32 v[84:85], v[82:83], v[78:79]
	v_pk_add_f32 v[50:51], v[56:57], v[70:71]
	v_pk_mul_f32 v[44:45], v[44:45], v[84:85] op_sel:[0,1] op_sel_hi:[0,0]
	v_pk_fma_f32 v[86:87], v[42:43], v[84:85], v[44:45] op_sel:[1,0,0] neg_lo:[0,0,1] neg_hi:[0,0,1]
	v_pk_fma_f32 v[42:43], v[42:43], v[84:85], v[44:45] op_sel:[1,0,0]
	v_pk_add_f32 v[44:45], v[56:57], v[70:71] neg_lo:[0,1] neg_hi:[0,1]
	v_mov_b32_e32 v87, v43
	v_pk_add_f32 v[42:43], v[54:55], v[68:69] neg_lo:[0,1] neg_hi:[0,1]
	v_pk_mov_b32 v[56:57], v[40:41], v[38:39] op_sel:[1,0]
	v_pk_add_f32 v[54:55], v[42:43], v[44:45] op_sel:[0,1] op_sel_hi:[1,0]
	v_pk_add_f32 v[42:43], v[42:43], v[44:45] op_sel:[0,1] op_sel_hi:[1,0] neg_lo:[0,1] neg_hi:[0,1]
	v_mov_b32_e32 v44, v54
	v_pk_mov_b32 v[68:69], v[42:43], v[54:55] op_sel:[1,0]
	v_mov_b32_e32 v45, v43
	v_pk_mul_f32 v[40:41], v[40:41], v[68:69] op_sel:[1,0]
	v_pk_mul_f32 v[24:25], v[28:29], v[4:5]
	v_pk_fma_f32 v[68:69], v[38:39], v[54:55], v[40:41] neg_lo:[0,0,1] neg_hi:[0,0,1]
	v_pk_fma_f32 v[38:39], v[38:39], v[44:45], v[40:41] op_sel_hi:[0,1,1]
	v_mov_b32_e32 v69, v39
	v_pk_mul_f32 v[38:39], v[60:61], v[56:57] op_sel_hi:[0,1]
	v_pk_fma_f32 v[40:41], v[28:29], v[6:7], v[38:39] op_sel_hi:[0,1,1]
	v_pk_fma_f32 v[28:29], v[28:29], v[6:7], v[38:39] op_sel_hi:[0,1,1] neg_lo:[0,0,1] neg_hi:[0,0,1]
	v_mov_b32_e32 v39, v29
	v_pk_mov_b32 v[28:29], v[28:29], v[40:41] op_sel:[1,0]
	v_pk_add_f32 v[56:57], v[106:107], v[106:107] op_sel:[0,1] op_sel_hi:[0,1] neg_lo:[0,1] neg_hi:[0,1]
	v_mov_b32_e32 v38, v40
	v_pk_add_f32 v[44:45], v[108:109], v[108:109] op_sel:[0,1] op_sel_hi:[0,1]
	v_pk_mul_f32 v[28:29], v[28:29], v[56:57]
	v_pk_mov_b32 v[56:57], v[92:93], v[90:91] op_sel:[1,0]
	v_pk_fma_f32 v[40:41], v[40:41], v[44:45], v[28:29] neg_lo:[0,0,1] neg_hi:[0,0,1]
	v_pk_fma_f32 v[28:29], v[38:39], v[44:45], v[28:29]
	v_pk_mov_b32 v[44:45], v[90:91], v[92:93] op_sel:[1,0]
	v_mov_b32_e32 v41, v29
	v_pk_add_f32 v[28:29], v[98:99], v[88:89] neg_lo:[0,1] neg_hi:[0,1]
	v_pk_add_f32 v[44:45], v[44:45], v[56:57] neg_lo:[0,1] neg_hi:[0,1]
	v_pk_add_f32 v[32:33], v[32:33], v[32:33] op_sel:[0,1] op_sel_hi:[0,1]
	v_pk_add_f32 v[56:57], v[28:29], v[44:45]
	v_pk_add_f32 v[28:29], v[28:29], v[44:45] neg_lo:[0,1] neg_hi:[0,1]
	v_mov_b32_e32 v44, v56
	v_pk_mov_b32 v[70:71], v[28:29], v[56:57] op_sel:[1,0]
	v_mov_b32_e32 v45, v29
	v_pk_mul_f32 v[70:71], v[32:33], v[70:71]
	v_pk_add_f32 v[30:31], v[30:31], v[30:31] op_sel:[0,1] op_sel_hi:[0,1] neg_lo:[0,1] neg_hi:[0,1]
	v_pk_fma_f32 v[84:85], v[30:31], v[56:57], v[70:71] neg_lo:[0,0,1] neg_hi:[0,0,1]
	v_pk_fma_f32 v[44:45], v[30:31], v[44:45], v[70:71]
	v_pk_mov_b32 v[48:49], v[76:77], v[48:49] op_sel:[1,0]
	v_mov_b32_e32 v85, v45
	v_pk_mov_b32 v[44:45], v[80:81], v[72:73] op_sel:[1,0]
	v_mov_b32_e32 v77, v53
	v_mov_b32_e32 v81, v73
	v_pk_add_f32 v[44:45], v[44:45], v[48:49] neg_lo:[0,1] neg_hi:[0,1]
	v_pk_add_f32 v[48:49], v[76:77], v[80:81] neg_lo:[0,1] neg_hi:[0,1]
	v_pk_add_f32 v[26:27], v[26:27], v[26:27] op_sel:[0,1] op_sel_hi:[0,1]
	v_pk_add_f32 v[52:53], v[48:49], v[44:45]
	v_pk_add_f32 v[44:45], v[48:49], v[44:45] neg_lo:[0,1] neg_hi:[0,1]
	v_mov_b32_e32 v48, v52
	v_pk_mov_b32 v[70:71], v[44:45], v[52:53] op_sel:[1,0]
	v_mov_b32_e32 v49, v45
	v_pk_mul_f32 v[70:71], v[26:27], v[70:71]
	v_pk_add_f32 v[22:23], v[22:23], v[22:23] op_sel:[0,1] op_sel_hi:[0,1] neg_lo:[0,1] neg_hi:[0,1]
	v_pk_add_f32 v[36:37], v[46:47], v[50:51]
	v_pk_fma_f32 v[72:73], v[22:23], v[52:53], v[70:71] neg_lo:[0,0,1] neg_hi:[0,0,1]
	v_pk_fma_f32 v[48:49], v[22:23], v[48:49], v[70:71]
	v_pk_add_f32 v[46:47], v[46:47], v[50:51] neg_lo:[0,1] neg_hi:[0,1]
	v_mov_b32_e32 v73, v49
	v_pk_mul_f32 v[48:49], v[10:11], v[46:47] op_sel_hi:[0,1]
	v_pk_fma_f32 v[50:51], v[8:9], v[46:47], v[48:49] op_sel:[1,0,1] op_sel_hi:[1,1,0] neg_lo:[0,0,1] neg_hi:[0,0,1]
	v_pk_fma_f32 v[46:47], v[8:9], v[46:47], v[48:49] op_sel:[1,0,1] op_sel_hi:[1,1,0]
	v_pk_add_f32 v[24:25], v[24:25], v[24:25] op_sel:[0,1] op_sel_hi:[0,1] neg_lo:[0,1] neg_hi:[0,1]
	v_mov_b32_e32 v51, v47
	v_pk_add_f32 v[46:47], v[110:111], v[112:113] neg_lo:[0,1] neg_hi:[0,1]
	v_pk_add_f32 v[20:21], v[20:21], v[20:21] op_sel:[1,0] op_sel_hi:[1,0]
	v_pk_mul_f32 v[24:25], v[24:25], v[46:47] op_sel:[0,1] op_sel_hi:[1,0]
	v_pk_add_f32 v[18:19], v[18:19], v[18:19] op_sel:[0,1] op_sel_hi:[0,1]
	v_pk_fma_f32 v[48:49], v[20:21], v[46:47], v[24:25] neg_lo:[0,0,1] neg_hi:[0,0,1]
; __device__ __forceinline__ unsigned cvt_pk_bf16(float lo, float hi) { unsigned r; asm volatile("v_cvt_pk_bf16_f32 %0, %1, %2" : "=v"(r) : "v"(lo), "v"(hi)); return r; }
; FFT_HD cf2 cmul(cf2 a, cf2 b) { return mk2(a.x * b.x - a.y * b.y, a.x * b.y + a.y * b.x); }
; template <int BANK, int WAITN> __device__ __forceinline__ void bg_finish1(BgState& b) {
;     if (WAITN == 32) asm volatile("s_waitcnt vmcnt(32)" ::: "memory"); else asm volatile("s_waitcnt vmcnt(0)" ::: "memory");
;     asm volatile("" : BG_TIE16(BANK * 32) :: "memory");
;     asm volatile("" : BG_TIE16(BANK * 32 + 16) :: "memory");
;     bf16_t* dst = b.dst[BANK];
;     if (dst != nullptr) {
; #pragma unroll
;         for (int c = 0; c < 4; ++c) { u32x4 w;
;             w.x = cvt_pk_bf16(b.r[(BANK * 8 + 0) * 4 + c], b.r[(BANK * 8 + 1) * 4 + c]); w.y = cvt_pk_bf16(b.r[(BANK * 8 + 2) * 4 + c], b.r[(BANK * 8 + 3) * 4 + c]);
;             w.z = cvt_pk_bf16(b.r[(BANK * 8 + 4) * 4 + c], b.r[(BANK * 8 + 5) * 4 + c]); w.w = cvt_pk_bf16(b.r[(BANK * 8 + 6) * 4 + c], b.r[(BANK * 8 + 7) * 4 + c]);
;             bf16_t* dp = dst + (c & 1) * 512 + (c >> 1) * b.o2[BANK];
;             asm volatile("global_store_dwordx4 %0, %1, off\n\ts_nop 1" :: "v"(dp), "v"(w) : "memory"); }
;     }
; }
; template <bool INV, int lS, class ZP> FFT_HD void fft_r16_pass(ZP z, int tid) {
;     ...
;             if (!INV) {
; #pragma unroll
;                 for (int j = 1; j < 16; ++j) x[j] = cmul(x[j], tw[j]);
;             }
; #pragma unroll
;             for (int j = 0; j < 16; ++j) z[pb + j * STEP] = x[j];
;         }
	v_pk_fma_f32 v[20:21], v[20:21], v[46:47], v[24:25]
	v_pk_add_f32 v[16:17], v[16:17], v[16:17] op_sel:[1,0] op_sel_hi:[1,0] neg_lo:[0,1] neg_hi:[0,1]
	v_mov_b32_e32 v49, v21
	v_pk_add_f32 v[20:21], v[94:95], v[100:101] neg_lo:[0,1] neg_hi:[0,1]
	v_pk_add_f32 v[14:15], v[14:15], v[14:15] op_sel:[0,1] op_sel_hi:[0,1]
	v_pk_mul_f32 v[18:19], v[18:19], v[20:21] op_sel:[0,1] op_sel_hi:[1,0]
	v_pk_add_f32 v[12:13], v[12:13], v[12:13] op_sel:[1,0] op_sel_hi:[1,0] neg_lo:[0,1] neg_hi:[0,1]
	v_pk_fma_f32 v[24:25], v[16:17], v[20:21], v[18:19] neg_lo:[0,0,1] neg_hi:[0,0,1]
	v_pk_fma_f32 v[16:17], v[16:17], v[20:21], v[18:19]
	s_movk_i32 s12, 0x200
	v_mov_b32_e32 v25, v17
	v_mov_b32_e32 v16, v78
	v_mov_b32_e32 v17, v83
	v_mov_b32_e32 v83, v79
	v_pk_add_f32 v[16:17], v[16:17], v[82:83] neg_lo:[0,1] neg_hi:[0,1]
	s_and_b64 vcc, exec, s[46:47]
	v_pk_mul_f32 v[14:15], v[14:15], v[16:17] op_sel:[0,1] op_sel_hi:[1,0]
	s_mov_b64 s[46:47], 0
	v_pk_fma_f32 v[18:19], v[12:13], v[16:17], v[14:15] neg_lo:[0,0,1] neg_hi:[0,0,1]
	v_pk_fma_f32 v[12:13], v[12:13], v[16:17], v[14:15]
	v_pk_add_f32 v[16:17], v[106:107], v[106:107] op_sel:[0,1] op_sel_hi:[0,1]
	v_mov_b32_e32 v19, v13
	v_pk_mul_f32 v[12:13], v[6:7], v[10:11] op_sel_hi:[1,0]
	s_nop 0
	v_pk_fma_f32 v[14:15], v[6:7], v[8:9], v[12:13] op_sel:[0,1,1] op_sel_hi:[1,1,0] neg_lo:[0,0,1] neg_hi:[0,0,1]
	v_pk_fma_f32 v[6:7], v[6:7], v[8:9], v[12:13] op_sel:[0,1,1] op_sel_hi:[1,1,0]
	v_mov_b32_e32 v12, v14
	v_mov_b32_e32 v13, v7
	v_pk_mov_b32 v[6:7], v[6:7], v[14:15] op_sel:[1,0]
	s_nop 0
	v_pk_mul_f32 v[6:7], v[6:7], v[54:55] op_sel:[0,1]
	s_nop 0
	v_pk_fma_f32 v[14:15], v[14:15], v[42:43], v[6:7] neg_lo:[0,0,1] neg_hi:[0,0,1]
	v_pk_fma_f32 v[6:7], v[12:13], v[42:43], v[6:7] op_sel_hi:[1,0,1]
	v_pk_add_f32 v[12:13], v[108:109], v[108:109] op_sel:[0,1] op_sel_hi:[0,1] neg_lo:[0,1] neg_hi:[0,1]
	v_mov_b32_e32 v15, v7
	v_pk_mul_f32 v[6:7], v[10:11], v[38:39] op_sel_hi:[0,1]
	v_pk_fma_f32 v[10:11], v[8:9], v[38:39], v[6:7] op_sel:[1,0,1] op_sel_hi:[1,1,0] neg_lo:[0,0,1] neg_hi:[0,0,1]
	v_pk_fma_f32 v[6:7], v[8:9], v[38:39], v[6:7] op_sel:[1,0,1] op_sel_hi:[1,1,0]
	v_mov_b32_e32 v8, v10
	v_mov_b32_e32 v9, v7
	v_pk_mov_b32 v[6:7], v[6:7], v[10:11] op_sel:[1,0]
	s_nop 0
	v_pk_mul_f32 v[6:7], v[6:7], v[16:17]
	s_nop 0
	v_pk_fma_f32 v[10:11], v[10:11], v[12:13], v[6:7] neg_lo:[0,0,1] neg_hi:[0,0,1]
	v_pk_fma_f32 v[6:7], v[8:9], v[12:13], v[6:7]
	s_nop 0
	v_mov_b32_e32 v11, v7
	v_pk_mul_f32 v[6:7], v[4:5], v[30:31]
	s_nop 0
	v_pk_fma_f32 v[8:9], v[4:5], v[32:33], v[6:7] op_sel:[0,0,1] op_sel_hi:[1,1,0] neg_lo:[1,0,0] neg_hi:[1,0,0]
	v_pk_fma_f32 v[6:7], v[4:5], v[32:33], v[6:7] op_sel:[0,0,1] op_sel_hi:[1,1,0]
	v_mov_b32_e32 v12, v8
	v_mov_b32_e32 v13, v7
	v_pk_mov_b32 v[6:7], v[6:7], v[8:9] op_sel:[1,0]
	s_nop 0
	v_pk_mul_f32 v[6:7], v[6:7], v[56:57] op_sel:[0,1]
	s_nop 0
	v_pk_fma_f32 v[8:9], v[8:9], v[28:29], v[6:7] neg_lo:[0,0,1] neg_hi:[0,0,1]
	v_pk_fma_f32 v[6:7], v[12:13], v[28:29], v[6:7] op_sel_hi:[1,0,1]
	s_nop 0
	v_mov_b32_e32 v9, v7
	v_pk_mul_f32 v[6:7], v[4:5], v[22:23]
	s_nop 0
	v_pk_fma_f32 v[12:13], v[4:5], v[26:27], v[6:7] op_sel:[0,0,1] op_sel_hi:[1,1,0] neg_lo:[1,0,0] neg_hi:[1,0,0]
	v_pk_fma_f32 v[4:5], v[4:5], v[26:27], v[6:7] op_sel:[0,0,1] op_sel_hi:[1,1,0]
	v_mov_b32_e32 v6, v12
	v_mov_b32_e32 v7, v5
	v_pk_mov_b32 v[4:5], v[4:5], v[12:13] op_sel:[1,0]
	s_nop 0
	v_pk_mul_f32 v[4:5], v[4:5], v[52:53] op_sel:[0,1]
	s_nop 0
	v_pk_fma_f32 v[12:13], v[12:13], v[44:45], v[4:5] neg_lo:[0,0,1] neg_hi:[0,0,1]
	v_pk_fma_f32 v[4:5], v[6:7], v[44:45], v[4:5] op_sel_hi:[1,0,1]
	s_nop 0
	v_mov_b32_e32 v13, v5
	ds_write_b64 v65, v[36:37]
	ds_write_b64 v65, v[96:97] offset:8448
	ds_write_b64 v65, v[74:75] offset:16896
	ds_write_b64 v65, v[86:87] offset:25344
	ds_write_b64 v65, v[68:69] offset:33792
	ds_write_b64 v65, v[40:41] offset:42240
	ds_write_b64 v65, v[84:85] offset:50688
	ds_write_b64 v65, v[72:73] offset:59136
	ds_write_b64 v67, v[50:51]
	ds_write_b64 v183, v[48:49]
	ds_write_b64 v184, v[24:25]
	ds_write_b64 v185, v[18:19]
	ds_write_b64 v186, v[14:15]
	ds_write_b64 v187, v[10:11]
	ds_write_b64 v188, v[8:9]
	ds_write_b64 v189, v[12:13]
	s_cbranch_vccnz .LBB0_646
	s_waitcnt lgkmcnt(0)
	s_barrier
	s_waitcnt vmcnt(32)
	v_cmp_ne_u64_e32 vcc, 0, v[2:3]
	s_and_saveexec_b64 s[46:47], vcc
	s_cbranch_execz .LBB0_649
	v_cvt_pk_bf16_f32 v4, v175, v177
	v_cvt_pk_bf16_f32 v5, v176, v179
	v_cvt_pk_bf16_f32 v6, v178, v181
	v_cvt_pk_bf16_f32 v7, v180, v182
	s_lshl_b32 s12, s48, 1
	global_store_dwordx4 v[2:3], v[4:7], off nt
	s_nop 1
	v_cvt_pk_bf16_f32 v4, v167, v169
	v_cvt_pk_bf16_f32 v5, v168, v171
	v_cvt_pk_bf16_f32 v6, v170, v173
	v_cvt_pk_bf16_f32 v7, v172, v174
	v_lshl_add_u64 v[8:9], v[2:3], 0, s[22:23]
	global_store_dwordx4 v[8:9], v[4:7], off nt
	s_nop 1
	v_cvt_pk_bf16_f32 v4, v159, v161
	v_cvt_pk_bf16_f32 v5, v160, v163
	v_cvt_pk_bf16_f32 v6, v162, v165
	v_cvt_pk_bf16_f32 v7, v164, v166
	v_lshl_add_u64 v[2:3], v[2:3], 0, s[12:13]
	global_store_dwordx4 v[2:3], v[4:7], off nt
	s_nop 1
	v_cvt_pk_bf16_f32 v2, v116, v153
	v_cvt_pk_bf16_f32 v3, v117, v155
	v_cvt_pk_bf16_f32 v4, v154, v157
	v_cvt_pk_bf16_f32 v5, v156, v158
	v_lshl_add_u64 v[6:7], v[8:9], 0, s[12:13]
	global_store_dwordx4 v[6:7], v[2:5], off nt
	s_nop 1

; __device__ __forceinline__ KP kparams() { KP q = (KP)__builtin_amdgcn_kernarg_segment_ptr(); asm volatile("" : "+s"(q)); return q; }
; FFT_HD cf2 mk2(float x, float y) { return (cf2){x, y}; }
; FFT_HD void fft_sincos(float frac, float& s, float& c) { s = __builtin_amdgcn_sinf(frac); c = __builtin_amdgcn_cosf(frac); }
; FFT_HD cf2 cmul(cf2 a, cf2 b) { return mk2(a.x * b.x - a.y * b.y, a.x * b.y + a.y * b.x); }
; template <int BANK> __device__ __forceinline__ void bg_issue1(BgState& b, int wg, int NW, int lane) {
;     KP kp = kparams();
;     const float* src; int ldS; bf16_t* dst; int o2;
;     bg_decode(b.st, wg, NW, lane, kp, src, ldS, dst, o2);
;     b.dst[BANK] = dst; b.o2[BANK] = o2;
;     asm volatile("s_nop 6" ::: "memory");
; #pragma unroll
;     for (int i = 0; i < 8; ++i) { const float* p = src + (size_t)i * ldS;
;         asm volatile("global_load_dword %0, %4, off\n\tglobal_load_dword %1, %4, off offset:256\n\tglobal_load_dword %2, %4, off offset:512\n\tglobal_load_dword %3, %4, off offset:768"
;                      : "=&v"(b.r[(BANK * 8 + i) * 4 + 0]), "=&v"(b.r[(BANK * 8 + i) * 4 + 1]), "=&v"(b.r[(BANK * 8 + i) * 4 + 2]), "=&v"(b.r[(BANK * 8 + i) * 4 + 3]) : "v"(p) : "memory"); }
;     b.st += 1;
; }
; FFT_HD void fft_gen_tw(float frac, cf2 (&tw)[16]) {
;     float sn, cs; fft_sincos(frac, sn, cs);
;     tw[1] = mk2(cs, -sn);
;     tw[2] = cmul(tw[1], tw[1]); tw[3] = cmul(tw[2], tw[1]); tw[4] = cmul(tw[2], tw[2]); tw[5] = cmul(tw[4], tw[1]); tw[6] = cmul(tw[4], tw[2]); tw[7] = cmul(tw[4], tw[3]);
;     tw[8] = cmul(tw[4], tw[4]);
; #pragma unroll
;     for (int j = 9; j < 16; ++j) tw[j] = cmul(tw[8], tw[j - 8]);
; }
; template <bool INV, int lS, class ZP> FFT_HD void fft_r16_pass(ZP z, int tid) {
;     constexpr int S = 1 << lS, STEP = (S >= 64) ? S + S / 32 : S;
;     constexpr float inv = 1.0f / (float)(16 * S);
;     cf2 tw[16];
;     if (lS != 10) {
;         fft_gen_tw((float)(tid & (S - 1)) * inv, tw);
;         const int w0 = tid, w1 = tid + 512;
;         const int pb0 = PADI(((w0 >> lS) << (lS + 4)) + (w0 & (S - 1))), pb1 = PADI(((w1 >> lS) << (lS + 4)) + (w1 & (S - 1)));
;         cf2 x[16], y[16];
; #pragma unroll
;         for (int j = 0; j < 16; ++j) x[j] = z[pb0 + j * STEP];
; #pragma unroll
;         for (int j = 0; j < 16; ++j) y[j] = z[pb1 + j * STEP];
.LBB0_659:
	s_nop 6
	s_lshl_b32 s12, s48, 2
	global_load_dword v176, v[2:3], off nt
	global_load_dword v168, v[2:3], off offset:256 nt
	global_load_dword v160, v[2:3], off offset:512 nt
	global_load_dword v57, v[2:3], off offset:768 nt
	v_lshl_add_u64 v[2:3], v[2:3], 0, s[12:13]
	v_and_b32_e32 v14, 63, v120
	global_load_dword v178, v[2:3], off nt
	global_load_dword v170, v[2:3], off offset:256 nt
	global_load_dword v162, v[2:3], off offset:512 nt
	global_load_dword v154, v[2:3], off offset:768 nt
	v_lshl_add_u64 v[2:3], v[2:3], 0, s[12:13]
	v_cvt_f32_ubyte0_e32 v4, v14
	global_load_dword v177, v[2:3], off nt
	global_load_dword v169, v[2:3], off offset:256 nt
	global_load_dword v161, v[2:3], off offset:512 nt
	global_load_dword v153, v[2:3], off offset:768 nt
	v_lshl_add_u64 v[2:3], v[2:3], 0, s[12:13]
	v_mul_f32_e32 v4, 0x3a800000, v4
	global_load_dword v180, v[2:3], off nt
	global_load_dword v172, v[2:3], off offset:256 nt
	global_load_dword v164, v[2:3], off offset:512 nt
	global_load_dword v156, v[2:3], off offset:768 nt
	v_lshl_add_u64 v[2:3], v[2:3], 0, s[12:13]
	v_sin_f32_e32 v39, v4
	v_cos_f32_e32 v38, v4
	global_load_dword v179, v[2:3], off nt
	global_load_dword v171, v[2:3], off offset:256 nt
	global_load_dword v163, v[2:3], off offset:512 nt
	global_load_dword v155, v[2:3], off offset:768 nt
	v_lshl_add_u64 v[2:3], v[2:3], 0, s[12:13]
	global_load_dword v181, v[2:3], off nt
	global_load_dword v173, v[2:3], off offset:256 nt
	global_load_dword v165, v[2:3], off offset:512 nt
	global_load_dword v157, v[2:3], off offset:768 nt
	v_lshl_add_u64 v[2:3], v[2:3], 0, s[12:13]
	global_load_dword v182, v[2:3], off nt
	global_load_dword v174, v[2:3], off offset:256 nt
	global_load_dword v166, v[2:3], off offset:512 nt
	global_load_dword v158, v[2:3], off offset:768 nt
	v_lshl_add_u64 v[2:3], v[2:3], 0, s[12:13]
	global_load_dword v183, v[2:3], off nt
	global_load_dword v175, v[2:3], off offset:256 nt
	global_load_dword v167, v[2:3], off offset:512 nt
	global_load_dword v159, v[2:3], off offset:768 nt
	v_pk_mul_f32 v[2:3], v[38:39], v[38:39]
	v_mul_f32_e64 v4, v38, -v39
	v_mov_b32_e32 v5, v2
	v_mov_b32_e32 v2, v4
	v_pk_add_f32 v[202:203], v[4:5], v[2:3]
	v_pk_add_f32 v[204:205], v[4:5], v[2:3] neg_lo:[0,1] neg_hi:[0,1]
	v_mov_b32_e32 v46, v202
	v_mov_b32_e32 v47, v205
	v_pk_mul_f32 v[8:9], v[46:47], v[46:47]
	v_pk_mul_f32 v[10:11], v[204:205], v[46:47] op_sel:[1,0] op_sel_hi:[0,1]
	v_mov_b32_e32 v2, v39
	v_mov_b32_e32 v3, v38
	v_pk_mov_b32 v[12:13], v[8:9], v[10:11] op_sel:[1,0]
	v_mov_b32_e32 v9, v10
	v_pk_mul_f32 v[4:5], v[2:3], v[46:47]
	v_pk_mul_f32 v[6:7], v[38:39], v[46:47]
	v_pk_add_f32 v[48:49], v[12:13], v[8:9] neg_lo:[0,1] neg_hi:[0,1]
	v_pk_add_f32 v[68:69], v[12:13], v[8:9]
	v_mov_b32_e32 v50, v48
	v_mov_b32_e32 v51, v69
	v_mov_b32_e32 v8, v6
	v_mov_b32_e32 v9, v5
	v_pk_mov_b32 v[4:5], v[6:7], v[4:5] op_sel:[1,0]
	v_pk_mul_f32 v[6:7], v[50:51], v[68:69] op_sel:[0,1] op_sel_hi:[1,0]
	v_pk_add_f32 v[72:73], v[8:9], v[4:5] neg_lo:[0,1] neg_hi:[0,1]
	v_pk_add_f32 v[70:71], v[8:9], v[4:5]
	v_pk_mul_f32 v[4:5], v[50:51], v[50:51]
	v_lshlrev_b32_e32 v184, 4, v120
	v_mov_b32_e32 v7, v4
	v_mov_b32_e32 v4, v6
	v_pk_add_f32 v[76:77], v[6:7], v[4:5]
	v_pk_add_f32 v[74:75], v[6:7], v[4:5] neg_lo:[0,1] neg_hi:[0,1]
	v_mov_b32_e32 v54, v76
	v_mov_b32_e32 v55, v75
	v_pk_mul_f32 v[86:87], v[2:3], v[54:55]
	v_and_b32_e32 v2, 0xfffffc00, v184
	v_lshlrev_b32_e32 v4, 3, v2
	v_lshlrev_b32_e32 v5, 3, v14
	v_add_u32_e32 v3, 0x2000, v2
	v_add3_u32 v4, 0, v4, v5
	v_ashrrev_i32_e32 v2, 2, v2
	v_add_u32_e32 v238, v4, v2
	v_add_u32_e32 v239, 0x800, v238
	v_add_u32_e32 v240, 0x1000, v238
	v_add_u32_e32 v241, 0x1800, v238
	ds_read2_b64 v[98:101], v238 offset1:66
	ds_read2_b64 v[102:105], v238 offset0:132 offset1:198
	ds_read2_b64 v[106:109], v239 offset0:8 offset1:74
	ds_read2_b64 v[110:113], v239 offset0:140 offset1:206
	ds_read2_b64 v[114:117], v240 offset0:16 offset1:82
	ds_read2_b64 v[186:189], v240 offset0:148 offset1:214
	ds_read2_b64 v[190:193], v241 offset0:24 offset1:90
	ds_read2_b64 v[198:201], v241 offset0:156 offset1:222
	s_mov_b32 s48, s27
	s_waitcnt lgkmcnt(5)
	v_pk_mov_b32 v[206:207], v[100:101], v[108:109] op_sel:[1,0]
	s_waitcnt lgkmcnt(3)
	v_mov_b32_e32 v210, v116
	s_waitcnt lgkmcnt(1)
	v_pk_mov_b32 v[208:209], v[116:117], v[192:193] op_sel:[1,0]
	v_mov_b32_e32 v211, v193
	v_pk_add_f32 v[206:207], v[206:207], v[208:209] neg_lo:[0,1] neg_hi:[0,1]
	v_mov_b32_e32 v208, v100
	v_mov_b32_e32 v209, v109
	v_pk_add_f32 v[208:209], v[208:209], v[210:211] neg_lo:[0,1] neg_hi:[0,1]
	v_pk_mov_b32 v[210:211], v[102:103], v[110:111] op_sel:[1,0]
	s_waitcnt lgkmcnt(0)
; FFT_HD cf2 mk2(float x, float y) { return (cf2){x, y}; }
; FFT_HD cf2 cmul(cf2 a, cf2 b) { return mk2(a.x * b.x - a.y * b.y, a.x * b.y + a.y * b.x); }
; FFT_HD cf2 cadd(cf2 a, cf2 b) { return mk2(a.x + b.x, a.y + b.y); }
; FFT_HD cf2 csub(cf2 a, cf2 b) { return mk2(a.x - b.x, a.y - b.y); }
; template <bool INV> FFT_HD void dft4(cf2& a, cf2& b, cf2& c, cf2& d) {
;     const cf2 s0 = cadd(a, c), s1 = csub(a, c), s2 = cadd(b, d), s3 = csub(b, d);
;     a = cadd(s0, s2); c = csub(s0, s2);
;     const cf2 r = INV ? mk2(-s3.y, s3.x) : mk2(s3.y, -s3.x);
;     b = cadd(s1, r); d = csub(s1, r);
; }
; template <bool INV> FFT_HD void dft16(cf2 (&x)[16]) {
;     const float C1 = 0.9238795325112867f, S1 = 0.3826834323650898f, H = 0.7071067811865476f;
; #pragma unroll
;     for (int b = 0; b < 4; ++b) dft4<INV>(x[b], x[4 + b], x[8 + b], x[12 + b]);
;     const float s = INV ? -1.f : 1.f;
;     x[4 + 1] = cmul(x[4 + 1], mk2(C1, -s * S1)); x[8 + 1] = cmul(x[8 + 1], mk2(H, -s * H));   x[12 + 1] = cmul(x[12 + 1], mk2(S1, -s * C1));
;     x[4 + 2] = cmul(x[4 + 2], mk2(H, -s * H));   x[8 + 2] = cmul(x[8 + 2], mk2(0.f, -s));     x[12 + 2] = cmul(x[12 + 2], mk2(-H, -s * H));
;     x[4 + 3] = cmul(x[4 + 3], mk2(S1, -s * C1)); x[8 + 3] = cmul(x[8 + 3], mk2(-H, -s * H));  x[12 + 3] = cmul(x[12 + 3], mk2(-C1, s * S1));
; #pragma unroll
;     for (int c = 0; c < 4; ++c) dft4<INV>(x[4 * c], x[4 * c + 1], x[4 * c + 2], x[4 * c + 3]);
; #pragma unroll
;     for (int c = 0; c < 4; ++c)
; #pragma unroll
;         for (int d = c + 1; d < 4; ++d) { const cf2 t = x[4 * c + d]; x[4 * c + d] = x[4 * d + c]; x[4 * d + c] = t; }
; }
	v_pk_mov_b32 v[212:213], v[186:187], v[198:199] op_sel:[1,0]
	v_mov_b32_e32 v214, v186
	v_pk_add_f32 v[210:211], v[210:211], v[212:213] neg_lo:[0,1] neg_hi:[0,1]
	v_mov_b32_e32 v212, v102
	v_mov_b32_e32 v213, v111
	v_mov_b32_e32 v215, v199
	v_pk_add_f32 v[212:213], v[212:213], v[214:215] neg_lo:[0,1] neg_hi:[0,1]
	v_pk_mov_b32 v[214:215], v[104:105], v[112:113] op_sel:[1,0]
	v_pk_mov_b32 v[216:217], v[188:189], v[200:201] op_sel:[1,0]
	v_mov_b32_e32 v218, v188
	v_pk_add_f32 v[214:215], v[214:215], v[216:217] neg_lo:[0,1] neg_hi:[0,1]
	v_mov_b32_e32 v216, v104
	v_mov_b32_e32 v217, v113
	v_mov_b32_e32 v219, v201
	v_pk_add_f32 v[216:217], v[216:217], v[218:219] neg_lo:[0,1] neg_hi:[0,1]
	v_mov_b32_e32 v219, v214
	v_mov_b32_e32 v218, v216
	v_mov_b32_e32 v220, v217
	v_mov_b32_e32 v221, v215
	v_add_f32_e32 v56, v212, v213
	v_pk_add_f32 v[222:223], v[218:219], v[220:221] neg_lo:[0,1] neg_hi:[0,1]
	v_pk_add_f32 v[218:219], v[218:219], v[220:221]
	v_mul_f32_e32 v235, 0x3f3504f3, v56
	v_mov_b32_e32 v223, v219
	v_mul_f32_e32 v56, 0x3ec3ef15, v219
	v_pk_add_f32 v[228:229], v[208:209], v[208:209] op_sel:[0,1] op_sel_hi:[0,1]
	s_mov_b32 s49, s26
	v_pk_add_f32 v[216:217], v[216:217], v[216:217] op_sel:[0,1] op_sel_hi:[0,1]
	v_sub_f32_e32 v234, v210, v211
	v_pk_fma_f32 v[220:221], v[222:223], s[30:31], v[56:57] op_sel_hi:[1,1,0] neg_lo:[0,0,1] neg_hi:[0,0,1]
	v_mul_f32_e32 v242, 0x3ec3ef15, v222
	v_mul_f32_e32 v243, 0x3f6c835e, v219
	v_pk_add_f32 v[218:219], v[98:99], v[114:115]
	v_pk_add_f32 v[222:223], v[106:107], v[190:191]
	v_pk_add_f32 v[98:99], v[98:99], v[114:115] neg_lo:[0,1] neg_hi:[0,1]
	v_pk_add_f32 v[106:107], v[106:107], v[190:191] neg_lo:[0,1] neg_hi:[0,1]
	v_pk_mul_f32 v[228:229], v[228:229], s[26:27]
	v_pk_add_f32 v[230:231], v[206:207], v[206:207] op_sel:[0,1] op_sel_hi:[0,1] neg_lo:[0,1] neg_hi:[0,1]
	v_pk_mul_f32 v[216:217], v[216:217], s[48:49]
	v_pk_add_f32 v[214:215], v[214:215], v[214:215] op_sel:[0,1] op_sel_hi:[0,1] neg_lo:[0,1] neg_hi:[0,1]
	v_pk_mov_b32 v[114:115], v[106:107], v[106:107] op_sel:[1,0]
	v_pk_add_f32 v[190:191], v[98:99], v[106:107] op_sel:[0,1] op_sel_hi:[1,0]
	v_pk_add_f32 v[106:107], v[98:99], v[106:107] op_sel:[0,1] op_sel_hi:[1,0] neg_lo:[0,1] neg_hi:[0,1]
	v_pk_fma_f32 v[232:233], v[230:231], s[48:49], v[228:229]
	v_pk_fma_f32 v[228:229], v[230:231], s[48:49], v[228:229] neg_lo:[0,0,1] neg_hi:[0,0,1]
	v_fmamk_f32 v230, v234, 0x3f3504f3, v235
	v_fma_f32 v234, v234, s25, -v235
	v_pk_fma_f32 v[236:237], v[214:215], s[26:27], v[216:217]
	v_pk_fma_f32 v[214:215], v[214:215], s[26:27], v[216:217] neg_lo:[0,0,1] neg_hi:[0,0,1]
	v_mov_b32_e32 v226, v190
	v_mov_b32_e32 v227, v107
	v_mov_b32_e32 v228, v232
	v_mov_b32_e32 v235, v234
	v_mov_b32_e32 v231, v234
	v_mov_b32_e32 v214, v236
	v_pk_add_f32 v[216:217], v[226:227], v[230:231]
	v_pk_add_f32 v[226:227], v[228:229], v[214:215]
	v_pk_mov_b32 v[106:107], v[106:107], v[232:233] op_sel:[1,0]
	v_pk_mov_b32 v[232:233], v[234:235], v[236:237] op_sel:[1,0]
	v_mov_b32_e32 v228, v190
	v_pk_add_f32 v[232:233], v[106:107], v[232:233] neg_lo:[0,1] neg_hi:[0,1]
	v_mov_b32_e32 v231, v215
	v_pk_add_f32 v[106:107], v[216:217], v[226:227]
	v_mov_b32_e32 v56, v39
	v_pk_add_f32 v[214:215], v[228:229], v[230:231] neg_lo:[0,1] neg_hi:[0,1]
	v_pk_mul_f32 v[228:229], v[56:57], v[106:107] op_sel_hi:[0,1]
	v_pk_add_f32 v[100:101], v[100:101], v[116:117]
	v_pk_add_f32 v[108:109], v[108:109], v[192:193]
	v_pk_add_f32 v[102:103], v[102:103], v[186:187]
	v_pk_add_f32 v[186:187], v[110:111], v[198:199]
	v_pk_add_f32 v[104:105], v[104:105], v[188:189]
	v_pk_add_f32 v[112:113], v[112:113], v[200:201]
	v_pk_fma_f32 v[230:231], v[38:39], v[106:107], v[228:229] op_sel:[0,0,1] op_sel_hi:[1,1,0]
	v_pk_fma_f32 v[106:107], v[38:39], v[106:107], v[228:229] op_sel:[0,0,1] op_sel_hi:[0,1,0] neg_lo:[0,0,1] neg_hi:[0,0,1]
	v_pk_add_f32 v[224:225], v[218:219], v[222:223]
	v_pk_add_f32 v[192:193], v[102:103], v[186:187]
	v_mov_b32_e32 v231, v107
	v_pk_add_f32 v[106:107], v[218:219], v[222:223] neg_lo:[0,1] neg_hi:[0,1]
	v_pk_add_f32 v[102:103], v[102:103], v[186:187] neg_lo:[0,1] neg_hi:[0,1]
	v_mov_b32_e32 v186, v104
	v_mov_b32_e32 v187, v101
	v_mov_b32_e32 v218, v112
	v_mov_b32_e32 v219, v109
	v_pk_add_f32 v[186:187], v[186:187], v[218:219] neg_lo:[0,1] neg_hi:[0,1]
	v_mov_b32_e32 v218, v100
	v_mov_b32_e32 v219, v104
	v_mov_b32_e32 v222, v108
	v_mov_b32_e32 v223, v112
	v_pk_add_f32 v[116:117], v[100:101], v[108:109]
	v_pk_add_f32 v[188:189], v[104:105], v[112:113]
	v_pk_add_f32 v[218:219], v[218:219], v[222:223] neg_lo:[0,1] neg_hi:[0,1]
	v_mov_b32_e32 v222, v101
	v_mov_b32_e32 v223, v105
	v_mov_b32_e32 v228, v109
	v_mov_b32_e32 v229, v113
	v_pk_mov_b32 v[100:101], v[104:105], v[100:101] op_sel:[1,0]
	v_pk_mov_b32 v[104:105], v[112:113], v[108:109] op_sel:[1,0]
	v_pk_add_f32 v[222:223], v[222:223], v[228:229] neg_lo:[0,1] neg_hi:[0,1]
	v_pk_add_f32 v[100:101], v[100:101], v[104:105] neg_lo:[0,1] neg_hi:[0,1]
	v_pk_fma_f32 v[104:105], v[102:103], 0, v[102:103] op_sel:[0,0,1] op_sel_hi:[1,0,0]
	v_pk_fma_f32 v[102:103], v[102:103], 0, v[102:103] op_sel:[0,0,1] op_sel_hi:[1,0,0] neg_lo:[0,0,1] neg_hi:[0,0,1]
	s_mov_b32 s50, s25
	s_mov_b32 s51, s24
	v_mov_b32_e32 v105, v103
	v_pk_mul_f32 v[102:103], v[222:223], s[50:51]
	v_pk_mul_f32 v[100:101], v[100:101], s[24:25]
	v_pk_fma_f32 v[102:103], v[218:219], s[50:51], v[102:103]
	v_pk_fma_f32 v[100:101], v[186:187], s[24:25], v[100:101] neg_lo:[0,0,1] neg_hi:[0,0,1]
	v_pk_add_f32 v[108:109], v[106:107], v[104:105]
	v_pk_add_f32 v[186:187], v[102:103], v[100:101]
	v_pk_mov_b32 v[44:45], v[204:205], v[202:203] op_sel:[1,0]
	v_pk_add_f32 v[112:113], v[108:109], v[186:187]
; FFT_HD cf2 mk2(float x, float y) { return (cf2){x, y}; }
; FFT_HD cf2 cmul(cf2 a, cf2 b) { return mk2(a.x * b.x - a.y * b.y, a.x * b.y + a.y * b.x); }
; template <bool INV> FFT_HD void dft16(cf2 (&x)[16]) {
;     const float C1 = 0.9238795325112867f, S1 = 0.3826834323650898f, H = 0.7071067811865476f;
; #pragma unroll
;     for (int b = 0; b < 4; ++b) dft4<INV>(x[b], x[4 + b], x[8 + b], x[12 + b]);
;     const float s = INV ? -1.f : 1.f;
;     x[4 + 1] = cmul(x[4 + 1], mk2(C1, -s * S1)); x[8 + 1] = cmul(x[8 + 1], mk2(H, -s * H));   x[12 + 1] = cmul(x[12 + 1], mk2(S1, -s * C1));
;     x[4 + 2] = cmul(x[4 + 2], mk2(H, -s * H));   x[8 + 2] = cmul(x[8 + 2], mk2(0.f, -s));     x[12 + 2] = cmul(x[12 + 2], mk2(-H, -s * H));
;     x[4 + 3] = cmul(x[4 + 3], mk2(S1, -s * C1)); x[8 + 3] = cmul(x[8 + 3], mk2(-H, -s * H));  x[12 + 3] = cmul(x[12 + 3], mk2(-C1, s * S1));
; #pragma unroll
;     for (int c = 0; c < 4; ++c) dft4<INV>(x[4 * c], x[4 * c + 1], x[4 * c + 2], x[4 * c + 3]);
; #pragma unroll
;     for (int c = 0; c < 4; ++c)
; #pragma unroll
;         for (int d = c + 1; d < 4; ++d) { const cf2 t = x[4 * c + d]; x[4 * c + d] = x[4 * d + c]; x[4 * d + c] = t; }
; }
; template <bool INV, int lS, class ZP> FFT_HD void fft_r16_pass(ZP z, int tid) {
;     ...
;         if (!INV) {
; #pragma unroll
;             for (int j = 1; j < 16; ++j) x[j] = cmul(x[j], tw[j]);
;         }
	s_mov_b32 s56, s26
	v_pk_mul_f32 v[202:203], v[202:203], v[112:113] op_sel:[0,1] op_sel_hi:[0,0]
	v_pk_fma_f32 v[218:219], v[204:205], v[112:113], v[202:203] op_sel:[1,0,0] neg_lo:[0,0,1] neg_hi:[0,0,1]
	v_pk_fma_f32 v[112:113], v[204:205], v[112:113], v[202:203] op_sel:[1,0,0]
	v_mov_b32_e32 v202, v206
	v_mov_b32_e32 v219, v113
	v_mov_b32_e32 v112, v208
	v_mov_b32_e32 v113, v212
	v_mov_b32_e32 v212, v209
	v_mov_b32_e32 v203, v210
	v_mov_b32_e32 v210, v207
	v_pk_add_f32 v[112:113], v[112:113], v[212:213] neg_lo:[0,1] neg_hi:[0,1]
	v_pk_add_f32 v[202:203], v[202:203], v[210:211]
	s_mov_b32 s57, s24
	v_pk_mov_b32 v[204:205], v[112:113], v[202:203] op_sel:[1,0]
	v_pk_mul_f32 v[206:207], v[202:203], s[56:57]
	v_pk_mov_b32 v[202:203], v[202:203], v[112:113] op_sel:[1,0]
	s_mov_b32 s28, s25
	s_mov_b32 s52, s27
	s_mov_b32 s53, s24
	s_mov_b32 s54, s24
	s_mov_b32 s55, s27
	v_pk_mul_f32 v[202:203], v[202:203], s[28:29]
	v_mov_b32_e32 v99, v242
	v_mov_b32_e32 v115, v243
	v_pk_fma_f32 v[202:203], v[204:205], s[54:55], v[202:203]
	v_pk_fma_f32 v[204:205], v[112:113], s[52:53], v[206:207]
	v_pk_add_f32 v[98:99], v[98:99], v[114:115] neg_lo:[0,1] neg_hi:[0,1]
	v_mov_b32_e32 v190, v220
	v_pk_add_f32 v[206:207], v[202:203], v[98:99]
	v_pk_add_f32 v[208:209], v[204:205], v[190:191]
	v_mov_b32_e32 v42, v72
	v_pk_add_f32 v[112:113], v[208:209], v[206:207]
	v_pk_mov_b32 v[40:41], v[70:71], v[72:73] op_sel:[1,0]
	v_pk_mul_f32 v[72:73], v[72:73], v[112:113] op_sel:[0,1] op_sel_hi:[0,0]
	v_mov_b32_e32 v43, v71
	v_pk_fma_f32 v[210:211], v[70:71], v[112:113], v[72:73] op_sel:[1,0,0] neg_lo:[0,0,1] neg_hi:[0,0,1]
	v_pk_fma_f32 v[70:71], v[70:71], v[112:113], v[72:73] op_sel:[1,0,0]
	v_pk_add_f32 v[72:73], v[116:117], v[188:189] neg_lo:[0,1] neg_hi:[0,1]
	v_mov_b32_e32 v211, v71
	v_pk_add_f32 v[70:71], v[224:225], v[192:193] neg_lo:[0,1] neg_hi:[0,1]
	v_pk_add_f32 v[198:199], v[224:225], v[192:193]
	v_pk_add_f32 v[200:201], v[116:117], v[188:189]
	v_pk_add_f32 v[188:189], v[70:71], v[72:73] op_sel:[0,1] op_sel_hi:[1,0]
	v_pk_add_f32 v[192:193], v[70:71], v[72:73] op_sel:[0,1] op_sel_hi:[1,0] neg_lo:[0,1] neg_hi:[0,1]
	v_mov_b32_e32 v70, v188
	v_pk_mov_b32 v[72:73], v[192:193], v[188:189] op_sel:[1,0]
	v_mov_b32_e32 v71, v193
	v_pk_mov_b32 v[112:113], v[68:69], v[48:49] op_sel:[1,0]
	v_pk_mul_f32 v[68:69], v[68:69], v[72:73] op_sel:[1,0]
	v_pk_add_f32 v[116:117], v[232:233], v[232:233] op_sel:[0,1] op_sel_hi:[0,1] neg_lo:[0,1] neg_hi:[0,1]
	v_pk_fma_f32 v[212:213], v[48:49], v[188:189], v[68:69] neg_lo:[0,0,1] neg_hi:[0,0,1]
	v_pk_fma_f32 v[68:69], v[48:49], v[70:71], v[68:69] op_sel_hi:[0,1,1]
	v_pk_mul_f32 v[70:71], v[56:57], v[112:113] op_sel_hi:[0,1]
	v_mov_b32_e32 v213, v69
	v_pk_fma_f32 v[68:69], v[38:39], v[50:51], v[70:71] op_sel_hi:[0,1,1]
	v_pk_fma_f32 v[72:73], v[38:39], v[50:51], v[70:71] op_sel_hi:[0,1,1] neg_lo:[0,0,1] neg_hi:[0,0,1]
	v_mov_b32_e32 v71, v73
	v_pk_mov_b32 v[72:73], v[72:73], v[68:69] op_sel:[1,0]
	v_pk_add_f32 v[104:105], v[106:107], v[104:105] neg_lo:[0,1] neg_hi:[0,1]
	v_pk_mov_b32 v[106:107], v[100:101], v[102:103] op_sel:[1,0]
	v_pk_mov_b32 v[100:101], v[102:103], v[100:101] op_sel:[1,0]
	v_mov_b32_e32 v70, v68
	v_pk_add_f32 v[114:115], v[214:215], v[214:215] op_sel:[0,1] op_sel_hi:[0,1]
	v_pk_mul_f32 v[116:117], v[72:73], v[116:117]
	v_pk_add_f32 v[100:101], v[106:107], v[100:101] neg_lo:[0,1] neg_hi:[0,1]
	v_pk_mul_f32 v[96:97], v[46:47], v[50:51]
	v_pk_fma_f32 v[222:223], v[68:69], v[114:115], v[116:117] neg_lo:[0,0,1] neg_hi:[0,0,1]
	v_pk_fma_f32 v[114:115], v[70:71], v[114:115], v[116:117]
	v_pk_add_f32 v[102:103], v[104:105], v[100:101]
	v_pk_add_f32 v[100:101], v[104:105], v[100:101] neg_lo:[0,1] neg_hi:[0,1]
	v_pk_mul_f32 v[94:95], v[44:45], v[50:51]
	v_mov_b32_e32 v223, v115
	v_pk_add_f32 v[114:115], v[96:97], v[96:97] op_sel:[0,1] op_sel_hi:[0,1]
	v_pk_mov_b32 v[96:97], v[100:101], v[102:103] op_sel:[1,0]
	v_mov_b32_e32 v104, v102
	v_mov_b32_e32 v105, v101
	v_pk_mul_f32 v[96:97], v[114:115], v[96:97]
	v_pk_add_f32 v[116:117], v[94:95], v[94:95] op_sel:[0,1] op_sel_hi:[0,1] neg_lo:[0,1] neg_hi:[0,1]
	v_pk_fma_f32 v[224:225], v[116:117], v[102:103], v[96:97] neg_lo:[0,0,1] neg_hi:[0,0,1]
	v_pk_fma_f32 v[94:95], v[116:117], v[104:105], v[96:97]
	v_pk_mov_b32 v[96:97], v[98:99], v[220:221] op_sel:[1,0]
	v_mov_b32_e32 v225, v95
	v_pk_mov_b32 v[94:95], v[202:203], v[204:205] op_sel:[1,0]
	v_mov_b32_e32 v99, v191
	v_mov_b32_e32 v203, v205
	v_pk_add_f32 v[94:95], v[94:95], v[96:97] neg_lo:[0,1] neg_hi:[0,1]
	v_pk_add_f32 v[96:97], v[98:99], v[202:203] neg_lo:[0,1] neg_hi:[0,1]
	v_pk_mul_f32 v[92:93], v[50:51], v[42:43]
	v_pk_add_f32 v[190:191], v[96:97], v[94:95]
	v_pk_add_f32 v[202:203], v[96:97], v[94:95] neg_lo:[0,1] neg_hi:[0,1]
	v_pk_mul_f32 v[84:85], v[50:51], v[40:41]
	v_pk_add_f32 v[104:105], v[92:93], v[92:93] op_sel:[0,1] op_sel_hi:[0,1]
	v_pk_mov_b32 v[92:93], v[202:203], v[190:191] op_sel:[1,0]
	v_mov_b32_e32 v94, v190
	v_mov_b32_e32 v95, v203
	v_pk_mul_f32 v[92:93], v[104:105], v[92:93]
	v_pk_add_f32 v[106:107], v[84:85], v[84:85] op_sel:[0,1] op_sel_hi:[0,1] neg_lo:[0,1] neg_hi:[0,1]
	v_pk_fma_f32 v[204:205], v[106:107], v[190:191], v[92:93] neg_lo:[0,0,1] neg_hi:[0,0,1]
	v_pk_fma_f32 v[84:85], v[106:107], v[94:95], v[92:93]
	v_pk_mul_f32 v[90:91], v[38:39], v[54:55]
	v_mov_b32_e32 v205, v85
	v_pk_add_f32 v[84:85], v[198:199], v[200:201] neg_lo:[0,1] neg_hi:[0,1]
	v_pk_add_f32 v[110:111], v[198:199], v[200:201]
	v_pk_mul_f32 v[92:93], v[76:77], v[84:85] op_sel_hi:[0,1]
	v_pk_fma_f32 v[198:199], v[74:75], v[84:85], v[92:93] op_sel:[1,0,1] op_sel_hi:[1,1,0] neg_lo:[0,0,1] neg_hi:[0,0,1]
; FFT_HD cf2 cmul(cf2 a, cf2 b) { return mk2(a.x * b.x - a.y * b.y, a.x * b.y + a.y * b.x); }
; FFT_HD cf2 cmulc(cf2 a, cf2 b) { return mk2(a.x * b.x + a.y * b.y, a.y * b.x - a.x * b.y); }
; template <bool INV, int lS, class ZP> FFT_HD void fft_r16_pass(ZP z, int tid) {
;     ...
;         if (!INV) {
; #pragma unroll
;             for (int j = 1; j < 16; ++j) x[j] = cmul(x[j], tw[j]);
;         }
; #pragma unroll
;         for (int j = 0; j < 16; ++j) z[pb0 + j * STEP] = x[j];
;         if (INV) {
; #pragma unroll
;             for (int j = 1; j < 16; ++j) y[j] = cmulc(y[j], tw[j]);
;         }
;         dft16<INV>(y);
	v_pk_fma_f32 v[84:85], v[74:75], v[84:85], v[92:93] op_sel:[1,0,1] op_sel_hi:[1,1,0]
	v_pk_add_f32 v[92:93], v[216:217], v[226:227] neg_lo:[0,1] neg_hi:[0,1]
	v_mov_b32_e32 v199, v85
	v_pk_add_f32 v[84:85], v[90:91], v[90:91] op_sel:[0,1] op_sel_hi:[0,1] neg_lo:[0,1] neg_hi:[0,1]
	v_pk_mov_b32 v[52:53], v[74:75], v[76:77] op_sel:[1,0]
	v_pk_mul_f32 v[90:91], v[84:85], v[92:93]
	v_pk_add_f32 v[86:87], v[86:87], v[86:87] op_sel:[1,0] op_sel_hi:[1,0]
	v_pk_mul_f32 v[88:89], v[46:47], v[52:53]
	v_pk_fma_f32 v[200:201], v[86:87], v[92:93], v[90:91] op_sel:[0,0,1] op_sel_hi:[1,1,0] neg_lo:[0,0,1] neg_hi:[0,0,1]
	v_pk_fma_f32 v[90:91], v[86:87], v[92:93], v[90:91] op_sel:[0,0,1] op_sel_hi:[1,1,0]
	v_pk_mul_f32 v[82:83], v[46:47], v[54:55]
	v_mov_b32_e32 v201, v91
	v_pk_add_f32 v[90:91], v[108:109], v[186:187] neg_lo:[0,1] neg_hi:[0,1]
	v_pk_add_f32 v[186:187], v[88:89], v[88:89] op_sel:[0,1] op_sel_hi:[0,1]
	v_pk_mul_f32 v[88:89], v[186:187], v[90:91]
	v_pk_add_f32 v[216:217], v[82:83], v[82:83] op_sel:[1,0] op_sel_hi:[1,0] neg_lo:[0,1] neg_hi:[0,1]
	v_pk_mul_f32 v[80:81], v[42:43], v[52:53]
	v_pk_fma_f32 v[220:221], v[216:217], v[90:91], v[88:89] op_sel:[0,0,1] op_sel_hi:[1,1,0] neg_lo:[0,0,1] neg_hi:[0,0,1]
	v_pk_fma_f32 v[82:83], v[216:217], v[90:91], v[88:89] op_sel:[0,0,1] op_sel_hi:[1,1,0]
	v_pk_mul_f32 v[78:79], v[42:43], v[54:55]
	v_mov_b32_e32 v221, v83
	v_mov_b32_e32 v82, v206
	v_mov_b32_e32 v83, v209
	v_mov_b32_e32 v209, v207
	v_pk_add_f32 v[82:83], v[82:83], v[208:209] neg_lo:[0,1] neg_hi:[0,1]
	v_pk_add_f32 v[80:81], v[80:81], v[80:81] op_sel:[0,1] op_sel_hi:[0,1]
	v_pk_mul_f32 v[88:89], v[80:81], v[82:83]
	v_pk_add_f32 v[78:79], v[78:79], v[78:79] op_sel:[1,0] op_sel_hi:[1,0] neg_lo:[0,1] neg_hi:[0,1]
	v_pk_add_f32 v[96:97], v[232:233], v[232:233] op_sel:[0,1] op_sel_hi:[0,1]
	v_pk_fma_f32 v[206:207], v[78:79], v[82:83], v[88:89] op_sel:[0,0,1] op_sel_hi:[1,1,0] neg_lo:[0,0,1] neg_hi:[0,0,1]
	v_pk_fma_f32 v[82:83], v[78:79], v[82:83], v[88:89] op_sel:[0,0,1] op_sel_hi:[1,1,0]
	v_pk_mul_f32 v[88:89], v[50:51], v[76:77] op_sel_hi:[1,0]
	v_mov_b32_e32 v207, v83
	v_pk_fma_f32 v[82:83], v[50:51], v[74:75], v[88:89] op_sel:[0,1,1] op_sel_hi:[1,1,0] neg_lo:[0,0,1] neg_hi:[0,0,1]
	v_pk_fma_f32 v[90:91], v[50:51], v[74:75], v[88:89] op_sel:[0,1,1] op_sel_hi:[1,1,0]
	v_mov_b32_e32 v88, v82
	v_mov_b32_e32 v89, v91
	v_pk_mov_b32 v[90:91], v[90:91], v[82:83] op_sel:[1,0]
	v_pk_add_f32 v[94:95], v[214:215], v[214:215] op_sel:[0,1] op_sel_hi:[0,1] neg_lo:[0,1] neg_hi:[0,1]
	v_pk_mul_f32 v[92:93], v[90:91], v[188:189] op_sel:[0,1]
	v_ashrrev_i32_e32 v2, 2, v3
	v_pk_fma_f32 v[188:189], v[82:83], v[192:193], v[92:93] neg_lo:[0,0,1] neg_hi:[0,0,1]
	v_pk_fma_f32 v[92:93], v[88:89], v[192:193], v[92:93] op_sel_hi:[1,0,1]
	v_add3_u32 v60, v4, v2, s71
	v_mov_b32_e32 v189, v93
	v_pk_mul_f32 v[92:93], v[76:77], v[70:71] op_sel_hi:[0,1]
	v_pk_fma_f32 v[76:77], v[74:75], v[70:71], v[92:93] op_sel:[1,0,1] op_sel_hi:[1,1,0] neg_lo:[0,0,1] neg_hi:[0,0,1]
	v_pk_fma_f32 v[92:93], v[74:75], v[70:71], v[92:93] op_sel:[1,0,1] op_sel_hi:[1,1,0]
	v_mov_b32_e32 v74, v76
	v_mov_b32_e32 v75, v93
	v_pk_mov_b32 v[92:93], v[92:93], v[76:77] op_sel:[1,0]
	v_add_u32_e32 v65, 0x800, v60
	v_pk_mul_f32 v[96:97], v[92:93], v[96:97]
	v_add_u32_e32 v67, 0x1000, v60
	v_pk_fma_f32 v[192:193], v[76:77], v[94:95], v[96:97] neg_lo:[0,0,1] neg_hi:[0,0,1]
	v_pk_fma_f32 v[94:95], v[74:75], v[94:95], v[96:97]
	v_pk_mul_f32 v[96:97], v[54:55], v[116:117]
	v_mov_b32_e32 v193, v95
	v_pk_fma_f32 v[94:95], v[54:55], v[114:115], v[96:97] op_sel:[0,0,1] op_sel_hi:[1,1,0] neg_lo:[1,0,0] neg_hi:[1,0,0]
	v_pk_fma_f32 v[98:99], v[54:55], v[114:115], v[96:97] op_sel:[0,0,1] op_sel_hi:[1,1,0]
	v_mov_b32_e32 v96, v94
	v_mov_b32_e32 v97, v99
	v_pk_mov_b32 v[98:99], v[98:99], v[94:95] op_sel:[1,0]
	v_add_u32_e32 v185, 0x1800, v60
	v_pk_mul_f32 v[102:103], v[98:99], v[102:103] op_sel:[0,1]
	ds_read2_b64 v[2:5], v60 offset1:66
	ds_read2_b64 v[18:21], v60 offset0:132 offset1:198
	v_pk_fma_f32 v[208:209], v[94:95], v[100:101], v[102:103] neg_lo:[0,0,1] neg_hi:[0,0,1]
	v_pk_fma_f32 v[100:101], v[96:97], v[100:101], v[102:103] op_sel_hi:[1,0,1]
	v_pk_mul_f32 v[102:103], v[54:55], v[106:107]
	ds_read2_b64 v[6:9], v65 offset0:8 offset1:74
	ds_read2_b64 v[22:25], v65 offset0:140 offset1:206
	ds_read2_b64 v[10:13], v67 offset0:16 offset1:82
	ds_read2_b64 v[26:29], v67 offset0:148 offset1:214
	ds_read2_b64 v[14:17], v185 offset0:24 offset1:90
	ds_read2_b64 v[30:33], v185 offset0:156 offset1:222
	v_mov_b32_e32 v209, v101
	v_pk_fma_f32 v[100:101], v[54:55], v[104:105], v[102:103] op_sel:[0,0,1] op_sel_hi:[1,1,0] neg_lo:[1,0,0] neg_hi:[1,0,0]
	v_pk_fma_f32 v[108:109], v[54:55], v[104:105], v[102:103] op_sel:[0,0,1] op_sel_hi:[1,1,0]
	v_mov_b32_e32 v102, v100
	v_mov_b32_e32 v103, v109
	v_pk_mov_b32 v[108:109], v[108:109], v[100:101] op_sel:[1,0]
	v_cmp_ne_u64_e32 vcc, 0, v[34:35]
	v_pk_mul_f32 v[190:191], v[108:109], v[190:191] op_sel:[0,1]
	s_nop 0
	v_pk_fma_f32 v[214:215], v[100:101], v[202:203], v[190:191] neg_lo:[0,0,1] neg_hi:[0,0,1]
	v_pk_fma_f32 v[190:191], v[102:103], v[202:203], v[190:191] op_sel_hi:[1,0,1]
	s_waitcnt lgkmcnt(1)
; FFT_HD cf2 mk2(float x, float y) { return (cf2){x, y}; }
; FFT_HD cf2 cmul(cf2 a, cf2 b) { return mk2(a.x * b.x - a.y * b.y, a.x * b.y + a.y * b.x); }
; FFT_HD cf2 cmulc(cf2 a, cf2 b) { return mk2(a.x * b.x + a.y * b.y, a.y * b.x - a.x * b.y); }
; FFT_HD cf2 cadd(cf2 a, cf2 b) { return mk2(a.x + b.x, a.y + b.y); }
; FFT_HD cf2 csub(cf2 a, cf2 b) { return mk2(a.x - b.x, a.y - b.y); }
; template <bool INV> FFT_HD void dft4(cf2& a, cf2& b, cf2& c, cf2& d) {
;     const cf2 s0 = cadd(a, c), s1 = csub(a, c), s2 = cadd(b, d), s3 = csub(b, d);
;     a = cadd(s0, s2); c = csub(s0, s2);
;     const cf2 r = INV ? mk2(-s3.y, s3.x) : mk2(s3.y, -s3.x);
;     b = cadd(s1, r); d = csub(s1, r);
; }
; template <bool INV> FFT_HD void dft16(cf2 (&x)[16]) {
;     const float C1 = 0.9238795325112867f, S1 = 0.3826834323650898f, H = 0.7071067811865476f;
; #pragma unroll
;     for (int b = 0; b < 4; ++b) dft4<INV>(x[b], x[4 + b], x[8 + b], x[12 + b]);
;     const float s = INV ? -1.f : 1.f;
;     x[4 + 1] = cmul(x[4 + 1], mk2(C1, -s * S1)); x[8 + 1] = cmul(x[8 + 1], mk2(H, -s * H));   x[12 + 1] = cmul(x[12 + 1], mk2(S1, -s * C1));
;     x[4 + 2] = cmul(x[4 + 2], mk2(H, -s * H));   x[8 + 2] = cmul(x[8 + 2], mk2(0.f, -s));     x[12 + 2] = cmul(x[12 + 2], mk2(-H, -s * H));
;     x[4 + 3] = cmul(x[4 + 3], mk2(S1, -s * C1)); x[8 + 3] = cmul(x[8 + 3], mk2(-H, -s * H));  x[12 + 3] = cmul(x[12 + 3], mk2(-C1, s * S1));
; #pragma unroll
;     for (int c = 0; c < 4; ++c) dft4<INV>(x[4 * c], x[4 * c + 1], x[4 * c + 2], x[4 * c + 3]);
; #pragma unroll
;     for (int c = 0; c < 4; ++c)
; #pragma unroll
;         for (int d = c + 1; d < 4; ++d) { const cf2 t = x[4 * c + d]; x[4 * c + d] = x[4 * d + c]; x[4 * d + c] = t; }
; }
; template <bool INV, int lS, class ZP> FFT_HD void fft_r16_pass(ZP z, int tid) {
;     ...
; #pragma unroll
;         for (int j = 0; j < 16; ++j) z[pb0 + j * STEP] = x[j];
;         if (INV) {
; #pragma unroll
;             for (int j = 1; j < 16; ++j) y[j] = cmulc(y[j], tw[j]);
;         }
;         dft16<INV>(y);
	v_pk_add_f32 v[202:203], v[6:7], v[14:15]
	v_mov_b32_e32 v215, v191
	ds_write2_b64 v238, v[110:111], v[230:231] offset1:66
	ds_write2_b64 v238, v[218:219], v[210:211] offset0:132 offset1:198
	ds_write2_b64 v239, v[212:213], v[222:223] offset0:8 offset1:74
	ds_write2_b64 v239, v[224:225], v[204:205] offset0:140 offset1:206
	ds_write2_b64 v240, v[198:199], v[200:201] offset0:16 offset1:82
	ds_write2_b64 v240, v[220:221], v[206:207] offset0:148 offset1:214
	ds_write2_b64 v241, v[188:189], v[192:193] offset0:24 offset1:90
	ds_write2_b64 v241, v[208:209], v[214:215] offset0:156 offset1:222
	v_pk_mov_b32 v[110:111], v[4:5], v[8:9] op_sel:[1,0]
	v_pk_mov_b32 v[188:189], v[12:13], v[16:17] op_sel:[1,0]
	v_mov_b32_e32 v190, v12
	v_pk_add_f32 v[110:111], v[110:111], v[188:189] neg_lo:[0,1] neg_hi:[0,1]
	v_mov_b32_e32 v188, v4
	v_mov_b32_e32 v189, v9
	v_mov_b32_e32 v191, v17
	v_pk_add_f32 v[188:189], v[188:189], v[190:191] neg_lo:[0,1] neg_hi:[0,1]
	v_pk_mov_b32 v[190:191], v[18:19], v[22:23] op_sel:[1,0]
	s_waitcnt lgkmcnt(8)
	v_pk_mov_b32 v[192:193], v[26:27], v[30:31] op_sel:[1,0]
	v_pk_mov_b32 v[206:207], v[20:21], v[4:5] op_sel:[1,0]
	v_pk_mov_b32 v[208:209], v[28:29], v[12:13] op_sel:[1,0]
	v_pk_add_f32 v[190:191], v[190:191], v[192:193] neg_lo:[0,1] neg_hi:[0,1]
	v_mov_b32_e32 v192, v18
	v_mov_b32_e32 v193, v23
	v_mov_b32_e32 v198, v26
	v_mov_b32_e32 v199, v31
	v_pk_add_f32 v[206:207], v[206:207], v[208:209]
	v_mov_b32_e32 v208, v4
	v_mov_b32_e32 v209, v20
	v_mov_b32_e32 v210, v12
	v_mov_b32_e32 v211, v28
	v_pk_add_f32 v[192:193], v[192:193], v[198:199] neg_lo:[0,1] neg_hi:[0,1]
	v_pk_add_f32 v[208:209], v[208:209], v[210:211]
	v_pk_mov_b32 v[210:211], v[24:25], v[8:9] op_sel:[1,0]
	v_pk_mov_b32 v[212:213], v[32:33], v[16:17] op_sel:[1,0]
	v_add_f32_e32 v39, v192, v193
	v_sub_f32_e32 v218, v190, v191
	v_sub_f32_e32 v219, v192, v193
	v_add_f32_e32 v200, v190, v191
	v_pk_mov_b32 v[190:191], v[20:21], v[24:25] op_sel:[1,0]
	v_pk_mov_b32 v[192:193], v[28:29], v[32:33] op_sel:[1,0]
	v_pk_add_f32 v[210:211], v[210:211], v[212:213]
	v_mov_b32_e32 v212, v8
	v_mov_b32_e32 v213, v24
	v_mov_b32_e32 v214, v16
	v_mov_b32_e32 v215, v32
	v_mov_b32_e32 v4, v20
	v_mov_b32_e32 v12, v28
	v_mov_b32_e32 v8, v24
	v_mov_b32_e32 v16, v32
	v_pk_add_f32 v[190:191], v[190:191], v[192:193] neg_lo:[0,1] neg_hi:[0,1]
	v_mov_b32_e32 v192, v20
	v_mov_b32_e32 v198, v28
	v_pk_add_f32 v[212:213], v[212:213], v[214:215]
	v_pk_add_f32 v[214:215], v[4:5], v[12:13]
	v_mov_b32_e32 v20, v5
	v_mov_b32_e32 v28, v13
	v_pk_add_f32 v[12:13], v[8:9], v[16:17]
	v_mov_b32_e32 v24, v9
	v_mov_b32_e32 v32, v17
	v_pk_add_f32 v[16:17], v[18:19], v[26:27]
	v_pk_add_f32 v[18:19], v[22:23], v[30:31]
	v_pk_add_f32 v[4:5], v[20:21], v[28:29]
	v_pk_add_f32 v[8:9], v[24:25], v[32:33]
	v_pk_add_f32 v[20:21], v[16:17], v[18:19] neg_lo:[0,1] neg_hi:[0,1]
	v_mov_b32_e32 v193, v25
	v_pk_add_f32 v[24:25], v[4:5], v[8:9] neg_lo:[0,1] neg_hi:[0,1]
	v_pk_add_f32 v[26:27], v[206:207], v[210:211] neg_lo:[0,1] neg_hi:[0,1]
	v_pk_fma_f32 v[28:29], v[20:21], 0, v[20:21] op_sel:[0,0,1] op_sel_hi:[1,0,0]
	v_pk_fma_f32 v[20:21], v[20:21], 0, v[20:21] op_sel:[0,0,1] op_sel_hi:[1,0,0] neg_lo:[0,0,1] neg_hi:[0,0,1]
	v_mov_b32_e32 v199, v33
	v_pk_add_f32 v[12:13], v[214:215], v[12:13] neg_lo:[0,1] neg_hi:[0,1]
	v_mov_b32_e32 v29, v21
	v_pk_mul_f32 v[20:21], v[24:25], s[50:51]
	v_pk_mul_f32 v[24:25], v[26:27], s[24:25]
	v_pk_add_f32 v[192:193], v[192:193], v[198:199] neg_lo:[0,1] neg_hi:[0,1]
	v_mul_f32_e32 v199, 0xbf3504f3, v200
	v_pk_add_f32 v[200:201], v[2:3], v[10:11]
	v_pk_add_f32 v[22:23], v[208:209], v[212:213] neg_lo:[0,1] neg_hi:[0,1]
	v_pk_fma_f32 v[12:13], v[12:13], s[24:25], v[24:25] neg_lo:[0,0,1] neg_hi:[0,0,1]
	v_mov_b32_e32 v24, v208
	v_mov_b32_e32 v25, v4
	v_mov_b32_e32 v26, v212
	v_mov_b32_e32 v27, v8
	v_mov_b32_e32 v4, v209
	v_mov_b32_e32 v8, v213
	v_pk_fma_f32 v[20:21], v[22:23], s[50:51], v[20:21]
	v_pk_add_f32 v[22:23], v[200:201], v[202:203]
	v_pk_add_f32 v[24:25], v[24:25], v[26:27]
	v_pk_add_f32 v[16:17], v[16:17], v[18:19]
	v_pk_add_f32 v[4:5], v[4:5], v[8:9]
	v_pk_add_f32 v[204:205], v[200:201], v[202:203] neg_lo:[0,1] neg_hi:[0,1]
	v_pk_add_f32 v[8:9], v[22:23], v[16:17]
	v_pk_add_f32 v[18:19], v[24:25], v[4:5]
	v_pk_mov_b32 v[26:27], v[22:23], v[24:25] op_sel:[1,0]
	v_pk_mov_b32 v[30:31], v[16:17], v[4:5] op_sel:[1,0]
	v_mov_b32_e32 v23, v25
	v_mov_b32_e32 v17, v5
	v_pk_add_f32 v[4:5], v[22:23], v[16:17] neg_lo:[0,1] neg_hi:[0,1]
	v_pk_add_f32 v[16:17], v[8:9], v[18:19]
	v_pk_add_f32 v[8:9], v[8:9], v[18:19] neg_lo:[0,1] neg_hi:[0,1]
	v_pk_add_f32 v[18:19], v[204:205], v[28:29]
	v_pk_add_f32 v[22:23], v[20:21], v[12:13]
	v_pk_add_f32 v[26:27], v[26:27], v[30:31] neg_lo:[0,1] neg_hi:[0,1]
	v_pk_add_f32 v[24:25], v[18:19], v[22:23]
	v_pk_add_f32 v[18:19], v[18:19], v[22:23] neg_lo:[0,1] neg_hi:[0,1]
	v_pk_mul_f32 v[22:23], v[46:47], v[24:25] op_sel:[0,1]
	v_pk_add_f32 v[2:3], v[2:3], v[10:11] neg_lo:[0,1] neg_hi:[0,1]
	v_pk_fma_f32 v[30:31], v[44:45], v[24:25], v[22:23] neg_lo:[0,0,1] neg_hi:[0,0,1]
	v_pk_fma_f32 v[22:23], v[44:45], v[24:25], v[22:23] op_sel_hi:[1,0,1]
	v_pk_add_f32 v[24:25], v[26:27], v[26:27] op_sel:[0,1] op_sel_hi:[0,1] neg_lo:[0,1] neg_hi:[0,1]
	v_mov_b32_e32 v31, v23
	v_pk_add_f32 v[22:23], v[4:5], v[4:5] op_sel:[0,1] op_sel_hi:[0,1]
	v_pk_mul_f32 v[24:25], v[112:113], v[24:25]
	v_pk_add_f32 v[10:11], v[188:189], v[188:189] op_sel:[0,1] op_sel_hi:[0,1] neg_lo:[0,1] neg_hi:[0,1]
	v_pk_fma_f32 v[32:33], v[48:49], v[22:23], v[24:25] neg_lo:[0,0,1] neg_hi:[0,0,1]
	v_pk_fma_f32 v[22:23], v[50:51], v[22:23], v[24:25]
	v_pk_mov_b32 v[24:25], v[12:13], v[20:21] op_sel:[1,0]
; FFT_HD cf2 mk2(float x, float y) { return (cf2){x, y}; }
; FFT_HD cf2 cmul(cf2 a, cf2 b) { return mk2(a.x * b.x - a.y * b.y, a.x * b.y + a.y * b.x); }
; FFT_HD cf2 cadd(cf2 a, cf2 b) { return mk2(a.x + b.x, a.y + b.y); }
; FFT_HD cf2 csub(cf2 a, cf2 b) { return mk2(a.x - b.x, a.y - b.y); }
; template <bool INV> FFT_HD void dft4(cf2& a, cf2& b, cf2& c, cf2& d) {
;     const cf2 s0 = cadd(a, c), s1 = csub(a, c), s2 = cadd(b, d), s3 = csub(b, d);
;     a = cadd(s0, s2); c = csub(s0, s2);
;     const cf2 r = INV ? mk2(-s3.y, s3.x) : mk2(s3.y, -s3.x);
;     b = cadd(s1, r); d = csub(s1, r);
; }
; template <bool INV> FFT_HD void dft16(cf2 (&x)[16]) {
;     const float C1 = 0.9238795325112867f, S1 = 0.3826834323650898f, H = 0.7071067811865476f;
; #pragma unroll
;     for (int b = 0; b < 4; ++b) dft4<INV>(x[b], x[4 + b], x[8 + b], x[12 + b]);
;     const float s = INV ? -1.f : 1.f;
;     x[4 + 1] = cmul(x[4 + 1], mk2(C1, -s * S1)); x[8 + 1] = cmul(x[8 + 1], mk2(H, -s * H));   x[12 + 1] = cmul(x[12 + 1], mk2(S1, -s * C1));
;     x[4 + 2] = cmul(x[4 + 2], mk2(H, -s * H));   x[8 + 2] = cmul(x[8 + 2], mk2(0.f, -s));     x[12 + 2] = cmul(x[12 + 2], mk2(-H, -s * H));
;     x[4 + 3] = cmul(x[4 + 3], mk2(S1, -s * C1)); x[8 + 3] = cmul(x[8 + 3], mk2(-H, -s * H));  x[12 + 3] = cmul(x[12 + 3], mk2(-C1, s * S1));
; #pragma unroll
;     for (int c = 0; c < 4; ++c) dft4<INV>(x[4 * c], x[4 * c + 1], x[4 * c + 2], x[4 * c + 3]);
; #pragma unroll
;     for (int c = 0; c < 4; ++c)
; #pragma unroll
;         for (int d = c + 1; d < 4; ++d) { const cf2 t = x[4 * c + d]; x[4 * c + d] = x[4 * d + c]; x[4 * d + c] = t; }
; }
	v_pk_mov_b32 v[12:13], v[20:21], v[12:13] op_sel:[1,0]
	v_mov_b32_e32 v33, v23
	v_pk_add_f32 v[22:23], v[204:205], v[28:29] neg_lo:[0,1] neg_hi:[0,1]
	v_pk_add_f32 v[12:13], v[24:25], v[12:13] neg_lo:[0,1] neg_hi:[0,1]
	v_pk_add_f32 v[6:7], v[6:7], v[14:15] neg_lo:[0,1] neg_hi:[0,1]
	v_pk_add_f32 v[20:21], v[22:23], v[12:13]
	v_pk_add_f32 v[12:13], v[22:23], v[12:13] neg_lo:[0,1] neg_hi:[0,1]
	v_mov_b32_e32 v22, v20
	v_pk_mov_b32 v[24:25], v[12:13], v[20:21] op_sel:[1,0]
	v_mov_b32_e32 v23, v13
	v_pk_mul_f32 v[24:25], v[114:115], v[24:25]
	v_pk_mul_f32 v[10:11], v[10:11], s[48:49]
	v_pk_fma_f32 v[28:29], v[116:117], v[20:21], v[24:25] neg_lo:[0,0,1] neg_hi:[0,0,1]
	v_pk_fma_f32 v[22:23], v[116:117], v[22:23], v[24:25]
	v_pk_add_f32 v[14:15], v[110:111], v[110:111] op_sel:[0,1] op_sel_hi:[0,1]
	v_mov_b32_e32 v29, v23
	v_pk_mul_f32 v[22:23], v[54:55], v[8:9] op_sel:[0,1]
	v_mul_f32_e32 v198, 0xbf3504f3, v219
	v_pk_fma_f32 v[24:25], v[52:53], v[8:9], v[22:23] neg_lo:[0,0,1] neg_hi:[0,0,1]
	v_pk_fma_f32 v[8:9], v[52:53], v[8:9], v[22:23] op_sel_hi:[1,0,1]
	v_sub_f32_e32 v198, v198, v199
	v_mov_b32_e32 v25, v9
	v_pk_mul_f32 v[8:9], v[186:187], v[18:19]
	v_fmac_f32_e32 v199, 0xbf3504f3, v219
	v_pk_fma_f32 v[22:23], v[216:217], v[18:19], v[8:9] op_sel:[0,0,1] op_sel_hi:[1,1,0] neg_lo:[0,0,1] neg_hi:[0,0,1]
	v_pk_fma_f32 v[8:9], v[216:217], v[18:19], v[8:9] op_sel:[0,0,1] op_sel_hi:[1,1,0]
	v_pk_fma_f32 v[18:19], v[14:15], s[26:27], v[10:11]
	v_pk_fma_f32 v[10:11], v[14:15], s[26:27], v[10:11] neg_lo:[0,0,1] neg_hi:[0,0,1]
	v_pk_add_f32 v[14:15], v[190:191], v[190:191] op_sel:[0,1] op_sel_hi:[0,1]
	v_mov_b32_e32 v23, v9
	v_pk_add_f32 v[8:9], v[2:3], v[6:7] op_sel:[0,1] op_sel_hi:[1,0] neg_lo:[0,1] neg_hi:[0,1]
	v_pk_add_f32 v[2:3], v[2:3], v[6:7] op_sel:[0,1] op_sel_hi:[1,0]
	v_mov_b32_e32 v19, v11
	v_pk_add_f32 v[10:11], v[192:193], v[192:193] op_sel:[0,1] op_sel_hi:[0,1] neg_lo:[0,1] neg_hi:[0,1]
	v_pk_mul_f32 v[14:15], v[14:15], s[48:49]
	v_mov_b32_e32 v6, v8
	v_mov_b32_e32 v7, v3
	v_pk_fma_f32 v[10:11], v[10:11], s[30:31], v[14:15] neg_lo:[0,0,1] neg_hi:[0,0,1]
	v_pk_add_f32 v[14:15], v[6:7], v[198:199]
	v_pk_add_f32 v[44:45], v[18:19], v[10:11]
	v_pk_add_f32 v[6:7], v[6:7], v[198:199] neg_lo:[0,1] neg_hi:[0,1]
	v_pk_add_f32 v[46:47], v[14:15], v[44:45]
	v_pk_add_f32 v[10:11], v[18:19], v[10:11] neg_lo:[0,1] neg_hi:[0,1]
	v_pk_mul_f32 v[42:43], v[42:43], v[46:47] op_sel:[0,1]
	v_pk_add_f32 v[14:15], v[14:15], v[44:45] neg_lo:[0,1] neg_hi:[0,1]
	v_pk_fma_f32 v[44:45], v[40:41], v[46:47], v[42:43] neg_lo:[0,0,1] neg_hi:[0,0,1]
	v_pk_fma_f32 v[40:41], v[40:41], v[46:47], v[42:43] op_sel_hi:[1,0,1]
	v_pk_add_f32 v[18:19], v[6:7], v[10:11] op_sel:[0,1] op_sel_hi:[1,0]
	v_pk_add_f32 v[6:7], v[6:7], v[10:11] op_sel:[0,1] op_sel_hi:[1,0] neg_lo:[0,1] neg_hi:[0,1]
	v_mov_b32_e32 v45, v41
	v_pk_mov_b32 v[40:41], v[6:7], v[18:19] op_sel:[1,0]
	v_mov_b32_e32 v10, v18
	v_mov_b32_e32 v11, v7
	v_pk_mul_f32 v[40:41], v[104:105], v[40:41]
	v_pk_add_f32 v[50:51], v[192:193], v[192:193] op_sel:[0,1] op_sel_hi:[0,1]
	v_pk_fma_f32 v[42:43], v[106:107], v[18:19], v[40:41] neg_lo:[0,0,1] neg_hi:[0,0,1]
	v_pk_fma_f32 v[10:11], v[106:107], v[10:11], v[40:41]
	v_mul_f32_e32 v39, 0x3f3504f3, v39
	v_mov_b32_e32 v43, v11
	v_pk_add_f32 v[10:11], v[188:189], v[188:189] op_sel:[0,1] op_sel_hi:[0,1]
	v_pk_mul_f32 v[10:11], v[10:11], s[26:27]
	v_pk_add_f32 v[40:41], v[110:111], v[110:111] op_sel:[0,1] op_sel_hi:[0,1] neg_lo:[0,1] neg_hi:[0,1]
	v_pk_mul_f32 v[50:51], v[50:51], s[48:49]
	v_pk_add_f32 v[52:53], v[190:191], v[190:191] op_sel:[0,1] op_sel_hi:[0,1] neg_lo:[0,1] neg_hi:[0,1]
	v_pk_fma_f32 v[46:47], v[40:41], s[48:49], v[10:11]
	v_pk_fma_f32 v[10:11], v[40:41], s[48:49], v[10:11] neg_lo:[0,0,1] neg_hi:[0,0,1]
	v_fma_f32 v48, v218, s25, -v39
	v_pk_fma_f32 v[54:55], v[52:53], s[26:27], v[50:51]
	v_pk_fma_f32 v[50:51], v[52:53], s[26:27], v[50:51] neg_lo:[0,0,1] neg_hi:[0,0,1]
	v_mov_b32_e32 v10, v46
	v_fmamk_f32 v40, v218, 0x3f3504f3, v39
	v_mov_b32_e32 v41, v48
	v_mov_b32_e32 v50, v54
	v_mov_b32_e32 v3, v9
	v_mov_b32_e32 v49, v48
	v_pk_add_f32 v[52:53], v[10:11], v[50:51]
	v_pk_add_f32 v[104:105], v[2:3], v[40:41]
	v_mov_b32_e32 v3, v11
	v_mov_b32_e32 v41, v51
	v_pk_add_f32 v[2:3], v[2:3], v[40:41] neg_lo:[0,1] neg_hi:[0,1]
; __device__ __forceinline__ unsigned cvt_pk_bf16(float lo, float hi) { unsigned r; asm volatile("v_cvt_pk_bf16_f32 %0, %1, %2" : "=v"(r) : "v"(lo), "v"(hi)); return r; }
; FFT_HD cf2 cmul(cf2 a, cf2 b) { return mk2(a.x * b.x - a.y * b.y, a.x * b.y + a.y * b.x); }
; template <int BANK, int WAITN> __device__ __forceinline__ void bg_finish1(BgState& b) {
;     if (WAITN == 32) asm volatile("s_waitcnt vmcnt(32)" ::: "memory"); else asm volatile("s_waitcnt vmcnt(0)" ::: "memory");
;     asm volatile("" : BG_TIE16(BANK * 32) :: "memory");
;     asm volatile("" : BG_TIE16(BANK * 32 + 16) :: "memory");
;     bf16_t* dst = b.dst[BANK];
;     if (dst != nullptr) {
; #pragma unroll
;         for (int c = 0; c < 4; ++c) { u32x4 w;
;             w.x = cvt_pk_bf16(b.r[(BANK * 8 + 0) * 4 + c], b.r[(BANK * 8 + 1) * 4 + c]); w.y = cvt_pk_bf16(b.r[(BANK * 8 + 2) * 4 + c], b.r[(BANK * 8 + 3) * 4 + c]);
;             w.z = cvt_pk_bf16(b.r[(BANK * 8 + 4) * 4 + c], b.r[(BANK * 8 + 5) * 4 + c]); w.w = cvt_pk_bf16(b.r[(BANK * 8 + 6) * 4 + c], b.r[(BANK * 8 + 7) * 4 + c]);
;             bf16_t* dp = dst + (c & 1) * 512 + (c >> 1) * b.o2[BANK];
;             asm volatile("global_store_dwordx4 %0, %1, off\n\ts_nop 1" :: "v"(dp), "v"(w) : "memory"); }
;     }
; }
; template <bool INV, int lS, class ZP> FFT_HD void fft_r16_pass(ZP z, int tid) {
;     ...
;         if (!INV) {
; #pragma unroll
;             for (int j = 1; j < 16; ++j) y[j] = cmul(y[j], tw[j]);
;         }
; #pragma unroll
;         for (int j = 0; j < 16; ++j) z[pb1 + j * STEP] = y[j];
	v_pk_mov_b32 v[8:9], v[8:9], v[46:47] op_sel:[1,0]
	v_pk_mov_b32 v[10:11], v[48:49], v[54:55] op_sel:[1,0]
	v_pk_add_f32 v[40:41], v[104:105], v[52:53]
	v_pk_add_f32 v[8:9], v[8:9], v[10:11] neg_lo:[0,1] neg_hi:[0,1]
	v_pk_mul_f32 v[46:47], v[56:57], v[40:41] op_sel_hi:[0,1]
	v_pk_fma_f32 v[48:49], v[38:39], v[40:41], v[46:47] op_sel:[0,0,1] op_sel_hi:[1,1,0]
	v_pk_fma_f32 v[38:39], v[38:39], v[40:41], v[46:47] op_sel:[0,0,1] op_sel_hi:[0,1,0] neg_lo:[0,0,1] neg_hi:[0,0,1]
	v_pk_add_f32 v[40:41], v[8:9], v[8:9] op_sel:[0,1] op_sel_hi:[0,1] neg_lo:[0,1] neg_hi:[0,1]
	v_mov_b32_e32 v49, v39
	v_pk_add_f32 v[38:39], v[2:3], v[2:3] op_sel:[0,1] op_sel_hi:[0,1]
	v_pk_mul_f32 v[40:41], v[72:73], v[40:41]
	v_pk_add_f32 v[10:11], v[104:105], v[52:53] neg_lo:[0,1] neg_hi:[0,1]
	v_pk_fma_f32 v[46:47], v[68:69], v[38:39], v[40:41] neg_lo:[0,0,1] neg_hi:[0,0,1]
	v_pk_fma_f32 v[38:39], v[70:71], v[38:39], v[40:41]
	v_pk_add_f32 v[4:5], v[4:5], v[4:5] op_sel:[0,1] op_sel_hi:[0,1] neg_lo:[0,1] neg_hi:[0,1]
	v_mov_b32_e32 v47, v39
	v_pk_mul_f32 v[38:39], v[84:85], v[10:11]
	v_pk_add_f32 v[2:3], v[2:3], v[2:3] op_sel:[0,1] op_sel_hi:[0,1] neg_lo:[0,1] neg_hi:[0,1]
	v_pk_fma_f32 v[40:41], v[86:87], v[10:11], v[38:39] op_sel:[0,0,1] op_sel_hi:[1,1,0] neg_lo:[0,0,1] neg_hi:[0,0,1]
	v_pk_fma_f32 v[10:11], v[86:87], v[10:11], v[38:39] op_sel:[0,0,1] op_sel_hi:[1,1,0]
	s_nop 0
	v_mov_b32_e32 v41, v11
	v_pk_mul_f32 v[10:11], v[80:81], v[14:15]
	s_nop 0
	v_pk_fma_f32 v[38:39], v[78:79], v[14:15], v[10:11] op_sel:[0,0,1] op_sel_hi:[1,1,0] neg_lo:[0,0,1] neg_hi:[0,0,1]
	v_pk_fma_f32 v[10:11], v[78:79], v[14:15], v[10:11] op_sel:[0,0,1] op_sel_hi:[1,1,0]
	s_nop 0
	v_mov_b32_e32 v39, v11
	v_pk_add_f32 v[10:11], v[26:27], v[26:27] op_sel:[0,1] op_sel_hi:[0,1]
	v_pk_mul_f32 v[10:11], v[90:91], v[10:11]
	s_nop 0
	v_pk_fma_f32 v[14:15], v[82:83], v[4:5], v[10:11] neg_lo:[0,0,1] neg_hi:[0,0,1]
	v_pk_fma_f32 v[4:5], v[88:89], v[4:5], v[10:11]
	s_nop 0
	v_mov_b32_e32 v15, v5
	v_pk_add_f32 v[4:5], v[8:9], v[8:9] op_sel:[0,1] op_sel_hi:[0,1]
	v_pk_mul_f32 v[4:5], v[92:93], v[4:5]
	s_nop 0
	v_pk_fma_f32 v[8:9], v[76:77], v[2:3], v[4:5] neg_lo:[0,0,1] neg_hi:[0,0,1]
	v_pk_fma_f32 v[2:3], v[74:75], v[2:3], v[4:5]
	s_nop 0
	v_mov_b32_e32 v9, v3
	v_pk_mul_f32 v[2:3], v[98:99], v[20:21] op_sel:[0,1]
	s_nop 0
	v_pk_fma_f32 v[4:5], v[94:95], v[12:13], v[2:3] neg_lo:[0,0,1] neg_hi:[0,0,1]
	v_pk_fma_f32 v[2:3], v[96:97], v[12:13], v[2:3] op_sel_hi:[1,0,1]
	s_nop 0
	v_mov_b32_e32 v5, v3
	v_pk_mul_f32 v[2:3], v[108:109], v[18:19] op_sel:[0,1]
	s_nop 0
	v_pk_fma_f32 v[10:11], v[100:101], v[6:7], v[2:3] neg_lo:[0,0,1] neg_hi:[0,0,1]
	v_pk_fma_f32 v[2:3], v[102:103], v[6:7], v[2:3] op_sel_hi:[1,0,1]
	s_nop 0
	v_mov_b32_e32 v11, v3
	ds_write2_b64 v60, v[16:17], v[48:49] offset1:66
	ds_write2_b64 v60, v[30:31], v[44:45] offset0:132 offset1:198
	ds_write2_b64 v65, v[32:33], v[46:47] offset0:8 offset1:74
	ds_write2_b64 v65, v[28:29], v[42:43] offset0:140 offset1:206
	ds_write2_b64 v67, v[24:25], v[40:41] offset0:16 offset1:82
	ds_write2_b64 v67, v[22:23], v[38:39] offset0:148 offset1:214
	ds_write2_b64 v185, v[14:15], v[8:9] offset0:24 offset1:90
	ds_write2_b64 v185, v[4:5], v[10:11] offset0:156 offset1:222
	s_waitcnt lgkmcnt(0)
	s_barrier
	s_waitcnt vmcnt(32)
	s_and_saveexec_b64 s[48:49], vcc
	s_cbranch_execz .LBB0_661
	v_cvt_pk_bf16_f32 v2, v145, v147
	v_cvt_pk_bf16_f32 v3, v146, v149
	v_cvt_pk_bf16_f32 v4, v148, v151
	v_cvt_pk_bf16_f32 v5, v150, v152
	v_lshl_add_u64 v[6:7], v[34:35], 0, s[22:23]
	global_store_dwordx4 v[34:35], v[2:5], off nt
	s_nop 1
	v_cvt_pk_bf16_f32 v2, v137, v139
	v_cvt_pk_bf16_f32 v3, v138, v141
	v_cvt_pk_bf16_f32 v4, v140, v143
	v_cvt_pk_bf16_f32 v5, v142, v144
	s_lshl_b32 s12, s44, 1
	global_store_dwordx4 v[6:7], v[2:5], off nt
	s_nop 1
	v_cvt_pk_bf16_f32 v2, v129, v131
	v_cvt_pk_bf16_f32 v3, v130, v133
	v_cvt_pk_bf16_f32 v4, v132, v135
	v_cvt_pk_bf16_f32 v5, v134, v136
	v_lshl_add_u64 v[8:9], v[34:35], 0, s[12:13]
	global_store_dwordx4 v[8:9], v[2:5], off nt
	s_nop 1
	v_cvt_pk_bf16_f32 v2, v121, v123
	v_cvt_pk_bf16_f32 v3, v122, v125
	v_cvt_pk_bf16_f32 v4, v124, v127
	v_cvt_pk_bf16_f32 v5, v126, v128
	v_lshl_add_u64 v[6:7], v[6:7], 0, s[12:13]
	global_store_dwordx4 v[6:7], v[2:5], off nt
	s_nop 1

; __device__ __forceinline__ KP kparams() { KP q = (KP)__builtin_amdgcn_kernarg_segment_ptr(); asm volatile("" : "+s"(q)); return q; }
; FFT_HD cf2 mk2(float x, float y) { return (cf2){x, y}; }
; FFT_HD void fft_sincos(float frac, float& s, float& c) { s = __builtin_amdgcn_sinf(frac); c = __builtin_amdgcn_cosf(frac); }
; FFT_HD cf2 cmul(cf2 a, cf2 b) { return mk2(a.x * b.x - a.y * b.y, a.x * b.y + a.y * b.x); }
; template <int BANK> __device__ __forceinline__ void bg_issue1(BgState& b, int wg, int NW, int lane) {
;     KP kp = kparams();
;     const float* src; int ldS; bf16_t* dst; int o2;
;     bg_decode(b.st, wg, NW, lane, kp, src, ldS, dst, o2);
;     b.dst[BANK] = dst; b.o2[BANK] = o2;
;     asm volatile("s_nop 6" ::: "memory");
; #pragma unroll
;     for (int i = 0; i < 8; ++i) { const float* p = src + (size_t)i * ldS;
;         asm volatile("global_load_dword %0, %4, off\n\tglobal_load_dword %1, %4, off offset:256\n\tglobal_load_dword %2, %4, off offset:512\n\tglobal_load_dword %3, %4, off offset:768"
;                      : "=&v"(b.r[(BANK * 8 + i) * 4 + 0]), "=&v"(b.r[(BANK * 8 + i) * 4 + 1]), "=&v"(b.r[(BANK * 8 + i) * 4 + 2]), "=&v"(b.r[(BANK * 8 + i) * 4 + 3]) : "v"(p) : "memory"); }
;     b.st += 1;
; }
; FFT_HD void fft_gen_tw(float frac, cf2 (&tw)[16]) {
;     float sn, cs; fft_sincos(frac, sn, cs);
;     tw[1] = mk2(cs, -sn);
;     tw[2] = cmul(tw[1], tw[1]); tw[3] = cmul(tw[2], tw[1]); tw[4] = cmul(tw[2], tw[2]); tw[5] = cmul(tw[4], tw[1]); tw[6] = cmul(tw[4], tw[2]); tw[7] = cmul(tw[4], tw[3]);
;     tw[8] = cmul(tw[4], tw[4]);
; #pragma unroll
;     for (int j = 9; j < 16; ++j) tw[j] = cmul(tw[8], tw[j - 8]);
; }
; template <bool INV, int lS, class ZP> FFT_HD void fft_r16_pass(ZP z, int tid) {
;     constexpr int S = 1 << lS, STEP = (S >= 64) ? S + S / 32 : S;
;     constexpr float inv = 1.0f / (float)(16 * S);
;     cf2 tw[16];
;     if (lS != 10) {
;         fft_gen_tw((float)(tid & (S - 1)) * inv, tw);
;         const int w0 = tid, w1 = tid + 512;
;         const int pb0 = PADI(((w0 >> lS) << (lS + 4)) + (w0 & (S - 1))), pb1 = PADI(((w1 >> lS) << (lS + 4)) + (w1 & (S - 1)));
;         cf2 x[16], y[16];
; #pragma unroll
;         for (int j = 0; j < 16; ++j) x[j] = z[pb0 + j * STEP];
; #pragma unroll
;         for (int j = 0; j < 16; ++j) y[j] = z[pb1 + j * STEP];
.LBB0_671:
	s_nop 6
	s_lshl_b32 s12, s44, 2
	global_load_dword v145, v[2:3], off nt
	global_load_dword v137, v[2:3], off offset:256 nt
	global_load_dword v129, v[2:3], off offset:512 nt
	global_load_dword v121, v[2:3], off offset:768 nt
	v_lshl_add_u64 v[2:3], v[2:3], 0, s[12:13]
	v_and_b32_e32 v14, 3, v120
	global_load_dword v147, v[2:3], off nt
	global_load_dword v139, v[2:3], off offset:256 nt
	global_load_dword v131, v[2:3], off offset:512 nt
	global_load_dword v123, v[2:3], off offset:768 nt
	v_lshl_add_u64 v[2:3], v[2:3], 0, s[12:13]
	v_cvt_f32_ubyte0_e32 v4, v14
	global_load_dword v146, v[2:3], off nt
	global_load_dword v138, v[2:3], off offset:256 nt
	global_load_dword v130, v[2:3], off offset:512 nt
	global_load_dword v122, v[2:3], off offset:768 nt
	v_lshl_add_u64 v[2:3], v[2:3], 0, s[12:13]
	v_mul_f32_e32 v4, 0x3c800000, v4
	global_load_dword v149, v[2:3], off nt
	global_load_dword v141, v[2:3], off offset:256 nt
	global_load_dword v133, v[2:3], off offset:512 nt
	global_load_dword v125, v[2:3], off offset:768 nt
	v_lshl_add_u64 v[2:3], v[2:3], 0, s[12:13]
	v_sin_f32_e32 v39, v4
	v_cos_f32_e32 v38, v4
	global_load_dword v148, v[2:3], off nt
	global_load_dword v140, v[2:3], off offset:256 nt
	global_load_dword v132, v[2:3], off offset:512 nt
	global_load_dword v124, v[2:3], off offset:768 nt
	v_lshl_add_u64 v[2:3], v[2:3], 0, s[12:13]
	global_load_dword v150, v[2:3], off nt
	global_load_dword v142, v[2:3], off offset:256 nt
	global_load_dword v134, v[2:3], off offset:512 nt
	global_load_dword v126, v[2:3], off offset:768 nt
	v_lshl_add_u64 v[2:3], v[2:3], 0, s[12:13]
	global_load_dword v151, v[2:3], off nt
	global_load_dword v143, v[2:3], off offset:256 nt
	global_load_dword v135, v[2:3], off offset:512 nt
	global_load_dword v127, v[2:3], off offset:768 nt
	v_lshl_add_u64 v[2:3], v[2:3], 0, s[12:13]
	global_load_dword v152, v[2:3], off nt
	global_load_dword v144, v[2:3], off offset:256 nt
	global_load_dword v136, v[2:3], off offset:512 nt
	global_load_dword v128, v[2:3], off offset:768 nt
	v_pk_mul_f32 v[2:3], v[38:39], v[38:39]
	v_mul_f32_e64 v4, v38, -v39
	v_mov_b32_e32 v5, v2
	v_mov_b32_e32 v2, v4
	v_pk_add_f32 v[192:193], v[4:5], v[2:3]
	v_pk_add_f32 v[202:203], v[4:5], v[2:3] neg_lo:[0,1] neg_hi:[0,1]
	v_mov_b32_e32 v46, v192
	v_mov_b32_e32 v47, v203
	v_pk_mul_f32 v[8:9], v[46:47], v[46:47]
	v_pk_mul_f32 v[10:11], v[202:203], v[46:47] op_sel:[1,0] op_sel_hi:[0,1]
	v_mov_b32_e32 v2, v39
	v_mov_b32_e32 v3, v38
	v_pk_mov_b32 v[12:13], v[8:9], v[10:11] op_sel:[1,0]
	v_mov_b32_e32 v9, v10
	v_pk_mul_f32 v[4:5], v[2:3], v[46:47]
	v_pk_mul_f32 v[6:7], v[38:39], v[46:47]
	v_pk_add_f32 v[48:49], v[12:13], v[8:9] neg_lo:[0,1] neg_hi:[0,1]
	v_pk_add_f32 v[68:69], v[12:13], v[8:9]
	v_mov_b32_e32 v50, v48
	v_mov_b32_e32 v51, v69
	v_mov_b32_e32 v8, v6
	v_mov_b32_e32 v9, v5
	v_pk_mov_b32 v[4:5], v[6:7], v[4:5] op_sel:[1,0]
	v_pk_mul_f32 v[6:7], v[50:51], v[68:69] op_sel:[0,1] op_sel_hi:[1,0]
	v_pk_add_f32 v[72:73], v[8:9], v[4:5] neg_lo:[0,1] neg_hi:[0,1]
	v_pk_add_f32 v[70:71], v[8:9], v[4:5]
	v_pk_mul_f32 v[4:5], v[50:51], v[50:51]
	s_mov_b32 s44, s27
	v_mov_b32_e32 v7, v4
	v_mov_b32_e32 v4, v6
	v_pk_add_f32 v[76:77], v[6:7], v[4:5]
	v_pk_add_f32 v[74:75], v[6:7], v[4:5] neg_lo:[0,1] neg_hi:[0,1]
	v_mov_b32_e32 v54, v76
	v_mov_b32_e32 v55, v75
	v_pk_mul_f32 v[84:85], v[2:3], v[54:55]
	v_and_b32_e32 v2, 0xffffffc0, v184
	v_ashrrev_i32_e32 v3, 5, v184
	v_add_u32_e32 v4, 0x2000, v2
	v_lshlrev_b32_e32 v2, 3, v2
	v_lshlrev_b32_e32 v5, 3, v14
	v_lshlrev_b32_e32 v3, 3, v3
	v_add3_u32 v2, 0, v2, v5
	v_and_b32_e32 v3, -16, v3
	v_add_u32_e32 v65, v2, v3
	ds_read2_b64 v[98:101], v65 offset1:4
	ds_read2_b64 v[102:105], v65 offset0:8 offset1:12
	ds_read2_b64 v[106:109], v65 offset0:16 offset1:20
	ds_read2_b64 v[110:113], v65 offset0:24 offset1:28
	ds_read2_b64 v[114:117], v65 offset0:32 offset1:36
	ds_read2_b64 v[184:187], v65 offset0:40 offset1:44
	ds_read2_b64 v[188:191], v65 offset0:48 offset1:52
	ds_read2_b64 v[198:201], v65 offset0:56 offset1:60
	s_waitcnt lgkmcnt(5)
	v_pk_mov_b32 v[204:205], v[100:101], v[108:109] op_sel:[1,0]
	s_waitcnt lgkmcnt(3)
	v_mov_b32_e32 v208, v116
	s_waitcnt lgkmcnt(2)
	v_mov_b32_e32 v212, v184
	s_waitcnt lgkmcnt(1)
	v_pk_mov_b32 v[206:207], v[116:117], v[190:191] op_sel:[1,0]
	v_mov_b32_e32 v209, v191
	v_pk_add_f32 v[204:205], v[204:205], v[206:207] neg_lo:[0,1] neg_hi:[0,1]
	v_mov_b32_e32 v206, v100
	v_mov_b32_e32 v207, v109
	v_pk_add_f32 v[206:207], v[206:207], v[208:209] neg_lo:[0,1] neg_hi:[0,1]
	v_pk_mov_b32 v[208:209], v[102:103], v[110:111] op_sel:[1,0]
	s_waitcnt lgkmcnt(0)
; FFT_HD cf2 mk2(float x, float y) { return (cf2){x, y}; }
; FFT_HD cf2 cmul(cf2 a, cf2 b) { return mk2(a.x * b.x - a.y * b.y, a.x * b.y + a.y * b.x); }
; FFT_HD cf2 cadd(cf2 a, cf2 b) { return mk2(a.x + b.x, a.y + b.y); }
; FFT_HD cf2 csub(cf2 a, cf2 b) { return mk2(a.x - b.x, a.y - b.y); }
; template <bool INV> FFT_HD void dft4(cf2& a, cf2& b, cf2& c, cf2& d) {
;     const cf2 s0 = cadd(a, c), s1 = csub(a, c), s2 = cadd(b, d), s3 = csub(b, d);
;     a = cadd(s0, s2); c = csub(s0, s2);
;     const cf2 r = INV ? mk2(-s3.y, s3.x) : mk2(s3.y, -s3.x);
;     b = cadd(s1, r); d = csub(s1, r);
; }
; template <bool INV> FFT_HD void dft16(cf2 (&x)[16]) {
;     const float C1 = 0.9238795325112867f, S1 = 0.3826834323650898f, H = 0.7071067811865476f;
; #pragma unroll
;     for (int b = 0; b < 4; ++b) dft4<INV>(x[b], x[4 + b], x[8 + b], x[12 + b]);
;     const float s = INV ? -1.f : 1.f;
;     x[4 + 1] = cmul(x[4 + 1], mk2(C1, -s * S1)); x[8 + 1] = cmul(x[8 + 1], mk2(H, -s * H));   x[12 + 1] = cmul(x[12 + 1], mk2(S1, -s * C1));
;     x[4 + 2] = cmul(x[4 + 2], mk2(H, -s * H));   x[8 + 2] = cmul(x[8 + 2], mk2(0.f, -s));     x[12 + 2] = cmul(x[12 + 2], mk2(-H, -s * H));
;     x[4 + 3] = cmul(x[4 + 3], mk2(S1, -s * C1)); x[8 + 3] = cmul(x[8 + 3], mk2(-H, -s * H));  x[12 + 3] = cmul(x[12 + 3], mk2(-C1, s * S1));
; #pragma unroll
;     for (int c = 0; c < 4; ++c) dft4<INV>(x[4 * c], x[4 * c + 1], x[4 * c + 2], x[4 * c + 3]);
; #pragma unroll
;     for (int c = 0; c < 4; ++c)
; #pragma unroll
;         for (int d = c + 1; d < 4; ++d) { const cf2 t = x[4 * c + d]; x[4 * c + d] = x[4 * d + c]; x[4 * d + c] = t; }
; }
	v_pk_mov_b32 v[210:211], v[184:185], v[198:199] op_sel:[1,0]
	v_mov_b32_e32 v213, v199
	v_pk_add_f32 v[208:209], v[208:209], v[210:211] neg_lo:[0,1] neg_hi:[0,1]
	v_mov_b32_e32 v210, v102
	v_mov_b32_e32 v211, v111
	v_pk_add_f32 v[210:211], v[210:211], v[212:213] neg_lo:[0,1] neg_hi:[0,1]
	v_pk_mov_b32 v[212:213], v[104:105], v[112:113] op_sel:[1,0]
	v_pk_mov_b32 v[214:215], v[186:187], v[200:201] op_sel:[1,0]
	v_mov_b32_e32 v216, v186
	v_pk_add_f32 v[212:213], v[212:213], v[214:215] neg_lo:[0,1] neg_hi:[0,1]
	v_mov_b32_e32 v214, v104
	v_mov_b32_e32 v215, v113
	v_mov_b32_e32 v217, v201
	v_pk_add_f32 v[214:215], v[214:215], v[216:217] neg_lo:[0,1] neg_hi:[0,1]
	v_mov_b32_e32 v217, v212
	v_mov_b32_e32 v216, v214
	v_mov_b32_e32 v218, v215
	v_mov_b32_e32 v219, v213
	v_add_f32_e32 v56, v210, v211
	v_pk_add_f32 v[220:221], v[216:217], v[218:219] neg_lo:[0,1] neg_hi:[0,1]
	v_pk_add_f32 v[216:217], v[216:217], v[218:219]
	v_mul_f32_e32 v232, 0x3f3504f3, v56
	v_mov_b32_e32 v221, v217
	v_mul_f32_e32 v56, 0x3ec3ef15, v217
	v_pk_add_f32 v[226:227], v[206:207], v[206:207] op_sel:[0,1] op_sel_hi:[0,1]
	s_mov_b32 s45, s26
	v_pk_add_f32 v[214:215], v[214:215], v[214:215] op_sel:[0,1] op_sel_hi:[0,1]
	v_sub_f32_e32 v67, v208, v209
	v_pk_fma_f32 v[218:219], v[220:221], s[30:31], v[56:57] op_sel_hi:[1,1,0] neg_lo:[0,0,1] neg_hi:[0,0,1]
	v_mul_f32_e32 v236, 0x3ec3ef15, v220
	v_mul_f32_e32 v237, 0x3f6c835e, v217
	v_pk_add_f32 v[216:217], v[98:99], v[114:115]
	v_pk_add_f32 v[220:221], v[106:107], v[188:189]
	v_pk_add_f32 v[98:99], v[98:99], v[114:115] neg_lo:[0,1] neg_hi:[0,1]
	v_pk_add_f32 v[106:107], v[106:107], v[188:189] neg_lo:[0,1] neg_hi:[0,1]
	v_pk_mul_f32 v[226:227], v[226:227], s[26:27]
	v_pk_add_f32 v[228:229], v[204:205], v[204:205] op_sel:[0,1] op_sel_hi:[0,1] neg_lo:[0,1] neg_hi:[0,1]
	v_pk_mul_f32 v[214:215], v[214:215], s[44:45]
	v_pk_add_f32 v[212:213], v[212:213], v[212:213] op_sel:[0,1] op_sel_hi:[0,1] neg_lo:[0,1] neg_hi:[0,1]
	v_pk_mov_b32 v[114:115], v[106:107], v[106:107] op_sel:[1,0]
	v_pk_add_f32 v[188:189], v[98:99], v[106:107] op_sel:[0,1] op_sel_hi:[1,0]
	v_pk_add_f32 v[106:107], v[98:99], v[106:107] op_sel:[0,1] op_sel_hi:[1,0] neg_lo:[0,1] neg_hi:[0,1]
	v_pk_fma_f32 v[230:231], v[228:229], s[44:45], v[226:227]
	v_pk_fma_f32 v[226:227], v[228:229], s[44:45], v[226:227] neg_lo:[0,0,1] neg_hi:[0,0,1]
	v_fmamk_f32 v228, v67, 0x3f3504f3, v232
	v_fma_f32 v232, v67, s25, -v232
	v_pk_fma_f32 v[234:235], v[212:213], s[26:27], v[214:215]
	v_pk_fma_f32 v[212:213], v[212:213], s[26:27], v[214:215] neg_lo:[0,0,1] neg_hi:[0,0,1]
	v_mov_b32_e32 v224, v188
	v_mov_b32_e32 v225, v107
	v_mov_b32_e32 v226, v230
	v_mov_b32_e32 v233, v232
	v_mov_b32_e32 v229, v232
	v_mov_b32_e32 v212, v234
	v_pk_add_f32 v[214:215], v[224:225], v[228:229]
	v_pk_add_f32 v[224:225], v[226:227], v[212:213]
	v_pk_mov_b32 v[106:107], v[106:107], v[230:231] op_sel:[1,0]
	v_pk_mov_b32 v[230:231], v[232:233], v[234:235] op_sel:[1,0]
	v_mov_b32_e32 v226, v188
	v_pk_add_f32 v[230:231], v[106:107], v[230:231] neg_lo:[0,1] neg_hi:[0,1]
	v_mov_b32_e32 v229, v213
	v_pk_add_f32 v[106:107], v[214:215], v[224:225]
	v_mov_b32_e32 v56, v39
	v_pk_add_f32 v[212:213], v[226:227], v[228:229] neg_lo:[0,1] neg_hi:[0,1]
	v_pk_mul_f32 v[226:227], v[56:57], v[106:107] op_sel_hi:[0,1]
	v_pk_add_f32 v[100:101], v[100:101], v[116:117]
	v_pk_add_f32 v[108:109], v[108:109], v[190:191]
	v_pk_add_f32 v[102:103], v[102:103], v[184:185]
	v_pk_add_f32 v[184:185], v[110:111], v[198:199]
	v_pk_add_f32 v[104:105], v[104:105], v[186:187]
	v_pk_add_f32 v[112:113], v[112:113], v[200:201]
	v_pk_fma_f32 v[228:229], v[38:39], v[106:107], v[226:227] op_sel:[0,0,1] op_sel_hi:[1,1,0]
	v_pk_fma_f32 v[106:107], v[38:39], v[106:107], v[226:227] op_sel:[0,0,1] op_sel_hi:[0,1,0] neg_lo:[0,0,1] neg_hi:[0,0,1]
	v_pk_add_f32 v[222:223], v[216:217], v[220:221]
	v_pk_add_f32 v[190:191], v[102:103], v[184:185]
	v_mov_b32_e32 v229, v107
	v_pk_add_f32 v[106:107], v[216:217], v[220:221] neg_lo:[0,1] neg_hi:[0,1]
	v_pk_add_f32 v[102:103], v[102:103], v[184:185] neg_lo:[0,1] neg_hi:[0,1]
	v_mov_b32_e32 v184, v104
	v_mov_b32_e32 v185, v101
	v_mov_b32_e32 v216, v112
	v_mov_b32_e32 v217, v109
	v_pk_add_f32 v[184:185], v[184:185], v[216:217] neg_lo:[0,1] neg_hi:[0,1]
	v_mov_b32_e32 v216, v100
	v_mov_b32_e32 v217, v104
	v_mov_b32_e32 v220, v108
	v_mov_b32_e32 v221, v112
	v_pk_add_f32 v[116:117], v[100:101], v[108:109]
	v_pk_add_f32 v[186:187], v[104:105], v[112:113]
	v_pk_add_f32 v[216:217], v[216:217], v[220:221] neg_lo:[0,1] neg_hi:[0,1]
	v_mov_b32_e32 v220, v101
	v_mov_b32_e32 v221, v105
	v_mov_b32_e32 v226, v109
	v_mov_b32_e32 v227, v113
	v_pk_mov_b32 v[100:101], v[104:105], v[100:101] op_sel:[1,0]
	v_pk_mov_b32 v[104:105], v[112:113], v[108:109] op_sel:[1,0]
	v_pk_add_f32 v[220:221], v[220:221], v[226:227] neg_lo:[0,1] neg_hi:[0,1]
	v_pk_add_f32 v[100:101], v[100:101], v[104:105] neg_lo:[0,1] neg_hi:[0,1]
	v_pk_fma_f32 v[104:105], v[102:103], 0, v[102:103] op_sel:[0,0,1] op_sel_hi:[1,0,0]
	v_pk_fma_f32 v[102:103], v[102:103], 0, v[102:103] op_sel:[0,0,1] op_sel_hi:[1,0,0] neg_lo:[0,0,1] neg_hi:[0,0,1]
	s_mov_b32 s50, s25
	s_mov_b32 s51, s24
	v_mov_b32_e32 v105, v103
	v_pk_mul_f32 v[102:103], v[220:221], s[50:51]
	v_pk_mul_f32 v[100:101], v[100:101], s[24:25]
	v_pk_fma_f32 v[102:103], v[216:217], s[50:51], v[102:103]
	v_pk_fma_f32 v[100:101], v[184:185], s[24:25], v[100:101] neg_lo:[0,0,1] neg_hi:[0,0,1]
	v_pk_add_f32 v[108:109], v[106:107], v[104:105]
	v_pk_add_f32 v[184:185], v[102:103], v[100:101]
	v_pk_mov_b32 v[44:45], v[202:203], v[192:193] op_sel:[1,0]
	v_pk_add_f32 v[112:113], v[108:109], v[184:185]
	s_mov_b32 s56, s26
; FFT_HD cf2 mk2(float x, float y) { return (cf2){x, y}; }
; FFT_HD cf2 cmul(cf2 a, cf2 b) { return mk2(a.x * b.x - a.y * b.y, a.x * b.y + a.y * b.x); }
; FFT_HD cf2 cadd(cf2 a, cf2 b) { return mk2(a.x + b.x, a.y + b.y); }
; FFT_HD cf2 csub(cf2 a, cf2 b) { return mk2(a.x - b.x, a.y - b.y); }
; template <bool INV> FFT_HD void dft4(cf2& a, cf2& b, cf2& c, cf2& d) {
;     const cf2 s0 = cadd(a, c), s1 = csub(a, c), s2 = cadd(b, d), s3 = csub(b, d);
;     a = cadd(s0, s2); c = csub(s0, s2);
;     const cf2 r = INV ? mk2(-s3.y, s3.x) : mk2(s3.y, -s3.x);
;     b = cadd(s1, r); d = csub(s1, r);
; }
; template <bool INV> FFT_HD void dft16(cf2 (&x)[16]) {
;     const float C1 = 0.9238795325112867f, S1 = 0.3826834323650898f, H = 0.7071067811865476f;
; #pragma unroll
;     for (int b = 0; b < 4; ++b) dft4<INV>(x[b], x[4 + b], x[8 + b], x[12 + b]);
;     const float s = INV ? -1.f : 1.f;
;     x[4 + 1] = cmul(x[4 + 1], mk2(C1, -s * S1)); x[8 + 1] = cmul(x[8 + 1], mk2(H, -s * H));   x[12 + 1] = cmul(x[12 + 1], mk2(S1, -s * C1));
;     x[4 + 2] = cmul(x[4 + 2], mk2(H, -s * H));   x[8 + 2] = cmul(x[8 + 2], mk2(0.f, -s));     x[12 + 2] = cmul(x[12 + 2], mk2(-H, -s * H));
;     x[4 + 3] = cmul(x[4 + 3], mk2(S1, -s * C1)); x[8 + 3] = cmul(x[8 + 3], mk2(-H, -s * H));  x[12 + 3] = cmul(x[12 + 3], mk2(-C1, s * S1));
; #pragma unroll
;     for (int c = 0; c < 4; ++c) dft4<INV>(x[4 * c], x[4 * c + 1], x[4 * c + 2], x[4 * c + 3]);
; #pragma unroll
;     for (int c = 0; c < 4; ++c)
; #pragma unroll
;         for (int d = c + 1; d < 4; ++d) { const cf2 t = x[4 * c + d]; x[4 * c + d] = x[4 * d + c]; x[4 * d + c] = t; }
; }
; template <bool INV, int lS, class ZP> FFT_HD void fft_r16_pass(ZP z, int tid) {
;     ...
;         dft16<INV>(x);
;         if (!INV) {
; #pragma unroll
;             for (int j = 1; j < 16; ++j) x[j] = cmul(x[j], tw[j]);
;         }
	v_pk_mul_f32 v[192:193], v[192:193], v[112:113] op_sel:[0,1] op_sel_hi:[0,0]
	v_pk_fma_f32 v[216:217], v[202:203], v[112:113], v[192:193] op_sel:[1,0,0] neg_lo:[0,0,1] neg_hi:[0,0,1]
	v_pk_fma_f32 v[112:113], v[202:203], v[112:113], v[192:193] op_sel:[1,0,0]
	v_mov_b32_e32 v192, v204
	v_mov_b32_e32 v217, v113
	v_mov_b32_e32 v112, v206
	v_mov_b32_e32 v113, v210
	v_mov_b32_e32 v210, v207
	v_mov_b32_e32 v193, v208
	v_mov_b32_e32 v208, v205
	v_pk_add_f32 v[112:113], v[112:113], v[210:211] neg_lo:[0,1] neg_hi:[0,1]
	v_pk_add_f32 v[192:193], v[192:193], v[208:209]
	s_mov_b32 s57, s24
	v_pk_mov_b32 v[202:203], v[112:113], v[192:193] op_sel:[1,0]
	v_pk_mul_f32 v[204:205], v[192:193], s[56:57]
	v_pk_mov_b32 v[192:193], v[192:193], v[112:113] op_sel:[1,0]
	s_mov_b32 s28, s25
	s_mov_b32 s52, s27
	s_mov_b32 s53, s24
	s_mov_b32 s54, s24
	s_mov_b32 s55, s27
	v_pk_mul_f32 v[192:193], v[192:193], s[28:29]
	v_mov_b32_e32 v99, v236
	v_mov_b32_e32 v115, v237
	v_pk_fma_f32 v[192:193], v[202:203], s[54:55], v[192:193]
	v_pk_fma_f32 v[202:203], v[112:113], s[52:53], v[204:205]
	v_pk_add_f32 v[98:99], v[98:99], v[114:115] neg_lo:[0,1] neg_hi:[0,1]
	v_mov_b32_e32 v188, v218
	v_pk_add_f32 v[204:205], v[192:193], v[98:99]
	v_pk_add_f32 v[206:207], v[202:203], v[188:189]
	v_mov_b32_e32 v42, v72
	v_pk_add_f32 v[112:113], v[206:207], v[204:205]
	v_pk_mov_b32 v[40:41], v[70:71], v[72:73] op_sel:[1,0]
	v_pk_mul_f32 v[72:73], v[72:73], v[112:113] op_sel:[0,1] op_sel_hi:[0,0]
	v_mov_b32_e32 v43, v71
	v_pk_fma_f32 v[208:209], v[70:71], v[112:113], v[72:73] op_sel:[1,0,0] neg_lo:[0,0,1] neg_hi:[0,0,1]
	v_pk_fma_f32 v[70:71], v[70:71], v[112:113], v[72:73] op_sel:[1,0,0]
	v_pk_add_f32 v[72:73], v[116:117], v[186:187] neg_lo:[0,1] neg_hi:[0,1]
	v_mov_b32_e32 v209, v71
	v_pk_add_f32 v[70:71], v[222:223], v[190:191] neg_lo:[0,1] neg_hi:[0,1]
	v_pk_add_f32 v[198:199], v[222:223], v[190:191]
	v_pk_add_f32 v[200:201], v[116:117], v[186:187]
	v_pk_add_f32 v[186:187], v[70:71], v[72:73] op_sel:[0,1] op_sel_hi:[1,0]
	v_pk_add_f32 v[190:191], v[70:71], v[72:73] op_sel:[0,1] op_sel_hi:[1,0] neg_lo:[0,1] neg_hi:[0,1]
	v_mov_b32_e32 v70, v186
	v_pk_mov_b32 v[72:73], v[190:191], v[186:187] op_sel:[1,0]
	v_mov_b32_e32 v71, v191
	v_pk_mov_b32 v[112:113], v[68:69], v[48:49] op_sel:[1,0]
	v_pk_mul_f32 v[68:69], v[68:69], v[72:73] op_sel:[1,0]
	v_pk_add_f32 v[116:117], v[230:231], v[230:231] op_sel:[0,1] op_sel_hi:[0,1] neg_lo:[0,1] neg_hi:[0,1]
	v_pk_fma_f32 v[210:211], v[48:49], v[186:187], v[68:69] neg_lo:[0,0,1] neg_hi:[0,0,1]
	v_pk_fma_f32 v[68:69], v[48:49], v[70:71], v[68:69] op_sel_hi:[0,1,1]
	v_pk_mul_f32 v[70:71], v[56:57], v[112:113] op_sel_hi:[0,1]
	v_mov_b32_e32 v211, v69
	v_pk_fma_f32 v[68:69], v[38:39], v[50:51], v[70:71] op_sel_hi:[0,1,1]
	v_pk_fma_f32 v[72:73], v[38:39], v[50:51], v[70:71] op_sel_hi:[0,1,1] neg_lo:[0,0,1] neg_hi:[0,0,1]
	v_mov_b32_e32 v71, v73
	v_pk_mov_b32 v[72:73], v[72:73], v[68:69] op_sel:[1,0]
	v_pk_add_f32 v[104:105], v[106:107], v[104:105] neg_lo:[0,1] neg_hi:[0,1]
	v_pk_mov_b32 v[106:107], v[100:101], v[102:103] op_sel:[1,0]
	v_pk_mov_b32 v[100:101], v[102:103], v[100:101] op_sel:[1,0]
	v_mov_b32_e32 v70, v68
	v_pk_add_f32 v[114:115], v[212:213], v[212:213] op_sel:[0,1] op_sel_hi:[0,1]
	v_pk_mul_f32 v[116:117], v[72:73], v[116:117]
	v_pk_add_f32 v[100:101], v[106:107], v[100:101] neg_lo:[0,1] neg_hi:[0,1]
	v_pk_mul_f32 v[96:97], v[46:47], v[50:51]
	v_pk_fma_f32 v[220:221], v[68:69], v[114:115], v[116:117] neg_lo:[0,0,1] neg_hi:[0,0,1]
	v_pk_fma_f32 v[114:115], v[70:71], v[114:115], v[116:117]
	v_pk_add_f32 v[102:103], v[104:105], v[100:101]
	v_pk_add_f32 v[100:101], v[104:105], v[100:101] neg_lo:[0,1] neg_hi:[0,1]
	v_pk_mul_f32 v[94:95], v[44:45], v[50:51]
	v_mov_b32_e32 v221, v115
	v_pk_add_f32 v[114:115], v[96:97], v[96:97] op_sel:[0,1] op_sel_hi:[0,1]
	v_pk_mov_b32 v[96:97], v[100:101], v[102:103] op_sel:[1,0]
	v_mov_b32_e32 v104, v102
	v_mov_b32_e32 v105, v101
	v_pk_mul_f32 v[96:97], v[114:115], v[96:97]
	v_pk_add_f32 v[116:117], v[94:95], v[94:95] op_sel:[0,1] op_sel_hi:[0,1] neg_lo:[0,1] neg_hi:[0,1]
	v_pk_fma_f32 v[222:223], v[116:117], v[102:103], v[96:97] neg_lo:[0,0,1] neg_hi:[0,0,1]
	v_pk_fma_f32 v[94:95], v[116:117], v[104:105], v[96:97]
	v_pk_mov_b32 v[96:97], v[98:99], v[218:219] op_sel:[1,0]
	v_mov_b32_e32 v223, v95
	v_pk_mov_b32 v[94:95], v[192:193], v[202:203] op_sel:[1,0]
	v_mov_b32_e32 v99, v189
	v_mov_b32_e32 v193, v203
	v_pk_add_f32 v[94:95], v[94:95], v[96:97] neg_lo:[0,1] neg_hi:[0,1]
	v_pk_add_f32 v[96:97], v[98:99], v[192:193] neg_lo:[0,1] neg_hi:[0,1]
	v_pk_mul_f32 v[92:93], v[50:51], v[42:43]
	v_pk_add_f32 v[188:189], v[96:97], v[94:95]
	v_pk_add_f32 v[192:193], v[96:97], v[94:95] neg_lo:[0,1] neg_hi:[0,1]
	v_pk_mul_f32 v[82:83], v[50:51], v[40:41]
	v_pk_add_f32 v[104:105], v[92:93], v[92:93] op_sel:[0,1] op_sel_hi:[0,1]
	v_pk_mov_b32 v[92:93], v[192:193], v[188:189] op_sel:[1,0]
	v_mov_b32_e32 v94, v188
	v_mov_b32_e32 v95, v193
	v_pk_mul_f32 v[92:93], v[104:105], v[92:93]
	v_pk_add_f32 v[106:107], v[82:83], v[82:83] op_sel:[0,1] op_sel_hi:[0,1] neg_lo:[0,1] neg_hi:[0,1]
	v_pk_fma_f32 v[202:203], v[106:107], v[188:189], v[92:93] neg_lo:[0,0,1] neg_hi:[0,0,1]
	v_pk_fma_f32 v[82:83], v[106:107], v[94:95], v[92:93]
	v_pk_mul_f32 v[90:91], v[38:39], v[54:55]
	v_mov_b32_e32 v203, v83
	v_pk_add_f32 v[82:83], v[198:199], v[200:201] neg_lo:[0,1] neg_hi:[0,1]
	v_pk_add_f32 v[110:111], v[198:199], v[200:201]
	v_pk_mul_f32 v[92:93], v[76:77], v[82:83] op_sel_hi:[0,1]
	v_pk_fma_f32 v[198:199], v[74:75], v[82:83], v[92:93] op_sel:[1,0,1] op_sel_hi:[1,1,0] neg_lo:[0,0,1] neg_hi:[0,0,1]
	v_pk_fma_f32 v[82:83], v[74:75], v[82:83], v[92:93] op_sel:[1,0,1] op_sel_hi:[1,1,0]
; FFT_HD cf2 mk2(float x, float y) { return (cf2){x, y}; }
; FFT_HD cf2 cmul(cf2 a, cf2 b) { return mk2(a.x * b.x - a.y * b.y, a.x * b.y + a.y * b.x); }
; FFT_HD cf2 cmulc(cf2 a, cf2 b) { return mk2(a.x * b.x + a.y * b.y, a.y * b.x - a.x * b.y); }
; FFT_HD cf2 cadd(cf2 a, cf2 b) { return mk2(a.x + b.x, a.y + b.y); }
; FFT_HD cf2 csub(cf2 a, cf2 b) { return mk2(a.x - b.x, a.y - b.y); }
; template <bool INV> FFT_HD void dft4(cf2& a, cf2& b, cf2& c, cf2& d) {
;     const cf2 s0 = cadd(a, c), s1 = csub(a, c), s2 = cadd(b, d), s3 = csub(b, d);
;     a = cadd(s0, s2); c = csub(s0, s2);
;     const cf2 r = INV ? mk2(-s3.y, s3.x) : mk2(s3.y, -s3.x);
;     b = cadd(s1, r); d = csub(s1, r);
; }
; template <bool INV> FFT_HD void dft16(cf2 (&x)[16]) {
;     const float C1 = 0.9238795325112867f, S1 = 0.3826834323650898f, H = 0.7071067811865476f;
; #pragma unroll
;     for (int b = 0; b < 4; ++b) dft4<INV>(x[b], x[4 + b], x[8 + b], x[12 + b]);
;     const float s = INV ? -1.f : 1.f;
;     x[4 + 1] = cmul(x[4 + 1], mk2(C1, -s * S1)); x[8 + 1] = cmul(x[8 + 1], mk2(H, -s * H));   x[12 + 1] = cmul(x[12 + 1], mk2(S1, -s * C1));
;     x[4 + 2] = cmul(x[4 + 2], mk2(H, -s * H));   x[8 + 2] = cmul(x[8 + 2], mk2(0.f, -s));     x[12 + 2] = cmul(x[12 + 2], mk2(-H, -s * H));
;     x[4 + 3] = cmul(x[4 + 3], mk2(S1, -s * C1)); x[8 + 3] = cmul(x[8 + 3], mk2(-H, -s * H));  x[12 + 3] = cmul(x[12 + 3], mk2(-C1, s * S1));
; #pragma unroll
;     for (int c = 0; c < 4; ++c) dft4<INV>(x[4 * c], x[4 * c + 1], x[4 * c + 2], x[4 * c + 3]);
; #pragma unroll
;     for (int c = 0; c < 4; ++c)
; #pragma unroll
;         for (int d = c + 1; d < 4; ++d) { const cf2 t = x[4 * c + d]; x[4 * c + d] = x[4 * d + c]; x[4 * d + c] = t; }
; }
; template <bool INV, int lS, class ZP> FFT_HD void fft_r16_pass(ZP z, int tid) {
;     ...
;         for (int j = 0; j < 16; ++j) x[j] = z[pb0 + j * STEP];
; #pragma unroll
;         for (int j = 0; j < 16; ++j) y[j] = z[pb1 + j * STEP];
;         if (INV) {
; #pragma unroll
;             for (int j = 1; j < 16; ++j) x[j] = cmulc(x[j], tw[j]);
;         }
;         dft16<INV>(x);
;         if (!INV) {
; #pragma unroll
;             for (int j = 1; j < 16; ++j) x[j] = cmul(x[j], tw[j]);
;         }
; #pragma unroll
;         for (int j = 0; j < 16; ++j) z[pb0 + j * STEP] = x[j];
	v_pk_add_f32 v[92:93], v[214:215], v[224:225] neg_lo:[0,1] neg_hi:[0,1]
	v_mov_b32_e32 v199, v83
	v_pk_add_f32 v[82:83], v[90:91], v[90:91] op_sel:[0,1] op_sel_hi:[0,1] neg_lo:[0,1] neg_hi:[0,1]
	v_pk_mov_b32 v[52:53], v[74:75], v[76:77] op_sel:[1,0]
	v_pk_mul_f32 v[90:91], v[82:83], v[92:93]
	v_pk_add_f32 v[84:85], v[84:85], v[84:85] op_sel:[1,0] op_sel_hi:[1,0]
	v_pk_mul_f32 v[88:89], v[46:47], v[52:53]
	v_pk_fma_f32 v[200:201], v[84:85], v[92:93], v[90:91] op_sel:[0,0,1] op_sel_hi:[1,1,0] neg_lo:[0,0,1] neg_hi:[0,0,1]
	v_pk_fma_f32 v[90:91], v[84:85], v[92:93], v[90:91] op_sel:[0,0,1] op_sel_hi:[1,1,0]
	v_pk_mul_f32 v[86:87], v[46:47], v[54:55]
	v_mov_b32_e32 v201, v91
	v_pk_add_f32 v[90:91], v[108:109], v[184:185] neg_lo:[0,1] neg_hi:[0,1]
	v_pk_add_f32 v[184:185], v[88:89], v[88:89] op_sel:[0,1] op_sel_hi:[0,1]
	v_pk_mul_f32 v[88:89], v[184:185], v[90:91]
	v_pk_add_f32 v[214:215], v[86:87], v[86:87] op_sel:[1,0] op_sel_hi:[1,0] neg_lo:[0,1] neg_hi:[0,1]
	v_pk_mul_f32 v[80:81], v[42:43], v[52:53]
	v_pk_fma_f32 v[218:219], v[214:215], v[90:91], v[88:89] op_sel:[0,0,1] op_sel_hi:[1,1,0] neg_lo:[0,0,1] neg_hi:[0,0,1]
	v_pk_fma_f32 v[86:87], v[214:215], v[90:91], v[88:89] op_sel:[0,0,1] op_sel_hi:[1,1,0]
	v_pk_mul_f32 v[78:79], v[42:43], v[54:55]
	v_mov_b32_e32 v219, v87
	v_mov_b32_e32 v86, v204
	v_mov_b32_e32 v87, v207
	v_mov_b32_e32 v207, v205
	v_pk_add_f32 v[86:87], v[86:87], v[206:207] neg_lo:[0,1] neg_hi:[0,1]
	v_pk_add_f32 v[80:81], v[80:81], v[80:81] op_sel:[0,1] op_sel_hi:[0,1]
	v_pk_mul_f32 v[88:89], v[80:81], v[86:87]
	v_pk_add_f32 v[78:79], v[78:79], v[78:79] op_sel:[1,0] op_sel_hi:[1,0] neg_lo:[0,1] neg_hi:[0,1]
	v_pk_add_f32 v[96:97], v[230:231], v[230:231] op_sel:[0,1] op_sel_hi:[0,1]
	v_pk_fma_f32 v[204:205], v[78:79], v[86:87], v[88:89] op_sel:[0,0,1] op_sel_hi:[1,1,0] neg_lo:[0,0,1] neg_hi:[0,0,1]
	v_pk_fma_f32 v[86:87], v[78:79], v[86:87], v[88:89] op_sel:[0,0,1] op_sel_hi:[1,1,0]
	v_pk_mul_f32 v[88:89], v[50:51], v[76:77] op_sel_hi:[1,0]
	v_mov_b32_e32 v205, v87
	v_pk_fma_f32 v[86:87], v[50:51], v[74:75], v[88:89] op_sel:[0,1,1] op_sel_hi:[1,1,0] neg_lo:[0,0,1] neg_hi:[0,0,1]
	v_pk_fma_f32 v[90:91], v[50:51], v[74:75], v[88:89] op_sel:[0,1,1] op_sel_hi:[1,1,0]
	v_mov_b32_e32 v88, v86
	v_mov_b32_e32 v89, v91
	v_pk_mov_b32 v[90:91], v[90:91], v[86:87] op_sel:[1,0]
	v_pk_add_f32 v[94:95], v[212:213], v[212:213] op_sel:[0,1] op_sel_hi:[0,1] neg_lo:[0,1] neg_hi:[0,1]
	v_pk_mul_f32 v[92:93], v[90:91], v[186:187] op_sel:[0,1]
	v_ashrrev_i32_e32 v3, 2, v4
	v_pk_fma_f32 v[186:187], v[86:87], v[190:191], v[92:93] neg_lo:[0,0,1] neg_hi:[0,0,1]
	v_pk_fma_f32 v[92:93], v[88:89], v[190:191], v[92:93] op_sel_hi:[1,0,1]
	v_add3_u32 v60, v2, v3, s71
	v_mov_b32_e32 v187, v93
	v_pk_mul_f32 v[92:93], v[76:77], v[70:71] op_sel_hi:[0,1]
	v_pk_fma_f32 v[76:77], v[74:75], v[70:71], v[92:93] op_sel:[1,0,1] op_sel_hi:[1,1,0] neg_lo:[0,0,1] neg_hi:[0,0,1]
	v_pk_fma_f32 v[92:93], v[74:75], v[70:71], v[92:93] op_sel:[1,0,1] op_sel_hi:[1,1,0]
	v_mov_b32_e32 v74, v76
	v_mov_b32_e32 v75, v93
	v_pk_mov_b32 v[92:93], v[92:93], v[76:77] op_sel:[1,0]
	ds_read2_b64 v[2:5], v60 offset1:4
	ds_read2_b64 v[18:21], v60 offset0:8 offset1:12
	ds_read2_b64 v[6:9], v60 offset0:16 offset1:20
	ds_read2_b64 v[22:25], v60 offset0:24 offset1:28
	ds_read2_b64 v[10:13], v60 offset0:32 offset1:36
	ds_read2_b64 v[26:29], v60 offset0:40 offset1:44
	ds_read2_b64 v[14:17], v60 offset0:48 offset1:52
	ds_read2_b64 v[30:33], v60 offset0:56 offset1:60
	v_pk_mul_f32 v[96:97], v[92:93], v[96:97]
	v_cmp_ne_u64_e32 vcc, 0, v[36:37]
	v_pk_fma_f32 v[190:191], v[76:77], v[94:95], v[96:97] neg_lo:[0,0,1] neg_hi:[0,0,1]
	v_pk_fma_f32 v[94:95], v[74:75], v[94:95], v[96:97]
	v_pk_mul_f32 v[96:97], v[54:55], v[116:117]
	v_mov_b32_e32 v191, v95
	v_pk_fma_f32 v[94:95], v[54:55], v[114:115], v[96:97] op_sel:[0,0,1] op_sel_hi:[1,1,0] neg_lo:[1,0,0] neg_hi:[1,0,0]
	v_pk_fma_f32 v[98:99], v[54:55], v[114:115], v[96:97] op_sel:[0,0,1] op_sel_hi:[1,1,0]
	v_mov_b32_e32 v96, v94
	v_mov_b32_e32 v97, v99
	v_pk_mov_b32 v[98:99], v[98:99], v[94:95] op_sel:[1,0]
	s_nop 0
	v_pk_mul_f32 v[102:103], v[98:99], v[102:103] op_sel:[0,1]
	s_nop 0
	v_pk_fma_f32 v[206:207], v[94:95], v[100:101], v[102:103] neg_lo:[0,0,1] neg_hi:[0,0,1]
	v_pk_fma_f32 v[100:101], v[96:97], v[100:101], v[102:103] op_sel_hi:[1,0,1]
	v_pk_mul_f32 v[102:103], v[54:55], v[106:107]
	v_mov_b32_e32 v207, v101
	v_pk_fma_f32 v[100:101], v[54:55], v[104:105], v[102:103] op_sel:[0,0,1] op_sel_hi:[1,1,0] neg_lo:[1,0,0] neg_hi:[1,0,0]
	v_pk_fma_f32 v[108:109], v[54:55], v[104:105], v[102:103] op_sel:[0,0,1] op_sel_hi:[1,1,0]
	v_mov_b32_e32 v102, v100
	v_mov_b32_e32 v103, v109
	v_pk_mov_b32 v[108:109], v[108:109], v[100:101] op_sel:[1,0]
	s_nop 0
	v_pk_mul_f32 v[188:189], v[108:109], v[188:189] op_sel:[0,1]
	s_nop 0
	v_pk_fma_f32 v[212:213], v[100:101], v[192:193], v[188:189] neg_lo:[0,0,1] neg_hi:[0,0,1]
	v_pk_fma_f32 v[188:189], v[102:103], v[192:193], v[188:189] op_sel_hi:[1,0,1]
	s_waitcnt lgkmcnt(2)
	v_mov_b32_e32 v192, v26
	v_mov_b32_e32 v213, v189
	ds_write2_b64 v65, v[110:111], v[228:229] offset1:4
	ds_write2_b64 v65, v[216:217], v[208:209] offset0:8 offset1:12
	ds_write2_b64 v65, v[210:211], v[220:221] offset0:16 offset1:20
	ds_write2_b64 v65, v[222:223], v[202:203] offset0:24 offset1:28
	ds_write2_b64 v65, v[198:199], v[200:201] offset0:32 offset1:36
	ds_write2_b64 v65, v[218:219], v[204:205] offset0:40 offset1:44
	ds_write2_b64 v65, v[186:187], v[190:191] offset0:48 offset1:52
	ds_write2_b64 v65, v[206:207], v[212:213] offset0:56 offset1:60
	v_pk_mov_b32 v[110:111], v[4:5], v[8:9] op_sel:[1,0]
	s_waitcnt lgkmcnt(9)
; FFT_HD cf2 mk2(float x, float y) { return (cf2){x, y}; }
; FFT_HD cf2 cmul(cf2 a, cf2 b) { return mk2(a.x * b.x - a.y * b.y, a.x * b.y + a.y * b.x); }
; FFT_HD cf2 cadd(cf2 a, cf2 b) { return mk2(a.x + b.x, a.y + b.y); }
; FFT_HD cf2 csub(cf2 a, cf2 b) { return mk2(a.x - b.x, a.y - b.y); }
; template <bool INV> FFT_HD void dft4(cf2& a, cf2& b, cf2& c, cf2& d) {
;     const cf2 s0 = cadd(a, c), s1 = csub(a, c), s2 = cadd(b, d), s3 = csub(b, d);
;     a = cadd(s0, s2); c = csub(s0, s2);
;     const cf2 r = INV ? mk2(-s3.y, s3.x) : mk2(s3.y, -s3.x);
;     b = cadd(s1, r); d = csub(s1, r);
; }
; template <bool INV> FFT_HD void dft16(cf2 (&x)[16]) {
;     const float C1 = 0.9238795325112867f, S1 = 0.3826834323650898f, H = 0.7071067811865476f;
; #pragma unroll
;     for (int b = 0; b < 4; ++b) dft4<INV>(x[b], x[4 + b], x[8 + b], x[12 + b]);
;     const float s = INV ? -1.f : 1.f;
;     x[4 + 1] = cmul(x[4 + 1], mk2(C1, -s * S1)); x[8 + 1] = cmul(x[8 + 1], mk2(H, -s * H));   x[12 + 1] = cmul(x[12 + 1], mk2(S1, -s * C1));
;     x[4 + 2] = cmul(x[4 + 2], mk2(H, -s * H));   x[8 + 2] = cmul(x[8 + 2], mk2(0.f, -s));     x[12 + 2] = cmul(x[12 + 2], mk2(-H, -s * H));
;     x[4 + 3] = cmul(x[4 + 3], mk2(S1, -s * C1)); x[8 + 3] = cmul(x[8 + 3], mk2(-H, -s * H));  x[12 + 3] = cmul(x[12 + 3], mk2(-C1, s * S1));
; #pragma unroll
;     for (int c = 0; c < 4; ++c) dft4<INV>(x[4 * c], x[4 * c + 1], x[4 * c + 2], x[4 * c + 3]);
; #pragma unroll
;     for (int c = 0; c < 4; ++c)
; #pragma unroll
;         for (int d = c + 1; d < 4; ++d) { const cf2 t = x[4 * c + d]; x[4 * c + d] = x[4 * d + c]; x[4 * d + c] = t; }
; }
; template <bool INV, int lS, class ZP> FFT_HD void fft_r16_pass(ZP z, int tid) {
;     ...
;         dft16<INV>(y);
;         if (!INV) {
; #pragma unroll
;             for (int j = 1; j < 16; ++j) y[j] = cmul(y[j], tw[j]);
;         }
	v_pk_mov_b32 v[186:187], v[12:13], v[16:17] op_sel:[1,0]
	v_mov_b32_e32 v188, v12
	v_pk_add_f32 v[110:111], v[110:111], v[186:187] neg_lo:[0,1] neg_hi:[0,1]
	v_mov_b32_e32 v186, v4
	v_mov_b32_e32 v187, v9
	v_mov_b32_e32 v189, v17
	v_pk_add_f32 v[186:187], v[186:187], v[188:189] neg_lo:[0,1] neg_hi:[0,1]
	v_pk_mov_b32 v[188:189], v[18:19], v[22:23] op_sel:[1,0]
	s_waitcnt lgkmcnt(8)
	v_pk_mov_b32 v[190:191], v[26:27], v[30:31] op_sel:[1,0]
	v_pk_mov_b32 v[204:205], v[20:21], v[4:5] op_sel:[1,0]
	v_pk_mov_b32 v[206:207], v[28:29], v[12:13] op_sel:[1,0]
	v_pk_add_f32 v[188:189], v[188:189], v[190:191] neg_lo:[0,1] neg_hi:[0,1]
	v_mov_b32_e32 v190, v18
	v_mov_b32_e32 v191, v23
	v_mov_b32_e32 v193, v31
	v_pk_add_f32 v[204:205], v[204:205], v[206:207]
	v_mov_b32_e32 v206, v4
	v_mov_b32_e32 v207, v20
	v_mov_b32_e32 v208, v12
	v_mov_b32_e32 v209, v28
	v_pk_add_f32 v[190:191], v[190:191], v[192:193] neg_lo:[0,1] neg_hi:[0,1]
	v_pk_add_f32 v[206:207], v[206:207], v[208:209]
	v_pk_mov_b32 v[208:209], v[24:25], v[8:9] op_sel:[1,0]
	v_pk_mov_b32 v[210:211], v[32:33], v[16:17] op_sel:[1,0]
	v_add_f32_e32 v39, v190, v191
	v_sub_f32_e32 v65, v188, v189
	v_sub_f32_e32 v67, v190, v191
	v_add_f32_e32 v198, v188, v189
	v_pk_mov_b32 v[188:189], v[20:21], v[24:25] op_sel:[1,0]
	v_pk_mov_b32 v[190:191], v[28:29], v[32:33] op_sel:[1,0]
	v_pk_add_f32 v[208:209], v[208:209], v[210:211]
	v_mov_b32_e32 v210, v8
	v_mov_b32_e32 v211, v24
	v_mov_b32_e32 v212, v16
	v_mov_b32_e32 v213, v32
	v_mov_b32_e32 v4, v20
	v_mov_b32_e32 v12, v28
	v_mov_b32_e32 v8, v24
	v_mov_b32_e32 v16, v32
	v_pk_add_f32 v[188:189], v[188:189], v[190:191] neg_lo:[0,1] neg_hi:[0,1]
	v_mov_b32_e32 v190, v20
	v_mov_b32_e32 v192, v28
	v_pk_add_f32 v[210:211], v[210:211], v[212:213]
	v_pk_add_f32 v[212:213], v[4:5], v[12:13]
	v_mov_b32_e32 v20, v5
	v_mov_b32_e32 v28, v13
	v_pk_add_f32 v[12:13], v[8:9], v[16:17]
	v_mov_b32_e32 v24, v9
	v_mov_b32_e32 v32, v17
	v_pk_add_f32 v[16:17], v[18:19], v[26:27]
	v_pk_add_f32 v[18:19], v[22:23], v[30:31]
	v_pk_add_f32 v[4:5], v[20:21], v[28:29]
	v_pk_add_f32 v[8:9], v[24:25], v[32:33]
	v_pk_add_f32 v[20:21], v[16:17], v[18:19] neg_lo:[0,1] neg_hi:[0,1]
	v_mov_b32_e32 v191, v25
	v_pk_add_f32 v[24:25], v[4:5], v[8:9] neg_lo:[0,1] neg_hi:[0,1]
	v_pk_add_f32 v[26:27], v[204:205], v[208:209] neg_lo:[0,1] neg_hi:[0,1]
	v_pk_fma_f32 v[28:29], v[20:21], 0, v[20:21] op_sel:[0,0,1] op_sel_hi:[1,0,0]
	v_pk_fma_f32 v[20:21], v[20:21], 0, v[20:21] op_sel:[0,0,1] op_sel_hi:[1,0,0] neg_lo:[0,0,1] neg_hi:[0,0,1]
	v_mov_b32_e32 v193, v33
	v_pk_add_f32 v[12:13], v[212:213], v[12:13] neg_lo:[0,1] neg_hi:[0,1]
	v_mov_b32_e32 v29, v21
	v_pk_mul_f32 v[20:21], v[24:25], s[50:51]
	v_pk_mul_f32 v[24:25], v[26:27], s[24:25]
	v_pk_add_f32 v[190:191], v[190:191], v[192:193] neg_lo:[0,1] neg_hi:[0,1]
	v_mul_f32_e32 v193, 0xbf3504f3, v198
	v_pk_add_f32 v[198:199], v[2:3], v[10:11]
	v_pk_add_f32 v[200:201], v[6:7], v[14:15]
	v_pk_add_f32 v[22:23], v[206:207], v[210:211] neg_lo:[0,1] neg_hi:[0,1]
	v_pk_fma_f32 v[12:13], v[12:13], s[24:25], v[24:25] neg_lo:[0,0,1] neg_hi:[0,0,1]
	v_mov_b32_e32 v24, v206
	v_mov_b32_e32 v25, v4
	v_mov_b32_e32 v26, v210
	v_mov_b32_e32 v27, v8
	v_mov_b32_e32 v4, v207
	v_mov_b32_e32 v8, v211
	v_pk_fma_f32 v[20:21], v[22:23], s[50:51], v[20:21]
	v_pk_add_f32 v[22:23], v[198:199], v[200:201]
	v_pk_add_f32 v[24:25], v[24:25], v[26:27]
	v_pk_add_f32 v[16:17], v[16:17], v[18:19]
	v_pk_add_f32 v[4:5], v[4:5], v[8:9]
	v_pk_add_f32 v[202:203], v[198:199], v[200:201] neg_lo:[0,1] neg_hi:[0,1]
	v_pk_add_f32 v[8:9], v[22:23], v[16:17]
	v_pk_add_f32 v[18:19], v[24:25], v[4:5]
	v_pk_mov_b32 v[26:27], v[22:23], v[24:25] op_sel:[1,0]
	v_pk_mov_b32 v[30:31], v[16:17], v[4:5] op_sel:[1,0]
	v_mov_b32_e32 v23, v25
	v_mov_b32_e32 v17, v5
	v_pk_add_f32 v[4:5], v[22:23], v[16:17] neg_lo:[0,1] neg_hi:[0,1]
	v_pk_add_f32 v[16:17], v[8:9], v[18:19]
	v_pk_add_f32 v[8:9], v[8:9], v[18:19] neg_lo:[0,1] neg_hi:[0,1]
	v_pk_add_f32 v[18:19], v[202:203], v[28:29]
	v_pk_add_f32 v[22:23], v[20:21], v[12:13]
	v_pk_add_f32 v[26:27], v[26:27], v[30:31] neg_lo:[0,1] neg_hi:[0,1]
	v_pk_add_f32 v[24:25], v[18:19], v[22:23]
	v_pk_add_f32 v[18:19], v[18:19], v[22:23] neg_lo:[0,1] neg_hi:[0,1]
	v_pk_mul_f32 v[22:23], v[46:47], v[24:25] op_sel:[0,1]
	v_pk_add_f32 v[2:3], v[2:3], v[10:11] neg_lo:[0,1] neg_hi:[0,1]
	v_pk_fma_f32 v[30:31], v[44:45], v[24:25], v[22:23] neg_lo:[0,0,1] neg_hi:[0,0,1]
	v_pk_fma_f32 v[22:23], v[44:45], v[24:25], v[22:23] op_sel_hi:[1,0,1]
	v_pk_add_f32 v[24:25], v[26:27], v[26:27] op_sel:[0,1] op_sel_hi:[0,1] neg_lo:[0,1] neg_hi:[0,1]
	v_mov_b32_e32 v31, v23
	v_pk_add_f32 v[22:23], v[4:5], v[4:5] op_sel:[0,1] op_sel_hi:[0,1]
	v_pk_mul_f32 v[24:25], v[112:113], v[24:25]
	v_pk_add_f32 v[10:11], v[186:187], v[186:187] op_sel:[0,1] op_sel_hi:[0,1] neg_lo:[0,1] neg_hi:[0,1]
	v_pk_fma_f32 v[32:33], v[48:49], v[22:23], v[24:25] neg_lo:[0,0,1] neg_hi:[0,0,1]
	v_pk_fma_f32 v[22:23], v[50:51], v[22:23], v[24:25]
	v_pk_mov_b32 v[24:25], v[12:13], v[20:21] op_sel:[1,0]
	v_pk_mov_b32 v[12:13], v[20:21], v[12:13] op_sel:[1,0]
	v_mov_b32_e32 v33, v23
	v_pk_add_f32 v[22:23], v[202:203], v[28:29] neg_lo:[0,1] neg_hi:[0,1]
	v_pk_add_f32 v[12:13], v[24:25], v[12:13] neg_lo:[0,1] neg_hi:[0,1]
	v_pk_add_f32 v[6:7], v[6:7], v[14:15] neg_lo:[0,1] neg_hi:[0,1]
	v_pk_add_f32 v[20:21], v[22:23], v[12:13]
	v_pk_add_f32 v[12:13], v[22:23], v[12:13] neg_lo:[0,1] neg_hi:[0,1]
	v_mov_b32_e32 v22, v20
	v_pk_mov_b32 v[24:25], v[12:13], v[20:21] op_sel:[1,0]
	v_mov_b32_e32 v23, v13
	v_pk_mul_f32 v[24:25], v[114:115], v[24:25]
	v_pk_mul_f32 v[10:11], v[10:11], s[44:45]
	v_pk_fma_f32 v[28:29], v[116:117], v[20:21], v[24:25] neg_lo:[0,0,1] neg_hi:[0,0,1]
; FFT_HD cf2 cmul(cf2 a, cf2 b) { return mk2(a.x * b.x - a.y * b.y, a.x * b.y + a.y * b.x); }
; template <bool INV, int lS, class ZP> FFT_HD void fft_r16_pass(ZP z, int tid) {
;     ...
;         dft16<INV>(y);
;         if (!INV) {
; #pragma unroll
;             for (int j = 1; j < 16; ++j) y[j] = cmul(y[j], tw[j]);
;         }
; #pragma unroll
;         for (int j = 0; j < 16; ++j) z[pb1 + j * STEP] = y[j];
	v_pk_fma_f32 v[22:23], v[116:117], v[22:23], v[24:25]
	v_pk_add_f32 v[14:15], v[110:111], v[110:111] op_sel:[0,1] op_sel_hi:[0,1]
	v_mov_b32_e32 v29, v23
	v_pk_mul_f32 v[22:23], v[54:55], v[8:9] op_sel:[0,1]
	v_mul_f32_e32 v192, 0xbf3504f3, v67
	v_pk_fma_f32 v[24:25], v[52:53], v[8:9], v[22:23] neg_lo:[0,0,1] neg_hi:[0,0,1]
	v_pk_fma_f32 v[8:9], v[52:53], v[8:9], v[22:23] op_sel_hi:[1,0,1]
	v_sub_f32_e32 v192, v192, v193
	v_mov_b32_e32 v25, v9
	v_pk_mul_f32 v[8:9], v[184:185], v[18:19]
	v_fmac_f32_e32 v193, 0xbf3504f3, v67
	v_pk_fma_f32 v[22:23], v[214:215], v[18:19], v[8:9] op_sel:[0,0,1] op_sel_hi:[1,1,0] neg_lo:[0,0,1] neg_hi:[0,0,1]
	v_pk_fma_f32 v[8:9], v[214:215], v[18:19], v[8:9] op_sel:[0,0,1] op_sel_hi:[1,1,0]
	v_pk_fma_f32 v[18:19], v[14:15], s[26:27], v[10:11]
	v_pk_fma_f32 v[10:11], v[14:15], s[26:27], v[10:11] neg_lo:[0,0,1] neg_hi:[0,0,1]
	v_pk_add_f32 v[14:15], v[188:189], v[188:189] op_sel:[0,1] op_sel_hi:[0,1]
	v_mov_b32_e32 v23, v9
	v_pk_add_f32 v[8:9], v[2:3], v[6:7] op_sel:[0,1] op_sel_hi:[1,0] neg_lo:[0,1] neg_hi:[0,1]
	v_pk_add_f32 v[2:3], v[2:3], v[6:7] op_sel:[0,1] op_sel_hi:[1,0]
	v_mov_b32_e32 v19, v11
	v_pk_add_f32 v[10:11], v[190:191], v[190:191] op_sel:[0,1] op_sel_hi:[0,1] neg_lo:[0,1] neg_hi:[0,1]
	v_pk_mul_f32 v[14:15], v[14:15], s[44:45]
	v_mov_b32_e32 v6, v8
	v_mov_b32_e32 v7, v3
	v_pk_fma_f32 v[10:11], v[10:11], s[30:31], v[14:15] neg_lo:[0,0,1] neg_hi:[0,0,1]
	v_pk_add_f32 v[14:15], v[6:7], v[192:193]
	v_pk_add_f32 v[44:45], v[18:19], v[10:11]
	v_pk_add_f32 v[6:7], v[6:7], v[192:193] neg_lo:[0,1] neg_hi:[0,1]
	v_pk_add_f32 v[46:47], v[14:15], v[44:45]
	v_pk_add_f32 v[10:11], v[18:19], v[10:11] neg_lo:[0,1] neg_hi:[0,1]
	v_pk_mul_f32 v[42:43], v[42:43], v[46:47] op_sel:[0,1]
	v_pk_add_f32 v[14:15], v[14:15], v[44:45] neg_lo:[0,1] neg_hi:[0,1]
	v_pk_fma_f32 v[44:45], v[40:41], v[46:47], v[42:43] neg_lo:[0,0,1] neg_hi:[0,0,1]
	v_pk_fma_f32 v[40:41], v[40:41], v[46:47], v[42:43] op_sel_hi:[1,0,1]
	v_pk_add_f32 v[18:19], v[6:7], v[10:11] op_sel:[0,1] op_sel_hi:[1,0]
	v_pk_add_f32 v[6:7], v[6:7], v[10:11] op_sel:[0,1] op_sel_hi:[1,0] neg_lo:[0,1] neg_hi:[0,1]
	v_mov_b32_e32 v45, v41
	v_pk_mov_b32 v[40:41], v[6:7], v[18:19] op_sel:[1,0]
	v_mov_b32_e32 v10, v18
	v_mov_b32_e32 v11, v7
	v_pk_mul_f32 v[40:41], v[104:105], v[40:41]
	v_pk_add_f32 v[50:51], v[190:191], v[190:191] op_sel:[0,1] op_sel_hi:[0,1]
	v_pk_fma_f32 v[42:43], v[106:107], v[18:19], v[40:41] neg_lo:[0,0,1] neg_hi:[0,0,1]
	v_pk_fma_f32 v[10:11], v[106:107], v[10:11], v[40:41]
	v_mul_f32_e32 v39, 0x3f3504f3, v39
	v_mov_b32_e32 v43, v11
	v_pk_add_f32 v[10:11], v[186:187], v[186:187] op_sel:[0,1] op_sel_hi:[0,1]
	v_pk_mul_f32 v[10:11], v[10:11], s[26:27]
	v_pk_add_f32 v[40:41], v[110:111], v[110:111] op_sel:[0,1] op_sel_hi:[0,1] neg_lo:[0,1] neg_hi:[0,1]
	v_pk_mul_f32 v[50:51], v[50:51], s[44:45]
	v_pk_add_f32 v[52:53], v[188:189], v[188:189] op_sel:[0,1] op_sel_hi:[0,1] neg_lo:[0,1] neg_hi:[0,1]
	v_pk_fma_f32 v[46:47], v[40:41], s[44:45], v[10:11]
	v_pk_fma_f32 v[10:11], v[40:41], s[44:45], v[10:11] neg_lo:[0,0,1] neg_hi:[0,0,1]
	v_fma_f32 v48, v65, s25, -v39
	v_pk_fma_f32 v[54:55], v[52:53], s[26:27], v[50:51]
	v_pk_fma_f32 v[50:51], v[52:53], s[26:27], v[50:51] neg_lo:[0,0,1] neg_hi:[0,0,1]
	v_mov_b32_e32 v10, v46
	v_fmamk_f32 v40, v65, 0x3f3504f3, v39
	v_mov_b32_e32 v41, v48
	v_mov_b32_e32 v50, v54
	v_mov_b32_e32 v3, v9
	v_mov_b32_e32 v49, v48
	v_pk_add_f32 v[52:53], v[10:11], v[50:51]
	v_pk_add_f32 v[104:105], v[2:3], v[40:41]
	v_mov_b32_e32 v3, v11
	v_mov_b32_e32 v41, v51
	v_pk_add_f32 v[2:3], v[2:3], v[40:41] neg_lo:[0,1] neg_hi:[0,1]
	v_pk_mov_b32 v[8:9], v[8:9], v[46:47] op_sel:[1,0]
	v_pk_mov_b32 v[10:11], v[48:49], v[54:55] op_sel:[1,0]
	v_pk_add_f32 v[40:41], v[104:105], v[52:53]
	v_pk_add_f32 v[8:9], v[8:9], v[10:11] neg_lo:[0,1] neg_hi:[0,1]
	v_pk_mul_f32 v[46:47], v[56:57], v[40:41] op_sel_hi:[0,1]
	v_pk_fma_f32 v[48:49], v[38:39], v[40:41], v[46:47] op_sel:[0,0,1] op_sel_hi:[1,1,0]
	v_pk_fma_f32 v[38:39], v[38:39], v[40:41], v[46:47] op_sel:[0,0,1] op_sel_hi:[0,1,0] neg_lo:[0,0,1] neg_hi:[0,0,1]
	v_pk_add_f32 v[40:41], v[8:9], v[8:9] op_sel:[0,1] op_sel_hi:[0,1] neg_lo:[0,1] neg_hi:[0,1]
	v_mov_b32_e32 v49, v39
	v_pk_add_f32 v[38:39], v[2:3], v[2:3] op_sel:[0,1] op_sel_hi:[0,1]
	v_pk_mul_f32 v[40:41], v[72:73], v[40:41]
	v_pk_add_f32 v[10:11], v[104:105], v[52:53] neg_lo:[0,1] neg_hi:[0,1]
	v_pk_fma_f32 v[46:47], v[68:69], v[38:39], v[40:41] neg_lo:[0,0,1] neg_hi:[0,0,1]
	v_pk_fma_f32 v[38:39], v[70:71], v[38:39], v[40:41]
	v_pk_add_f32 v[4:5], v[4:5], v[4:5] op_sel:[0,1] op_sel_hi:[0,1] neg_lo:[0,1] neg_hi:[0,1]
	v_mov_b32_e32 v47, v39
	v_pk_mul_f32 v[38:39], v[82:83], v[10:11]
	v_pk_add_f32 v[2:3], v[2:3], v[2:3] op_sel:[0,1] op_sel_hi:[0,1] neg_lo:[0,1] neg_hi:[0,1]
	v_pk_fma_f32 v[40:41], v[84:85], v[10:11], v[38:39] op_sel:[0,0,1] op_sel_hi:[1,1,0] neg_lo:[0,0,1] neg_hi:[0,0,1]
	v_pk_fma_f32 v[10:11], v[84:85], v[10:11], v[38:39] op_sel:[0,0,1] op_sel_hi:[1,1,0]
	s_nop 0
	v_mov_b32_e32 v41, v11
	v_pk_mul_f32 v[10:11], v[80:81], v[14:15]
	s_nop 0
	v_pk_fma_f32 v[38:39], v[78:79], v[14:15], v[10:11] op_sel:[0,0,1] op_sel_hi:[1,1,0] neg_lo:[0,0,1] neg_hi:[0,0,1]
	v_pk_fma_f32 v[10:11], v[78:79], v[14:15], v[10:11] op_sel:[0,0,1] op_sel_hi:[1,1,0]
	s_nop 0
	v_mov_b32_e32 v39, v11
	v_pk_add_f32 v[10:11], v[26:27], v[26:27] op_sel:[0,1] op_sel_hi:[0,1]
	v_pk_mul_f32 v[10:11], v[90:91], v[10:11]
	s_nop 0
	v_pk_fma_f32 v[14:15], v[86:87], v[4:5], v[10:11] neg_lo:[0,0,1] neg_hi:[0,0,1]
	v_pk_fma_f32 v[4:5], v[88:89], v[4:5], v[10:11]
	s_nop 0
	v_mov_b32_e32 v15, v5
	v_pk_add_f32 v[4:5], v[8:9], v[8:9] op_sel:[0,1] op_sel_hi:[0,1]
	v_pk_mul_f32 v[4:5], v[92:93], v[4:5]
	s_nop 0
	v_pk_fma_f32 v[8:9], v[76:77], v[2:3], v[4:5] neg_lo:[0,0,1] neg_hi:[0,0,1]
	v_pk_fma_f32 v[2:3], v[74:75], v[2:3], v[4:5]
	s_nop 0
	v_mov_b32_e32 v9, v3
	v_pk_mul_f32 v[2:3], v[98:99], v[20:21] op_sel:[0,1]
	s_nop 0
	v_pk_fma_f32 v[4:5], v[94:95], v[12:13], v[2:3] neg_lo:[0,0,1] neg_hi:[0,0,1]
	v_pk_fma_f32 v[2:3], v[96:97], v[12:13], v[2:3] op_sel_hi:[1,0,1]
	s_nop 0
	v_mov_b32_e32 v5, v3
	v_pk_mul_f32 v[2:3], v[108:109], v[18:19] op_sel:[0,1]
	s_nop 0
	v_pk_fma_f32 v[10:11], v[100:101], v[6:7], v[2:3] neg_lo:[0,0,1] neg_hi:[0,0,1]
	v_pk_fma_f32 v[2:3], v[102:103], v[6:7], v[2:3] op_sel_hi:[1,0,1]
	s_nop 0
	v_mov_b32_e32 v11, v3
	ds_write2_b64 v60, v[16:17], v[48:49] offset1:4
	ds_write2_b64 v60, v[30:31], v[44:45] offset0:8 offset1:12
	ds_write2_b64 v60, v[32:33], v[46:47] offset0:16 offset1:20
	ds_write2_b64 v60, v[28:29], v[42:43] offset0:24 offset1:28
	ds_write2_b64 v60, v[24:25], v[40:41] offset0:32 offset1:36
	ds_write2_b64 v60, v[22:23], v[38:39] offset0:40 offset1:44
	ds_write2_b64 v60, v[14:15], v[8:9] offset0:48 offset1:52
	ds_write2_b64 v60, v[4:5], v[10:11] offset0:56 offset1:60
	s_waitcnt lgkmcnt(0)
	s_barrier
; __device__ __forceinline__ unsigned cvt_pk_bf16(float lo, float hi) { unsigned r; asm volatile("v_cvt_pk_bf16_f32 %0, %1, %2" : "=v"(r) : "v"(lo), "v"(hi)); return r; }
; template <int BANK, int WAITN> __device__ __forceinline__ void bg_finish1(BgState& b) {
;     if (WAITN == 32) asm volatile("s_waitcnt vmcnt(32)" ::: "memory"); else asm volatile("s_waitcnt vmcnt(0)" ::: "memory");
;     asm volatile("" : BG_TIE16(BANK * 32) :: "memory");
;     asm volatile("" : BG_TIE16(BANK * 32 + 16) :: "memory");
;     bf16_t* dst = b.dst[BANK];
;     if (dst != nullptr) {
; #pragma unroll
;         for (int c = 0; c < 4; ++c) { u32x4 w;
;             w.x = cvt_pk_bf16(b.r[(BANK * 8 + 0) * 4 + c], b.r[(BANK * 8 + 1) * 4 + c]); w.y = cvt_pk_bf16(b.r[(BANK * 8 + 2) * 4 + c], b.r[(BANK * 8 + 3) * 4 + c]);
;             w.z = cvt_pk_bf16(b.r[(BANK * 8 + 4) * 4 + c], b.r[(BANK * 8 + 5) * 4 + c]); w.w = cvt_pk_bf16(b.r[(BANK * 8 + 6) * 4 + c], b.r[(BANK * 8 + 7) * 4 + c]);
;             bf16_t* dp = dst + (c & 1) * 512 + (c >> 1) * b.o2[BANK];
;             asm volatile("global_store_dwordx4 %0, %1, off\n\ts_nop 1" :: "v"(dp), "v"(w) : "memory"); }
;     }
; }
	s_waitcnt vmcnt(32)
	s_and_saveexec_b64 s[44:45], vcc
	s_cbranch_execz .LBB0_673
	v_cvt_pk_bf16_f32 v2, v176, v178
	v_cvt_pk_bf16_f32 v3, v177, v180
	v_cvt_pk_bf16_f32 v4, v179, v181
	v_cvt_pk_bf16_f32 v5, v182, v183
	v_lshl_add_u64 v[6:7], v[36:37], 0, s[22:23]
	global_store_dwordx4 v[36:37], v[2:5], off nt
	s_nop 1
	v_cvt_pk_bf16_f32 v2, v168, v170
	v_cvt_pk_bf16_f32 v3, v169, v172
	v_cvt_pk_bf16_f32 v4, v171, v173
	v_cvt_pk_bf16_f32 v5, v174, v175
	s_lshl_b32 s12, s46, 1
	global_store_dwordx4 v[6:7], v[2:5], off nt
	s_nop 1
	v_cvt_pk_bf16_f32 v2, v160, v162
	v_cvt_pk_bf16_f32 v3, v161, v164
	v_cvt_pk_bf16_f32 v4, v163, v165
	v_cvt_pk_bf16_f32 v5, v166, v167
	v_lshl_add_u64 v[8:9], v[36:37], 0, s[12:13]
	global_store_dwordx4 v[8:9], v[2:5], off nt
	s_nop 1
	v_cvt_pk_bf16_f32 v2, v57, v154
	v_cvt_pk_bf16_f32 v3, v153, v156
	v_cvt_pk_bf16_f32 v4, v155, v157
	v_cvt_pk_bf16_f32 v5, v158, v159
	v_lshl_add_u64 v[6:7], v[6:7], 0, s[12:13]
	global_store_dwordx4 v[6:7], v[2:5], off nt
	s_nop 1

; template <int BANK> __device__ __forceinline__ void bg_issue1(BgState& b, int wg, int NW, int lane) {
;     ...
;     for (int i = 0; i < 8; ++i) { const float* p = src + (size_t)i * ldS;
;         asm volatile("global_load_dword %0, %4, off\n\tglobal_load_dword %1, %4, off offset:256\n\tglobal_load_dword %2, %4, off offset:512\n\tglobal_load_dword %3, %4, off offset:768"
;                      : "=&v"(b.r[(BANK * 8 + i) * 4 + 0]), "=&v"(b.r[(BANK * 8 + i) * 4 + 1]), "=&v"(b.r[(BANK * 8 + i) * 4 + 2]), "=&v"(b.r[(BANK * 8 + i) * 4 + 3]) : "v"(p) : "memory"); }
;     b.st += 1;
; }
; template <bool INV, class ZP> FFT_HD void fft_r4_pass(ZP z, int tid, int nthr) {
;     for (int w = tid; w < FN / 4; w += nthr) {
;         const int base = PADI(4 * w);
;         cf2 a = z[base], b = z[base + 1], c = z[base + 2], d = z[base + 3];
.LBB0_683:
	s_nop 6
	global_load_dword v89, v[4:5], off nt
	global_load_dword v74, v[4:5], off offset:256 nt
	global_load_dword v50, v[4:5], off offset:512 nt
	global_load_dword v42, v[4:5], off offset:768 nt
	s_lshl_b32 s12, s46, 2
	v_lshl_add_u64 v[4:5], v[4:5], 0, s[12:13]
	global_load_dword v92, v[4:5], off nt
	global_load_dword v76, v[4:5], off offset:256 nt
	global_load_dword v52, v[4:5], off offset:512 nt
	global_load_dword v44, v[4:5], off offset:768 nt
	v_lshl_add_u64 v[4:5], v[4:5], 0, s[12:13]
	global_load_dword v91, v[4:5], off nt
	global_load_dword v75, v[4:5], off offset:256 nt
	global_load_dword v51, v[4:5], off offset:512 nt
	global_load_dword v43, v[4:5], off offset:768 nt
	v_lshl_add_u64 v[4:5], v[4:5], 0, s[12:13]
	global_load_dword v94, v[4:5], off nt
	global_load_dword v78, v[4:5], off offset:256 nt
	global_load_dword v54, v[4:5], off offset:512 nt
	global_load_dword v46, v[4:5], off offset:768 nt
	v_lshl_add_u64 v[4:5], v[4:5], 0, s[12:13]
	global_load_dword v93, v[4:5], off nt
	global_load_dword v77, v[4:5], off offset:256 nt
	global_load_dword v53, v[4:5], off offset:512 nt
	global_load_dword v45, v[4:5], off offset:768 nt
	v_lshl_add_u64 v[4:5], v[4:5], 0, s[12:13]
	global_load_dword v96, v[4:5], off nt
	global_load_dword v80, v[4:5], off offset:256 nt
	global_load_dword v56, v[4:5], off offset:512 nt
	global_load_dword v48, v[4:5], off offset:768 nt
	v_lshl_add_u64 v[4:5], v[4:5], 0, s[12:13]
	global_load_dword v95, v[4:5], off nt
	global_load_dword v79, v[4:5], off offset:256 nt
	global_load_dword v55, v[4:5], off offset:512 nt
	global_load_dword v47, v[4:5], off offset:768 nt
	v_lshl_add_u64 v[4:5], v[4:5], 0, s[12:13]
	global_load_dword v97, v[4:5], off nt
	global_load_dword v81, v[4:5], off offset:256 nt
	global_load_dword v57, v[4:5], off offset:512 nt
	global_load_dword v49, v[4:5], off offset:768 nt
	v_cmp_gt_i32_e32 vcc, s75, v120
	s_and_saveexec_b64 s[46:47], vcc
	s_cbranch_execz .LBB0_686
	v_lshl_add_u32 v4, v120, 5, 0
	s_mov_b64 s[50:51], 0

; __device__ __forceinline__ unsigned cvt_pk_bf16(float lo, float hi) { unsigned r; asm volatile("v_cvt_pk_bf16_f32 %0, %1, %2" : "=v"(r) : "v"(lo), "v"(hi)); return r; }
; template <int BANK, int WAITN> __device__ __forceinline__ void bg_finish1(BgState& b) {
;     if (WAITN == 32) asm volatile("s_waitcnt vmcnt(32)" ::: "memory"); else asm volatile("s_waitcnt vmcnt(0)" ::: "memory");
;     asm volatile("" : BG_TIE16(BANK * 32) :: "memory");
;     asm volatile("" : BG_TIE16(BANK * 32 + 16) :: "memory");
;     bf16_t* dst = b.dst[BANK];
;     if (dst != nullptr) {
; #pragma unroll
;         for (int c = 0; c < 4; ++c) { u32x4 w;
;             w.x = cvt_pk_bf16(b.r[(BANK * 8 + 0) * 4 + c], b.r[(BANK * 8 + 1) * 4 + c]); w.y = cvt_pk_bf16(b.r[(BANK * 8 + 2) * 4 + c], b.r[(BANK * 8 + 3) * 4 + c]);
;             w.z = cvt_pk_bf16(b.r[(BANK * 8 + 4) * 4 + c], b.r[(BANK * 8 + 5) * 4 + c]); w.w = cvt_pk_bf16(b.r[(BANK * 8 + 6) * 4 + c], b.r[(BANK * 8 + 7) * 4 + c]);
;             bf16_t* dp = dst + (c & 1) * 512 + (c >> 1) * b.o2[BANK];
;             asm volatile("global_store_dwordx4 %0, %1, off\n\ts_nop 1" :: "v"(dp), "v"(w) : "memory"); }
;     }
; }
.LBB0_686:
	s_or_b64 exec, exec, s[46:47]
	s_waitcnt lgkmcnt(0)
	s_barrier
	s_waitcnt vmcnt(32)
	v_cmp_ne_u64_e32 vcc, 0, v[34:35]
	s_and_saveexec_b64 s[46:47], vcc
	s_cbranch_execz .LBB0_688
	v_cvt_pk_bf16_f32 v4, v145, v147
	v_cvt_pk_bf16_f32 v5, v146, v149
	v_cvt_pk_bf16_f32 v6, v148, v150
	v_cvt_pk_bf16_f32 v7, v151, v152
	v_lshl_add_u64 v[8:9], v[34:35], 0, s[22:23]
	global_store_dwordx4 v[34:35], v[4:7], off nt
	s_nop 1
	v_cvt_pk_bf16_f32 v4, v137, v139
	v_cvt_pk_bf16_f32 v5, v138, v141
	v_cvt_pk_bf16_f32 v6, v140, v142
	v_cvt_pk_bf16_f32 v7, v143, v144
	s_lshl_b32 s12, s48, 1
	global_store_dwordx4 v[8:9], v[4:7], off nt
	s_nop 1
	v_cvt_pk_bf16_f32 v4, v129, v131
	v_cvt_pk_bf16_f32 v5, v130, v133
	v_cvt_pk_bf16_f32 v6, v132, v134
	v_cvt_pk_bf16_f32 v7, v135, v136
	v_lshl_add_u64 v[10:11], v[34:35], 0, s[12:13]
	global_store_dwordx4 v[10:11], v[4:7], off nt
	s_nop 1
	v_cvt_pk_bf16_f32 v4, v121, v123
	v_cvt_pk_bf16_f32 v5, v122, v125
	v_cvt_pk_bf16_f32 v6, v124, v126
	v_cvt_pk_bf16_f32 v7, v127, v128
	v_lshl_add_u64 v[8:9], v[8:9], 0, s[12:13]
	global_store_dwordx4 v[8:9], v[4:7], off nt
	s_nop 1

; __device__ __forceinline__ float bf_lo(unsigned w) { return __uint_as_float(w << 16); }
; __device__ __forceinline__ float bf_hi(unsigned w) { return __uint_as_float(w & 0xffff0000u); }
; FFT_HD cf2 mk2(float x, float y) { return (cf2){x, y}; }
; FFT_HD cf2 cmul(cf2 a, cf2 b) { return mk2(a.x * b.x - a.y * b.y, a.x * b.y + a.y * b.x); }
; FFT_HD int fpos(int k) { return ((k & 15) << 10) + (((k >> 4) & 15) << 6) + (((k >> 8) & 15) << 2) + (k >> 12); }
; #define SEG_WAIT() asm volatile("s_waitcnt vmcnt(32)\n\ts_nop 7" ::: "memory")
; #define BG_I(x) bg_issue1<x>(bg, bgwg, bgNW, bglane)
; template <int BANK> __device__ __forceinline__ void bg_issue1(BgState& b, int wg, int NW, int lane) {
;     ...
;     for (int i = 0; i < 8; ++i) { const float* p = src + (size_t)i * ldS;
;         asm volatile("global_load_dword %0, %4, off\n\tglobal_load_dword %1, %4, off offset:256\n\tglobal_load_dword %2, %4, off offset:512\n\tglobal_load_dword %3, %4, off offset:768"
;                      : "=&v"(b.r[(BANK * 8 + i) * 4 + 0]), "=&v"(b.r[(BANK * 8 + i) * 4 + 1]), "=&v"(b.r[(BANK * 8 + i) * 4 + 2]), "=&v"(b.r[(BANK * 8 + i) * 4 + 3]) : "v"(p) : "memory"); }
; __device__ __forceinline__ void hy_fft_phase(LAS unsigned char* lds, int bid, int G, const bf16_t* vgT, bf16_t* zT, const float* a3, const float* wout, const float* skip, float* filt, float4* gspec) {
;     ...
;                 BG_I(0);
;                 SEG_WAIT(); asm volatile("" : SEG_TIE8(gq, 0), SEG_TIE8(gq, 8), "+v"(gh) :: "memory");
; #pragma unroll
;                 for (int i = 0; i < 16; ++i) { const int k = tid + NTHR * i;
;                     const int p1 = PADI(fpos(k)), p2 = PADI(fpos((FN - k) & (FN - 1)));
;                     const cf2 zk = z[p1], zm = z[p2];
;                     const cf2 V1 = mk2(0.5f * (zk.x + zm.x), 0.5f * (zk.y - zm.y)), V2 = mk2(0.5f * (zk.y + zm.y), -0.5f * (zk.x - zm.x));
;                     const cf2 Y1 = cmul(V1, mk2(bf_lo(gq[i].x), bf_hi(gq[i].x))), Y2 = cmul(V2, mk2(bf_lo(gq[i].y), bf_hi(gq[i].y)));
;                     z[p1] = mk2(Y1.x - Y2.y, Y1.y + Y2.x); z[p2] = mk2(Y1.x + Y2.y, Y2.x - Y1.y); }
.LBB0_698:
	s_nop 6
	s_lshl_b32 s12, s48, 2
	global_load_dword v106, v[40:41], off nt
	global_load_dword v98, v[40:41], off offset:256 nt
	global_load_dword v82, v[40:41], off offset:512 nt
	global_load_dword v68, v[40:41], off offset:768 nt
	v_lshl_add_u64 v[70:71], v[40:41], 0, s[12:13]
	global_load_dword v108, v[70:71], off nt
	global_load_dword v100, v[70:71], off offset:256 nt
	global_load_dword v84, v[70:71], off offset:512 nt
	global_load_dword v41, v[70:71], off offset:768 nt
	v_lshl_add_u64 v[70:71], v[70:71], 0, s[12:13]
	v_lshlrev_b32_e32 v65, 2, v114
	global_load_dword v107, v[70:71], off nt
	global_load_dword v99, v[70:71], off offset:256 nt
	global_load_dword v83, v[70:71], off offset:512 nt
	global_load_dword v40, v[70:71], off offset:768 nt
	v_lshl_add_u64 v[72:73], v[70:71], 0, s[12:13]
	v_lshlrev_b32_e32 v60, 10, v114
	v_and_b32_e32 v65, 0x3c0, v65
	global_load_dword v110, v[72:73], off nt
	global_load_dword v102, v[72:73], off offset:256 nt
	global_load_dword v86, v[72:73], off offset:512 nt
	global_load_dword v70, v[72:73], off offset:768 nt
	v_lshl_add_u64 v[72:73], v[72:73], 0, s[12:13]
	v_and_or_b32 v60, v60, s79, v65
	v_lshrrev_b32_e32 v65, 6, v114
	global_load_dword v109, v[72:73], off nt
	global_load_dword v101, v[72:73], off offset:256 nt
	global_load_dword v85, v[72:73], off offset:512 nt
	global_load_dword v69, v[72:73], off offset:768 nt
	v_lshl_add_u64 v[116:117], v[72:73], 0, s[12:13]
	v_ashrrev_i32_e32 v67, 12, v114
	v_and_or_b32 v65, v65, 60, v60
	global_load_dword v112, v[116:117], off nt
	global_load_dword v104, v[116:117], off offset:256 nt
	global_load_dword v88, v[116:117], off offset:512 nt
	global_load_dword v72, v[116:117], off offset:768 nt
	v_lshl_add_u64 v[116:117], v[116:117], 0, s[12:13]
	v_add_u32_e32 v67, v65, v67
	global_load_dword v111, v[116:117], off nt
	global_load_dword v103, v[116:117], off offset:256 nt
	global_load_dword v87, v[116:117], off offset:512 nt
	global_load_dword v71, v[116:117], off offset:768 nt
	v_lshl_add_u64 v[116:117], v[116:117], 0, s[12:13]
	v_ashrrev_i32_e32 v115, 5, v67
	global_load_dword v113, v[116:117], off nt
	global_load_dword v105, v[116:117], off offset:256 nt
	global_load_dword v90, v[116:117], off offset:512 nt
	global_load_dword v73, v[116:117], off offset:768 nt
	v_sub_u32_e32 v116, 0, v114
	v_lshlrev_b32_e32 v115, 3, v115
	v_lshlrev_b32_e32 v121, 2, v116
	v_lshlrev_b32_e32 v67, 3, v67
	v_and_b32_e32 v115, -16, v115
	v_and_b32_e32 v117, 0x3000, v116
	v_lshlrev_b32_e32 v120, 10, v116
	v_and_b32_e32 v121, 0x3c0, v121
	v_add3_u32 v67, 0, v67, v115
	v_lshrrev_b32_e32 v115, 3, v116
	s_waitcnt vmcnt(32)
	s_nop 7
	v_and_or_b32 v120, v120, s79, v121
	v_and_b32_e32 v115, 0x1e0, v115
	v_lshrrev_b32_e32 v116, 9, v117
	v_add3_u32 v115, 0, v115, v116
	v_lshlrev_b32_e32 v116, 3, v120
	v_lshrrev_b32_e32 v117, 2, v120
	v_add3_u32 v115, v115, v116, v117
	ds_read_b64 v[116:117], v67
	ds_read_b64 v[120:121], v115
	v_cmp_eq_u32_e32 vcc, 0, v114
	s_waitcnt lgkmcnt(0)
	v_pk_add_f32 v[122:123], v[116:117], v[120:121]
	v_pk_add_f32 v[116:117], v[116:117], v[120:121] neg_lo:[0,1] neg_hi:[0,1]
	v_lshlrev_b32_e32 v121, 16, v39
	v_pk_mul_f32 v[116:117], v[116:117], s[34:35]
	v_lshlrev_b32_e32 v120, 16, v38
	v_and_b32_e32 v39, 0xffff0000, v39
	v_and_b32_e32 v38, 0xffff0000, v38
	v_pk_mul_f32 v[122:123], v[122:123], 0.5 op_sel_hi:[1,0]
	v_pk_mul_f32 v[124:125], v[116:117], v[38:39] op_sel:[1,0] op_sel_hi:[0,1]
	v_pk_mul_f32 v[116:117], v[116:117], v[120:121] op_sel:[1,0] op_sel_hi:[0,1]
	v_pk_fma_f32 v[124:125], v[122:123], v[120:121], v[124:125] neg_lo:[0,0,1] neg_hi:[0,0,1]
	v_pk_fma_f32 v[38:39], v[122:123], v[38:39], v[116:117]
	s_nop 0
	v_pk_add_f32 v[116:117], v[124:125], v[38:39] op_sel:[0,1] op_sel_hi:[1,0] neg_lo:[0,1] neg_hi:[0,1]
	v_pk_add_f32 v[38:39], v[124:125], v[38:39] op_sel:[0,1] op_sel_hi:[1,0]
	v_mov_b32_e32 v120, v116
	v_mov_b32_e32 v121, v39
	v_mov_b32_e32 v39, v117
	ds_write_b64 v67, v[120:121]
	ds_write_b64 v115, v[38:39]
	v_add_u32_e32 v38, 0x200, v114
	v_lshrrev_b32_e32 v39, 6, v38
	v_and_b32_e32 v39, 60, v39
	v_ashrrev_i32_e32 v38, 12, v38
	v_add3_u32 v38, v60, v38, v39
	v_ashrrev_i32_e32 v39, 5, v38
	v_sub_u32_e32 v67, 0xfffffe00, v114
	v_lshlrev_b32_e32 v39, 3, v39
	v_lshlrev_b32_e32 v117, 2, v67
	v_lshlrev_b32_e32 v38, 3, v38
	v_and_b32_e32 v39, -16, v39
	v_and_b32_e32 v115, 0x3000, v67
	v_lshlrev_b32_e32 v116, 10, v67
	v_and_b32_e32 v117, 0x3c0, v117
	v_add3_u32 v124, 0, v38, v39
	v_lshrrev_b32_e32 v38, 3, v67
	v_and_or_b32 v116, v116, s79, v117
	v_and_b32_e32 v38, 0x1e0, v38
	v_lshrrev_b32_e32 v39, 9, v115
	v_add3_u32 v38, 0, v38, v39
	v_lshlrev_b32_e32 v39, 3, v116
	v_lshrrev_b32_e32 v67, 2, v116
	v_add3_u32 v67, v38, v39, v67
	ds_read_b64 v[38:39], v124
	ds_read_b64 v[116:117], v67
	s_waitcnt lgkmcnt(0)
; __device__ __forceinline__ float bf_lo(unsigned w) { return __uint_as_float(w << 16); }
; __device__ __forceinline__ float bf_hi(unsigned w) { return __uint_as_float(w & 0xffff0000u); }
; FFT_HD cf2 mk2(float x, float y) { return (cf2){x, y}; }
; FFT_HD cf2 cmul(cf2 a, cf2 b) { return mk2(a.x * b.x - a.y * b.y, a.x * b.y + a.y * b.x); }
; FFT_HD int fpos(int k) { return ((k & 15) << 10) + (((k >> 4) & 15) << 6) + (((k >> 8) & 15) << 2) + (k >> 12); }
; __device__ __forceinline__ void hy_fft_phase(LAS unsigned char* lds, int bid, int G, const bf16_t* vgT, bf16_t* zT, const float* a3, const float* wout, const float* skip, float* filt, float4* gspec) {
;     ...
;                 for (int i = 0; i < 16; ++i) { const int k = tid + NTHR * i;
;                     const int p1 = PADI(fpos(k)), p2 = PADI(fpos((FN - k) & (FN - 1)));
;                     const cf2 zk = z[p1], zm = z[p2];
;                     const cf2 V1 = mk2(0.5f * (zk.x + zm.x), 0.5f * (zk.y - zm.y)), V2 = mk2(0.5f * (zk.y + zm.y), -0.5f * (zk.x - zm.x));
;                     const cf2 Y1 = cmul(V1, mk2(bf_lo(gq[i].x), bf_hi(gq[i].x))), Y2 = cmul(V2, mk2(bf_lo(gq[i].y), bf_hi(gq[i].y)));
;                     z[p1] = mk2(Y1.x - Y2.y, Y1.y + Y2.x); z[p2] = mk2(Y1.x + Y2.y, Y2.x - Y1.y); }
	v_pk_add_f32 v[120:121], v[38:39], v[116:117]
	v_pk_add_f32 v[38:39], v[38:39], v[116:117] neg_lo:[0,1] neg_hi:[0,1]
	v_lshlrev_b32_e32 v117, 16, v37
	v_pk_mul_f32 v[38:39], v[38:39], s[34:35]
	v_lshlrev_b32_e32 v116, 16, v36
	v_and_b32_e32 v37, 0xffff0000, v37
	v_and_b32_e32 v36, 0xffff0000, v36
	v_pk_mul_f32 v[120:121], v[120:121], 0.5 op_sel_hi:[1,0]
	v_pk_mul_f32 v[122:123], v[38:39], v[36:37] op_sel:[1,0] op_sel_hi:[0,1]
	v_pk_mul_f32 v[38:39], v[38:39], v[116:117] op_sel:[1,0] op_sel_hi:[0,1]
	v_pk_fma_f32 v[122:123], v[120:121], v[116:117], v[122:123] neg_lo:[0,0,1] neg_hi:[0,0,1]
	v_pk_fma_f32 v[36:37], v[120:121], v[36:37], v[38:39]
	s_nop 0
	v_pk_add_f32 v[38:39], v[122:123], v[36:37] op_sel:[0,1] op_sel_hi:[1,0] neg_lo:[0,1] neg_hi:[0,1]
	v_pk_add_f32 v[36:37], v[122:123], v[36:37] op_sel:[0,1] op_sel_hi:[1,0]
	v_mov_b32_e32 v116, v38
	v_mov_b32_e32 v117, v37
	v_mov_b32_e32 v37, v39
	ds_write_b64 v124, v[116:117]
	ds_write_b64 v67, v[36:37]
	v_add_u32_e32 v36, 0x400, v114
	v_lshrrev_b32_e32 v37, 6, v36
	v_and_b32_e32 v37, 60, v37
	v_ashrrev_i32_e32 v36, 12, v36
	v_add3_u32 v36, v60, v36, v37
	v_ashrrev_i32_e32 v37, 5, v36
	v_sub_u32_e32 v38, 0xfffffc00, v114
	v_lshlrev_b32_e32 v115, 2, v38
	v_lshlrev_b32_e32 v37, 3, v37
	v_lshlrev_b32_e32 v67, 10, v38
	v_and_b32_e32 v115, 0x3c0, v115
	v_lshlrev_b32_e32 v36, 3, v36
	v_and_b32_e32 v37, -16, v37
	v_and_b32_e32 v39, 0x3000, v38
	v_and_or_b32 v67, v67, s79, v115
	v_add3_u32 v115, 0, v36, v37
	v_lshrrev_b32_e32 v36, 3, v38
	v_and_b32_e32 v36, 0x1e0, v36
	v_lshrrev_b32_e32 v37, 9, v39
	v_add3_u32 v36, 0, v36, v37
	v_lshlrev_b32_e32 v37, 3, v67
	v_lshrrev_b32_e32 v38, 2, v67
	v_add3_u32 v67, v36, v37, v38
	ds_read_b64 v[36:37], v115
	ds_read_b64 v[38:39], v67
	s_waitcnt lgkmcnt(0)
	v_pk_add_f32 v[116:117], v[36:37], v[38:39]
	v_pk_add_f32 v[36:37], v[36:37], v[38:39] neg_lo:[0,1] neg_hi:[0,1]
	v_lshlrev_b32_e32 v39, 16, v35
	v_pk_mul_f32 v[36:37], v[36:37], s[34:35]
	v_lshlrev_b32_e32 v38, 16, v34
	v_and_b32_e32 v35, 0xffff0000, v35
	v_and_b32_e32 v34, 0xffff0000, v34
	v_pk_mul_f32 v[116:117], v[116:117], 0.5 op_sel_hi:[1,0]
	v_pk_mul_f32 v[120:121], v[36:37], v[34:35] op_sel:[1,0] op_sel_hi:[0,1]
	v_pk_mul_f32 v[36:37], v[36:37], v[38:39] op_sel:[1,0] op_sel_hi:[0,1]
	v_pk_fma_f32 v[120:121], v[116:117], v[38:39], v[120:121] neg_lo:[0,0,1] neg_hi:[0,0,1]
	v_pk_fma_f32 v[34:35], v[116:117], v[34:35], v[36:37]
	s_nop 0
	v_pk_add_f32 v[36:37], v[120:121], v[34:35] op_sel:[0,1] op_sel_hi:[1,0] neg_lo:[0,1] neg_hi:[0,1]
	v_pk_add_f32 v[34:35], v[120:121], v[34:35] op_sel:[0,1] op_sel_hi:[1,0]
	v_mov_b32_e32 v38, v36
	v_mov_b32_e32 v39, v35
	v_mov_b32_e32 v35, v37
	ds_write_b64 v115, v[38:39]
	ds_write_b64 v67, v[34:35]
	v_add_u32_e32 v34, 0x600, v114
	v_lshrrev_b32_e32 v35, 6, v34
	v_and_b32_e32 v35, 60, v35
	v_ashrrev_i32_e32 v34, 12, v34
	v_add3_u32 v34, v60, v34, v35
	v_ashrrev_i32_e32 v35, 5, v34
	v_sub_u32_e32 v36, 0xfffffa00, v114
	v_lshlrev_b32_e32 v35, 3, v35
	v_lshlrev_b32_e32 v39, 2, v36
	v_lshlrev_b32_e32 v34, 3, v34
	v_and_b32_e32 v35, -16, v35
	v_and_b32_e32 v37, 0x3000, v36
	v_lshlrev_b32_e32 v38, 10, v36
	v_and_b32_e32 v39, 0x3c0, v39
	v_add3_u32 v67, 0, v34, v35
	v_lshrrev_b32_e32 v34, 3, v36
	v_and_or_b32 v38, v38, s79, v39
	v_and_b32_e32 v34, 0x1e0, v34
	v_lshrrev_b32_e32 v35, 9, v37
	v_add3_u32 v34, 0, v34, v35
	v_lshlrev_b32_e32 v35, 3, v38
	v_lshrrev_b32_e32 v36, 2, v38
	v_add3_u32 v115, v34, v35, v36
	ds_read_b64 v[34:35], v67
	ds_read_b64 v[36:37], v115
	s_waitcnt lgkmcnt(0)
	v_pk_add_f32 v[38:39], v[34:35], v[36:37]
	v_pk_add_f32 v[34:35], v[34:35], v[36:37] neg_lo:[0,1] neg_hi:[0,1]
	v_lshlrev_b32_e32 v37, 16, v33
	v_pk_mul_f32 v[34:35], v[34:35], s[34:35]
	v_lshlrev_b32_e32 v36, 16, v32
	v_and_b32_e32 v33, 0xffff0000, v33
	v_and_b32_e32 v32, 0xffff0000, v32
	v_pk_mul_f32 v[38:39], v[38:39], 0.5 op_sel_hi:[1,0]
	v_pk_mul_f32 v[116:117], v[34:35], v[32:33] op_sel:[1,0] op_sel_hi:[0,1]
	v_pk_mul_f32 v[34:35], v[34:35], v[36:37] op_sel:[1,0] op_sel_hi:[0,1]
	v_pk_fma_f32 v[116:117], v[38:39], v[36:37], v[116:117] neg_lo:[0,0,1] neg_hi:[0,0,1]
	v_pk_fma_f32 v[32:33], v[38:39], v[32:33], v[34:35]
	s_nop 0
	v_pk_add_f32 v[34:35], v[116:117], v[32:33] op_sel:[0,1] op_sel_hi:[1,0] neg_lo:[0,1] neg_hi:[0,1]
	v_pk_add_f32 v[32:33], v[116:117], v[32:33] op_sel:[0,1] op_sel_hi:[1,0]
	v_mov_b32_e32 v36, v34
	v_mov_b32_e32 v37, v33
	v_mov_b32_e32 v33, v35
	ds_write_b64 v67, v[36:37]
	ds_write_b64 v115, v[32:33]
	v_add_u32_e32 v32, 0x800, v114
	v_lshrrev_b32_e32 v33, 6, v32
	v_and_b32_e32 v33, 60, v33
	v_ashrrev_i32_e32 v32, 12, v32
	v_add3_u32 v32, v60, v32, v33
	v_ashrrev_i32_e32 v33, 5, v32
	v_sub_u32_e32 v34, 0xfffff800, v114
	v_lshlrev_b32_e32 v33, 3, v33
	v_lshlrev_b32_e32 v37, 2, v34
	v_lshlrev_b32_e32 v32, 3, v32
	v_and_b32_e32 v33, -16, v33
	v_and_b32_e32 v35, 0x3000, v34
	v_lshlrev_b32_e32 v36, 10, v34
	v_and_b32_e32 v37, 0x3c0, v37
	v_add3_u32 v67, 0, v32, v33
	v_lshrrev_b32_e32 v32, 3, v34
	v_and_or_b32 v36, v36, s79, v37
	v_and_b32_e32 v32, 0x1e0, v32
	v_lshrrev_b32_e32 v33, 9, v35
	v_add3_u32 v32, 0, v32, v33
	v_lshlrev_b32_e32 v33, 3, v36
	v_lshrrev_b32_e32 v34, 2, v36
	v_add3_u32 v115, v32, v33, v34
	ds_read_b64 v[32:33], v67
	ds_read_b64 v[34:35], v115
	s_waitcnt lgkmcnt(0)
; __device__ __forceinline__ float bf_lo(unsigned w) { return __uint_as_float(w << 16); }
; __device__ __forceinline__ float bf_hi(unsigned w) { return __uint_as_float(w & 0xffff0000u); }
; FFT_HD cf2 mk2(float x, float y) { return (cf2){x, y}; }
; FFT_HD cf2 cmul(cf2 a, cf2 b) { return mk2(a.x * b.x - a.y * b.y, a.x * b.y + a.y * b.x); }
; FFT_HD int fpos(int k) { return ((k & 15) << 10) + (((k >> 4) & 15) << 6) + (((k >> 8) & 15) << 2) + (k >> 12); }
; __device__ __forceinline__ void hy_fft_phase(LAS unsigned char* lds, int bid, int G, const bf16_t* vgT, bf16_t* zT, const float* a3, const float* wout, const float* skip, float* filt, float4* gspec) {
;     ...
;                 for (int i = 0; i < 16; ++i) { const int k = tid + NTHR * i;
;                     const int p1 = PADI(fpos(k)), p2 = PADI(fpos((FN - k) & (FN - 1)));
;                     const cf2 zk = z[p1], zm = z[p2];
;                     const cf2 V1 = mk2(0.5f * (zk.x + zm.x), 0.5f * (zk.y - zm.y)), V2 = mk2(0.5f * (zk.y + zm.y), -0.5f * (zk.x - zm.x));
;                     const cf2 Y1 = cmul(V1, mk2(bf_lo(gq[i].x), bf_hi(gq[i].x))), Y2 = cmul(V2, mk2(bf_lo(gq[i].y), bf_hi(gq[i].y)));
;                     z[p1] = mk2(Y1.x - Y2.y, Y1.y + Y2.x); z[p2] = mk2(Y1.x + Y2.y, Y2.x - Y1.y); }
	v_pk_add_f32 v[36:37], v[32:33], v[34:35]
	v_pk_add_f32 v[32:33], v[32:33], v[34:35] neg_lo:[0,1] neg_hi:[0,1]
	v_lshlrev_b32_e32 v35, 16, v31
	v_pk_mul_f32 v[32:33], v[32:33], s[34:35]
	v_lshlrev_b32_e32 v34, 16, v30
	v_and_b32_e32 v31, 0xffff0000, v31
	v_and_b32_e32 v30, 0xffff0000, v30
	v_pk_mul_f32 v[36:37], v[36:37], 0.5 op_sel_hi:[1,0]
	v_pk_mul_f32 v[38:39], v[32:33], v[30:31] op_sel:[1,0] op_sel_hi:[0,1]
	v_pk_mul_f32 v[32:33], v[32:33], v[34:35] op_sel:[1,0] op_sel_hi:[0,1]
	v_pk_fma_f32 v[38:39], v[36:37], v[34:35], v[38:39] neg_lo:[0,0,1] neg_hi:[0,0,1]
	v_pk_fma_f32 v[30:31], v[36:37], v[30:31], v[32:33]
	s_nop 0
	v_pk_add_f32 v[32:33], v[38:39], v[30:31] op_sel:[0,1] op_sel_hi:[1,0] neg_lo:[0,1] neg_hi:[0,1]
	v_pk_add_f32 v[30:31], v[38:39], v[30:31] op_sel:[0,1] op_sel_hi:[1,0]
	v_mov_b32_e32 v34, v32
	v_mov_b32_e32 v35, v31
	v_mov_b32_e32 v31, v33
	ds_write_b64 v67, v[34:35]
	ds_write_b64 v115, v[30:31]
	v_add_u32_e32 v30, 0xa00, v114
	v_lshrrev_b32_e32 v31, 6, v30
	v_and_b32_e32 v31, 60, v31
	v_ashrrev_i32_e32 v30, 12, v30
	v_add3_u32 v30, v60, v30, v31
	v_ashrrev_i32_e32 v31, 5, v30
	v_sub_u32_e32 v32, 0xfffff600, v114
	v_lshlrev_b32_e32 v31, 3, v31
	v_lshlrev_b32_e32 v35, 2, v32
	v_lshlrev_b32_e32 v30, 3, v30
	v_and_b32_e32 v31, -16, v31
	v_and_b32_e32 v33, 0x3000, v32
	v_lshlrev_b32_e32 v34, 10, v32
	v_and_b32_e32 v35, 0x3c0, v35
	v_add3_u32 v38, 0, v30, v31
	v_lshrrev_b32_e32 v30, 3, v32
	v_and_or_b32 v34, v34, s79, v35
	v_and_b32_e32 v30, 0x1e0, v30
	v_lshrrev_b32_e32 v31, 9, v33
	v_add3_u32 v30, 0, v30, v31
	v_lshlrev_b32_e32 v31, 3, v34
	v_lshrrev_b32_e32 v32, 2, v34
	v_add3_u32 v39, v30, v31, v32
	ds_read_b64 v[30:31], v38
	ds_read_b64 v[32:33], v39
	s_waitcnt lgkmcnt(0)
	v_pk_add_f32 v[34:35], v[30:31], v[32:33]
	v_pk_add_f32 v[30:31], v[30:31], v[32:33] neg_lo:[0,1] neg_hi:[0,1]
	v_lshlrev_b32_e32 v33, 16, v29
	v_pk_mul_f32 v[30:31], v[30:31], s[34:35]
	v_lshlrev_b32_e32 v32, 16, v28
	v_and_b32_e32 v29, 0xffff0000, v29
	v_and_b32_e32 v28, 0xffff0000, v28
	v_pk_mul_f32 v[34:35], v[34:35], 0.5 op_sel_hi:[1,0]
	v_pk_mul_f32 v[36:37], v[30:31], v[28:29] op_sel:[1,0] op_sel_hi:[0,1]
	v_pk_mul_f32 v[30:31], v[30:31], v[32:33] op_sel:[1,0] op_sel_hi:[0,1]
	v_pk_fma_f32 v[36:37], v[34:35], v[32:33], v[36:37] neg_lo:[0,0,1] neg_hi:[0,0,1]
	v_pk_fma_f32 v[28:29], v[34:35], v[28:29], v[30:31]
	s_nop 0
	v_pk_add_f32 v[30:31], v[36:37], v[28:29] op_sel:[0,1] op_sel_hi:[1,0] neg_lo:[0,1] neg_hi:[0,1]
	v_pk_add_f32 v[28:29], v[36:37], v[28:29] op_sel:[0,1] op_sel_hi:[1,0]
	v_mov_b32_e32 v32, v30
	v_mov_b32_e32 v33, v29
	v_mov_b32_e32 v29, v31
	ds_write_b64 v38, v[32:33]
	ds_write_b64 v39, v[28:29]
	v_add_u32_e32 v28, 0xc00, v114
	v_lshrrev_b32_e32 v29, 6, v28
	v_and_b32_e32 v29, 60, v29
	v_ashrrev_i32_e32 v28, 12, v28
	v_add3_u32 v28, v60, v28, v29
	v_ashrrev_i32_e32 v29, 5, v28
	v_sub_u32_e32 v30, 0xfffff400, v114
	v_lshlrev_b32_e32 v29, 3, v29
	v_lshlrev_b32_e32 v33, 2, v30
	v_lshlrev_b32_e32 v28, 3, v28
	v_and_b32_e32 v29, -16, v29
	v_and_b32_e32 v31, 0x3000, v30
	v_lshlrev_b32_e32 v32, 10, v30
	v_and_b32_e32 v33, 0x3c0, v33
	v_add3_u32 v36, 0, v28, v29
	v_lshrrev_b32_e32 v28, 3, v30
	v_and_or_b32 v32, v32, s79, v33
	v_and_b32_e32 v28, 0x1e0, v28
	v_lshrrev_b32_e32 v29, 9, v31
	v_add3_u32 v28, 0, v28, v29
	v_lshlrev_b32_e32 v29, 3, v32
	v_lshrrev_b32_e32 v30, 2, v32
	v_add3_u32 v37, v28, v29, v30
	ds_read_b64 v[28:29], v36
	ds_read_b64 v[30:31], v37
	s_waitcnt lgkmcnt(0)
	v_pk_add_f32 v[32:33], v[28:29], v[30:31]
	v_pk_add_f32 v[28:29], v[28:29], v[30:31] neg_lo:[0,1] neg_hi:[0,1]
	v_lshlrev_b32_e32 v31, 16, v27
	v_pk_mul_f32 v[28:29], v[28:29], s[34:35]
	v_lshlrev_b32_e32 v30, 16, v26
	v_and_b32_e32 v27, 0xffff0000, v27
	v_and_b32_e32 v26, 0xffff0000, v26
	v_pk_mul_f32 v[32:33], v[32:33], 0.5 op_sel_hi:[1,0]
	v_pk_mul_f32 v[34:35], v[28:29], v[26:27] op_sel:[1,0] op_sel_hi:[0,1]
	v_pk_mul_f32 v[28:29], v[28:29], v[30:31] op_sel:[1,0] op_sel_hi:[0,1]
	v_pk_fma_f32 v[34:35], v[32:33], v[30:31], v[34:35] neg_lo:[0,0,1] neg_hi:[0,0,1]
	v_pk_fma_f32 v[26:27], v[32:33], v[26:27], v[28:29]
	s_nop 0
	v_pk_add_f32 v[28:29], v[34:35], v[26:27] op_sel:[0,1] op_sel_hi:[1,0] neg_lo:[0,1] neg_hi:[0,1]
	v_pk_add_f32 v[26:27], v[34:35], v[26:27] op_sel:[0,1] op_sel_hi:[1,0]
	v_mov_b32_e32 v30, v28
	v_mov_b32_e32 v31, v27
	v_mov_b32_e32 v27, v29
	ds_write_b64 v36, v[30:31]
	ds_write_b64 v37, v[26:27]
	v_add_u32_e32 v26, 0xe00, v114
	v_lshrrev_b32_e32 v27, 6, v26
	v_and_b32_e32 v27, 60, v27
	v_ashrrev_i32_e32 v26, 12, v26
	v_add3_u32 v26, v60, v26, v27
	v_ashrrev_i32_e32 v27, 5, v26
	v_sub_u32_e32 v28, 0xfffff200, v114
	v_lshlrev_b32_e32 v27, 3, v27
	v_lshlrev_b32_e32 v31, 2, v28
	v_lshlrev_b32_e32 v26, 3, v26
	v_and_b32_e32 v27, -16, v27
	v_and_b32_e32 v29, 0x3000, v28
	v_lshlrev_b32_e32 v30, 10, v28
	v_and_b32_e32 v31, 0x3c0, v31
	v_add3_u32 v34, 0, v26, v27
	v_lshrrev_b32_e32 v26, 3, v28
	v_and_or_b32 v30, v30, s79, v31
	v_and_b32_e32 v26, 0x1e0, v26
	v_lshrrev_b32_e32 v27, 9, v29
	v_add3_u32 v26, 0, v26, v27
	v_lshlrev_b32_e32 v27, 3, v30
	v_lshrrev_b32_e32 v28, 2, v30
	v_add3_u32 v35, v26, v27, v28
	ds_read_b64 v[26:27], v34
	ds_read_b64 v[28:29], v35
	s_waitcnt lgkmcnt(0)
; __device__ __forceinline__ float bf_lo(unsigned w) { return __uint_as_float(w << 16); }
; __device__ __forceinline__ float bf_hi(unsigned w) { return __uint_as_float(w & 0xffff0000u); }
; FFT_HD cf2 mk2(float x, float y) { return (cf2){x, y}; }
; FFT_HD cf2 cmul(cf2 a, cf2 b) { return mk2(a.x * b.x - a.y * b.y, a.x * b.y + a.y * b.x); }
; FFT_HD int fpos(int k) { return ((k & 15) << 10) + (((k >> 4) & 15) << 6) + (((k >> 8) & 15) << 2) + (k >> 12); }
; __device__ __forceinline__ void hy_fft_phase(LAS unsigned char* lds, int bid, int G, const bf16_t* vgT, bf16_t* zT, const float* a3, const float* wout, const float* skip, float* filt, float4* gspec) {
;     ...
;                 for (int i = 0; i < 16; ++i) { const int k = tid + NTHR * i;
;                     const int p1 = PADI(fpos(k)), p2 = PADI(fpos((FN - k) & (FN - 1)));
;                     const cf2 zk = z[p1], zm = z[p2];
;                     const cf2 V1 = mk2(0.5f * (zk.x + zm.x), 0.5f * (zk.y - zm.y)), V2 = mk2(0.5f * (zk.y + zm.y), -0.5f * (zk.x - zm.x));
;                     const cf2 Y1 = cmul(V1, mk2(bf_lo(gq[i].x), bf_hi(gq[i].x))), Y2 = cmul(V2, mk2(bf_lo(gq[i].y), bf_hi(gq[i].y)));
;                     z[p1] = mk2(Y1.x - Y2.y, Y1.y + Y2.x); z[p2] = mk2(Y1.x + Y2.y, Y2.x - Y1.y); }
	v_pk_add_f32 v[30:31], v[26:27], v[28:29]
	v_pk_add_f32 v[26:27], v[26:27], v[28:29] neg_lo:[0,1] neg_hi:[0,1]
	v_lshlrev_b32_e32 v29, 16, v25
	v_pk_mul_f32 v[26:27], v[26:27], s[34:35]
	v_lshlrev_b32_e32 v28, 16, v24
	v_and_b32_e32 v25, 0xffff0000, v25
	v_and_b32_e32 v24, 0xffff0000, v24
	v_pk_mul_f32 v[30:31], v[30:31], 0.5 op_sel_hi:[1,0]
	v_pk_mul_f32 v[32:33], v[26:27], v[24:25] op_sel:[1,0] op_sel_hi:[0,1]
	v_pk_mul_f32 v[26:27], v[26:27], v[28:29] op_sel:[1,0] op_sel_hi:[0,1]
	v_pk_fma_f32 v[32:33], v[30:31], v[28:29], v[32:33] neg_lo:[0,0,1] neg_hi:[0,0,1]
	v_pk_fma_f32 v[24:25], v[30:31], v[24:25], v[26:27]
	s_nop 0
	v_pk_add_f32 v[26:27], v[32:33], v[24:25] op_sel:[0,1] op_sel_hi:[1,0] neg_lo:[0,1] neg_hi:[0,1]
	v_pk_add_f32 v[24:25], v[32:33], v[24:25] op_sel:[0,1] op_sel_hi:[1,0]
	v_mov_b32_e32 v28, v26
	v_mov_b32_e32 v29, v25
	v_mov_b32_e32 v25, v27
	ds_write_b64 v34, v[28:29]
	ds_write_b64 v35, v[24:25]
	v_add_u32_e32 v24, 0x1000, v114
	v_ashrrev_i32_e32 v24, 12, v24
	v_add_u32_e32 v24, v65, v24
	v_ashrrev_i32_e32 v25, 5, v24
	v_sub_u32_e32 v26, 0xfffff000, v114
	v_lshlrev_b32_e32 v25, 3, v25
	v_lshlrev_b32_e32 v29, 2, v26
	v_lshlrev_b32_e32 v24, 3, v24
	v_and_b32_e32 v25, -16, v25
	v_and_b32_e32 v27, 0x3000, v26
	v_lshlrev_b32_e32 v28, 10, v26
	v_and_b32_e32 v29, 0x3c0, v29
	v_add3_u32 v32, 0, v24, v25
	v_lshrrev_b32_e32 v24, 3, v26
	v_and_or_b32 v28, v28, s79, v29
	v_and_b32_e32 v24, 0x1e0, v24
	v_lshrrev_b32_e32 v25, 9, v27
	v_add3_u32 v24, 0, v24, v25
	v_lshlrev_b32_e32 v25, 3, v28
	v_lshrrev_b32_e32 v26, 2, v28
	v_add3_u32 v33, v24, v25, v26
	ds_read_b64 v[24:25], v32
	ds_read_b64 v[26:27], v33
	s_waitcnt lgkmcnt(0)
	v_pk_add_f32 v[28:29], v[24:25], v[26:27]
	v_pk_add_f32 v[24:25], v[24:25], v[26:27] neg_lo:[0,1] neg_hi:[0,1]
	v_lshlrev_b32_e32 v27, 16, v23
	v_pk_mul_f32 v[24:25], v[24:25], s[34:35]
	v_lshlrev_b32_e32 v26, 16, v22
	v_and_b32_e32 v23, 0xffff0000, v23
	v_and_b32_e32 v22, 0xffff0000, v22
	v_pk_mul_f32 v[28:29], v[28:29], 0.5 op_sel_hi:[1,0]
	v_pk_mul_f32 v[30:31], v[24:25], v[22:23] op_sel:[1,0] op_sel_hi:[0,1]
	v_pk_mul_f32 v[24:25], v[24:25], v[26:27] op_sel:[1,0] op_sel_hi:[0,1]
	v_pk_fma_f32 v[30:31], v[28:29], v[26:27], v[30:31] neg_lo:[0,0,1] neg_hi:[0,0,1]
	v_pk_fma_f32 v[22:23], v[28:29], v[22:23], v[24:25]
	s_nop 0
	v_pk_add_f32 v[24:25], v[30:31], v[22:23] op_sel:[0,1] op_sel_hi:[1,0] neg_lo:[0,1] neg_hi:[0,1]
	v_pk_add_f32 v[22:23], v[30:31], v[22:23] op_sel:[0,1] op_sel_hi:[1,0]
	v_mov_b32_e32 v26, v24
	v_mov_b32_e32 v27, v23
	v_mov_b32_e32 v23, v25
	ds_write_b64 v32, v[26:27]
	ds_write_b64 v33, v[22:23]
	v_add_u32_e32 v22, 0x1200, v114
	v_lshrrev_b32_e32 v23, 6, v22
	v_and_b32_e32 v23, 60, v23
	v_ashrrev_i32_e32 v22, 12, v22
	v_add3_u32 v22, v60, v22, v23
	v_ashrrev_i32_e32 v23, 5, v22
	v_sub_u32_e32 v24, 0xffffee00, v114
	v_lshlrev_b32_e32 v23, 3, v23
	v_lshlrev_b32_e32 v27, 2, v24
	v_lshlrev_b32_e32 v22, 3, v22
	v_and_b32_e32 v23, -16, v23
	v_and_b32_e32 v25, 0x3000, v24
	v_lshlrev_b32_e32 v26, 10, v24
	v_and_b32_e32 v27, 0x3c0, v27
	v_add3_u32 v30, 0, v22, v23
	v_lshrrev_b32_e32 v22, 3, v24
	v_and_or_b32 v26, v26, s79, v27
	v_and_b32_e32 v22, 0x1e0, v22
	v_lshrrev_b32_e32 v23, 9, v25
	v_add3_u32 v22, 0, v22, v23
	v_lshlrev_b32_e32 v23, 3, v26
	v_lshrrev_b32_e32 v24, 2, v26
	v_add3_u32 v31, v22, v23, v24
	ds_read_b64 v[22:23], v30
	ds_read_b64 v[24:25], v31
	s_waitcnt lgkmcnt(0)
	v_pk_add_f32 v[26:27], v[22:23], v[24:25]
	v_pk_add_f32 v[22:23], v[22:23], v[24:25] neg_lo:[0,1] neg_hi:[0,1]
	v_lshlrev_b32_e32 v25, 16, v21
	v_pk_mul_f32 v[22:23], v[22:23], s[34:35]
	v_lshlrev_b32_e32 v24, 16, v20
	v_and_b32_e32 v21, 0xffff0000, v21
	v_and_b32_e32 v20, 0xffff0000, v20
	v_pk_mul_f32 v[26:27], v[26:27], 0.5 op_sel_hi:[1,0]
	v_pk_mul_f32 v[28:29], v[22:23], v[20:21] op_sel:[1,0] op_sel_hi:[0,1]
	v_pk_mul_f32 v[22:23], v[22:23], v[24:25] op_sel:[1,0] op_sel_hi:[0,1]
	v_pk_fma_f32 v[28:29], v[26:27], v[24:25], v[28:29] neg_lo:[0,0,1] neg_hi:[0,0,1]
	v_pk_fma_f32 v[20:21], v[26:27], v[20:21], v[22:23]
	s_nop 0
	v_pk_add_f32 v[22:23], v[28:29], v[20:21] op_sel:[0,1] op_sel_hi:[1,0] neg_lo:[0,1] neg_hi:[0,1]
	v_pk_add_f32 v[20:21], v[28:29], v[20:21] op_sel:[0,1] op_sel_hi:[1,0]
	v_mov_b32_e32 v24, v22
	v_mov_b32_e32 v25, v21
	v_mov_b32_e32 v21, v23
	ds_write_b64 v30, v[24:25]
	ds_write_b64 v31, v[20:21]
	v_add_u32_e32 v20, 0x1400, v114
	v_lshrrev_b32_e32 v21, 6, v20
	v_and_b32_e32 v21, 60, v21
	v_ashrrev_i32_e32 v20, 12, v20
	v_add3_u32 v20, v60, v20, v21
	v_ashrrev_i32_e32 v21, 5, v20
	v_sub_u32_e32 v22, 0xffffec00, v114
	v_lshlrev_b32_e32 v21, 3, v21
	v_lshlrev_b32_e32 v25, 2, v22
	v_lshlrev_b32_e32 v20, 3, v20
	v_and_b32_e32 v21, -16, v21
	v_and_b32_e32 v23, 0x3000, v22
	v_lshlrev_b32_e32 v24, 10, v22
	v_and_b32_e32 v25, 0x3c0, v25
	v_add3_u32 v28, 0, v20, v21
	v_lshrrev_b32_e32 v20, 3, v22
	v_and_or_b32 v24, v24, s79, v25
	v_and_b32_e32 v20, 0x1e0, v20
	v_lshrrev_b32_e32 v21, 9, v23
	v_add3_u32 v20, 0, v20, v21
	v_lshlrev_b32_e32 v21, 3, v24
	v_lshrrev_b32_e32 v22, 2, v24
	v_add3_u32 v29, v20, v21, v22
	ds_read_b64 v[20:21], v28
	ds_read_b64 v[22:23], v29
	s_waitcnt lgkmcnt(0)
; __device__ __forceinline__ float bf_lo(unsigned w) { return __uint_as_float(w << 16); }
; __device__ __forceinline__ float bf_hi(unsigned w) { return __uint_as_float(w & 0xffff0000u); }
; FFT_HD cf2 mk2(float x, float y) { return (cf2){x, y}; }
; FFT_HD cf2 cmul(cf2 a, cf2 b) { return mk2(a.x * b.x - a.y * b.y, a.x * b.y + a.y * b.x); }
; FFT_HD int fpos(int k) { return ((k & 15) << 10) + (((k >> 4) & 15) << 6) + (((k >> 8) & 15) << 2) + (k >> 12); }
; __device__ __forceinline__ void hy_fft_phase(LAS unsigned char* lds, int bid, int G, const bf16_t* vgT, bf16_t* zT, const float* a3, const float* wout, const float* skip, float* filt, float4* gspec) {
;     ...
;                 for (int i = 0; i < 16; ++i) { const int k = tid + NTHR * i;
;                     const int p1 = PADI(fpos(k)), p2 = PADI(fpos((FN - k) & (FN - 1)));
;                     const cf2 zk = z[p1], zm = z[p2];
;                     const cf2 V1 = mk2(0.5f * (zk.x + zm.x), 0.5f * (zk.y - zm.y)), V2 = mk2(0.5f * (zk.y + zm.y), -0.5f * (zk.x - zm.x));
;                     const cf2 Y1 = cmul(V1, mk2(bf_lo(gq[i].x), bf_hi(gq[i].x))), Y2 = cmul(V2, mk2(bf_lo(gq[i].y), bf_hi(gq[i].y)));
;                     z[p1] = mk2(Y1.x - Y2.y, Y1.y + Y2.x); z[p2] = mk2(Y1.x + Y2.y, Y2.x - Y1.y); }
	v_pk_add_f32 v[24:25], v[20:21], v[22:23]
	v_pk_add_f32 v[20:21], v[20:21], v[22:23] neg_lo:[0,1] neg_hi:[0,1]
	v_lshlrev_b32_e32 v23, 16, v19
	v_pk_mul_f32 v[20:21], v[20:21], s[34:35]
	v_lshlrev_b32_e32 v22, 16, v18
	v_and_b32_e32 v19, 0xffff0000, v19
	v_and_b32_e32 v18, 0xffff0000, v18
	v_pk_mul_f32 v[24:25], v[24:25], 0.5 op_sel_hi:[1,0]
	v_pk_mul_f32 v[26:27], v[20:21], v[18:19] op_sel:[1,0] op_sel_hi:[0,1]
	v_pk_mul_f32 v[20:21], v[20:21], v[22:23] op_sel:[1,0] op_sel_hi:[0,1]
	v_pk_fma_f32 v[26:27], v[24:25], v[22:23], v[26:27] neg_lo:[0,0,1] neg_hi:[0,0,1]
	v_pk_fma_f32 v[18:19], v[24:25], v[18:19], v[20:21]
	s_nop 0
	v_pk_add_f32 v[20:21], v[26:27], v[18:19] op_sel:[0,1] op_sel_hi:[1,0] neg_lo:[0,1] neg_hi:[0,1]
	v_pk_add_f32 v[18:19], v[26:27], v[18:19] op_sel:[0,1] op_sel_hi:[1,0]
	v_mov_b32_e32 v22, v20
	v_mov_b32_e32 v23, v19
	v_mov_b32_e32 v19, v21
	ds_write_b64 v28, v[22:23]
	ds_write_b64 v29, v[18:19]
	v_add_u32_e32 v18, 0x1600, v114
	v_lshrrev_b32_e32 v19, 6, v18
	v_and_b32_e32 v19, 60, v19
	v_ashrrev_i32_e32 v18, 12, v18
	v_add3_u32 v18, v60, v18, v19
	v_ashrrev_i32_e32 v19, 5, v18
	v_sub_u32_e32 v20, 0xffffea00, v114
	v_lshlrev_b32_e32 v19, 3, v19
	v_lshlrev_b32_e32 v23, 2, v20
	v_lshlrev_b32_e32 v18, 3, v18
	v_and_b32_e32 v19, -16, v19
	v_and_b32_e32 v21, 0x3000, v20
	v_lshlrev_b32_e32 v22, 10, v20
	v_and_b32_e32 v23, 0x3c0, v23
	v_add3_u32 v26, 0, v18, v19
	v_lshrrev_b32_e32 v18, 3, v20
	v_and_or_b32 v22, v22, s79, v23
	v_and_b32_e32 v18, 0x1e0, v18
	v_lshrrev_b32_e32 v19, 9, v21
	v_add3_u32 v18, 0, v18, v19
	v_lshlrev_b32_e32 v19, 3, v22
	v_lshrrev_b32_e32 v20, 2, v22
	v_add3_u32 v27, v18, v19, v20
	ds_read_b64 v[18:19], v26
	ds_read_b64 v[20:21], v27
	s_waitcnt lgkmcnt(0)
	v_pk_add_f32 v[22:23], v[18:19], v[20:21]
	v_pk_add_f32 v[18:19], v[18:19], v[20:21] neg_lo:[0,1] neg_hi:[0,1]
	v_lshlrev_b32_e32 v21, 16, v17
	v_pk_mul_f32 v[18:19], v[18:19], s[34:35]
	v_lshlrev_b32_e32 v20, 16, v16
	v_and_b32_e32 v17, 0xffff0000, v17
	v_and_b32_e32 v16, 0xffff0000, v16
	v_pk_mul_f32 v[22:23], v[22:23], 0.5 op_sel_hi:[1,0]
	v_pk_mul_f32 v[24:25], v[18:19], v[16:17] op_sel:[1,0] op_sel_hi:[0,1]
	v_pk_mul_f32 v[18:19], v[18:19], v[20:21] op_sel:[1,0] op_sel_hi:[0,1]
	v_pk_fma_f32 v[24:25], v[22:23], v[20:21], v[24:25] neg_lo:[0,0,1] neg_hi:[0,0,1]
	v_pk_fma_f32 v[16:17], v[22:23], v[16:17], v[18:19]
	s_nop 0
	v_pk_add_f32 v[18:19], v[24:25], v[16:17] op_sel:[0,1] op_sel_hi:[1,0] neg_lo:[0,1] neg_hi:[0,1]
	v_pk_add_f32 v[16:17], v[24:25], v[16:17] op_sel:[0,1] op_sel_hi:[1,0]
	v_mov_b32_e32 v20, v18
	v_mov_b32_e32 v21, v17
	v_mov_b32_e32 v17, v19
	ds_write_b64 v26, v[20:21]
	ds_write_b64 v27, v[16:17]
	v_add_u32_e32 v16, 0x1800, v114
	v_lshrrev_b32_e32 v17, 6, v16
	v_and_b32_e32 v17, 60, v17
	v_ashrrev_i32_e32 v16, 12, v16
	v_add3_u32 v16, v60, v16, v17
	v_ashrrev_i32_e32 v17, 5, v16
	v_sub_u32_e32 v18, 0xffffe800, v114
	v_lshlrev_b32_e32 v17, 3, v17
	v_lshlrev_b32_e32 v21, 2, v18
	v_lshlrev_b32_e32 v16, 3, v16
	v_and_b32_e32 v17, -16, v17
	v_and_b32_e32 v19, 0x3000, v18
	v_lshlrev_b32_e32 v20, 10, v18
	v_and_b32_e32 v21, 0x3c0, v21
	v_add3_u32 v24, 0, v16, v17
	v_lshrrev_b32_e32 v16, 3, v18
	v_and_or_b32 v20, v20, s79, v21
	v_and_b32_e32 v16, 0x1e0, v16
	v_lshrrev_b32_e32 v17, 9, v19
	v_add3_u32 v16, 0, v16, v17
	v_lshlrev_b32_e32 v17, 3, v20
	v_lshrrev_b32_e32 v18, 2, v20
	v_add3_u32 v25, v16, v17, v18
	ds_read_b64 v[16:17], v24
	ds_read_b64 v[18:19], v25
	s_waitcnt lgkmcnt(0)
	v_pk_add_f32 v[20:21], v[16:17], v[18:19]
	v_pk_add_f32 v[16:17], v[16:17], v[18:19] neg_lo:[0,1] neg_hi:[0,1]
	v_lshlrev_b32_e32 v19, 16, v15
	v_pk_mul_f32 v[16:17], v[16:17], s[34:35]
	v_lshlrev_b32_e32 v18, 16, v14
	v_and_b32_e32 v15, 0xffff0000, v15
	v_and_b32_e32 v14, 0xffff0000, v14
	v_pk_mul_f32 v[20:21], v[20:21], 0.5 op_sel_hi:[1,0]
	v_pk_mul_f32 v[22:23], v[16:17], v[14:15] op_sel:[1,0] op_sel_hi:[0,1]
	v_pk_mul_f32 v[16:17], v[16:17], v[18:19] op_sel:[1,0] op_sel_hi:[0,1]
	v_pk_fma_f32 v[22:23], v[20:21], v[18:19], v[22:23] neg_lo:[0,0,1] neg_hi:[0,0,1]
	v_pk_fma_f32 v[14:15], v[20:21], v[14:15], v[16:17]
	s_nop 0
	v_pk_add_f32 v[16:17], v[22:23], v[14:15] op_sel:[0,1] op_sel_hi:[1,0] neg_lo:[0,1] neg_hi:[0,1]
	v_pk_add_f32 v[14:15], v[22:23], v[14:15] op_sel:[0,1] op_sel_hi:[1,0]
	v_mov_b32_e32 v18, v16
	v_mov_b32_e32 v19, v15
	v_mov_b32_e32 v15, v17
	ds_write_b64 v24, v[18:19]
	ds_write_b64 v25, v[14:15]
	v_add_u32_e32 v14, 0x1a00, v114
	v_lshrrev_b32_e32 v15, 6, v14
	v_and_b32_e32 v15, 60, v15
	v_ashrrev_i32_e32 v14, 12, v14
	v_add3_u32 v14, v60, v14, v15
	v_ashrrev_i32_e32 v15, 5, v14
	v_sub_u32_e32 v16, 0xffffe600, v114
	v_lshlrev_b32_e32 v15, 3, v15
	v_lshlrev_b32_e32 v19, 2, v16
	v_lshlrev_b32_e32 v14, 3, v14
	v_and_b32_e32 v15, -16, v15
	v_and_b32_e32 v17, 0x3000, v16
	v_lshlrev_b32_e32 v18, 10, v16
	v_and_b32_e32 v19, 0x3c0, v19
	v_add3_u32 v22, 0, v14, v15
	v_lshrrev_b32_e32 v14, 3, v16
	v_and_or_b32 v18, v18, s79, v19
	v_and_b32_e32 v14, 0x1e0, v14
	v_lshrrev_b32_e32 v15, 9, v17
	v_add3_u32 v14, 0, v14, v15
	v_lshlrev_b32_e32 v15, 3, v18
	v_lshrrev_b32_e32 v16, 2, v18
	v_add3_u32 v23, v14, v15, v16
	ds_read_b64 v[14:15], v22
	ds_read_b64 v[16:17], v23
	s_waitcnt lgkmcnt(0)
; __device__ __forceinline__ unsigned cvt_pk_bf16(float lo, float hi) { unsigned r; asm volatile("v_cvt_pk_bf16_f32 %0, %1, %2" : "=v"(r) : "v"(lo), "v"(hi)); return r; }
; __device__ __forceinline__ float bf_lo(unsigned w) { return __uint_as_float(w << 16); }
; FFT_HD cf2 mk2(float x, float y) { return (cf2){x, y}; }
; template <int BANK, int WAITN> __device__ __forceinline__ void bg_finish1(BgState& b) {
;     if (WAITN == 32) asm volatile("s_waitcnt vmcnt(32)" ::: "memory"); else asm volatile("s_waitcnt vmcnt(0)" ::: "memory");
;     asm volatile("" : BG_TIE16(BANK * 32) :: "memory");
;     asm volatile("" : BG_TIE16(BANK * 32 + 16) :: "memory");
;     bf16_t* dst = b.dst[BANK];
;     if (dst != nullptr) {
; #pragma unroll
;         for (int c = 0; c < 4; ++c) { u32x4 w;
;             w.x = cvt_pk_bf16(b.r[(BANK * 8 + 0) * 4 + c], b.r[(BANK * 8 + 1) * 4 + c]); w.y = cvt_pk_bf16(b.r[(BANK * 8 + 2) * 4 + c], b.r[(BANK * 8 + 3) * 4 + c]);
;             w.z = cvt_pk_bf16(b.r[(BANK * 8 + 4) * 4 + c], b.r[(BANK * 8 + 5) * 4 + c]); w.w = cvt_pk_bf16(b.r[(BANK * 8 + 6) * 4 + c], b.r[(BANK * 8 + 7) * 4 + c]);
;             bf16_t* dp = dst + (c & 1) * 512 + (c >> 1) * b.o2[BANK];
;             asm volatile("global_store_dwordx4 %0, %1, off\n\ts_nop 1" :: "v"(dp), "v"(w) : "memory"); }
;     }
; }
; __device__ __forceinline__ void hy_fft_phase(LAS unsigned char* lds, int bid, int G, const bf16_t* vgT, bf16_t* zT, const float* a3, const float* wout, const float* skip, float* filt, float4* gspec) {
;     ...
;                 for (int i = 0; i < 16; ++i) { const int k = tid + NTHR * i;
;                     const int p1 = PADI(fpos(k)), p2 = PADI(fpos((FN - k) & (FN - 1)));
;                     const cf2 zk = z[p1], zm = z[p2];
;                     const cf2 V1 = mk2(0.5f * (zk.x + zm.x), 0.5f * (zk.y - zm.y)), V2 = mk2(0.5f * (zk.y + zm.y), -0.5f * (zk.x - zm.x));
;                     const cf2 Y1 = cmul(V1, mk2(bf_lo(gq[i].x), bf_hi(gq[i].x))), Y2 = cmul(V2, mk2(bf_lo(gq[i].y), bf_hi(gq[i].y)));
;                     z[p1] = mk2(Y1.x - Y2.y, Y1.y + Y2.x); z[p2] = mk2(Y1.x + Y2.y, Y2.x - Y1.y); }
;                 if (tid == 0) { const int k = FN / 2, p1 = PADI(fpos(k)); const cf2 zk = z[p1]; const float4 g1 = make_float4(bf_lo(gh.x), bf_hi(gh.x), bf_lo(gh.y), bf_hi(gh.y));
;                     z[p1] = mk2(zk.x * g1.x, zk.y * g1.z); }
;                 BG_F(1);
	v_pk_add_f32 v[18:19], v[14:15], v[16:17]
	v_pk_add_f32 v[14:15], v[14:15], v[16:17] neg_lo:[0,1] neg_hi:[0,1]
	v_lshlrev_b32_e32 v17, 16, v13
	v_pk_mul_f32 v[14:15], v[14:15], s[34:35]
	v_lshlrev_b32_e32 v16, 16, v12
	v_and_b32_e32 v13, 0xffff0000, v13
	v_and_b32_e32 v12, 0xffff0000, v12
	v_pk_mul_f32 v[18:19], v[18:19], 0.5 op_sel_hi:[1,0]
	v_pk_mul_f32 v[20:21], v[14:15], v[12:13] op_sel:[1,0] op_sel_hi:[0,1]
	v_pk_mul_f32 v[14:15], v[14:15], v[16:17] op_sel:[1,0] op_sel_hi:[0,1]
	v_pk_fma_f32 v[20:21], v[18:19], v[16:17], v[20:21] neg_lo:[0,0,1] neg_hi:[0,0,1]
	v_pk_fma_f32 v[12:13], v[18:19], v[12:13], v[14:15]
	s_nop 0
	v_pk_add_f32 v[14:15], v[20:21], v[12:13] op_sel:[0,1] op_sel_hi:[1,0] neg_lo:[0,1] neg_hi:[0,1]
	v_pk_add_f32 v[12:13], v[20:21], v[12:13] op_sel:[0,1] op_sel_hi:[1,0]
	v_mov_b32_e32 v16, v14
	v_mov_b32_e32 v17, v13
	v_mov_b32_e32 v13, v15
	ds_write_b64 v22, v[16:17]
	ds_write_b64 v23, v[12:13]
	v_add_u32_e32 v12, 0x1c00, v114
	v_lshrrev_b32_e32 v13, 6, v12
	v_and_b32_e32 v13, 60, v13
	v_ashrrev_i32_e32 v12, 12, v12
	v_add3_u32 v12, v60, v12, v13
	v_ashrrev_i32_e32 v13, 5, v12
	v_sub_u32_e32 v14, 0xffffe400, v114
	v_lshlrev_b32_e32 v13, 3, v13
	v_lshlrev_b32_e32 v17, 2, v14
	v_lshlrev_b32_e32 v12, 3, v12
	v_and_b32_e32 v13, -16, v13
	v_and_b32_e32 v15, 0x3000, v14
	v_lshlrev_b32_e32 v16, 10, v14
	v_and_b32_e32 v17, 0x3c0, v17
	v_add3_u32 v20, 0, v12, v13
	v_lshrrev_b32_e32 v12, 3, v14
	v_and_or_b32 v16, v16, s79, v17
	v_and_b32_e32 v12, 0x1e0, v12
	v_lshrrev_b32_e32 v13, 9, v15
	v_add3_u32 v12, 0, v12, v13
	v_lshlrev_b32_e32 v13, 3, v16
	v_lshrrev_b32_e32 v14, 2, v16
	v_add3_u32 v21, v12, v13, v14
	ds_read_b64 v[12:13], v20
	ds_read_b64 v[14:15], v21
	s_waitcnt lgkmcnt(0)
	v_pk_add_f32 v[16:17], v[12:13], v[14:15]
	v_pk_add_f32 v[12:13], v[12:13], v[14:15] neg_lo:[0,1] neg_hi:[0,1]
	v_lshlrev_b32_e32 v15, 16, v11
	v_pk_mul_f32 v[12:13], v[12:13], s[34:35]
	v_lshlrev_b32_e32 v14, 16, v10
	v_and_b32_e32 v11, 0xffff0000, v11
	v_and_b32_e32 v10, 0xffff0000, v10
	v_pk_mul_f32 v[16:17], v[16:17], 0.5 op_sel_hi:[1,0]
	v_pk_mul_f32 v[18:19], v[12:13], v[10:11] op_sel:[1,0] op_sel_hi:[0,1]
	v_pk_mul_f32 v[12:13], v[12:13], v[14:15] op_sel:[1,0] op_sel_hi:[0,1]
	v_pk_fma_f32 v[18:19], v[16:17], v[14:15], v[18:19] neg_lo:[0,0,1] neg_hi:[0,0,1]
	v_pk_fma_f32 v[10:11], v[16:17], v[10:11], v[12:13]
	s_nop 0
	v_pk_add_f32 v[12:13], v[18:19], v[10:11] op_sel:[0,1] op_sel_hi:[1,0] neg_lo:[0,1] neg_hi:[0,1]
	v_pk_add_f32 v[10:11], v[18:19], v[10:11] op_sel:[0,1] op_sel_hi:[1,0]
	v_mov_b32_e32 v14, v12
	v_mov_b32_e32 v15, v11
	v_mov_b32_e32 v11, v13
	ds_write_b64 v20, v[14:15]
	ds_write_b64 v21, v[10:11]
	v_add_u32_e32 v10, 0x1e00, v114
	v_lshrrev_b32_e32 v11, 6, v10
	v_and_b32_e32 v11, 60, v11
	v_ashrrev_i32_e32 v10, 12, v10
	v_add3_u32 v10, v60, v10, v11
	v_ashrrev_i32_e32 v11, 5, v10
	v_sub_u32_e32 v12, 0xffffe200, v114
	v_lshlrev_b32_e32 v11, 3, v11
	v_lshlrev_b32_e32 v15, 2, v12
	v_lshlrev_b32_e32 v10, 3, v10
	v_and_b32_e32 v11, -16, v11
	v_and_b32_e32 v13, 0x3000, v12
	v_lshlrev_b32_e32 v14, 10, v12
	v_and_b32_e32 v15, 0x3c0, v15
	v_add3_u32 v18, 0, v10, v11
	v_lshrrev_b32_e32 v10, 3, v12
	v_and_or_b32 v14, v14, s79, v15
	v_and_b32_e32 v10, 0x1e0, v10
	v_lshrrev_b32_e32 v11, 9, v13
	v_add3_u32 v10, 0, v10, v11
	v_lshlrev_b32_e32 v11, 3, v14
	v_lshrrev_b32_e32 v12, 2, v14
	v_add3_u32 v19, v10, v11, v12
	ds_read_b64 v[10:11], v18
	ds_read_b64 v[12:13], v19
	s_waitcnt lgkmcnt(0)
	v_pk_add_f32 v[14:15], v[10:11], v[12:13]
	v_pk_add_f32 v[10:11], v[10:11], v[12:13] neg_lo:[0,1] neg_hi:[0,1]
	v_lshlrev_b32_e32 v13, 16, v9
	v_pk_mul_f32 v[10:11], v[10:11], s[34:35]
	v_lshlrev_b32_e32 v12, 16, v8
	v_and_b32_e32 v9, 0xffff0000, v9
	v_and_b32_e32 v8, 0xffff0000, v8
	v_pk_mul_f32 v[14:15], v[14:15], 0.5 op_sel_hi:[1,0]
	v_pk_mul_f32 v[16:17], v[10:11], v[8:9] op_sel:[1,0] op_sel_hi:[0,1]
	v_pk_mul_f32 v[10:11], v[10:11], v[12:13] op_sel:[1,0] op_sel_hi:[0,1]
	v_pk_fma_f32 v[16:17], v[14:15], v[12:13], v[16:17] neg_lo:[0,0,1] neg_hi:[0,0,1]
	v_pk_fma_f32 v[8:9], v[14:15], v[8:9], v[10:11]
	s_nop 0
	v_pk_add_f32 v[10:11], v[16:17], v[8:9] op_sel:[0,1] op_sel_hi:[1,0] neg_lo:[0,1] neg_hi:[0,1]
	v_pk_add_f32 v[8:9], v[16:17], v[8:9] op_sel:[0,1] op_sel_hi:[1,0]
	v_mov_b32_e32 v12, v10
	v_mov_b32_e32 v13, v9
	v_mov_b32_e32 v9, v11
	ds_write_b64 v18, v[12:13]
	ds_write_b64 v19, v[8:9]
	s_and_saveexec_b64 s[48:49], vcc
	s_cbranch_execz .LBB0_700
	ds_read_b64 v[8:9], v61 offset:16
	v_lshlrev_b32_e32 v7, 16, v7
	v_lshlrev_b32_e32 v6, 16, v6
	s_waitcnt lgkmcnt(0)
	v_pk_mul_f32 v[6:7], v[8:9], v[6:7]
	ds_write_b64 v61, v[6:7] offset:16
.LBB0_700:
	s_or_b64 exec, exec, s[48:49]
	s_waitcnt vmcnt(32)
	v_cmp_ne_u64_e32 vcc, 0, v[2:3]
	s_and_saveexec_b64 s[48:49], vcc
	s_cbranch_execz .LBB0_702
	v_cvt_pk_bf16_f32 v6, v89, v92
	v_cvt_pk_bf16_f32 v7, v91, v94
	v_cvt_pk_bf16_f32 v8, v93, v96
	v_cvt_pk_bf16_f32 v9, v95, v97
	s_lshl_b32 s12, s44, 1
	global_store_dwordx4 v[2:3], v[6:9], off nt
	s_nop 1
	v_cvt_pk_bf16_f32 v6, v74, v76
	v_cvt_pk_bf16_f32 v7, v75, v78
	v_cvt_pk_bf16_f32 v8, v77, v80
	v_cvt_pk_bf16_f32 v9, v79, v81
	v_lshl_add_u64 v[10:11], v[2:3], 0, s[22:23]
	global_store_dwordx4 v[10:11], v[6:9], off nt
	s_nop 1
	v_cvt_pk_bf16_f32 v6, v50, v52
	v_cvt_pk_bf16_f32 v7, v51, v54
	v_cvt_pk_bf16_f32 v8, v53, v56
	v_cvt_pk_bf16_f32 v9, v55, v57
	v_lshl_add_u64 v[2:3], v[2:3], 0, s[12:13]
	global_store_dwordx4 v[2:3], v[6:9], off nt
	s_nop 1
	v_cvt_pk_bf16_f32 v6, v42, v44
	v_cvt_pk_bf16_f32 v7, v43, v46
	v_cvt_pk_bf16_f32 v8, v45, v48
	v_cvt_pk_bf16_f32 v9, v47, v49
	v_lshl_add_u64 v[2:3], v[10:11], 0, s[12:13]
	global_store_dwordx4 v[2:3], v[6:9], off nt
	s_nop 1

; template <int BANK> __device__ __forceinline__ void bg_issue1(BgState& b, int wg, int NW, int lane) {
;     ...
;     for (int i = 0; i < 8; ++i) { const float* p = src + (size_t)i * ldS;
;         asm volatile("global_load_dword %0, %4, off\n\tglobal_load_dword %1, %4, off offset:256\n\tglobal_load_dword %2, %4, off offset:512\n\tglobal_load_dword %3, %4, off offset:768"
;                      : "=&v"(b.r[(BANK * 8 + i) * 4 + 0]), "=&v"(b.r[(BANK * 8 + i) * 4 + 1]), "=&v"(b.r[(BANK * 8 + i) * 4 + 2]), "=&v"(b.r[(BANK * 8 + i) * 4 + 3]) : "v"(p) : "memory"); }
;     b.st += 1;
; }
; template <bool INV, class ZP> FFT_HD void fft_r4_pass(ZP z, int tid, int nthr) {
;     for (int w = tid; w < FN / 4; w += nthr) {
;         const int base = PADI(4 * w);
;         cf2 a = z[base], b = z[base + 1], c = z[base + 2], d = z[base + 3];
.LBB0_712:
	s_nop 6
	global_load_dword v153, v[2:3], off nt
	global_load_dword v145, v[2:3], off offset:256 nt
	global_load_dword v137, v[2:3], off offset:512 nt
	global_load_dword v129, v[2:3], off offset:768 nt
	s_lshl_b32 s12, s44, 2
	v_lshl_add_u64 v[2:3], v[2:3], 0, s[12:13]
	global_load_dword v155, v[2:3], off nt
	global_load_dword v147, v[2:3], off offset:256 nt
	global_load_dword v139, v[2:3], off offset:512 nt
	global_load_dword v131, v[2:3], off offset:768 nt
	v_lshl_add_u64 v[2:3], v[2:3], 0, s[12:13]
	global_load_dword v154, v[2:3], off nt
	global_load_dword v146, v[2:3], off offset:256 nt
	global_load_dword v138, v[2:3], off offset:512 nt
	global_load_dword v130, v[2:3], off offset:768 nt
	v_lshl_add_u64 v[2:3], v[2:3], 0, s[12:13]
	global_load_dword v157, v[2:3], off nt
	global_load_dword v149, v[2:3], off offset:256 nt
	global_load_dword v141, v[2:3], off offset:512 nt
	global_load_dword v133, v[2:3], off offset:768 nt
	v_lshl_add_u64 v[2:3], v[2:3], 0, s[12:13]
	global_load_dword v156, v[2:3], off nt
	global_load_dword v148, v[2:3], off offset:256 nt
	global_load_dword v140, v[2:3], off offset:512 nt
	global_load_dword v132, v[2:3], off offset:768 nt
	v_lshl_add_u64 v[2:3], v[2:3], 0, s[12:13]
	global_load_dword v159, v[2:3], off nt
	global_load_dword v151, v[2:3], off offset:256 nt
	global_load_dword v143, v[2:3], off offset:512 nt
	global_load_dword v135, v[2:3], off offset:768 nt
	v_lshl_add_u64 v[2:3], v[2:3], 0, s[12:13]
	global_load_dword v158, v[2:3], off nt
	global_load_dword v150, v[2:3], off offset:256 nt
	global_load_dword v142, v[2:3], off offset:512 nt
	global_load_dword v134, v[2:3], off offset:768 nt
	v_lshl_add_u64 v[2:3], v[2:3], 0, s[12:13]
	global_load_dword v160, v[2:3], off nt
	global_load_dword v152, v[2:3], off offset:256 nt
	global_load_dword v144, v[2:3], off offset:512 nt
	global_load_dword v136, v[2:3], off offset:768 nt
	v_cmp_gt_i32_e32 vcc, s75, v128
	s_and_saveexec_b64 s[44:45], vcc
	s_cbranch_execz .LBB0_715
	v_lshl_add_u32 v2, v128, 5, 0
	s_mov_b64 s[50:51], 0
	v_mov_b32_e32 v3, v128

; __device__ __forceinline__ unsigned cvt_pk_bf16(float lo, float hi) { unsigned r; asm volatile("v_cvt_pk_bf16_f32 %0, %1, %2" : "=v"(r) : "v"(lo), "v"(hi)); return r; }
; #define BG_I(x) bg_issue1<x>(bg, bgwg, bgNW, bglane)
; #define BG_F(y) bg_finish1<y, 32>(bg)
; template <int BANK, int WAITN> __device__ __forceinline__ void bg_finish1(BgState& b) {
;     if (WAITN == 32) asm volatile("s_waitcnt vmcnt(32)" ::: "memory"); else asm volatile("s_waitcnt vmcnt(0)" ::: "memory");
;     asm volatile("" : BG_TIE16(BANK * 32) :: "memory");
;     asm volatile("" : BG_TIE16(BANK * 32 + 16) :: "memory");
;     bf16_t* dst = b.dst[BANK];
;     if (dst != nullptr) {
; #pragma unroll
;         for (int c = 0; c < 4; ++c) { u32x4 w;
;             w.x = cvt_pk_bf16(b.r[(BANK * 8 + 0) * 4 + c], b.r[(BANK * 8 + 1) * 4 + c]); w.y = cvt_pk_bf16(b.r[(BANK * 8 + 2) * 4 + c], b.r[(BANK * 8 + 3) * 4 + c]);
;             w.z = cvt_pk_bf16(b.r[(BANK * 8 + 4) * 4 + c], b.r[(BANK * 8 + 5) * 4 + c]); w.w = cvt_pk_bf16(b.r[(BANK * 8 + 6) * 4 + c], b.r[(BANK * 8 + 7) * 4 + c]);
;             bf16_t* dp = dst + (c & 1) * 512 + (c >> 1) * b.o2[BANK];
;             asm volatile("global_store_dwordx4 %0, %1, off\n\ts_nop 1" :: "v"(dp), "v"(w) : "memory"); }
;     }
; }
; __device__ __forceinline__ void hy_fft_phase(LAS unsigned char* lds, int bid, int G, const bf16_t* vgT, bf16_t* zT, const float* a3, const float* wout, const float* skip, float* filt, float4* gspec) {
;     ...
;             BG_I(1); fft_r4_pass<true>(z, tid, NTHR); __syncthreads(); BG_F(0);
.LBB0_715:
	s_or_b64 exec, exec, s[44:45]
	s_waitcnt lgkmcnt(0)
	s_barrier
	s_waitcnt vmcnt(32)
	v_cmp_ne_u64_e32 vcc, 0, v[4:5]
	s_and_saveexec_b64 s[44:45], vcc
	s_cbranch_execz .LBB0_717
	v_cvt_pk_bf16_f32 v6, v106, v108
	v_cvt_pk_bf16_f32 v7, v107, v110
	v_cvt_pk_bf16_f32 v8, v109, v112
	v_cvt_pk_bf16_f32 v9, v111, v113
	s_lshl_b32 s12, s46, 1
	global_store_dwordx4 v[4:5], v[6:9], off nt
	s_nop 1
	v_cvt_pk_bf16_f32 v6, v98, v100
	v_cvt_pk_bf16_f32 v7, v99, v102
	v_cvt_pk_bf16_f32 v8, v101, v104
	v_cvt_pk_bf16_f32 v9, v103, v105
	v_lshl_add_u64 v[10:11], v[4:5], 0, s[22:23]
	global_store_dwordx4 v[10:11], v[6:9], off nt
	s_nop 1
	v_cvt_pk_bf16_f32 v6, v82, v84
	v_cvt_pk_bf16_f32 v7, v83, v86
	v_lshl_add_u64 v[2:3], v[4:5], 0, s[12:13]
	v_cvt_pk_bf16_f32 v8, v85, v88
	v_cvt_pk_bf16_f32 v9, v87, v90
	s_nop 0
	global_store_dwordx4 v[2:3], v[6:9], off nt
	s_nop 1
	v_cvt_pk_bf16_f32 v2, v68, v41
	v_cvt_pk_bf16_f32 v3, v40, v70
	v_cvt_pk_bf16_f32 v4, v69, v72
	v_cvt_pk_bf16_f32 v5, v71, v73
	v_lshl_add_u64 v[6:7], v[10:11], 0, s[12:13]
	global_store_dwordx4 v[6:7], v[2:5], off nt
	s_nop 1

; FFT_HD cf2 mk2(float x, float y) { return (cf2){x, y}; }
; FFT_HD void fft_sincos(float frac, float& s, float& c) { s = __builtin_amdgcn_sinf(frac); c = __builtin_amdgcn_cosf(frac); }
; FFT_HD cf2 cmul(cf2 a, cf2 b) { return mk2(a.x * b.x - a.y * b.y, a.x * b.y + a.y * b.x); }
; template <int BANK> __device__ __forceinline__ void bg_issue1(BgState& b, int wg, int NW, int lane) {
;     ...
;     for (int i = 0; i < 8; ++i) { const float* p = src + (size_t)i * ldS;
;         asm volatile("global_load_dword %0, %4, off\n\tglobal_load_dword %1, %4, off offset:256\n\tglobal_load_dword %2, %4, off offset:512\n\tglobal_load_dword %3, %4, off offset:768"
;                      : "=&v"(b.r[(BANK * 8 + i) * 4 + 0]), "=&v"(b.r[(BANK * 8 + i) * 4 + 1]), "=&v"(b.r[(BANK * 8 + i) * 4 + 2]), "=&v"(b.r[(BANK * 8 + i) * 4 + 3]) : "v"(p) : "memory"); }
; FFT_HD void fft_gen_tw(float frac, cf2 (&tw)[16]) {
;     float sn, cs; fft_sincos(frac, sn, cs);
;     tw[1] = mk2(cs, -sn);
;     tw[2] = cmul(tw[1], tw[1]); tw[3] = cmul(tw[2], tw[1]); tw[4] = cmul(tw[2], tw[2]); tw[5] = cmul(tw[4], tw[1]); tw[6] = cmul(tw[4], tw[2]); tw[7] = cmul(tw[4], tw[3]);
;     tw[8] = cmul(tw[4], tw[4]);
; #pragma unroll
;     for (int j = 9; j < 16; ++j) tw[j] = cmul(tw[8], tw[j - 8]);
; }
; template <bool INV, int lS, class ZP> FFT_HD void fft_r16_pass(ZP z, int tid) {
;     constexpr int S = 1 << lS, STEP = (S >= 64) ? S + S / 32 : S;
;     constexpr float inv = 1.0f / (float)(16 * S);
;     cf2 tw[16];
;     if (lS != 10) {
;         fft_gen_tw((float)(tid & (S - 1)) * inv, tw);
;         const int w0 = tid, w1 = tid + 512;
;         const int pb0 = PADI(((w0 >> lS) << (lS + 4)) + (w0 & (S - 1))), pb1 = PADI(((w1 >> lS) << (lS + 4)) + (w1 & (S - 1)));
;         cf2 x[16], y[16];
; #pragma unroll
;         for (int j = 0; j < 16; ++j) x[j] = z[pb0 + j * STEP];
; #pragma unroll
;         for (int j = 0; j < 16; ++j) y[j] = z[pb1 + j * STEP];
.LBB0_727:
	s_nop 6
	s_lshl_b32 s12, s46, 2
	v_and_b32_e32 v24, 3, v128
	global_load_dword v161, v[2:3], off nt
	global_load_dword v120, v[2:3], off offset:256 nt
	global_load_dword v110, v[2:3], off offset:512 nt
	global_load_dword v102, v[2:3], off offset:768 nt
	v_lshl_add_u64 v[2:3], v[2:3], 0, s[12:13]
	v_cvt_f32_ubyte0_e32 v4, v24
	global_load_dword v163, v[2:3], off nt
	global_load_dword v122, v[2:3], off offset:256 nt
	global_load_dword v112, v[2:3], off offset:512 nt
	global_load_dword v104, v[2:3], off offset:768 nt
	v_lshl_add_u64 v[2:3], v[2:3], 0, s[12:13]
	v_mul_f32_e32 v4, 0x3c800000, v4
	global_load_dword v162, v[2:3], off nt
	global_load_dword v121, v[2:3], off offset:256 nt
	global_load_dword v111, v[2:3], off offset:512 nt
	global_load_dword v103, v[2:3], off offset:768 nt
	v_lshl_add_u64 v[2:3], v[2:3], 0, s[12:13]
	v_sin_f32_e32 v94, v4
	global_load_dword v165, v[2:3], off nt
	global_load_dword v124, v[2:3], off offset:256 nt
	global_load_dword v114, v[2:3], off offset:512 nt
	global_load_dword v106, v[2:3], off offset:768 nt
	v_lshl_add_u64 v[2:3], v[2:3], 0, s[12:13]
	v_cos_f32_e32 v96, v4
	global_load_dword v164, v[2:3], off nt
	global_load_dword v123, v[2:3], off offset:256 nt
	global_load_dword v113, v[2:3], off offset:512 nt
	global_load_dword v105, v[2:3], off offset:768 nt
	v_lshl_add_u64 v[2:3], v[2:3], 0, s[12:13]
	global_load_dword v167, v[2:3], off nt
	global_load_dword v126, v[2:3], off offset:256 nt
	global_load_dword v116, v[2:3], off offset:512 nt
	global_load_dword v108, v[2:3], off offset:768 nt
	v_lshl_add_u64 v[2:3], v[2:3], 0, s[12:13]
	global_load_dword v166, v[2:3], off nt
	global_load_dword v125, v[2:3], off offset:256 nt
	global_load_dword v115, v[2:3], off offset:512 nt
	global_load_dword v107, v[2:3], off offset:768 nt
	v_lshl_add_u64 v[2:3], v[2:3], 0, s[12:13]
	v_xor_b32_e32 v97, 0x80000000, v94
	global_load_dword v168, v[2:3], off nt
	global_load_dword v127, v[2:3], off offset:256 nt
	global_load_dword v117, v[2:3], off offset:512 nt
	global_load_dword v109, v[2:3], off offset:768 nt
	v_mov_b32_e32 v95, v96
	v_mov_b32_e32 v2, v94
	v_mov_b32_e32 v3, v97
	v_pk_mul_f32 v[2:3], v[94:95], v[2:3]
	v_lshlrev_b32_e32 v169, 4, v128
	v_pk_fma_f32 v[38:39], v[96:97], v[96:97], v[2:3] op_sel_hi:[0,1,1] neg_lo:[0,0,1] neg_hi:[0,0,1]
	v_pk_fma_f32 v[40:41], v[96:97], v[96:97], v[2:3] op_sel_hi:[0,1,1]
	v_pk_mov_b32 v[4:5], v[40:41], v[38:39] op_sel:[1,0]
	v_mov_b32_e32 v2, v38
	v_mov_b32_e32 v3, v41
	v_pk_mul_f32 v[10:11], v[40:41], v[4:5] op_sel:[1,0]
	v_mov_b32_e32 v97, v94
	v_pk_fma_f32 v[56:57], v[38:39], v[2:3], v[10:11] op_sel_hi:[0,1,1] neg_lo:[0,0,1] neg_hi:[0,0,1]
	v_pk_fma_f32 v[186:187], v[38:39], v[2:3], v[10:11] op_sel_hi:[0,1,1]
	v_mov_b32_e32 v68, v56
	v_mov_b32_e32 v69, v187
	v_pk_mul_f32 v[18:19], v[68:69], v[68:69]
	v_pk_mul_f32 v[20:21], v[68:69], v[186:187] op_sel:[0,1] op_sel_hi:[1,0]
	v_mov_b32_e32 v22, v18
	v_mov_b32_e32 v23, v20
	v_pk_mov_b32 v[18:19], v[18:19], v[20:21] op_sel:[1,0]
	v_pk_mul_f32 v[6:7], v[96:97], v[2:3]
	v_pk_add_f32 v[48:49], v[22:23], v[18:19] neg_lo:[0,1] neg_hi:[0,1]
	v_pk_add_f32 v[52:53], v[22:23], v[18:19]
	v_pk_mul_f32 v[8:9], v[94:95], v[2:3]
	v_mov_b32_e32 v188, v48
	v_mov_b32_e32 v189, v53
	v_pk_mul_f32 v[14:15], v[2:3], v[68:69]
	v_pk_mul_f32 v[16:17], v[4:5], v[68:69]
	v_pk_mul_f32 v[190:191], v[2:3], v[188:189]
	v_pk_mul_f32 v[192:193], v[4:5], v[188:189]
	v_mov_b32_e32 v2, v6
	v_mov_b32_e32 v3, v9
	v_pk_mov_b32 v[4:5], v[6:7], v[8:9] op_sel:[1,0]
	v_pk_mul_f32 v[10:11], v[96:97], v[68:69]
	v_pk_add_f32 v[72:73], v[2:3], v[4:5]
	v_pk_add_f32 v[54:55], v[2:3], v[4:5] neg_lo:[0,1] neg_hi:[0,1]
	v_pk_mul_f32 v[12:13], v[94:95], v[68:69]
	v_mov_b32_e32 v2, v72
	v_mov_b32_e32 v3, v55
	v_pk_mov_b32 v[4:5], v[54:55], v[72:73] op_sel:[1,0]
	v_pk_mul_f32 v[6:7], v[68:69], v[2:3]
	v_pk_mul_f32 v[8:9], v[68:69], v[4:5]
	v_pk_mul_f32 v[100:101], v[2:3], v[188:189]
	v_pk_mul_f32 v[98:99], v[4:5], v[188:189]
	v_mov_b32_e32 v2, v10
	v_mov_b32_e32 v3, v13
	v_pk_mov_b32 v[4:5], v[10:11], v[12:13] op_sel:[1,0]
	v_pk_mov_b32 v[70:71], v[186:187], v[56:57] op_sel:[1,0]
	v_pk_add_f32 v[202:203], v[2:3], v[4:5]
	v_pk_add_f32 v[204:205], v[2:3], v[4:5] neg_lo:[0,1] neg_hi:[0,1]
	v_mov_b32_e32 v2, v14
	v_mov_b32_e32 v3, v16
	v_mov_b32_e32 v16, v15
	v_pk_add_f32 v[46:47], v[2:3], v[16:17] neg_lo:[0,1] neg_hi:[0,1]
	v_pk_add_f32 v[50:51], v[2:3], v[16:17]
	v_mov_b32_e32 v2, v46
	v_mov_b32_e32 v3, v51
	v_pk_mul_f32 v[210:211], v[188:189], v[2:3]
	v_pk_mov_b32 v[2:3], v[50:51], v[46:47] op_sel:[1,0]
	v_lshlrev_b32_e32 v5, 3, v24
	v_pk_mul_f32 v[212:213], v[188:189], v[2:3]
	v_mov_b32_e32 v2, v6
	v_mov_b32_e32 v3, v8
	v_mov_b32_e32 v8, v7
	v_pk_add_f32 v[78:79], v[2:3], v[8:9] neg_lo:[0,1] neg_hi:[0,1]
	v_pk_add_f32 v[80:81], v[2:3], v[8:9]
	v_mov_b32_e32 v2, v78
	v_mov_b32_e32 v3, v81
	v_pk_mul_f32 v[214:215], v[188:189], v[2:3]
	v_pk_mov_b32 v[2:3], v[80:81], v[78:79] op_sel:[1,0]
	v_mov_b32_e32 v42, v202
	v_pk_mul_f32 v[216:217], v[188:189], v[2:3]
	v_and_b32_e32 v2, 0xffffffc0, v169
	v_bfe_i32 v3, v128, 1, 27
	v_add_u32_e32 v4, 0x2000, v2
	v_lshlrev_b32_e32 v2, 3, v2
	v_lshlrev_b32_e32 v3, 3, v3
	v_add3_u32 v2, 0, v2, v5
	v_and_b32_e32 v3, -16, v3
	v_add_u32_e32 v65, v2, v3
	ds_read2_b64 v[170:173], v65 offset1:4
	ds_read2_b64 v[74:77], v65 offset0:8 offset1:12
	ds_read2_b64 v[82:85], v65 offset0:16 offset1:20
	ds_read2_b64 v[86:89], v65 offset0:24 offset1:28
	ds_read2_b64 v[90:93], v65 offset0:32 offset1:36
	ds_read2_b64 v[174:177], v65 offset0:40 offset1:44
	ds_read2_b64 v[178:181], v65 offset0:48 offset1:52
	ds_read2_b64 v[182:185], v65 offset0:56 offset1:60
	s_waitcnt lgkmcnt(6)
; FFT_HD cf2 mk2(float x, float y) { return (cf2){x, y}; }
; FFT_HD cf2 cmul(cf2 a, cf2 b) { return mk2(a.x * b.x - a.y * b.y, a.x * b.y + a.y * b.x); }
; FFT_HD cf2 cmulc(cf2 a, cf2 b) { return mk2(a.x * b.x + a.y * b.y, a.y * b.x - a.x * b.y); }
; FFT_HD cf2 cadd(cf2 a, cf2 b) { return mk2(a.x + b.x, a.y + b.y); }
; FFT_HD cf2 csub(cf2 a, cf2 b) { return mk2(a.x - b.x, a.y - b.y); }
; template <bool INV> FFT_HD void dft4(cf2& a, cf2& b, cf2& c, cf2& d) {
;     const cf2 s0 = cadd(a, c), s1 = csub(a, c), s2 = cadd(b, d), s3 = csub(b, d);
;     a = cadd(s0, s2); c = csub(s0, s2);
;     const cf2 r = INV ? mk2(-s3.y, s3.x) : mk2(s3.y, -s3.x);
;     b = cadd(s1, r); d = csub(s1, r);
; }
; template <bool INV> FFT_HD void dft16(cf2 (&x)[16]) {
;     const float C1 = 0.9238795325112867f, S1 = 0.3826834323650898f, H = 0.7071067811865476f;
; #pragma unroll
;     for (int b = 0; b < 4; ++b) dft4<INV>(x[b], x[4 + b], x[8 + b], x[12 + b]);
;     const float s = INV ? -1.f : 1.f;
;     x[4 + 1] = cmul(x[4 + 1], mk2(C1, -s * S1)); x[8 + 1] = cmul(x[8 + 1], mk2(H, -s * H));   x[12 + 1] = cmul(x[12 + 1], mk2(S1, -s * C1));
;     x[4 + 2] = cmul(x[4 + 2], mk2(H, -s * H));   x[8 + 2] = cmul(x[8 + 2], mk2(0.f, -s));     x[12 + 2] = cmul(x[12 + 2], mk2(-H, -s * H));
;     x[4 + 3] = cmul(x[4 + 3], mk2(S1, -s * C1)); x[8 + 3] = cmul(x[8 + 3], mk2(-H, -s * H));  x[12 + 3] = cmul(x[12 + 3], mk2(-C1, s * S1));
; #pragma unroll
;     for (int c = 0; c < 4; ++c) dft4<INV>(x[4 * c], x[4 * c + 1], x[4 * c + 2], x[4 * c + 3]);
; #pragma unroll
;     for (int c = 0; c < 4; ++c)
; #pragma unroll
;         for (int d = c + 1; d < 4; ++d) { const cf2 t = x[4 * c + d]; x[4 * c + d] = x[4 * d + c]; x[4 * d + c] = t; }
; }
; template <bool INV, int lS, class ZP> FFT_HD void fft_r16_pass(ZP z, int tid) {
;     ...
;         if (INV) {
; #pragma unroll
;             for (int j = 1; j < 16; ++j) x[j] = cmulc(x[j], tw[j]);
;         }
;         dft16<INV>(x);
	v_pk_mul_f32 v[218:219], v[40:41], v[74:75] op_sel:[1,1] op_sel_hi:[1,0]
	v_mov_b32_e32 v43, v205
	v_pk_fma_f32 v[220:221], v[38:39], v[74:75], v[218:219] op_sel_hi:[0,1,1]
	v_pk_fma_f32 v[218:219], v[38:39], v[74:75], v[218:219] op_sel_hi:[0,1,1] neg_lo:[0,0,1] neg_hi:[0,0,1]
	v_pk_mul_f32 v[74:75], v[54:55], v[76:77] op_sel:[1,1] op_sel_hi:[1,0]
	v_pk_mov_b32 v[44:45], v[204:205], v[202:203] op_sel:[1,0]
	v_pk_fma_f32 v[222:223], v[72:73], v[76:77], v[74:75] op_sel_hi:[0,1,1]
	v_pk_fma_f32 v[224:225], v[72:73], v[76:77], v[74:75] op_sel_hi:[0,1,1] neg_lo:[0,0,1] neg_hi:[0,0,1]
	s_waitcnt lgkmcnt(5)
	v_pk_mul_f32 v[74:75], v[186:187], v[82:83] op_sel:[1,1] op_sel_hi:[1,0]
	v_mul_f32_e32 v54, v94, v53
	v_pk_fma_f32 v[186:187], v[56:57], v[82:83], v[74:75]
	v_pk_fma_f32 v[74:75], v[56:57], v[82:83], v[74:75] op_sel_hi:[0,1,1] neg_lo:[0,0,1] neg_hi:[0,0,1]
	v_mov_b32_e32 v187, v75
	v_pk_mul_f32 v[74:75], v[204:205], v[84:85] op_sel:[1,1] op_sel_hi:[1,0]
	s_waitcnt lgkmcnt(3)
	v_mov_b32_e32 v82, v92
	v_pk_fma_f32 v[204:205], v[202:203], v[84:85], v[74:75] op_sel_hi:[0,1,1]
	v_pk_fma_f32 v[202:203], v[202:203], v[84:85], v[74:75] op_sel_hi:[0,1,1] neg_lo:[0,0,1] neg_hi:[0,0,1]
	v_pk_mul_f32 v[74:75], v[50:51], v[86:87] op_sel:[1,1] op_sel_hi:[1,0]
	v_pk_mov_b32 v[84:85], v[92:93], v[172:173] op_sel:[1,0]
	v_pk_fma_f32 v[226:227], v[46:47], v[86:87], v[74:75] op_sel_hi:[0,1,1]
	v_pk_fma_f32 v[228:229], v[46:47], v[86:87], v[74:75] op_sel_hi:[0,1,1] neg_lo:[0,0,1] neg_hi:[0,0,1]
	v_pk_mul_f32 v[74:75], v[80:81], v[88:89] op_sel:[1,1] op_sel_hi:[1,0]
	v_mov_b32_e32 v83, v173
	v_pk_fma_f32 v[230:231], v[78:79], v[88:89], v[74:75] op_sel_hi:[0,1,1]
	v_pk_fma_f32 v[232:233], v[78:79], v[88:89], v[74:75] op_sel_hi:[0,1,1] neg_lo:[0,0,1] neg_hi:[0,0,1]
	v_pk_mul_f32 v[74:75], v[52:53], v[90:91] op_sel:[1,1] op_sel_hi:[1,0]
	v_pk_mul_f32 v[200:201], v[70:71], v[188:189]
	v_pk_fma_f32 v[234:235], v[48:49], v[90:91], v[74:75]
	v_pk_fma_f32 v[74:75], v[48:49], v[90:91], v[74:75] op_sel_hi:[0,1,1] neg_lo:[0,0,1] neg_hi:[0,0,1]
	v_mov_b32_e32 v235, v75
	v_pk_fma_f32 v[74:75], v[96:97], v[188:189], v[54:55] op_sel_hi:[1,1,0]
	v_mul_f32_e32 v54, v96, v53
	v_pk_fma_f32 v[76:77], v[94:95], v[188:189], v[54:55] op_sel_hi:[1,1,0] neg_lo:[1,0,0] neg_hi:[1,0,0]
	v_mov_b32_e32 v75, v96
	v_mov_b32_e32 v77, v94
	v_pk_mul_f32 v[86:87], v[76:77], v[84:85]
	v_pk_add_f32 v[88:89], v[192:193], v[192:193] op_sel:[0,1] op_sel_hi:[0,1]
	v_pk_fma_f32 v[172:173], v[74:75], v[82:83], v[86:87]
	v_pk_mul_f32 v[82:83], v[76:77], v[82:83]
	v_pk_mul_f32 v[198:199], v[68:69], v[188:189]
	v_pk_mul_f32 v[206:207], v[188:189], v[42:43]
	v_pk_mul_f32 v[208:209], v[188:189], v[44:45]
	v_pk_fma_f32 v[188:189], v[74:75], v[84:85], v[82:83] neg_lo:[0,0,1] neg_hi:[0,0,1]
	v_pk_add_f32 v[86:87], v[190:191], v[190:191] op_sel:[0,1] op_sel_hi:[0,1] neg_lo:[0,1] neg_hi:[0,1]
	s_waitcnt lgkmcnt(2)
	v_pk_mul_f32 v[82:83], v[88:89], v[174:175]
	v_pk_add_f32 v[94:95], v[200:201], v[200:201] op_sel:[0,1] op_sel_hi:[0,1]
	v_pk_fma_f32 v[190:191], v[86:87], v[174:175], v[82:83] op_sel:[0,0,1] op_sel_hi:[1,1,0]
	v_pk_fma_f32 v[174:175], v[86:87], v[174:175], v[82:83] op_sel:[0,0,1] op_sel_hi:[1,1,0] neg_lo:[0,0,1] neg_hi:[0,0,1]
	v_pk_add_f32 v[96:97], v[198:199], v[198:199] op_sel:[0,1] op_sel_hi:[0,1] neg_lo:[0,1] neg_hi:[0,1]
	s_waitcnt lgkmcnt(1)
	v_pk_mul_f32 v[82:83], v[94:95], v[178:179]
	v_pk_add_f32 v[84:85], v[206:207], v[206:207] op_sel:[0,1] op_sel_hi:[0,1] neg_lo:[0,1] neg_hi:[0,1]
	v_pk_fma_f32 v[192:193], v[96:97], v[178:179], v[82:83] op_sel:[0,0,1] op_sel_hi:[1,1,0]
	v_pk_fma_f32 v[82:83], v[96:97], v[178:179], v[82:83] op_sel:[0,0,1] op_sel_hi:[1,1,0] neg_lo:[0,0,1] neg_hi:[0,0,1]
	v_pk_add_f32 v[92:93], v[212:213], v[212:213] op_sel:[0,1] op_sel_hi:[0,1]
	v_mov_b32_e32 v193, v83
	v_pk_add_f32 v[82:83], v[208:209], v[208:209] op_sel:[0,1] op_sel_hi:[0,1]
	v_pk_mul_f32 v[90:91], v[82:83], v[180:181]
	s_waitcnt lgkmcnt(0)
	v_pk_mul_f32 v[198:199], v[92:93], v[182:183]
	v_pk_fma_f32 v[178:179], v[84:85], v[180:181], v[90:91] op_sel:[0,0,1] op_sel_hi:[1,1,0]
	v_pk_fma_f32 v[180:181], v[84:85], v[180:181], v[90:91] op_sel:[0,0,1] op_sel_hi:[1,1,0] neg_lo:[0,0,1] neg_hi:[0,0,1]
	v_pk_add_f32 v[90:91], v[210:211], v[210:211] op_sel:[0,1] op_sel_hi:[0,1] neg_lo:[0,1] neg_hi:[0,1]
	v_mov_b32_e32 v202, v204
	v_mov_b32_e32 v179, v181
	v_pk_fma_f32 v[200:201], v[90:91], v[182:183], v[198:199] op_sel:[0,0,1] op_sel_hi:[1,1,0]
	v_pk_fma_f32 v[182:183], v[90:91], v[182:183], v[198:199] op_sel:[0,0,1] op_sel_hi:[1,1,0] neg_lo:[0,0,1] neg_hi:[0,0,1]
	v_mov_b32_e32 v221, v219
	v_mov_b32_e32 v228, v226
	v_mov_b32_e32 v191, v175
	v_mov_b32_e32 v182, v200
	v_pk_add_f32 v[210:211], v[188:189], v[172:173] op_sel:[1,0] op_sel_hi:[0,1]
	v_pk_add_f32 v[212:213], v[202:203], v[178:179]
	v_pk_mov_b32 v[204:205], v[172:173], v[204:205] op_sel:[1,0]
	v_mov_b32_e32 v202, v189
	v_mov_b32_e32 v173, v181
	v_mov_b32_e32 v236, v188
	v_pk_add_f32 v[172:173], v[202:203], v[172:173] neg_lo:[0,1] neg_hi:[0,1]
	v_pk_add_f32 v[188:189], v[220:221], v[190:191]
	v_pk_add_f32 v[202:203], v[228:229], v[182:183]
	v_mov_b32_e32 v221, v229
	v_mov_b32_e32 v191, v183
	v_mov_b32_e32 v237, v178
	v_pk_add_f32 v[182:183], v[220:221], v[190:191] neg_lo:[0,1] neg_hi:[0,1]
	v_pk_add_f32 v[190:191], v[188:189], v[202:203]
	v_pk_add_f32 v[188:189], v[188:189], v[202:203] neg_lo:[0,1] neg_hi:[0,1]
	v_pk_add_f32 v[198:199], v[170:171], v[234:235]
	v_pk_add_f32 v[206:207], v[186:187], v[192:193]
	v_pk_add_f32 v[178:179], v[204:205], v[236:237] neg_lo:[0,1] neg_hi:[0,1]
	v_pk_mov_b32 v[204:205], v[218:219], v[226:227] op_sel:[1,0]
; FFT_HD cf2 mk2(float x, float y) { return (cf2){x, y}; }
; FFT_HD cf2 cmul(cf2 a, cf2 b) { return mk2(a.x * b.x - a.y * b.y, a.x * b.y + a.y * b.x); }
; FFT_HD cf2 cadd(cf2 a, cf2 b) { return mk2(a.x + b.x, a.y + b.y); }
; FFT_HD cf2 csub(cf2 a, cf2 b) { return mk2(a.x - b.x, a.y - b.y); }
; template <bool INV> FFT_HD void dft4(cf2& a, cf2& b, cf2& c, cf2& d) {
;     const cf2 s0 = cadd(a, c), s1 = csub(a, c), s2 = cadd(b, d), s3 = csub(b, d);
;     a = cadd(s0, s2); c = csub(s0, s2);
;     const cf2 r = INV ? mk2(-s3.y, s3.x) : mk2(s3.y, -s3.x);
;     b = cadd(s1, r); d = csub(s1, r);
; }
; template <bool INV> FFT_HD void dft16(cf2 (&x)[16]) {
;     const float C1 = 0.9238795325112867f, S1 = 0.3826834323650898f, H = 0.7071067811865476f;
; #pragma unroll
;     for (int b = 0; b < 4; ++b) dft4<INV>(x[b], x[4 + b], x[8 + b], x[12 + b]);
;     const float s = INV ? -1.f : 1.f;
;     x[4 + 1] = cmul(x[4 + 1], mk2(C1, -s * S1)); x[8 + 1] = cmul(x[8 + 1], mk2(H, -s * H));   x[12 + 1] = cmul(x[12 + 1], mk2(S1, -s * C1));
;     x[4 + 2] = cmul(x[4 + 2], mk2(H, -s * H));   x[8 + 2] = cmul(x[8 + 2], mk2(0.f, -s));     x[12 + 2] = cmul(x[12 + 2], mk2(-H, -s * H));
;     x[4 + 3] = cmul(x[4 + 3], mk2(S1, -s * C1)); x[8 + 3] = cmul(x[8 + 3], mk2(-H, -s * H));  x[12 + 3] = cmul(x[12 + 3], mk2(-C1, s * S1));
; #pragma unroll
;     for (int c = 0; c < 4; ++c) dft4<INV>(x[4 * c], x[4 * c + 1], x[4 * c + 2], x[4 * c + 3]);
; #pragma unroll
;     for (int c = 0; c < 4; ++c)
; #pragma unroll
;         for (int d = c + 1; d < 4; ++d) { const cf2 t = x[4 * c + d]; x[4 * c + d] = x[4 * d + c]; x[4 * d + c] = t; }
; }
; template <bool INV, int lS, class ZP> FFT_HD void fft_r16_pass(ZP z, int tid) {
;     ...
;         for (int j = 0; j < 16; ++j) x[j] = z[pb0 + j * STEP];
; #pragma unroll
;         for (int j = 0; j < 16; ++j) y[j] = z[pb1 + j * STEP];
	v_pk_mov_b32 v[174:175], v[174:175], v[200:201] op_sel:[1,0]
	v_pk_fma_f32 v[202:203], v[188:189], 0, v[188:189] op_sel:[0,0,1] op_sel_hi:[1,0,0] neg_lo:[0,0,1] neg_hi:[0,0,1]
	v_pk_fma_f32 v[188:189], v[188:189], 0, v[188:189] op_sel:[0,0,1] op_sel_hi:[1,0,0]
	v_pk_add_f32 v[208:209], v[198:199], v[206:207]
	v_pk_add_f32 v[174:175], v[204:205], v[174:175] neg_lo:[0,1] neg_hi:[0,1]
	v_pk_add_f32 v[198:199], v[198:199], v[206:207] neg_lo:[0,1] neg_hi:[0,1]
	v_mov_b32_e32 v203, v189
	v_mov_b32_e32 v223, v225
	v_sub_f32_e32 v54, v182, v183
	v_pk_mov_b32 v[200:201], v[224:225], v[230:231] op_sel:[1,0]
	v_pk_add_f32 v[186:187], v[186:187], v[192:193] neg_lo:[0,1] neg_hi:[0,1]
	v_pk_add_f32 v[224:225], v[172:173], v[172:173] op_sel:[0,1] op_sel_hi:[0,1] neg_lo:[0,1] neg_hi:[0,1]
	v_pk_add_f32 v[226:227], v[178:179], v[178:179] op_sel:[0,1] op_sel_hi:[0,1]
	v_pk_add_f32 v[188:189], v[198:199], v[202:203]
	v_pk_add_f32 v[198:199], v[198:199], v[202:203] neg_lo:[0,1] neg_hi:[0,1]
	v_mov_b32_e32 v202, v182
	v_mov_b32_e32 v203, v172
	v_mov_b32_e32 v172, v183
	v_mov_b32_e32 v182, v174
	v_mov_b32_e32 v183, v178
	v_mov_b32_e32 v178, v175
	v_add_f32_e32 v67, v174, v175
	v_pk_add_f32 v[170:171], v[170:171], v[234:235] neg_lo:[0,1] neg_hi:[0,1]
	v_pk_mov_b32 v[192:193], v[186:187], v[186:187] op_sel:[1,0]
	v_pk_add_f32 v[172:173], v[202:203], v[172:173]
	v_pk_add_f32 v[174:175], v[182:183], v[178:179] neg_lo:[0,1] neg_hi:[0,1]
	v_pk_add_f32 v[220:221], v[208:209], v[190:191]
	v_pk_add_f32 v[190:191], v[208:209], v[190:191] neg_lo:[0,1] neg_hi:[0,1]
	v_pk_add_f32 v[208:209], v[170:171], v[186:187] op_sel:[0,1] op_sel_hi:[1,0] neg_lo:[0,1] neg_hi:[0,1]
	v_pk_add_f32 v[186:187], v[170:171], v[186:187] op_sel:[0,1] op_sel_hi:[1,0]
	v_mul_f32_e32 v170, 0x3ec3ef15, v173
	v_mul_f32_e32 v192, 0x3f6c835e, v175
	v_ashrrev_i32_e32 v3, 2, v4
	v_pk_add_f32 v[170:171], v[170:171], v[192:193] neg_lo:[0,1] neg_hi:[0,1]
	v_mov_b32_e32 v192, v214
	v_mov_b32_e32 v193, v100
	v_mov_b32_e32 v100, v215
	v_add3_u32 v60, v2, v3, s71
	v_pk_add_f32 v[100:101], v[192:193], v[100:101] neg_lo:[0,1] neg_hi:[0,1]
	v_mov_b32_e32 v192, v216
	v_mov_b32_e32 v193, v98
	v_mov_b32_e32 v98, v217
	ds_read2_b64 v[2:5], v60 offset1:4
	ds_read2_b64 v[30:33], v60 offset0:8 offset1:12
	ds_read2_b64 v[14:17], v60 offset0:16 offset1:20
	ds_read2_b64 v[26:29], v60 offset0:24 offset1:28
	ds_read2_b64 v[10:13], v60 offset0:32 offset1:36
	ds_read2_b64 v[22:25], v60 offset0:40 offset1:44
	ds_read2_b64 v[6:9], v60 offset0:48 offset1:52
	ds_read2_b64 v[18:21], v60 offset0:56 offset1:60
	v_pk_add_f32 v[98:99], v[192:193], v[98:99]
	s_waitcnt lgkmcnt(5)
	v_pk_mul_f32 v[70:71], v[70:71], v[14:15] op_sel_hi:[1,0]
	v_mul_f32_e32 v73, 0x3f3504f3, v54
	v_mul_f32_e32 v219, 0x3f3504f3, v67
	v_pk_mul_f32 v[192:193], v[98:99], v[176:177] op_sel:[1,1] op_sel_hi:[1,0]
	v_pk_fma_f32 v[56:57], v[56:57], v[14:15], v[70:71] op_sel:[0,1,0] neg_lo:[0,0,1] neg_hi:[0,0,1]
	v_pk_fma_f32 v[14:15], v[68:69], v[14:15], v[70:71] op_sel:[0,1,0]
	v_mov_b32_e32 v80, v55
	v_mov_b32_e32 v68, v33
	s_waitcnt lgkmcnt(4)
	v_mov_b32_e32 v69, v29
	v_sub_f32_e32 v218, v73, v219
	v_pk_fma_f32 v[202:203], v[100:101], v[176:177], v[192:193] op_sel:[1,0,0]
	v_pk_fma_f32 v[176:177], v[100:101], v[176:177], v[192:193] op_sel:[1,0,0] neg_lo:[0,0,1] neg_hi:[0,0,1]
	v_pk_mul_f32 v[192:193], v[98:99], v[184:185] op_sel:[0,1] op_sel_hi:[0,0]
	v_mov_b32_e32 v57, v15
	v_mov_b32_e32 v73, v78
	v_mov_b32_e32 v14, v32
	v_mov_b32_e32 v15, v28
	v_pk_mul_f32 v[68:69], v[80:81], v[68:69]
	v_mov_b32_e32 v203, v177
	v_pk_fma_f32 v[206:207], v[100:101], v[184:185], v[192:193] op_sel_hi:[0,1,1]
	v_pk_fma_f32 v[184:185], v[100:101], v[184:185], v[192:193] op_sel_hi:[0,1,1] neg_lo:[0,0,1] neg_hi:[0,0,1]
	v_pk_fma_f32 v[14:15], v[72:73], v[14:15], v[68:69]
	v_mov_b32_e32 v68, v29
	v_mov_b32_e32 v69, v33
	v_mov_b32_e32 v29, v32
	s_waitcnt lgkmcnt(3)
	v_pk_mul_f32 v[32:33], v[52:53], v[10:11] op_sel:[1,1] op_sel_hi:[1,0]
	v_mov_b32_e32 v232, v230
	v_mov_b32_e32 v204, v222
	v_mov_b32_e32 v205, v233
	v_mov_b32_e32 v184, v206
	v_pk_add_f32 v[192:193], v[222:223], v[202:203]
	v_pk_mov_b32 v[176:177], v[176:177], v[206:207] op_sel:[1,0]
	v_mov_b32_e32 v203, v185
	v_pk_fma_f32 v[52:53], v[48:49], v[10:11], v[32:33]
	v_pk_fma_f32 v[10:11], v[48:49], v[10:11], v[32:33] op_sel_hi:[0,1,1] neg_lo:[0,0,1] neg_hi:[0,0,1]
	v_pk_add_f32 v[214:215], v[232:233], v[184:185]
	v_pk_add_f32 v[176:177], v[200:201], v[176:177] neg_lo:[0,1] neg_hi:[0,1]
	v_pk_add_f32 v[184:185], v[204:205], v[202:203] neg_lo:[0,1] neg_hi:[0,1]
	v_mov_b32_e32 v53, v11
	s_waitcnt lgkmcnt(1)
	v_pk_mul_f32 v[10:11], v[96:97], v[6:7]
	v_mov_b32_e32 v202, v184
	v_mov_b32_e32 v203, v176
	v_mov_b32_e32 v204, v185
	v_mov_b32_e32 v205, v177
	v_pk_fma_f32 v[32:33], v[94:95], v[6:7], v[10:11] op_sel:[0,0,1] op_sel_hi:[1,1,0] neg_lo:[1,0,0] neg_hi:[1,0,0]
	v_pk_fma_f32 v[6:7], v[94:95], v[6:7], v[10:11] op_sel:[0,0,1] op_sel_hi:[1,1,0]
	v_pk_add_f32 v[206:207], v[202:203], v[204:205]
	v_pk_add_f32 v[202:203], v[202:203], v[204:205] neg_lo:[0,1] neg_hi:[0,1]
	v_mov_b32_e32 v33, v7
	v_mov_b32_e32 v7, v24
	s_waitcnt lgkmcnt(0)
; FFT_HD cf2 mk2(float x, float y) { return (cf2){x, y}; }
; FFT_HD cf2 cmul(cf2 a, cf2 b) { return mk2(a.x * b.x - a.y * b.y, a.x * b.y + a.y * b.x); }
; FFT_HD cf2 cmulc(cf2 a, cf2 b) { return mk2(a.x * b.x + a.y * b.y, a.y * b.x - a.x * b.y); }
; FFT_HD cf2 cadd(cf2 a, cf2 b) { return mk2(a.x + b.x, a.y + b.y); }
; FFT_HD cf2 csub(cf2 a, cf2 b) { return mk2(a.x - b.x, a.y - b.y); }
; template <bool INV> FFT_HD void dft4(cf2& a, cf2& b, cf2& c, cf2& d) {
;     const cf2 s0 = cadd(a, c), s1 = csub(a, c), s2 = cadd(b, d), s3 = csub(b, d);
;     a = cadd(s0, s2); c = csub(s0, s2);
;     const cf2 r = INV ? mk2(-s3.y, s3.x) : mk2(s3.y, -s3.x);
;     b = cadd(s1, r); d = csub(s1, r);
; }
; template <bool INV> FFT_HD void dft16(cf2 (&x)[16]) {
;     const float C1 = 0.9238795325112867f, S1 = 0.3826834323650898f, H = 0.7071067811865476f;
; #pragma unroll
;     for (int b = 0; b < 4; ++b) dft4<INV>(x[b], x[4 + b], x[8 + b], x[12 + b]);
;     const float s = INV ? -1.f : 1.f;
;     x[4 + 1] = cmul(x[4 + 1], mk2(C1, -s * S1)); x[8 + 1] = cmul(x[8 + 1], mk2(H, -s * H));   x[12 + 1] = cmul(x[12 + 1], mk2(S1, -s * C1));
;     x[4 + 2] = cmul(x[4 + 2], mk2(H, -s * H));   x[8 + 2] = cmul(x[8 + 2], mk2(0.f, -s));     x[12 + 2] = cmul(x[12 + 2], mk2(-H, -s * H));
;     x[4 + 3] = cmul(x[4 + 3], mk2(S1, -s * C1)); x[8 + 3] = cmul(x[8 + 3], mk2(-H, -s * H));  x[12 + 3] = cmul(x[12 + 3], mk2(-C1, s * S1));
; #pragma unroll
;     for (int c = 0; c < 4; ++c) dft4<INV>(x[4 * c], x[4 * c + 1], x[4 * c + 2], x[4 * c + 3]);
; #pragma unroll
;     for (int c = 0; c < 4; ++c)
; #pragma unroll
;         for (int d = c + 1; d < 4; ++d) { const cf2 t = x[4 * c + d]; x[4 * c + d] = x[4 * d + c]; x[4 * d + c] = t; }
; }
; template <bool INV, int lS, class ZP> FFT_HD void fft_r16_pass(ZP z, int tid) {
;     ...
;         if (INV) {
; #pragma unroll
;             for (int j = 1; j < 16; ++j) y[j] = cmulc(y[j], tw[j]);
;         }
;         dft16<INV>(y);
	v_mov_b32_e32 v24, v21
	s_mov_b32 s46, s27
	s_mov_b32 s47, s26
	v_fmac_f32_e32 v219, 0x3f3504f3, v54
	v_mov_b32_e32 v207, v203
	v_mul_f32_e32 v54, 0x3f6c835e, v203
	v_mov_b32_e32 v6, v20
	v_pk_mul_f32 v[10:11], v[98:99], v[24:25]
	v_pk_add_f32 v[180:181], v[210:211], v[212:213]
	v_pk_mul_f32 v[226:227], v[226:227], s[46:47]
	v_pk_add_f32 v[200:201], v[192:193], v[214:215]
	v_pk_fma_f32 v[204:205], v[206:207], s[14:15], v[54:55] op_sel_hi:[1,1,0] neg_lo:[0,0,1] neg_hi:[0,0,1]
	v_pk_add_f32 v[176:177], v[176:177], v[176:177] op_sel:[0,1] op_sel_hi:[0,1]
	v_mov_b32_e32 v54, v81
	v_pk_fma_f32 v[10:11], v[100:101], v[6:7], v[10:11]
	v_pk_mul_f32 v[6:7], v[98:99], v[6:7]
	v_mov_b32_e32 v209, v187
	v_pk_fma_f32 v[228:229], v[224:225], s[26:27], v[226:227] neg_lo:[0,0,1] neg_hi:[0,0,1]
	v_pk_fma_f32 v[224:225], v[224:225], s[26:27], v[226:227]
	v_pk_add_f32 v[216:217], v[180:181], v[200:201]
	v_pk_add_f32 v[184:185], v[184:185], v[184:185] op_sel:[0,1] op_sel_hi:[0,1] neg_lo:[0,1] neg_hi:[0,1]
	v_pk_mul_f32 v[176:177], v[176:177], s[26:27]
	v_mov_b32_e32 v79, v72
	v_pk_mul_f32 v[28:29], v[54:55], v[28:29]
	v_pk_fma_f32 v[6:7], v[100:101], v[24:25], v[6:7] neg_lo:[0,0,1] neg_hi:[0,0,1]
	v_pk_add_f32 v[20:21], v[2:3], v[52:53] neg_lo:[0,1] neg_hi:[0,1]
	v_pk_add_f32 v[24:25], v[56:57], v[32:33] neg_lo:[0,1] neg_hi:[0,1]
	v_mov_b32_e32 v229, v225
	v_pk_add_f32 v[224:225], v[208:209], v[218:219]
	v_pk_add_f32 v[208:209], v[208:209], v[218:219] neg_lo:[0,1] neg_hi:[0,1]
	v_pk_add_f32 v[218:219], v[220:221], v[216:217]
	v_pk_add_f32 v[216:217], v[220:221], v[216:217] neg_lo:[0,1] neg_hi:[0,1]
	v_pk_fma_f32 v[220:221], v[184:185], s[46:47], v[176:177] neg_lo:[0,0,1] neg_hi:[0,0,1]
	v_pk_fma_f32 v[176:177], v[184:185], s[46:47], v[176:177]
	v_pk_fma_f32 v[28:29], v[78:79], v[68:69], v[28:29] neg_lo:[0,0,1] neg_hi:[0,0,1]
	v_pk_add_f32 v[48:49], v[20:21], v[24:25]
	v_pk_add_f32 v[54:55], v[20:21], v[24:25] neg_lo:[0,1] neg_hi:[0,1]
	v_mov_b32_e32 v221, v177
	v_mov_b32_e32 v49, v55
	v_pk_add_f32 v[54:55], v[14:15], v[10:11] op_sel:[0,1] op_sel_hi:[1,0] neg_lo:[0,1] neg_hi:[0,1]
	v_pk_add_f32 v[68:69], v[28:29], v[6:7] neg_lo:[0,1] neg_hi:[0,1]
	v_pk_add_f32 v[176:177], v[228:229], v[220:221]
	v_pk_add_f32 v[70:71], v[68:69], v[54:55]
	v_pk_add_f32 v[72:73], v[68:69], v[54:55] neg_lo:[0,1] neg_hi:[0,1]
	v_pk_mul_f32 v[40:41], v[40:41], v[30:31] op_sel:[1,0]
	v_pk_add_f32 v[184:185], v[224:225], v[176:177]
	v_pk_add_f32 v[176:177], v[224:225], v[176:177] neg_lo:[0,1] neg_hi:[0,1]
	v_mov_b32_e32 v225, v192
	v_mov_b32_e32 v227, v214
	v_mov_b32_e32 v192, v211
	v_mov_b32_e32 v214, v213
	v_mov_b32_e32 v78, v70
	v_mov_b32_e32 v79, v73
	v_pk_mov_b32 v[70:71], v[72:73], v[70:71] op_sel:[1,0]
	v_pk_fma_f32 v[72:73], v[38:39], v[30:31], v[40:41] op_sel:[0,0,1] op_sel_hi:[0,1,0]
	v_pk_fma_f32 v[30:31], v[38:39], v[30:31], v[40:41] op_sel:[0,0,1] op_sel_hi:[0,1,0] neg_lo:[0,0,1] neg_hi:[0,0,1]
	v_pk_mul_f32 v[38:39], v[50:51], v[26:27] op_sel:[1,1] op_sel_hi:[1,0]
	s_mov_b32 s52, s25
	s_mov_b32 s53, s27
	v_mov_b32_e32 v224, v210
	v_mov_b32_e32 v226, v212
	v_pk_add_f32 v[192:193], v[192:193], v[214:215] neg_lo:[0,1] neg_hi:[0,1]
	s_mov_b32 s12, s25
	v_pk_fma_f32 v[40:41], v[46:47], v[26:27], v[38:39] op_sel_hi:[0,1,1]
	v_pk_fma_f32 v[26:27], v[46:47], v[26:27], v[38:39] op_sel_hi:[0,1,1] neg_lo:[0,0,1] neg_hi:[0,0,1]
	v_pk_mul_f32 v[38:39], v[88:89], v[22:23]
	v_pk_mul_f32 v[178:179], v[174:175], s[52:53]
	v_pk_add_f32 v[224:225], v[224:225], v[226:227] neg_lo:[0,1] neg_hi:[0,1]
	s_mov_b32 s53, s24
	v_pk_mul_f32 v[192:193], v[192:193], s[12:13] op_sel_hi:[1,0]
	v_pk_fma_f32 v[46:47], v[86:87], v[22:23], v[38:39] op_sel:[0,0,1] op_sel_hi:[1,1,0]
	v_pk_fma_f32 v[22:23], v[86:87], v[22:23], v[38:39] op_sel:[0,0,1] op_sel_hi:[1,1,0] neg_lo:[0,0,1] neg_hi:[0,0,1]
	v_pk_mul_f32 v[38:39], v[92:93], v[18:19]
	v_pk_fma_f32 v[210:211], v[224:225], s[52:53], v[192:193] neg_lo:[0,0,1] neg_hi:[0,0,1]
	v_pk_fma_f32 v[212:213], v[224:225], s[52:53], v[192:193]
	v_pk_fma_f32 v[192:193], v[224:225], s[12:13], v[192:193] op_sel_hi:[1,0,1] neg_lo:[0,0,1] neg_hi:[0,0,1]
	s_mov_b32 s12, s29
	v_pk_fma_f32 v[50:51], v[90:91], v[18:19], v[38:39] op_sel:[0,0,1] op_sel_hi:[1,1,0]
	v_pk_fma_f32 v[18:19], v[90:91], v[18:19], v[38:39] op_sel:[0,0,1] op_sel_hi:[1,1,0] neg_lo:[0,0,1] neg_hi:[0,0,1]
	v_pk_mul_f32 v[70:71], v[70:71], s[12:13] op_sel_hi:[1,0]
	v_mov_b32_e32 v73, v31
	v_mov_b32_e32 v26, v40
	v_mov_b32_e32 v47, v23
	v_mov_b32_e32 v18, v50
	v_pk_fma_f32 v[70:71], v[78:79], s[38:39], v[70:71]
	v_pk_add_f32 v[38:39], v[72:73], v[46:47]
	v_pk_add_f32 v[78:79], v[26:27], v[18:19]
	v_pk_mov_b32 v[30:31], v[30:31], v[40:41] op_sel:[1,0]
	v_pk_mov_b32 v[22:23], v[22:23], v[50:51] op_sel:[1,0]
	v_mov_b32_e32 v73, v27
	v_pk_add_f32 v[22:23], v[30:31], v[22:23] neg_lo:[0,1] neg_hi:[0,1]
	v_mov_b32_e32 v47, v19
	v_pk_add_f32 v[26:27], v[38:39], v[78:79] neg_lo:[0,1] neg_hi:[0,1]
	v_pk_add_f32 v[18:19], v[72:73], v[46:47] neg_lo:[0,1] neg_hi:[0,1]
	v_sub_f32_e32 v40, v22, v23
	v_pk_fma_f32 v[30:31], v[26:27], 0, v[26:27] op_sel:[0,0,1] op_sel_hi:[1,0,0] neg_lo:[0,0,1] neg_hi:[0,0,1]
	v_pk_fma_f32 v[26:27], v[26:27], 0, v[26:27] op_sel:[0,0,1] op_sel_hi:[1,0,0]
	v_pk_add_f32 v[46:47], v[18:19], v[18:19] op_sel:[0,1] op_sel_hi:[0,1]
	v_mul_f32_e32 v26, 0x3f3504f3, v40
	v_pk_mul_f32 v[44:45], v[44:45], v[16:17] op_sel_hi:[1,0]
	v_mov_b32_e32 v31, v27
	v_pk_fma_f32 v[26:27], v[46:47], s[24:25], v[26:27] op_sel_hi:[1,1,0] neg_lo:[0,0,1] neg_hi:[0,0,1]
	v_pk_fma_f32 v[46:47], v[42:43], v[16:17], v[44:45] op_sel:[0,1,0] neg_lo:[0,0,1] neg_hi:[0,0,1]
	v_pk_fma_f32 v[16:17], v[42:43], v[16:17], v[44:45] op_sel:[0,1,0]
; FFT_HD cf2 mk2(float x, float y) { return (cf2){x, y}; }
; FFT_HD cf2 cmul(cf2 a, cf2 b) { return mk2(a.x * b.x - a.y * b.y, a.x * b.y + a.y * b.x); }
; FFT_HD cf2 cmulc(cf2 a, cf2 b) { return mk2(a.x * b.x + a.y * b.y, a.y * b.x - a.x * b.y); }
; FFT_HD cf2 cadd(cf2 a, cf2 b) { return mk2(a.x + b.x, a.y + b.y); }
; FFT_HD cf2 csub(cf2 a, cf2 b) { return mk2(a.x - b.x, a.y - b.y); }
; template <bool INV> FFT_HD void dft4(cf2& a, cf2& b, cf2& c, cf2& d) {
;     const cf2 s0 = cadd(a, c), s1 = csub(a, c), s2 = cadd(b, d), s3 = csub(b, d);
;     a = cadd(s0, s2); c = csub(s0, s2);
;     const cf2 r = INV ? mk2(-s3.y, s3.x) : mk2(s3.y, -s3.x);
;     b = cadd(s1, r); d = csub(s1, r);
; }
; template <bool INV> FFT_HD void dft16(cf2 (&x)[16]) {
;     const float C1 = 0.9238795325112867f, S1 = 0.3826834323650898f, H = 0.7071067811865476f;
; #pragma unroll
;     for (int b = 0; b < 4; ++b) dft4<INV>(x[b], x[4 + b], x[8 + b], x[12 + b]);
;     const float s = INV ? -1.f : 1.f;
;     x[4 + 1] = cmul(x[4 + 1], mk2(C1, -s * S1)); x[8 + 1] = cmul(x[8 + 1], mk2(H, -s * H));   x[12 + 1] = cmul(x[12 + 1], mk2(S1, -s * C1));
;     x[4 + 2] = cmul(x[4 + 2], mk2(H, -s * H));   x[8 + 2] = cmul(x[8 + 2], mk2(0.f, -s));     x[12 + 2] = cmul(x[12 + 2], mk2(-H, -s * H));
;     x[4 + 3] = cmul(x[4 + 3], mk2(S1, -s * C1)); x[8 + 3] = cmul(x[8 + 3], mk2(-H, -s * H));  x[12 + 3] = cmul(x[12 + 3], mk2(-C1, s * S1));
; #pragma unroll
;     for (int c = 0; c < 4; ++c) dft4<INV>(x[4 * c], x[4 * c + 1], x[4 * c + 2], x[4 * c + 3]);
; #pragma unroll
;     for (int c = 0; c < 4; ++c)
; #pragma unroll
;         for (int d = c + 1; d < 4; ++d) { const cf2 t = x[4 * c + d]; x[4 * c + d] = x[4 * d + c]; x[4 * d + c] = t; }
; }
; template <bool INV, int lS, class ZP> FFT_HD void fft_r16_pass(ZP z, int tid) {
;     ...
;         if (INV) {
; #pragma unroll
;             for (int j = 1; j < 16; ++j) y[j] = cmulc(y[j], tw[j]);
;         }
;         dft16<INV>(y);
	v_mov_b32_e32 v43, v5
	v_pk_mov_b32 v[4:5], v[12:13], v[4:5] op_sel:[1,0]
	v_mov_b32_e32 v42, v12
	v_pk_mul_f32 v[12:13], v[76:77], v[4:5]
	v_mov_b32_e32 v16, v46
	v_pk_fma_f32 v[12:13], v[74:75], v[42:43], v[12:13]
	v_pk_mul_f32 v[42:43], v[76:77], v[42:43]
	v_pk_add_f32 v[2:3], v[2:3], v[52:53]
	v_pk_fma_f32 v[4:5], v[74:75], v[4:5], v[42:43] neg_lo:[0,0,1] neg_hi:[0,0,1]
	v_pk_mul_f32 v[42:43], v[84:85], v[8:9]
	v_pk_add_f32 v[32:33], v[56:57], v[32:33]
	v_pk_fma_f32 v[44:45], v[82:83], v[8:9], v[42:43] op_sel:[0,0,1] op_sel_hi:[1,1,0] neg_lo:[1,0,0] neg_hi:[1,0,0]
	v_pk_fma_f32 v[8:9], v[82:83], v[8:9], v[42:43] op_sel:[0,0,1] op_sel_hi:[1,1,0]
	v_pk_add_f32 v[42:43], v[12:13], v[4:5] op_sel:[1,0] op_sel_hi:[0,1]
	v_mov_b32_e32 v45, v9
	v_pk_add_f32 v[50:51], v[16:17], v[44:45]
	v_mov_b32_e32 v16, v13
	v_mov_b32_e32 v8, v4
	v_pk_mov_b32 v[4:5], v[4:5], v[46:47] op_sel:[1,0]
	v_mov_b32_e32 v13, v44
	v_pk_add_f32 v[8:9], v[16:17], v[8:9] neg_lo:[0,1] neg_hi:[0,1]
	v_pk_add_f32 v[4:5], v[4:5], v[12:13] neg_lo:[0,1] neg_hi:[0,1]
	v_pk_add_f32 v[12:13], v[42:43], v[50:51]
	v_pk_add_f32 v[16:17], v[42:43], v[50:51] neg_lo:[0,1] neg_hi:[0,1]
	v_sub_f32_e32 v42, v4, v5
	v_add_f32_e32 v44, v8, v9
	v_mul_f32_e32 v43, 0x3f6c835e, v42
	v_mul_f32_e32 v45, 0x3ec3ef15, v44
	v_mul_f32_e32 v46, 0x3ec3ef15, v42
	v_mul_f32_e32 v50, 0x3f6c835e, v44
	v_mul_f32_e32 v42, 0x3f3504f3, v17
	v_mul_f32_e32 v44, 0x3f3504f3, v16
	v_pk_mov_b32 v[52:53], v[28:29], v[14:15] op_sel:[1,0]
	v_mov_b32_e32 v56, v7
	v_mov_b32_e32 v57, v11
	v_mov_b32_e32 v29, v15
	v_mov_b32_e32 v7, v10
	v_pk_add_f32 v[8:9], v[8:9], v[8:9] op_sel:[0,1] op_sel_hi:[0,1] neg_lo:[0,1] neg_hi:[0,1]
	v_pk_add_f32 v[52:53], v[52:53], v[56:57]
	v_pk_add_f32 v[6:7], v[28:29], v[6:7]
	v_pk_add_f32 v[4:5], v[4:5], v[4:5] op_sel:[0,1] op_sel_hi:[0,1]
	v_pk_mul_f32 v[8:9], v[8:9], s[46:47]
	v_add_f32_e32 v16, v42, v44
	v_fma_f32 v17, v17, s25, -v44
	v_mov_b32_e32 v44, v24
	v_mov_b32_e32 v51, v25
	v_mov_b32_e32 v24, v54
	v_mov_b32_e32 v25, v18
	v_mov_b32_e32 v18, v68
	s_mov_b32 s50, s24
	s_mov_b32 s51, s26
	v_pk_add_f32 v[10:11], v[52:53], v[6:7]
	v_pk_add_f32 v[6:7], v[52:53], v[6:7] neg_lo:[0,1] neg_hi:[0,1]
	v_pk_fma_f32 v[14:15], v[4:5], s[26:27], v[8:9]
	v_pk_fma_f32 v[4:5], v[4:5], s[26:27], v[8:9] neg_lo:[0,0,1] neg_hi:[0,0,1]
	v_pk_add_f32 v[18:19], v[24:25], v[18:19] neg_lo:[0,1] neg_hi:[0,1]
	v_pk_mov_b32 v[24:25], v[68:69], v[22:23] op_sel:[1,0]
	v_mov_b32_e32 v22, v55
	v_pk_fma_f32 v[182:183], v[172:173], s[50:51], v[178:179] neg_lo:[0,0,1] neg_hi:[0,0,1]
	v_pk_fma_f32 v[178:179], v[172:173], s[50:51], v[178:179]
	s_mov_b32 s50, s27
	s_mov_b32 s51, s25
	v_pk_add_f32 v[40:41], v[2:3], v[32:33] op_sel:[0,1] op_sel_hi:[1,0] neg_lo:[0,1] neg_hi:[0,1]
	v_mul_f32_e32 v4, 0x3f3504f3, v6
	v_pk_add_f32 v[28:29], v[38:39], v[78:79]
	v_pk_add_f32 v[2:3], v[2:3], v[32:33] op_sel:[0,1] op_sel_hi:[1,0]
	v_pk_add_f32 v[22:23], v[24:25], v[22:23]
	v_mov_b32_e32 v15, v5
	v_pk_add_f32 v[8:9], v[12:13], v[10:11] neg_lo:[0,1] neg_hi:[0,1]
	v_pk_fma_f32 v[4:5], v[6:7], s[52:53], v[4:5] op_sel:[1,0,0] op_sel_hi:[1,1,0] neg_lo:[0,0,1] neg_hi:[0,0,1]
	v_pk_add_f32 v[6:7], v[2:3], v[28:29] neg_lo:[0,1] neg_hi:[0,1]
	v_pk_add_f32 v[10:11], v[12:13], v[10:11]
	v_pk_add_f32 v[2:3], v[2:3], v[28:29]
	v_pk_mul_f32 v[24:25], v[22:23], s[50:51]
	v_pk_mul_f32 v[22:23], v[22:23], s[36:37]
	v_pk_add_f32 v[12:13], v[2:3], v[10:11] op_sel:[0,1] op_sel_hi:[1,0]
	v_pk_add_f32 v[2:3], v[2:3], v[10:11] op_sel:[0,1] op_sel_hi:[1,0] neg_lo:[0,1] neg_hi:[0,1]
	v_pk_add_f32 v[10:11], v[6:7], v[8:9] neg_lo:[0,1] neg_hi:[0,1]
	v_pk_add_f32 v[6:7], v[6:7], v[8:9]
	v_mov_b32_e32 v42, v20
	v_mov_b32_e32 v47, v21
	v_pk_fma_f32 v[22:23], v[18:19], s[50:51], v[22:23] neg_lo:[0,0,1] neg_hi:[0,0,1]
	v_mov_b32_e32 v207, v174
	v_mov_b32_e32 v8, v10
	v_mov_b32_e32 v9, v7
	v_mov_b32_e32 v7, v11
	v_pk_add_f32 v[10:11], v[42:43], v[44:45] neg_lo:[0,1] neg_hi:[0,1]
	v_pk_add_f32 v[20:21], v[46:47], v[50:51]
	v_pk_mov_b32 v[28:29], v[22:23], v[22:23] op_sel:[1,0]
	v_pk_fma_f32 v[18:19], v[18:19], s[36:37], v[24:25]
	v_pk_mul_f32 v[174:175], v[206:207], s[36:37]
	v_pk_mov_b32 v[172:173], v[202:203], v[172:173] op_sel:[1,0]
	v_pk_add_f32 v[22:23], v[10:11], v[22:23] op_sel:[0,1] op_sel_hi:[1,0] neg_lo:[0,1] neg_hi:[0,1]
	v_pk_add_f32 v[24:25], v[20:21], v[18:19] neg_lo:[0,1] neg_hi:[0,1]
	v_pk_mov_b32 v[32:33], v[10:11], v[20:21] op_sel:[1,0]
	v_pk_mov_b32 v[38:39], v[28:29], v[18:19] op_sel:[1,0]
	v_mov_b32_e32 v11, v21
	v_mov_b32_e32 v29, v19
	v_mov_b32_e32 v183, v179
	v_pk_fma_f32 v[172:173], v[172:173], s[50:51], v[174:175] neg_lo:[0,0,1] neg_hi:[0,0,1]
	v_mov_b32_e32 v174, v186
	v_mov_b32_e32 v175, v204
	v_pk_add_f32 v[10:11], v[10:11], v[28:29]
	v_pk_add_f32 v[20:21], v[22:23], v[24:25] neg_lo:[0,1] neg_hi:[0,1]
	v_pk_add_f32 v[28:29], v[24:25], v[22:23]
	v_pk_add_f32 v[22:23], v[24:25], v[22:23] neg_lo:[0,1] neg_hi:[0,1]
	v_mov_b32_e32 v187, v171
	v_pk_mov_b32 v[178:179], v[178:179], v[170:171] op_sel:[1,0]
	v_pk_mov_b32 v[214:215], v[210:211], v[212:213] op_sel:[1,0]
	v_mov_b32_e32 v213, v192
	v_mov_b32_e32 v210, v193
	v_pk_add_f32 v[170:171], v[170:171], v[172:173]
; __device__ __forceinline__ unsigned cvt_pk_bf16(float lo, float hi) { unsigned r; asm volatile("v_cvt_pk_bf16_f32 %0, %1, %2" : "=v"(r) : "v"(lo), "v"(hi)); return r; }
; FFT_HD cf2 cmul(cf2 a, cf2 b) { return mk2(a.x * b.x - a.y * b.y, a.x * b.y + a.y * b.x); }
; FFT_HD cf2 cmulc(cf2 a, cf2 b) { return mk2(a.x * b.x + a.y * b.y, a.y * b.x - a.x * b.y); }
; template <int BANK, int WAITN> __device__ __forceinline__ void bg_finish1(BgState& b) {
;     if (WAITN == 32) asm volatile("s_waitcnt vmcnt(32)" ::: "memory"); else asm volatile("s_waitcnt vmcnt(0)" ::: "memory");
;     asm volatile("" : BG_TIE16(BANK * 32) :: "memory");
;     asm volatile("" : BG_TIE16(BANK * 32 + 16) :: "memory");
;     bf16_t* dst = b.dst[BANK];
;     if (dst != nullptr) {
; #pragma unroll
;         for (int c = 0; c < 4; ++c) { u32x4 w;
;             w.x = cvt_pk_bf16(b.r[(BANK * 8 + 0) * 4 + c], b.r[(BANK * 8 + 1) * 4 + c]); w.y = cvt_pk_bf16(b.r[(BANK * 8 + 2) * 4 + c], b.r[(BANK * 8 + 3) * 4 + c]);
;             w.z = cvt_pk_bf16(b.r[(BANK * 8 + 4) * 4 + c], b.r[(BANK * 8 + 5) * 4 + c]); w.w = cvt_pk_bf16(b.r[(BANK * 8 + 6) * 4 + c], b.r[(BANK * 8 + 7) * 4 + c]);
;             bf16_t* dp = dst + (c & 1) * 512 + (c >> 1) * b.o2[BANK];
;             asm volatile("global_store_dwordx4 %0, %1, off\n\ts_nop 1" :: "v"(dp), "v"(w) : "memory"); }
;     }
; }
; template <bool INV, int lS, class ZP> FFT_HD void fft_r16_pass(ZP z, int tid) {
;     ...
; #pragma unroll
;         for (int j = 0; j < 16; ++j) z[pb0 + j * STEP] = x[j];
;         if (INV) {
; #pragma unroll
;             for (int j = 1; j < 16; ++j) y[j] = cmulc(y[j], tw[j]);
;         }
;         dft16<INV>(y);
;         if (!INV) {
; #pragma unroll
;             for (int j = 1; j < 16; ++j) y[j] = cmul(y[j], tw[j]);
;         }
; #pragma unroll
;         for (int j = 0; j < 16; ++j) z[pb1 + j * STEP] = y[j];
	v_pk_add_f32 v[174:175], v[182:183], v[174:175]
	v_mov_b32_e32 v183, v173
	v_mov_b32_e32 v205, v172
	v_mov_b32_e32 v21, v29
	v_mov_b32_e32 v29, v23
	v_pk_add_f32 v[22:23], v[40:41], v[30:31] neg_lo:[0,1] neg_hi:[0,1]
	v_pk_add_f32 v[24:25], v[16:17], v[4:5] neg_lo:[0,1] neg_hi:[0,1]
	v_pk_add_f32 v[30:31], v[40:41], v[30:31]
	v_pk_add_f32 v[4:5], v[16:17], v[4:5]
	v_pk_add_f32 v[180:181], v[180:181], v[200:201] neg_lo:[0,1] neg_hi:[0,1]
	v_pk_add_f32 v[220:221], v[228:229], v[220:221] neg_lo:[0,1] neg_hi:[0,1]
	v_pk_add_f32 v[214:215], v[192:193], v[214:215]
	v_pk_add_f32 v[192:193], v[212:213], v[210:211] neg_lo:[0,1] neg_hi:[0,1]
	v_pk_add_f32 v[202:203], v[170:171], v[174:175]
	v_mov_b32_e32 v206, v174
	v_mov_b32_e32 v207, v171
	v_mov_b32_e32 v171, v175
	v_pk_add_f32 v[174:175], v[186:187], v[182:183] neg_lo:[0,1] neg_hi:[0,1]
	v_pk_add_f32 v[172:173], v[178:179], v[204:205] neg_lo:[0,1] neg_hi:[0,1]
	v_pk_add_f32 v[32:33], v[32:33], v[38:39]
	v_pk_add_f32 v[16:17], v[30:31], v[4:5] op_sel:[0,1] op_sel_hi:[1,0]
	v_pk_add_f32 v[4:5], v[30:31], v[4:5] op_sel:[0,1] op_sel_hi:[1,0] neg_lo:[0,1] neg_hi:[0,1]
	v_pk_add_f32 v[30:31], v[22:23], v[24:25] neg_lo:[0,1] neg_hi:[0,1]
	v_pk_add_f32 v[22:23], v[22:23], v[24:25]
	v_pk_add_f32 v[200:201], v[190:191], v[180:181] op_sel:[0,1] op_sel_hi:[1,0] neg_lo:[0,1] neg_hi:[0,1]
	v_pk_add_f32 v[180:181], v[190:191], v[180:181] op_sel:[0,1] op_sel_hi:[1,0]
	v_pk_add_f32 v[222:223], v[208:209], v[220:221] op_sel:[0,1] op_sel_hi:[1,0] neg_lo:[0,1] neg_hi:[0,1]
	v_pk_add_f32 v[208:209], v[208:209], v[220:221] op_sel:[0,1] op_sel_hi:[1,0]
	v_pk_add_f32 v[210:211], v[198:199], v[192:193] neg_lo:[0,1] neg_hi:[0,1]
	v_pk_add_f32 v[192:193], v[198:199], v[192:193]
	v_pk_add_f32 v[178:179], v[174:175], v[172:173] neg_lo:[0,1] neg_hi:[0,1]
	v_pk_add_f32 v[172:173], v[174:175], v[172:173]
	v_pk_add_f32 v[18:19], v[10:11], v[32:33]
	v_pk_add_f32 v[10:11], v[10:11], v[32:33] neg_lo:[0,1] neg_hi:[0,1]
	v_mov_b32_e32 v24, v30
	v_mov_b32_e32 v25, v23
	v_mov_b32_e32 v23, v31
	v_pk_add_f32 v[30:31], v[48:49], v[26:27] neg_lo:[0,1] neg_hi:[0,1]
	v_pk_add_f32 v[32:33], v[14:15], v[70:71] neg_lo:[0,1] neg_hi:[0,1]
	v_pk_add_f32 v[26:27], v[48:49], v[26:27]
	v_pk_add_f32 v[14:15], v[14:15], v[70:71]
	v_mov_b32_e32 v191, v181
	v_mov_b32_e32 v221, v209
	v_mov_b32_e32 v199, v193
	v_mov_b32_e32 v175, v173
	v_mov_b32_e32 v181, v201
	v_mov_b32_e32 v209, v223
	v_mov_b32_e32 v193, v211
	v_mov_b32_e32 v173, v179
	v_pk_add_f32 v[38:39], v[26:27], v[14:15] op_sel:[0,1] op_sel_hi:[1,0]
	v_pk_add_f32 v[14:15], v[26:27], v[14:15] op_sel:[0,1] op_sel_hi:[1,0] neg_lo:[0,1] neg_hi:[0,1]
	v_pk_add_f32 v[26:27], v[30:31], v[32:33] neg_lo:[0,1] neg_hi:[0,1]
	v_pk_add_f32 v[30:31], v[30:31], v[32:33]
	v_mov_b32_e32 v190, v200
	v_mov_b32_e32 v220, v222
	v_pk_add_f32 v[224:225], v[188:189], v[214:215]
	v_pk_add_f32 v[188:189], v[188:189], v[214:215] neg_lo:[0,1] neg_hi:[0,1]
	v_mov_b32_e32 v198, v210
	v_pk_add_f32 v[170:171], v[206:207], v[170:171] neg_lo:[0,1] neg_hi:[0,1]
	v_mov_b32_e32 v174, v178
	ds_write2_b64 v65, v[218:219], v[184:185] offset1:4
	ds_write2_b64 v65, v[224:225], v[202:203] offset0:8 offset1:12
	ds_write2_b64 v65, v[190:191], v[220:221] offset0:16 offset1:20
	ds_write2_b64 v65, v[198:199], v[174:175] offset0:24 offset1:28
	ds_write2_b64 v65, v[216:217], v[176:177] offset0:32 offset1:36
	ds_write2_b64 v65, v[188:189], v[170:171] offset0:40 offset1:44
	ds_write2_b64 v65, v[180:181], v[208:209] offset0:48 offset1:52
	ds_write2_b64 v65, v[192:193], v[172:173] offset0:56 offset1:60
	v_mov_b32_e32 v32, v26
	v_mov_b32_e32 v33, v31
	v_mov_b32_e32 v31, v27
	ds_write2_b64 v60, v[12:13], v[18:19] offset1:4
	ds_write2_b64 v60, v[16:17], v[38:39] offset0:8 offset1:12
	ds_write2_b64 v60, v[8:9], v[20:21] offset0:16 offset1:20
	ds_write2_b64 v60, v[24:25], v[32:33] offset0:24 offset1:28
	ds_write2_b64 v60, v[2:3], v[10:11] offset0:32 offset1:36
	ds_write2_b64 v60, v[4:5], v[14:15] offset0:40 offset1:44
	ds_write2_b64 v60, v[6:7], v[28:29] offset0:48 offset1:52
	ds_write2_b64 v60, v[22:23], v[30:31] offset0:56 offset1:60
	s_waitcnt lgkmcnt(0)
	s_barrier
	s_waitcnt vmcnt(32)
	v_cmp_ne_u64_e32 vcc, 0, v[34:35]
	s_and_saveexec_b64 s[46:47], vcc
	s_cbranch_execz .LBB0_729
	v_cvt_pk_bf16_f32 v2, v153, v155
	v_cvt_pk_bf16_f32 v3, v154, v157
	v_cvt_pk_bf16_f32 v4, v156, v159
	v_cvt_pk_bf16_f32 v5, v158, v160
	v_lshl_add_u64 v[6:7], v[34:35], 0, s[22:23]
	global_store_dwordx4 v[34:35], v[2:5], off nt
	s_nop 1
	v_cvt_pk_bf16_f32 v2, v145, v147
	v_cvt_pk_bf16_f32 v3, v146, v149
	v_cvt_pk_bf16_f32 v4, v148, v151
	v_cvt_pk_bf16_f32 v5, v150, v152
	s_lshl_b32 s12, s48, 1
	global_store_dwordx4 v[6:7], v[2:5], off nt
	s_nop 1
	v_cvt_pk_bf16_f32 v2, v137, v139
	v_cvt_pk_bf16_f32 v3, v138, v141
	v_cvt_pk_bf16_f32 v4, v140, v143
	v_cvt_pk_bf16_f32 v5, v142, v144
	v_lshl_add_u64 v[8:9], v[34:35], 0, s[12:13]
	global_store_dwordx4 v[8:9], v[2:5], off nt
	s_nop 1
	v_cvt_pk_bf16_f32 v2, v129, v131
	v_cvt_pk_bf16_f32 v3, v130, v133
	v_cvt_pk_bf16_f32 v4, v132, v135
	v_cvt_pk_bf16_f32 v5, v134, v136
	v_lshl_add_u64 v[6:7], v[6:7], 0, s[12:13]
	global_store_dwordx4 v[6:7], v[2:5], off nt
	s_nop 1

; FFT_HD cf2 mk2(float x, float y) { return (cf2){x, y}; }
; FFT_HD void fft_sincos(float frac, float& s, float& c) { s = __builtin_amdgcn_sinf(frac); c = __builtin_amdgcn_cosf(frac); }
; FFT_HD cf2 cmul(cf2 a, cf2 b) { return mk2(a.x * b.x - a.y * b.y, a.x * b.y + a.y * b.x); }
; template <int BANK> __device__ __forceinline__ void bg_issue1(BgState& b, int wg, int NW, int lane) {
;     ...
;     for (int i = 0; i < 8; ++i) { const float* p = src + (size_t)i * ldS;
;         asm volatile("global_load_dword %0, %4, off\n\tglobal_load_dword %1, %4, off offset:256\n\tglobal_load_dword %2, %4, off offset:512\n\tglobal_load_dword %3, %4, off offset:768"
;                      : "=&v"(b.r[(BANK * 8 + i) * 4 + 0]), "=&v"(b.r[(BANK * 8 + i) * 4 + 1]), "=&v"(b.r[(BANK * 8 + i) * 4 + 2]), "=&v"(b.r[(BANK * 8 + i) * 4 + 3]) : "v"(p) : "memory"); }
; FFT_HD void fft_gen_tw(float frac, cf2 (&tw)[16]) {
;     float sn, cs; fft_sincos(frac, sn, cs);
;     tw[1] = mk2(cs, -sn);
;     tw[2] = cmul(tw[1], tw[1]); tw[3] = cmul(tw[2], tw[1]); tw[4] = cmul(tw[2], tw[2]); tw[5] = cmul(tw[4], tw[1]); tw[6] = cmul(tw[4], tw[2]); tw[7] = cmul(tw[4], tw[3]);
;     tw[8] = cmul(tw[4], tw[4]);
; #pragma unroll
;     for (int j = 9; j < 16; ++j) tw[j] = cmul(tw[8], tw[j - 8]);
; }
; template <bool INV, int lS, class ZP> FFT_HD void fft_r16_pass(ZP z, int tid) {
;     constexpr int S = 1 << lS, STEP = (S >= 64) ? S + S / 32 : S;
;     constexpr float inv = 1.0f / (float)(16 * S);
;     cf2 tw[16];
;     if (lS != 10) {
;         fft_gen_tw((float)(tid & (S - 1)) * inv, tw);
;         const int w0 = tid, w1 = tid + 512;
;         const int pb0 = PADI(((w0 >> lS) << (lS + 4)) + (w0 & (S - 1))), pb1 = PADI(((w1 >> lS) << (lS + 4)) + (w1 & (S - 1)));
;         cf2 x[16], y[16];
; #pragma unroll
;         for (int j = 0; j < 16; ++j) x[j] = z[pb0 + j * STEP];
; #pragma unroll
;         for (int j = 0; j < 16; ++j) y[j] = z[pb1 + j * STEP];
.LBB0_739:
	s_nop 6
	s_lshl_b32 s12, s48, 2
	v_and_b32_e32 v24, 63, v128
	global_load_dword v153, v[2:3], off nt
	global_load_dword v145, v[2:3], off offset:256 nt
	global_load_dword v137, v[2:3], off offset:512 nt
	global_load_dword v129, v[2:3], off offset:768 nt
	v_lshl_add_u64 v[2:3], v[2:3], 0, s[12:13]
	v_cvt_f32_ubyte0_e32 v4, v24
	global_load_dword v155, v[2:3], off nt
	global_load_dword v147, v[2:3], off offset:256 nt
	global_load_dword v139, v[2:3], off offset:512 nt
	global_load_dword v131, v[2:3], off offset:768 nt
	v_lshl_add_u64 v[2:3], v[2:3], 0, s[12:13]
	v_mul_f32_e32 v4, 0x3a800000, v4
	global_load_dword v154, v[2:3], off nt
	global_load_dword v146, v[2:3], off offset:256 nt
	global_load_dword v138, v[2:3], off offset:512 nt
	global_load_dword v130, v[2:3], off offset:768 nt
	v_lshl_add_u64 v[2:3], v[2:3], 0, s[12:13]
	v_sin_f32_e32 v186, v4
	global_load_dword v157, v[2:3], off nt
	global_load_dword v149, v[2:3], off offset:256 nt
	global_load_dword v141, v[2:3], off offset:512 nt
	global_load_dword v133, v[2:3], off offset:768 nt
	v_lshl_add_u64 v[2:3], v[2:3], 0, s[12:13]
	v_cos_f32_e32 v78, v4
	global_load_dword v156, v[2:3], off nt
	global_load_dword v148, v[2:3], off offset:256 nt
	global_load_dword v140, v[2:3], off offset:512 nt
	global_load_dword v132, v[2:3], off offset:768 nt
	v_lshl_add_u64 v[2:3], v[2:3], 0, s[12:13]
	global_load_dword v159, v[2:3], off nt
	global_load_dword v151, v[2:3], off offset:256 nt
	global_load_dword v143, v[2:3], off offset:512 nt
	global_load_dword v135, v[2:3], off offset:768 nt
	v_lshl_add_u64 v[2:3], v[2:3], 0, s[12:13]
	global_load_dword v158, v[2:3], off nt
	global_load_dword v150, v[2:3], off offset:256 nt
	global_load_dword v142, v[2:3], off offset:512 nt
	global_load_dword v134, v[2:3], off offset:768 nt
	v_lshl_add_u64 v[2:3], v[2:3], 0, s[12:13]
	v_xor_b32_e32 v79, 0x80000000, v186
	global_load_dword v160, v[2:3], off nt
	global_load_dword v152, v[2:3], off offset:256 nt
	global_load_dword v144, v[2:3], off offset:512 nt
	global_load_dword v136, v[2:3], off offset:768 nt
	v_mov_b32_e32 v187, v78
	v_mov_b32_e32 v2, v186
	v_mov_b32_e32 v3, v79
	v_pk_mul_f32 v[2:3], v[186:187], v[2:3]
	s_mov_b32 s48, s27
	v_pk_fma_f32 v[38:39], v[78:79], v[78:79], v[2:3] op_sel_hi:[0,1,1] neg_lo:[0,0,1] neg_hi:[0,0,1]
	v_pk_fma_f32 v[40:41], v[78:79], v[78:79], v[2:3] op_sel_hi:[0,1,1]
	v_pk_mov_b32 v[4:5], v[40:41], v[38:39] op_sel:[1,0]
	v_mov_b32_e32 v2, v38
	v_mov_b32_e32 v3, v41
	v_pk_mul_f32 v[10:11], v[40:41], v[4:5] op_sel:[1,0]
	v_mov_b32_e32 v79, v186
	v_pk_fma_f32 v[56:57], v[38:39], v[2:3], v[10:11] op_sel_hi:[0,1,1] neg_lo:[0,0,1] neg_hi:[0,0,1]
	v_pk_fma_f32 v[74:75], v[38:39], v[2:3], v[10:11] op_sel_hi:[0,1,1]
	v_mov_b32_e32 v68, v56
	v_mov_b32_e32 v69, v75
	v_pk_mul_f32 v[18:19], v[68:69], v[68:69]
	v_pk_mul_f32 v[20:21], v[68:69], v[74:75] op_sel:[0,1] op_sel_hi:[1,0]
	v_mov_b32_e32 v22, v18
	v_mov_b32_e32 v23, v20
	v_pk_mov_b32 v[18:19], v[18:19], v[20:21] op_sel:[1,0]
	v_pk_mul_f32 v[6:7], v[78:79], v[2:3]
	v_pk_add_f32 v[48:49], v[22:23], v[18:19] neg_lo:[0,1] neg_hi:[0,1]
	v_pk_add_f32 v[52:53], v[22:23], v[18:19]
	v_pk_mul_f32 v[8:9], v[186:187], v[2:3]
	v_mov_b32_e32 v188, v48
	v_mov_b32_e32 v189, v53
	v_pk_mul_f32 v[14:15], v[2:3], v[68:69]
	v_pk_mul_f32 v[16:17], v[4:5], v[68:69]
	v_pk_mul_f32 v[190:191], v[2:3], v[188:189]
	v_pk_mul_f32 v[192:193], v[4:5], v[188:189]
	v_mov_b32_e32 v2, v6
	v_mov_b32_e32 v3, v9
	v_pk_mov_b32 v[4:5], v[6:7], v[8:9] op_sel:[1,0]
	v_pk_mul_f32 v[10:11], v[78:79], v[68:69]
	v_pk_add_f32 v[72:73], v[2:3], v[4:5]
	v_pk_add_f32 v[54:55], v[2:3], v[4:5] neg_lo:[0,1] neg_hi:[0,1]
	v_pk_mul_f32 v[12:13], v[186:187], v[68:69]
	v_mov_b32_e32 v2, v72
	v_mov_b32_e32 v3, v55
	v_pk_mov_b32 v[4:5], v[54:55], v[72:73] op_sel:[1,0]
	v_pk_mul_f32 v[6:7], v[68:69], v[2:3]
	v_pk_mul_f32 v[8:9], v[68:69], v[4:5]
	v_pk_mul_f32 v[100:101], v[2:3], v[188:189]
	v_pk_mul_f32 v[98:99], v[4:5], v[188:189]
	v_mov_b32_e32 v2, v10
	v_mov_b32_e32 v3, v13
	v_pk_mov_b32 v[4:5], v[10:11], v[12:13] op_sel:[1,0]
	v_pk_mov_b32 v[70:71], v[74:75], v[56:57] op_sel:[1,0]
	v_pk_add_f32 v[202:203], v[2:3], v[4:5]
	v_pk_add_f32 v[204:205], v[2:3], v[4:5] neg_lo:[0,1] neg_hi:[0,1]
	v_mov_b32_e32 v2, v14
	v_mov_b32_e32 v3, v16
	v_mov_b32_e32 v16, v15
	v_pk_add_f32 v[46:47], v[2:3], v[16:17] neg_lo:[0,1] neg_hi:[0,1]
	v_pk_add_f32 v[50:51], v[2:3], v[16:17]
	v_mov_b32_e32 v2, v46
	v_mov_b32_e32 v3, v51
	v_pk_mul_f32 v[210:211], v[188:189], v[2:3]
	v_pk_mov_b32 v[2:3], v[50:51], v[46:47] op_sel:[1,0]
	v_lshlrev_b32_e32 v5, 3, v24
	v_pk_mul_f32 v[212:213], v[188:189], v[2:3]
	v_mov_b32_e32 v2, v6
	v_mov_b32_e32 v3, v8
	v_mov_b32_e32 v8, v7
	v_pk_add_f32 v[76:77], v[2:3], v[8:9] neg_lo:[0,1] neg_hi:[0,1]
	v_pk_add_f32 v[80:81], v[2:3], v[8:9]
	v_mov_b32_e32 v2, v76
	v_mov_b32_e32 v3, v81
	v_pk_mul_f32 v[214:215], v[188:189], v[2:3]
	v_pk_mov_b32 v[2:3], v[80:81], v[76:77] op_sel:[1,0]
	v_mov_b32_e32 v42, v202
	v_pk_mul_f32 v[216:217], v[188:189], v[2:3]
	v_and_b32_e32 v2, 0xfffffc00, v169
	v_lshlrev_b32_e32 v4, 3, v2
	v_add_u32_e32 v3, 0x2000, v2
	v_add3_u32 v4, 0, v4, v5
	v_ashrrev_i32_e32 v2, 2, v2
	v_add_u32_e32 v238, v4, v2
	v_add_u32_e32 v239, 0x800, v238
	ds_read2_b64 v[170:173], v238 offset1:66
	ds_read2_b64 v[82:85], v238 offset0:132 offset1:198
	ds_read2_b64 v[86:89], v239 offset0:8 offset1:74
	ds_read2_b64 v[90:93], v239 offset0:140 offset1:206
	v_add_u32_e32 v240, 0x1000, v238
	ds_read2_b64 v[94:97], v240 offset0:16 offset1:82
	ds_read2_b64 v[174:177], v240 offset0:148 offset1:214
	v_mov_b32_e32 v43, v205
	s_waitcnt lgkmcnt(3)
; FFT_HD cf2 mk2(float x, float y) { return (cf2){x, y}; }
; FFT_HD cf2 cmul(cf2 a, cf2 b) { return mk2(a.x * b.x - a.y * b.y, a.x * b.y + a.y * b.x); }
; FFT_HD cf2 cmulc(cf2 a, cf2 b) { return mk2(a.x * b.x + a.y * b.y, a.y * b.x - a.x * b.y); }
; FFT_HD cf2 cadd(cf2 a, cf2 b) { return mk2(a.x + b.x, a.y + b.y); }
; FFT_HD cf2 csub(cf2 a, cf2 b) { return mk2(a.x - b.x, a.y - b.y); }
; template <bool INV> FFT_HD void dft4(cf2& a, cf2& b, cf2& c, cf2& d) {
;     const cf2 s0 = cadd(a, c), s1 = csub(a, c), s2 = cadd(b, d), s3 = csub(b, d);
;     a = cadd(s0, s2); c = csub(s0, s2);
;     const cf2 r = INV ? mk2(-s3.y, s3.x) : mk2(s3.y, -s3.x);
;     b = cadd(s1, r); d = csub(s1, r);
; }
; template <bool INV> FFT_HD void dft16(cf2 (&x)[16]) {
;     const float C1 = 0.9238795325112867f, S1 = 0.3826834323650898f, H = 0.7071067811865476f;
; #pragma unroll
;     for (int b = 0; b < 4; ++b) dft4<INV>(x[b], x[4 + b], x[8 + b], x[12 + b]);
;     const float s = INV ? -1.f : 1.f;
;     x[4 + 1] = cmul(x[4 + 1], mk2(C1, -s * S1)); x[8 + 1] = cmul(x[8 + 1], mk2(H, -s * H));   x[12 + 1] = cmul(x[12 + 1], mk2(S1, -s * C1));
;     x[4 + 2] = cmul(x[4 + 2], mk2(H, -s * H));   x[8 + 2] = cmul(x[8 + 2], mk2(0.f, -s));     x[12 + 2] = cmul(x[12 + 2], mk2(-H, -s * H));
;     x[4 + 3] = cmul(x[4 + 3], mk2(S1, -s * C1)); x[8 + 3] = cmul(x[8 + 3], mk2(-H, -s * H));  x[12 + 3] = cmul(x[12 + 3], mk2(-C1, s * S1));
; #pragma unroll
;     for (int c = 0; c < 4; ++c) dft4<INV>(x[4 * c], x[4 * c + 1], x[4 * c + 2], x[4 * c + 3]);
; #pragma unroll
;     for (int c = 0; c < 4; ++c)
; #pragma unroll
;         for (int d = c + 1; d < 4; ++d) { const cf2 t = x[4 * c + d]; x[4 * c + d] = x[4 * d + c]; x[4 * d + c] = t; }
; }
; template <bool INV, int lS, class ZP> FFT_HD void fft_r16_pass(ZP z, int tid) {
;     ...
;         if (INV) {
; #pragma unroll
;             for (int j = 1; j < 16; ++j) x[j] = cmulc(x[j], tw[j]);
;         }
;         dft16<INV>(x);
	v_pk_mul_f32 v[74:75], v[74:75], v[86:87] op_sel:[1,1] op_sel_hi:[1,0]
	v_pk_mov_b32 v[44:45], v[204:205], v[202:203] op_sel:[1,0]
	v_pk_fma_f32 v[226:227], v[56:57], v[86:87], v[74:75]
	v_pk_fma_f32 v[74:75], v[56:57], v[86:87], v[74:75] op_sel_hi:[0,1,1] neg_lo:[0,0,1] neg_hi:[0,0,1]
	v_mov_b32_e32 v227, v75
	v_pk_mul_f32 v[74:75], v[204:205], v[88:89] op_sel:[1,1] op_sel_hi:[1,0]
	v_pk_mul_f32 v[218:219], v[40:41], v[82:83] op_sel:[1,1] op_sel_hi:[1,0]
	v_pk_fma_f32 v[204:205], v[202:203], v[88:89], v[74:75] op_sel_hi:[0,1,1]
	v_pk_fma_f32 v[202:203], v[202:203], v[88:89], v[74:75] op_sel_hi:[0,1,1] neg_lo:[0,0,1] neg_hi:[0,0,1]
	s_waitcnt lgkmcnt(2)
	v_pk_mul_f32 v[74:75], v[50:51], v[90:91] op_sel:[1,1] op_sel_hi:[1,0]
	v_pk_fma_f32 v[220:221], v[38:39], v[82:83], v[218:219] op_sel_hi:[0,1,1]
	v_pk_fma_f32 v[228:229], v[46:47], v[90:91], v[74:75] op_sel_hi:[0,1,1]
	v_pk_fma_f32 v[230:231], v[46:47], v[90:91], v[74:75] op_sel_hi:[0,1,1] neg_lo:[0,0,1] neg_hi:[0,0,1]
	v_pk_mul_f32 v[74:75], v[80:81], v[92:93] op_sel:[1,1] op_sel_hi:[1,0]
	v_pk_fma_f32 v[218:219], v[38:39], v[82:83], v[218:219] op_sel_hi:[0,1,1] neg_lo:[0,0,1] neg_hi:[0,0,1]
	v_pk_fma_f32 v[232:233], v[76:77], v[92:93], v[74:75] op_sel_hi:[0,1,1]
	v_pk_fma_f32 v[234:235], v[76:77], v[92:93], v[74:75] op_sel_hi:[0,1,1] neg_lo:[0,0,1] neg_hi:[0,0,1]
	s_waitcnt lgkmcnt(1)
	v_pk_mul_f32 v[74:75], v[52:53], v[94:95] op_sel:[1,1] op_sel_hi:[1,0]
	v_pk_mul_f32 v[82:83], v[54:55], v[84:85] op_sel:[1,1] op_sel_hi:[1,0]
	v_pk_fma_f32 v[236:237], v[48:49], v[94:95], v[74:75]
	v_pk_fma_f32 v[74:75], v[48:49], v[94:95], v[74:75] op_sel_hi:[0,1,1] neg_lo:[0,0,1] neg_hi:[0,0,1]
	v_mul_f32_e32 v54, v186, v53
	v_mov_b32_e32 v237, v75
	v_pk_fma_f32 v[74:75], v[78:79], v[188:189], v[54:55] op_sel_hi:[1,1,0]
	v_mul_f32_e32 v54, v78, v53
	v_add_u32_e32 v241, 0x1800, v238
	v_mov_b32_e32 v75, v78
	v_pk_fma_f32 v[78:79], v[186:187], v[188:189], v[54:55] op_sel_hi:[1,1,0] neg_lo:[1,0,0] neg_hi:[1,0,0]
	ds_read2_b64 v[178:181], v241 offset0:24 offset1:90
	ds_read2_b64 v[182:185], v241 offset0:156 offset1:222
	v_pk_fma_f32 v[222:223], v[72:73], v[84:85], v[82:83] op_sel_hi:[0,1,1]
	v_pk_fma_f32 v[224:225], v[72:73], v[84:85], v[82:83] op_sel_hi:[0,1,1] neg_lo:[0,0,1] neg_hi:[0,0,1]
	v_mov_b32_e32 v79, v186
	v_pk_mov_b32 v[84:85], v[96:97], v[172:173] op_sel:[1,0]
	v_mov_b32_e32 v82, v96
	v_mov_b32_e32 v83, v173
	v_pk_mul_f32 v[86:87], v[78:79], v[84:85]
	v_pk_mul_f32 v[200:201], v[70:71], v[188:189]
	v_pk_fma_f32 v[172:173], v[74:75], v[82:83], v[86:87]
	v_pk_mul_f32 v[82:83], v[78:79], v[82:83]
	v_pk_add_f32 v[88:89], v[192:193], v[192:193] op_sel:[0,1] op_sel_hi:[0,1]
	v_pk_mul_f32 v[198:199], v[68:69], v[188:189]
	v_pk_fma_f32 v[186:187], v[74:75], v[84:85], v[82:83] neg_lo:[0,0,1] neg_hi:[0,0,1]
	v_pk_add_f32 v[86:87], v[190:191], v[190:191] op_sel:[0,1] op_sel_hi:[0,1] neg_lo:[0,1] neg_hi:[0,1]
	s_waitcnt lgkmcnt(2)
	v_pk_mul_f32 v[82:83], v[88:89], v[174:175]
	v_pk_add_f32 v[94:95], v[200:201], v[200:201] op_sel:[0,1] op_sel_hi:[0,1]
	v_pk_mul_f32 v[206:207], v[188:189], v[42:43]
	v_pk_mul_f32 v[208:209], v[188:189], v[44:45]
	v_pk_fma_f32 v[188:189], v[86:87], v[174:175], v[82:83] op_sel:[0,0,1] op_sel_hi:[1,1,0]
	v_pk_fma_f32 v[174:175], v[86:87], v[174:175], v[82:83] op_sel:[0,0,1] op_sel_hi:[1,1,0] neg_lo:[0,0,1] neg_hi:[0,0,1]
	v_pk_add_f32 v[96:97], v[198:199], v[198:199] op_sel:[0,1] op_sel_hi:[0,1] neg_lo:[0,1] neg_hi:[0,1]
	s_waitcnt lgkmcnt(1)
	v_pk_mul_f32 v[82:83], v[94:95], v[178:179]
	v_pk_add_f32 v[84:85], v[206:207], v[206:207] op_sel:[0,1] op_sel_hi:[0,1] neg_lo:[0,1] neg_hi:[0,1]
	v_pk_fma_f32 v[190:191], v[96:97], v[178:179], v[82:83] op_sel:[0,0,1] op_sel_hi:[1,1,0]
	v_pk_fma_f32 v[82:83], v[96:97], v[178:179], v[82:83] op_sel:[0,0,1] op_sel_hi:[1,1,0] neg_lo:[0,0,1] neg_hi:[0,0,1]
	v_pk_add_f32 v[92:93], v[212:213], v[212:213] op_sel:[0,1] op_sel_hi:[0,1]
	v_mov_b32_e32 v191, v83
	v_pk_add_f32 v[82:83], v[208:209], v[208:209] op_sel:[0,1] op_sel_hi:[0,1]
	v_pk_mul_f32 v[90:91], v[82:83], v[180:181]
	s_waitcnt lgkmcnt(0)
	v_pk_mul_f32 v[192:193], v[92:93], v[182:183]
	v_pk_fma_f32 v[178:179], v[84:85], v[180:181], v[90:91] op_sel:[0,0,1] op_sel_hi:[1,1,0]
	v_pk_fma_f32 v[180:181], v[84:85], v[180:181], v[90:91] op_sel:[0,0,1] op_sel_hi:[1,1,0] neg_lo:[0,0,1] neg_hi:[0,0,1]
	v_pk_add_f32 v[90:91], v[210:211], v[210:211] op_sel:[0,1] op_sel_hi:[0,1] neg_lo:[0,1] neg_hi:[0,1]
	v_mov_b32_e32 v202, v204
	v_mov_b32_e32 v179, v181
	v_pk_fma_f32 v[198:199], v[90:91], v[182:183], v[192:193] op_sel:[0,0,1] op_sel_hi:[1,1,0]
	v_pk_fma_f32 v[182:183], v[90:91], v[182:183], v[192:193] op_sel:[0,0,1] op_sel_hi:[1,1,0] neg_lo:[0,0,1] neg_hi:[0,0,1]
	v_mov_b32_e32 v221, v219
	v_mov_b32_e32 v230, v228
	v_mov_b32_e32 v189, v175
	v_mov_b32_e32 v182, v198
	v_pk_add_f32 v[208:209], v[186:187], v[172:173] op_sel:[1,0] op_sel_hi:[0,1]
	v_pk_add_f32 v[210:211], v[202:203], v[178:179]
	v_pk_mov_b32 v[204:205], v[172:173], v[204:205] op_sel:[1,0]
	v_mov_b32_e32 v202, v187
	v_mov_b32_e32 v173, v181
	v_ashrrev_i32_e32 v2, 2, v3
	v_mov_b32_e32 v212, v186
	v_pk_add_f32 v[172:173], v[202:203], v[172:173] neg_lo:[0,1] neg_hi:[0,1]
	v_pk_add_f32 v[186:187], v[220:221], v[188:189]
	v_pk_add_f32 v[202:203], v[230:231], v[182:183]
	v_mov_b32_e32 v221, v231
	v_mov_b32_e32 v189, v183
	v_add3_u32 v60, v4, v2, s71
	v_pk_add_f32 v[192:193], v[170:171], v[236:237]
	v_pk_add_f32 v[200:201], v[226:227], v[190:191]
	v_pk_add_f32 v[182:183], v[220:221], v[188:189] neg_lo:[0,1] neg_hi:[0,1]
	v_pk_add_f32 v[188:189], v[186:187], v[202:203]
	v_pk_add_f32 v[186:187], v[186:187], v[202:203] neg_lo:[0,1] neg_hi:[0,1]
; FFT_HD cf2 mk2(float x, float y) { return (cf2){x, y}; }
; FFT_HD cf2 cmul(cf2 a, cf2 b) { return mk2(a.x * b.x - a.y * b.y, a.x * b.y + a.y * b.x); }
; FFT_HD cf2 cmulc(cf2 a, cf2 b) { return mk2(a.x * b.x + a.y * b.y, a.y * b.x - a.x * b.y); }
; FFT_HD cf2 cadd(cf2 a, cf2 b) { return mk2(a.x + b.x, a.y + b.y); }
; FFT_HD cf2 csub(cf2 a, cf2 b) { return mk2(a.x - b.x, a.y - b.y); }
; template <bool INV> FFT_HD void dft4(cf2& a, cf2& b, cf2& c, cf2& d) {
;     const cf2 s0 = cadd(a, c), s1 = csub(a, c), s2 = cadd(b, d), s3 = csub(b, d);
;     a = cadd(s0, s2); c = csub(s0, s2);
;     const cf2 r = INV ? mk2(-s3.y, s3.x) : mk2(s3.y, -s3.x);
;     b = cadd(s1, r); d = csub(s1, r);
; }
; template <bool INV> FFT_HD void dft16(cf2 (&x)[16]) {
;     const float C1 = 0.9238795325112867f, S1 = 0.3826834323650898f, H = 0.7071067811865476f;
; #pragma unroll
;     for (int b = 0; b < 4; ++b) dft4<INV>(x[b], x[4 + b], x[8 + b], x[12 + b]);
;     const float s = INV ? -1.f : 1.f;
;     x[4 + 1] = cmul(x[4 + 1], mk2(C1, -s * S1)); x[8 + 1] = cmul(x[8 + 1], mk2(H, -s * H));   x[12 + 1] = cmul(x[12 + 1], mk2(S1, -s * C1));
;     x[4 + 2] = cmul(x[4 + 2], mk2(H, -s * H));   x[8 + 2] = cmul(x[8 + 2], mk2(0.f, -s));     x[12 + 2] = cmul(x[12 + 2], mk2(-H, -s * H));
;     x[4 + 3] = cmul(x[4 + 3], mk2(S1, -s * C1)); x[8 + 3] = cmul(x[8 + 3], mk2(-H, -s * H));  x[12 + 3] = cmul(x[12 + 3], mk2(-C1, s * S1));
; #pragma unroll
;     for (int c = 0; c < 4; ++c) dft4<INV>(x[4 * c], x[4 * c + 1], x[4 * c + 2], x[4 * c + 3]);
; #pragma unroll
;     for (int c = 0; c < 4; ++c)
; #pragma unroll
;         for (int d = c + 1; d < 4; ++d) { const cf2 t = x[4 * c + d]; x[4 * c + d] = x[4 * d + c]; x[4 * d + c] = t; }
; }
; template <bool INV, int lS, class ZP> FFT_HD void fft_r16_pass(ZP z, int tid) {
;     ...
;         for (int j = 0; j < 16; ++j) x[j] = z[pb0 + j * STEP];
; #pragma unroll
;         for (int j = 0; j < 16; ++j) y[j] = z[pb1 + j * STEP];
;         if (INV) {
; #pragma unroll
;             for (int j = 1; j < 16; ++j) x[j] = cmulc(x[j], tw[j]);
;         }
;         dft16<INV>(x);
	v_add_u32_e32 v65, 0x800, v60
	v_pk_add_f32 v[206:207], v[192:193], v[200:201]
	v_pk_add_f32 v[192:193], v[192:193], v[200:201] neg_lo:[0,1] neg_hi:[0,1]
	v_pk_fma_f32 v[200:201], v[186:187], 0, v[186:187] op_sel:[0,0,1] op_sel_hi:[1,0,0] neg_lo:[0,0,1] neg_hi:[0,0,1]
	v_pk_fma_f32 v[186:187], v[186:187], 0, v[186:187] op_sel:[0,0,1] op_sel_hi:[1,0,0]
	ds_read2_b64 v[2:5], v60 offset1:66
	ds_read2_b64 v[30:33], v60 offset0:132 offset1:198
	ds_read2_b64 v[14:17], v65 offset0:8 offset1:74
	ds_read2_b64 v[22:25], v65 offset0:140 offset1:206
	v_mov_b32_e32 v201, v187
	v_mov_b32_e32 v223, v225
	v_mov_b32_e32 v213, v178
	v_pk_mov_b32 v[174:175], v[174:175], v[198:199] op_sel:[1,0]
	v_pk_mov_b32 v[198:199], v[224:225], v[232:233] op_sel:[1,0]
	v_pk_add_f32 v[224:225], v[172:173], v[172:173] op_sel:[0,1] op_sel_hi:[0,1] neg_lo:[0,1] neg_hi:[0,1]
	v_pk_add_f32 v[186:187], v[192:193], v[200:201]
	v_pk_add_f32 v[192:193], v[192:193], v[200:201] neg_lo:[0,1] neg_hi:[0,1]
	v_mov_b32_e32 v200, v182
	v_mov_b32_e32 v201, v172
	v_mov_b32_e32 v172, v183
	v_add_u32_e32 v67, 0x1000, v60
	v_pk_add_f32 v[178:179], v[204:205], v[212:213] neg_lo:[0,1] neg_hi:[0,1]
	v_pk_mov_b32 v[204:205], v[218:219], v[228:229] op_sel:[1,0]
	v_pk_add_f32 v[172:173], v[200:201], v[172:173]
	v_mov_b32_e32 v200, v214
	v_mov_b32_e32 v201, v100
	v_mov_b32_e32 v100, v215
	ds_read2_b64 v[10:13], v67 offset0:16 offset1:82
	ds_read2_b64 v[26:29], v67 offset0:148 offset1:214
	v_pk_add_f32 v[174:175], v[204:205], v[174:175] neg_lo:[0,1] neg_hi:[0,1]
	v_pk_add_f32 v[100:101], v[200:201], v[100:101] neg_lo:[0,1] neg_hi:[0,1]
	v_mov_b32_e32 v200, v216
	v_mov_b32_e32 v201, v98
	v_mov_b32_e32 v98, v217
	v_add_u32_e32 v169, 0x1800, v60
	v_sub_f32_e32 v54, v182, v183
	v_pk_add_f32 v[190:191], v[226:227], v[190:191] neg_lo:[0,1] neg_hi:[0,1]
	v_pk_add_f32 v[226:227], v[178:179], v[178:179] op_sel:[0,1] op_sel_hi:[0,1]
	v_mov_b32_e32 v182, v174
	v_mov_b32_e32 v183, v178
	v_mov_b32_e32 v178, v175
	v_pk_add_f32 v[98:99], v[200:201], v[98:99]
	s_waitcnt lgkmcnt(3)
	v_pk_mul_f32 v[70:71], v[70:71], v[14:15] op_sel_hi:[1,0]
	ds_read2_b64 v[6:9], v169 offset0:24 offset1:90
	ds_read2_b64 v[18:21], v169 offset0:156 offset1:222
	v_add_f32_e32 v73, v174, v175
	v_pk_add_f32 v[218:219], v[206:207], v[188:189]
	v_pk_add_f32 v[188:189], v[206:207], v[188:189] neg_lo:[0,1] neg_hi:[0,1]
	v_pk_add_f32 v[170:171], v[170:171], v[236:237] neg_lo:[0,1] neg_hi:[0,1]
	v_pk_mov_b32 v[206:207], v[190:191], v[190:191] op_sel:[1,0]
	v_pk_add_f32 v[174:175], v[182:183], v[178:179] neg_lo:[0,1] neg_hi:[0,1]
	v_pk_mul_f32 v[200:201], v[98:99], v[176:177] op_sel:[1,1] op_sel_hi:[1,0]
	v_pk_fma_f32 v[56:57], v[56:57], v[14:15], v[70:71] op_sel:[0,1,0] neg_lo:[0,0,1] neg_hi:[0,0,1]
	v_pk_fma_f32 v[14:15], v[68:69], v[14:15], v[70:71] op_sel:[0,1,0]
	v_mov_b32_e32 v80, v55
	v_mov_b32_e32 v68, v33
	s_waitcnt lgkmcnt(4)
	v_mov_b32_e32 v69, v25
	v_mul_f32_e32 v213, 0x3f3504f3, v73
	v_pk_add_f32 v[220:221], v[170:171], v[190:191] op_sel:[0,1] op_sel_hi:[1,0] neg_lo:[0,1] neg_hi:[0,1]
	v_pk_add_f32 v[190:191], v[170:171], v[190:191] op_sel:[0,1] op_sel_hi:[1,0]
	v_mul_f32_e32 v170, 0x3ec3ef15, v173
	v_mul_f32_e32 v206, 0x3f6c835e, v175
	v_pk_fma_f32 v[202:203], v[100:101], v[176:177], v[200:201] op_sel:[1,0,0]
	v_pk_fma_f32 v[176:177], v[100:101], v[176:177], v[200:201] op_sel:[1,0,0] neg_lo:[0,0,1] neg_hi:[0,0,1]
	v_pk_mul_f32 v[200:201], v[98:99], v[184:185] op_sel:[0,1] op_sel_hi:[0,0]
	v_mov_b32_e32 v57, v15
	v_mov_b32_e32 v73, v76
	v_mov_b32_e32 v14, v32
	v_mov_b32_e32 v15, v24
	v_pk_mul_f32 v[68:69], v[80:81], v[68:69]
	v_pk_add_f32 v[170:171], v[170:171], v[206:207] neg_lo:[0,1] neg_hi:[0,1]
	v_mov_b32_e32 v203, v177
	v_pk_fma_f32 v[206:207], v[100:101], v[184:185], v[200:201] op_sel_hi:[0,1,1]
	v_pk_fma_f32 v[184:185], v[100:101], v[184:185], v[200:201] op_sel_hi:[0,1,1] neg_lo:[0,0,1] neg_hi:[0,0,1]
	v_pk_fma_f32 v[14:15], v[72:73], v[14:15], v[68:69]
	v_mov_b32_e32 v68, v25
	v_mov_b32_e32 v69, v33
	v_mov_b32_e32 v25, v32
	s_waitcnt lgkmcnt(3)
	v_pk_mul_f32 v[32:33], v[52:53], v[10:11] op_sel:[1,1] op_sel_hi:[1,0]
	v_mov_b32_e32 v234, v232
	v_mov_b32_e32 v204, v222
	v_mov_b32_e32 v205, v235
	v_mov_b32_e32 v184, v206
	v_pk_add_f32 v[200:201], v[222:223], v[202:203]
	v_pk_mov_b32 v[176:177], v[176:177], v[206:207] op_sel:[1,0]
	v_mov_b32_e32 v203, v185
	v_pk_fma_f32 v[52:53], v[48:49], v[10:11], v[32:33]
	v_pk_fma_f32 v[10:11], v[48:49], v[10:11], v[32:33] op_sel_hi:[0,1,1] neg_lo:[0,0,1] neg_hi:[0,0,1]
	v_pk_add_f32 v[214:215], v[234:235], v[184:185]
	v_pk_add_f32 v[176:177], v[198:199], v[176:177] neg_lo:[0,1] neg_hi:[0,1]
	v_pk_add_f32 v[184:185], v[204:205], v[202:203] neg_lo:[0,1] neg_hi:[0,1]
	v_mov_b32_e32 v53, v11
	s_waitcnt lgkmcnt(1)
	v_pk_mul_f32 v[10:11], v[96:97], v[6:7]
	v_mov_b32_e32 v202, v184
	v_mov_b32_e32 v203, v176
	v_mov_b32_e32 v204, v185
	v_mov_b32_e32 v205, v177
	v_pk_fma_f32 v[32:33], v[94:95], v[6:7], v[10:11] op_sel:[0,0,1] op_sel_hi:[1,1,0] neg_lo:[1,0,0] neg_hi:[1,0,0]
	v_pk_fma_f32 v[6:7], v[94:95], v[6:7], v[10:11] op_sel:[0,0,1] op_sel_hi:[1,1,0]
	v_mul_f32_e32 v77, 0x3f3504f3, v54
	v_pk_add_f32 v[206:207], v[202:203], v[204:205]
	v_pk_add_f32 v[202:203], v[202:203], v[204:205] neg_lo:[0,1] neg_hi:[0,1]
	v_mov_b32_e32 v33, v7
	v_mov_b32_e32 v7, v28
	s_waitcnt lgkmcnt(0)
; FFT_HD cf2 mk2(float x, float y) { return (cf2){x, y}; }
; FFT_HD cf2 cmul(cf2 a, cf2 b) { return mk2(a.x * b.x - a.y * b.y, a.x * b.y + a.y * b.x); }
; FFT_HD cf2 cadd(cf2 a, cf2 b) { return mk2(a.x + b.x, a.y + b.y); }
; FFT_HD cf2 csub(cf2 a, cf2 b) { return mk2(a.x - b.x, a.y - b.y); }
; template <bool INV> FFT_HD void dft4(cf2& a, cf2& b, cf2& c, cf2& d) {
;     const cf2 s0 = cadd(a, c), s1 = csub(a, c), s2 = cadd(b, d), s3 = csub(b, d);
;     a = cadd(s0, s2); c = csub(s0, s2);
;     const cf2 r = INV ? mk2(-s3.y, s3.x) : mk2(s3.y, -s3.x);
;     b = cadd(s1, r); d = csub(s1, r);
; }
; template <bool INV> FFT_HD void dft16(cf2 (&x)[16]) {
;     const float C1 = 0.9238795325112867f, S1 = 0.3826834323650898f, H = 0.7071067811865476f;
; #pragma unroll
;     for (int b = 0; b < 4; ++b) dft4<INV>(x[b], x[4 + b], x[8 + b], x[12 + b]);
;     const float s = INV ? -1.f : 1.f;
;     x[4 + 1] = cmul(x[4 + 1], mk2(C1, -s * S1)); x[8 + 1] = cmul(x[8 + 1], mk2(H, -s * H));   x[12 + 1] = cmul(x[12 + 1], mk2(S1, -s * C1));
;     x[4 + 2] = cmul(x[4 + 2], mk2(H, -s * H));   x[8 + 2] = cmul(x[8 + 2], mk2(0.f, -s));     x[12 + 2] = cmul(x[12 + 2], mk2(-H, -s * H));
;     x[4 + 3] = cmul(x[4 + 3], mk2(S1, -s * C1)); x[8 + 3] = cmul(x[8 + 3], mk2(-H, -s * H));  x[12 + 3] = cmul(x[12 + 3], mk2(-C1, s * S1));
; #pragma unroll
;     for (int c = 0; c < 4; ++c) dft4<INV>(x[4 * c], x[4 * c + 1], x[4 * c + 2], x[4 * c + 3]);
; #pragma unroll
;     for (int c = 0; c < 4; ++c)
; #pragma unroll
;         for (int d = c + 1; d < 4; ++d) { const cf2 t = x[4 * c + d]; x[4 * c + d] = x[4 * d + c]; x[4 * d + c] = t; }
; }
	v_mov_b32_e32 v28, v21
	s_mov_b32 s49, s26
	v_sub_f32_e32 v212, v77, v213
	v_fmac_f32_e32 v213, 0x3f3504f3, v54
	v_mov_b32_e32 v207, v203
	v_mul_f32_e32 v54, 0x3f6c835e, v203
	v_mov_b32_e32 v6, v20
	v_pk_mul_f32 v[10:11], v[98:99], v[28:29]
	v_pk_add_f32 v[180:181], v[208:209], v[210:211]
	v_pk_mul_f32 v[226:227], v[226:227], s[48:49]
	v_pk_add_f32 v[198:199], v[200:201], v[214:215]
	v_pk_fma_f32 v[204:205], v[206:207], s[14:15], v[54:55] op_sel_hi:[1,1,0] neg_lo:[0,0,1] neg_hi:[0,0,1]
	v_pk_add_f32 v[176:177], v[176:177], v[176:177] op_sel:[0,1] op_sel_hi:[0,1]
	v_mov_b32_e32 v54, v81
	v_pk_fma_f32 v[10:11], v[100:101], v[6:7], v[10:11]
	v_pk_mul_f32 v[6:7], v[98:99], v[6:7]
	v_mov_b32_e32 v221, v191
	v_pk_fma_f32 v[228:229], v[224:225], s[26:27], v[226:227] neg_lo:[0,0,1] neg_hi:[0,0,1]
	v_pk_fma_f32 v[224:225], v[224:225], s[26:27], v[226:227]
	v_pk_add_f32 v[216:217], v[180:181], v[198:199]
	v_pk_add_f32 v[184:185], v[184:185], v[184:185] op_sel:[0,1] op_sel_hi:[0,1] neg_lo:[0,1] neg_hi:[0,1]
	v_pk_mul_f32 v[176:177], v[176:177], s[26:27]
	v_mov_b32_e32 v77, v72
	v_pk_mul_f32 v[24:25], v[54:55], v[24:25]
	v_pk_fma_f32 v[6:7], v[100:101], v[28:29], v[6:7] neg_lo:[0,0,1] neg_hi:[0,0,1]
	v_pk_add_f32 v[20:21], v[2:3], v[52:53] neg_lo:[0,1] neg_hi:[0,1]
	v_pk_add_f32 v[28:29], v[56:57], v[32:33] neg_lo:[0,1] neg_hi:[0,1]
	v_mov_b32_e32 v229, v225
	v_pk_add_f32 v[224:225], v[220:221], v[212:213]
	v_pk_add_f32 v[212:213], v[220:221], v[212:213] neg_lo:[0,1] neg_hi:[0,1]
	v_pk_add_f32 v[220:221], v[218:219], v[216:217]
	v_pk_add_f32 v[216:217], v[218:219], v[216:217] neg_lo:[0,1] neg_hi:[0,1]
	v_pk_fma_f32 v[218:219], v[184:185], s[48:49], v[176:177] neg_lo:[0,0,1] neg_hi:[0,0,1]
	v_pk_fma_f32 v[176:177], v[184:185], s[48:49], v[176:177]
	v_pk_fma_f32 v[24:25], v[76:77], v[68:69], v[24:25] neg_lo:[0,0,1] neg_hi:[0,0,1]
	v_pk_add_f32 v[48:49], v[20:21], v[28:29]
	v_pk_add_f32 v[54:55], v[20:21], v[28:29] neg_lo:[0,1] neg_hi:[0,1]
	v_mov_b32_e32 v219, v177
	v_mov_b32_e32 v49, v55
	v_pk_add_f32 v[54:55], v[14:15], v[10:11] op_sel:[0,1] op_sel_hi:[1,0] neg_lo:[0,1] neg_hi:[0,1]
	v_pk_add_f32 v[68:69], v[24:25], v[6:7] neg_lo:[0,1] neg_hi:[0,1]
	v_pk_add_f32 v[176:177], v[228:229], v[218:219]
	v_pk_add_f32 v[70:71], v[68:69], v[54:55]
	v_pk_add_f32 v[72:73], v[68:69], v[54:55] neg_lo:[0,1] neg_hi:[0,1]
	v_pk_mul_f32 v[40:41], v[40:41], v[30:31] op_sel:[1,0]
	v_pk_add_f32 v[184:185], v[224:225], v[176:177]
	v_pk_add_f32 v[176:177], v[224:225], v[176:177] neg_lo:[0,1] neg_hi:[0,1]
	v_mov_b32_e32 v225, v200
	v_mov_b32_e32 v227, v214
	v_mov_b32_e32 v200, v209
	v_mov_b32_e32 v214, v211
	v_mov_b32_e32 v76, v70
	v_mov_b32_e32 v77, v73
	v_pk_mov_b32 v[70:71], v[72:73], v[70:71] op_sel:[1,0]
	v_pk_fma_f32 v[72:73], v[38:39], v[30:31], v[40:41] op_sel:[0,0,1] op_sel_hi:[0,1,0]
	v_pk_fma_f32 v[30:31], v[38:39], v[30:31], v[40:41] op_sel:[0,0,1] op_sel_hi:[0,1,0] neg_lo:[0,0,1] neg_hi:[0,0,1]
	v_pk_mul_f32 v[38:39], v[50:51], v[22:23] op_sel:[1,1] op_sel_hi:[1,0]
	s_mov_b32 s52, s25
	s_mov_b32 s53, s27
	v_mov_b32_e32 v224, v208
	v_mov_b32_e32 v226, v210
	v_pk_add_f32 v[200:201], v[200:201], v[214:215] neg_lo:[0,1] neg_hi:[0,1]
	s_mov_b32 s12, s25
	v_pk_fma_f32 v[40:41], v[46:47], v[22:23], v[38:39] op_sel_hi:[0,1,1]
	v_pk_fma_f32 v[22:23], v[46:47], v[22:23], v[38:39] op_sel_hi:[0,1,1] neg_lo:[0,0,1] neg_hi:[0,0,1]
	v_pk_mul_f32 v[38:39], v[88:89], v[26:27]
	v_pk_mul_f32 v[178:179], v[174:175], s[52:53]
	v_pk_add_f32 v[224:225], v[224:225], v[226:227] neg_lo:[0,1] neg_hi:[0,1]
	s_mov_b32 s53, s24
	v_pk_mul_f32 v[200:201], v[200:201], s[12:13] op_sel_hi:[1,0]
	v_pk_fma_f32 v[46:47], v[86:87], v[26:27], v[38:39] op_sel:[0,0,1] op_sel_hi:[1,1,0]
	v_pk_fma_f32 v[26:27], v[86:87], v[26:27], v[38:39] op_sel:[0,0,1] op_sel_hi:[1,1,0] neg_lo:[0,0,1] neg_hi:[0,0,1]
	v_pk_mul_f32 v[38:39], v[92:93], v[18:19]
	v_pk_fma_f32 v[208:209], v[224:225], s[52:53], v[200:201] neg_lo:[0,0,1] neg_hi:[0,0,1]
	v_pk_fma_f32 v[210:211], v[224:225], s[52:53], v[200:201]
	v_pk_fma_f32 v[200:201], v[224:225], s[12:13], v[200:201] op_sel_hi:[1,0,1] neg_lo:[0,0,1] neg_hi:[0,0,1]
	s_mov_b32 s12, s29
	v_pk_fma_f32 v[50:51], v[90:91], v[18:19], v[38:39] op_sel:[0,0,1] op_sel_hi:[1,1,0]
	v_pk_fma_f32 v[18:19], v[90:91], v[18:19], v[38:39] op_sel:[0,0,1] op_sel_hi:[1,1,0] neg_lo:[0,0,1] neg_hi:[0,0,1]
	v_pk_mul_f32 v[70:71], v[70:71], s[12:13] op_sel_hi:[1,0]
	v_mov_b32_e32 v73, v31
	v_mov_b32_e32 v22, v40
	v_mov_b32_e32 v47, v27
	v_mov_b32_e32 v18, v50
	v_pk_fma_f32 v[70:71], v[76:77], s[38:39], v[70:71]
	v_pk_add_f32 v[38:39], v[72:73], v[46:47]
	v_pk_add_f32 v[76:77], v[22:23], v[18:19]
	v_pk_mov_b32 v[30:31], v[30:31], v[40:41] op_sel:[1,0]
	v_pk_mov_b32 v[26:27], v[26:27], v[50:51] op_sel:[1,0]
	v_mov_b32_e32 v73, v23
	v_pk_add_f32 v[26:27], v[30:31], v[26:27] neg_lo:[0,1] neg_hi:[0,1]
	v_mov_b32_e32 v47, v19
	v_pk_add_f32 v[22:23], v[38:39], v[76:77] neg_lo:[0,1] neg_hi:[0,1]
	v_pk_add_f32 v[18:19], v[72:73], v[46:47] neg_lo:[0,1] neg_hi:[0,1]
	v_sub_f32_e32 v40, v26, v27
	v_pk_fma_f32 v[30:31], v[22:23], 0, v[22:23] op_sel:[0,0,1] op_sel_hi:[1,0,0] neg_lo:[0,0,1] neg_hi:[0,0,1]
	v_pk_fma_f32 v[22:23], v[22:23], 0, v[22:23] op_sel:[0,0,1] op_sel_hi:[1,0,0]
	v_pk_add_f32 v[46:47], v[18:19], v[18:19] op_sel:[0,1] op_sel_hi:[0,1]
	v_mul_f32_e32 v22, 0x3f3504f3, v40
	v_pk_mul_f32 v[44:45], v[44:45], v[16:17] op_sel_hi:[1,0]
	v_mov_b32_e32 v31, v23
	v_pk_fma_f32 v[22:23], v[46:47], s[24:25], v[22:23] op_sel_hi:[1,1,0] neg_lo:[0,0,1] neg_hi:[0,0,1]
	v_pk_fma_f32 v[46:47], v[42:43], v[16:17], v[44:45] op_sel:[0,1,0] neg_lo:[0,0,1] neg_hi:[0,0,1]
	v_pk_fma_f32 v[16:17], v[42:43], v[16:17], v[44:45] op_sel:[0,1,0]
; FFT_HD cf2 mk2(float x, float y) { return (cf2){x, y}; }
; FFT_HD cf2 cmul(cf2 a, cf2 b) { return mk2(a.x * b.x - a.y * b.y, a.x * b.y + a.y * b.x); }
; FFT_HD cf2 cadd(cf2 a, cf2 b) { return mk2(a.x + b.x, a.y + b.y); }
; FFT_HD cf2 csub(cf2 a, cf2 b) { return mk2(a.x - b.x, a.y - b.y); }
; template <bool INV> FFT_HD void dft4(cf2& a, cf2& b, cf2& c, cf2& d) {
;     const cf2 s0 = cadd(a, c), s1 = csub(a, c), s2 = cadd(b, d), s3 = csub(b, d);
;     a = cadd(s0, s2); c = csub(s0, s2);
;     const cf2 r = INV ? mk2(-s3.y, s3.x) : mk2(s3.y, -s3.x);
;     b = cadd(s1, r); d = csub(s1, r);
; }
; template <bool INV> FFT_HD void dft16(cf2 (&x)[16]) {
;     const float C1 = 0.9238795325112867f, S1 = 0.3826834323650898f, H = 0.7071067811865476f;
; #pragma unroll
;     for (int b = 0; b < 4; ++b) dft4<INV>(x[b], x[4 + b], x[8 + b], x[12 + b]);
;     const float s = INV ? -1.f : 1.f;
;     x[4 + 1] = cmul(x[4 + 1], mk2(C1, -s * S1)); x[8 + 1] = cmul(x[8 + 1], mk2(H, -s * H));   x[12 + 1] = cmul(x[12 + 1], mk2(S1, -s * C1));
;     x[4 + 2] = cmul(x[4 + 2], mk2(H, -s * H));   x[8 + 2] = cmul(x[8 + 2], mk2(0.f, -s));     x[12 + 2] = cmul(x[12 + 2], mk2(-H, -s * H));
;     x[4 + 3] = cmul(x[4 + 3], mk2(S1, -s * C1)); x[8 + 3] = cmul(x[8 + 3], mk2(-H, -s * H));  x[12 + 3] = cmul(x[12 + 3], mk2(-C1, s * S1));
; #pragma unroll
;     for (int c = 0; c < 4; ++c) dft4<INV>(x[4 * c], x[4 * c + 1], x[4 * c + 2], x[4 * c + 3]);
; #pragma unroll
;     for (int c = 0; c < 4; ++c)
; #pragma unroll
;         for (int d = c + 1; d < 4; ++d) { const cf2 t = x[4 * c + d]; x[4 * c + d] = x[4 * d + c]; x[4 * d + c] = t; }
; }
	v_mov_b32_e32 v43, v5
	v_pk_mov_b32 v[4:5], v[12:13], v[4:5] op_sel:[1,0]
	v_mov_b32_e32 v42, v12
	v_pk_mul_f32 v[12:13], v[78:79], v[4:5]
	v_mov_b32_e32 v16, v46
	v_pk_fma_f32 v[12:13], v[74:75], v[42:43], v[12:13]
	v_pk_mul_f32 v[42:43], v[78:79], v[42:43]
	v_pk_add_f32 v[2:3], v[2:3], v[52:53]
	v_pk_fma_f32 v[4:5], v[74:75], v[4:5], v[42:43] neg_lo:[0,0,1] neg_hi:[0,0,1]
	v_pk_mul_f32 v[42:43], v[84:85], v[8:9]
	v_pk_add_f32 v[32:33], v[56:57], v[32:33]
	v_pk_fma_f32 v[44:45], v[82:83], v[8:9], v[42:43] op_sel:[0,0,1] op_sel_hi:[1,1,0] neg_lo:[1,0,0] neg_hi:[1,0,0]
	v_pk_fma_f32 v[8:9], v[82:83], v[8:9], v[42:43] op_sel:[0,0,1] op_sel_hi:[1,1,0]
	v_pk_add_f32 v[42:43], v[12:13], v[4:5] op_sel:[1,0] op_sel_hi:[0,1]
	v_mov_b32_e32 v45, v9
	v_pk_add_f32 v[50:51], v[16:17], v[44:45]
	v_mov_b32_e32 v16, v13
	v_mov_b32_e32 v8, v4
	v_pk_add_f32 v[8:9], v[16:17], v[8:9] neg_lo:[0,1] neg_hi:[0,1]
	v_pk_mov_b32 v[4:5], v[4:5], v[46:47] op_sel:[1,0]
	v_mov_b32_e32 v13, v44
	v_pk_add_f32 v[4:5], v[4:5], v[12:13] neg_lo:[0,1] neg_hi:[0,1]
	v_add_f32_e32 v44, v8, v9
	v_pk_mov_b32 v[52:53], v[24:25], v[14:15] op_sel:[1,0]
	v_mov_b32_e32 v56, v7
	v_mov_b32_e32 v57, v11
	v_mov_b32_e32 v25, v15
	v_mov_b32_e32 v7, v10
	v_pk_add_f32 v[8:9], v[8:9], v[8:9] op_sel:[0,1] op_sel_hi:[0,1] neg_lo:[0,1] neg_hi:[0,1]
	v_pk_add_f32 v[12:13], v[42:43], v[50:51]
	v_pk_add_f32 v[16:17], v[42:43], v[50:51] neg_lo:[0,1] neg_hi:[0,1]
	v_sub_f32_e32 v42, v4, v5
	v_pk_add_f32 v[52:53], v[52:53], v[56:57]
	v_pk_add_f32 v[6:7], v[24:25], v[6:7]
	v_pk_add_f32 v[4:5], v[4:5], v[4:5] op_sel:[0,1] op_sel_hi:[0,1]
	v_pk_mul_f32 v[8:9], v[8:9], s[48:49]
	v_pk_add_f32 v[10:11], v[52:53], v[6:7]
	v_pk_add_f32 v[6:7], v[52:53], v[6:7] neg_lo:[0,1] neg_hi:[0,1]
	v_pk_fma_f32 v[14:15], v[4:5], s[26:27], v[8:9]
	v_pk_fma_f32 v[4:5], v[4:5], s[26:27], v[8:9] neg_lo:[0,0,1] neg_hi:[0,0,1]
	v_pk_add_f32 v[40:41], v[2:3], v[32:33] op_sel:[0,1] op_sel_hi:[1,0] neg_lo:[0,1] neg_hi:[0,1]
	v_mul_f32_e32 v4, 0x3f3504f3, v6
	v_pk_add_f32 v[24:25], v[38:39], v[76:77]
	v_pk_add_f32 v[2:3], v[2:3], v[32:33] op_sel:[0,1] op_sel_hi:[1,0]
	v_mov_b32_e32 v15, v5
	v_pk_fma_f32 v[4:5], v[6:7], s[52:53], v[4:5] op_sel:[1,0,0] op_sel_hi:[1,1,0] neg_lo:[0,0,1] neg_hi:[0,0,1]
	v_pk_add_f32 v[6:7], v[2:3], v[24:25] neg_lo:[0,1] neg_hi:[0,1]
	v_pk_add_f32 v[2:3], v[2:3], v[24:25]
	v_mov_b32_e32 v24, v54
	v_mov_b32_e32 v25, v18
	v_mov_b32_e32 v18, v68
	s_mov_b32 s50, s24
	s_mov_b32 s51, s26
	v_pk_add_f32 v[18:19], v[24:25], v[18:19] neg_lo:[0,1] neg_hi:[0,1]
	v_pk_mov_b32 v[24:25], v[68:69], v[26:27] op_sel:[1,0]
	v_mov_b32_e32 v26, v55
	v_pk_fma_f32 v[182:183], v[172:173], s[50:51], v[178:179] neg_lo:[0,0,1] neg_hi:[0,0,1]
	v_pk_fma_f32 v[178:179], v[172:173], s[50:51], v[178:179]
	s_mov_b32 s50, s27
	s_mov_b32 s51, s25
	v_pk_add_f32 v[24:25], v[24:25], v[26:27]
	v_mul_f32_e32 v43, 0x3f6c835e, v42
	v_mul_f32_e32 v45, 0x3ec3ef15, v44
	v_mul_f32_e32 v46, 0x3ec3ef15, v42
	v_mul_f32_e32 v50, 0x3f6c835e, v44
	v_mul_f32_e32 v42, 0x3f3504f3, v17
	v_mul_f32_e32 v44, 0x3f3504f3, v16
	v_pk_add_f32 v[8:9], v[12:13], v[10:11] neg_lo:[0,1] neg_hi:[0,1]
	v_pk_add_f32 v[10:11], v[12:13], v[10:11]
	v_pk_mul_f32 v[26:27], v[24:25], s[50:51]
	v_pk_mul_f32 v[24:25], v[24:25], s[36:37]
	v_add_f32_e32 v16, v42, v44
	v_fma_f32 v17, v17, s25, -v44
	v_pk_add_f32 v[12:13], v[2:3], v[10:11] op_sel:[0,1] op_sel_hi:[1,0]
	v_pk_add_f32 v[2:3], v[2:3], v[10:11] op_sel:[0,1] op_sel_hi:[1,0] neg_lo:[0,1] neg_hi:[0,1]
	v_pk_add_f32 v[10:11], v[6:7], v[8:9] neg_lo:[0,1] neg_hi:[0,1]
	v_pk_add_f32 v[6:7], v[6:7], v[8:9]
	v_mov_b32_e32 v42, v20
	v_mov_b32_e32 v44, v28
	v_mov_b32_e32 v47, v21
	v_mov_b32_e32 v51, v29
	v_pk_fma_f32 v[24:25], v[18:19], s[50:51], v[24:25] neg_lo:[0,0,1] neg_hi:[0,0,1]
	v_mov_b32_e32 v207, v174
	v_mov_b32_e32 v8, v10
	v_mov_b32_e32 v9, v7
	v_mov_b32_e32 v7, v11
	v_pk_add_f32 v[10:11], v[42:43], v[44:45] neg_lo:[0,1] neg_hi:[0,1]
	v_pk_add_f32 v[20:21], v[46:47], v[50:51]
	v_pk_mov_b32 v[28:29], v[24:25], v[24:25] op_sel:[1,0]
	v_pk_fma_f32 v[18:19], v[18:19], s[36:37], v[26:27]
	v_pk_mul_f32 v[174:175], v[206:207], s[36:37]
	v_pk_mov_b32 v[172:173], v[202:203], v[172:173] op_sel:[1,0]
	v_pk_add_f32 v[24:25], v[10:11], v[24:25] op_sel:[0,1] op_sel_hi:[1,0] neg_lo:[0,1] neg_hi:[0,1]
	v_pk_add_f32 v[26:27], v[20:21], v[18:19] neg_lo:[0,1] neg_hi:[0,1]
	v_pk_mov_b32 v[32:33], v[10:11], v[20:21] op_sel:[1,0]
	v_pk_mov_b32 v[38:39], v[28:29], v[18:19] op_sel:[1,0]
	v_mov_b32_e32 v11, v21
	v_mov_b32_e32 v29, v19
	v_mov_b32_e32 v183, v179
	v_pk_fma_f32 v[172:173], v[172:173], s[50:51], v[174:175] neg_lo:[0,0,1] neg_hi:[0,0,1]
	v_mov_b32_e32 v174, v190
	v_mov_b32_e32 v175, v204
	v_pk_add_f32 v[10:11], v[10:11], v[28:29]
	v_pk_add_f32 v[20:21], v[24:25], v[26:27] neg_lo:[0,1] neg_hi:[0,1]
	v_pk_add_f32 v[28:29], v[26:27], v[24:25]
	v_pk_add_f32 v[24:25], v[26:27], v[24:25] neg_lo:[0,1] neg_hi:[0,1]
	v_mov_b32_e32 v191, v171
	v_pk_mov_b32 v[178:179], v[178:179], v[170:171] op_sel:[1,0]
	v_pk_mov_b32 v[214:215], v[208:209], v[210:211] op_sel:[1,0]
	v_mov_b32_e32 v211, v200
	v_mov_b32_e32 v208, v201
	v_pk_add_f32 v[170:171], v[170:171], v[172:173]
; __device__ __forceinline__ unsigned cvt_pk_bf16(float lo, float hi) { unsigned r; asm volatile("v_cvt_pk_bf16_f32 %0, %1, %2" : "=v"(r) : "v"(lo), "v"(hi)); return r; }
; FFT_HD cf2 cmul(cf2 a, cf2 b) { return mk2(a.x * b.x - a.y * b.y, a.x * b.y + a.y * b.x); }
; FFT_HD cf2 cmulc(cf2 a, cf2 b) { return mk2(a.x * b.x + a.y * b.y, a.y * b.x - a.x * b.y); }
; template <int BANK, int WAITN> __device__ __forceinline__ void bg_finish1(BgState& b) {
;     if (WAITN == 32) asm volatile("s_waitcnt vmcnt(32)" ::: "memory"); else asm volatile("s_waitcnt vmcnt(0)" ::: "memory");
;     asm volatile("" : BG_TIE16(BANK * 32) :: "memory");
;     asm volatile("" : BG_TIE16(BANK * 32 + 16) :: "memory");
;     bf16_t* dst = b.dst[BANK];
;     if (dst != nullptr) {
; #pragma unroll
;         for (int c = 0; c < 4; ++c) { u32x4 w;
;             w.x = cvt_pk_bf16(b.r[(BANK * 8 + 0) * 4 + c], b.r[(BANK * 8 + 1) * 4 + c]); w.y = cvt_pk_bf16(b.r[(BANK * 8 + 2) * 4 + c], b.r[(BANK * 8 + 3) * 4 + c]);
;             w.z = cvt_pk_bf16(b.r[(BANK * 8 + 4) * 4 + c], b.r[(BANK * 8 + 5) * 4 + c]); w.w = cvt_pk_bf16(b.r[(BANK * 8 + 6) * 4 + c], b.r[(BANK * 8 + 7) * 4 + c]);
;             bf16_t* dp = dst + (c & 1) * 512 + (c >> 1) * b.o2[BANK];
;             asm volatile("global_store_dwordx4 %0, %1, off\n\ts_nop 1" :: "v"(dp), "v"(w) : "memory"); }
;     }
; }
; template <bool INV, int lS, class ZP> FFT_HD void fft_r16_pass(ZP z, int tid) {
;     ...
; #pragma unroll
;         for (int j = 0; j < 16; ++j) z[pb0 + j * STEP] = x[j];
;         if (INV) {
; #pragma unroll
;             for (int j = 1; j < 16; ++j) y[j] = cmulc(y[j], tw[j]);
;         }
;         dft16<INV>(y);
;         if (!INV) {
; #pragma unroll
;             for (int j = 1; j < 16; ++j) y[j] = cmul(y[j], tw[j]);
;         }
; #pragma unroll
;         for (int j = 0; j < 16; ++j) z[pb1 + j * STEP] = y[j];
	v_pk_add_f32 v[174:175], v[182:183], v[174:175]
	v_mov_b32_e32 v183, v173
	v_mov_b32_e32 v205, v172
	v_mov_b32_e32 v21, v29
	v_mov_b32_e32 v29, v25
	v_pk_add_f32 v[24:25], v[40:41], v[30:31] neg_lo:[0,1] neg_hi:[0,1]
	v_pk_add_f32 v[26:27], v[16:17], v[4:5] neg_lo:[0,1] neg_hi:[0,1]
	v_pk_add_f32 v[30:31], v[40:41], v[30:31]
	v_pk_add_f32 v[4:5], v[16:17], v[4:5]
	v_pk_add_f32 v[180:181], v[180:181], v[198:199] neg_lo:[0,1] neg_hi:[0,1]
	v_pk_add_f32 v[218:219], v[228:229], v[218:219] neg_lo:[0,1] neg_hi:[0,1]
	v_pk_add_f32 v[214:215], v[200:201], v[214:215]
	v_pk_add_f32 v[200:201], v[210:211], v[208:209] neg_lo:[0,1] neg_hi:[0,1]
	v_pk_add_f32 v[202:203], v[170:171], v[174:175]
	v_mov_b32_e32 v206, v174
	v_mov_b32_e32 v207, v171
	v_mov_b32_e32 v171, v175
	v_pk_add_f32 v[174:175], v[190:191], v[182:183] neg_lo:[0,1] neg_hi:[0,1]
	v_pk_add_f32 v[172:173], v[178:179], v[204:205] neg_lo:[0,1] neg_hi:[0,1]
	v_pk_add_f32 v[32:33], v[32:33], v[38:39]
	v_pk_add_f32 v[16:17], v[30:31], v[4:5] op_sel:[0,1] op_sel_hi:[1,0]
	v_pk_add_f32 v[4:5], v[30:31], v[4:5] op_sel:[0,1] op_sel_hi:[1,0] neg_lo:[0,1] neg_hi:[0,1]
	v_pk_add_f32 v[30:31], v[24:25], v[26:27] neg_lo:[0,1] neg_hi:[0,1]
	v_pk_add_f32 v[24:25], v[24:25], v[26:27]
	v_pk_add_f32 v[198:199], v[188:189], v[180:181] op_sel:[0,1] op_sel_hi:[1,0] neg_lo:[0,1] neg_hi:[0,1]
	v_pk_add_f32 v[180:181], v[188:189], v[180:181] op_sel:[0,1] op_sel_hi:[1,0]
	v_pk_add_f32 v[222:223], v[212:213], v[218:219] op_sel:[0,1] op_sel_hi:[1,0] neg_lo:[0,1] neg_hi:[0,1]
	v_pk_add_f32 v[212:213], v[212:213], v[218:219] op_sel:[0,1] op_sel_hi:[1,0]
	v_pk_add_f32 v[208:209], v[192:193], v[200:201] neg_lo:[0,1] neg_hi:[0,1]
	v_pk_add_f32 v[192:193], v[192:193], v[200:201]
	v_pk_add_f32 v[178:179], v[174:175], v[172:173] neg_lo:[0,1] neg_hi:[0,1]
	v_pk_add_f32 v[172:173], v[174:175], v[172:173]
	v_pk_add_f32 v[18:19], v[10:11], v[32:33]
	v_pk_add_f32 v[10:11], v[10:11], v[32:33] neg_lo:[0,1] neg_hi:[0,1]
	v_mov_b32_e32 v26, v30
	v_mov_b32_e32 v27, v25
	v_mov_b32_e32 v25, v31
	v_pk_add_f32 v[30:31], v[48:49], v[22:23] neg_lo:[0,1] neg_hi:[0,1]
	v_pk_add_f32 v[32:33], v[14:15], v[70:71] neg_lo:[0,1] neg_hi:[0,1]
	v_pk_add_f32 v[22:23], v[48:49], v[22:23]
	v_pk_add_f32 v[14:15], v[14:15], v[70:71]
	v_mov_b32_e32 v189, v181
	v_mov_b32_e32 v219, v213
	v_mov_b32_e32 v201, v193
	v_mov_b32_e32 v175, v173
	v_mov_b32_e32 v181, v199
	v_mov_b32_e32 v213, v223
	v_mov_b32_e32 v193, v209
	v_mov_b32_e32 v173, v179
	v_pk_add_f32 v[38:39], v[22:23], v[14:15] op_sel:[0,1] op_sel_hi:[1,0]
	v_pk_add_f32 v[14:15], v[22:23], v[14:15] op_sel:[0,1] op_sel_hi:[1,0] neg_lo:[0,1] neg_hi:[0,1]
	v_pk_add_f32 v[22:23], v[30:31], v[32:33] neg_lo:[0,1] neg_hi:[0,1]
	v_pk_add_f32 v[30:31], v[30:31], v[32:33]
	v_mov_b32_e32 v188, v198
	v_mov_b32_e32 v218, v222
	v_pk_add_f32 v[224:225], v[186:187], v[214:215]
	v_pk_add_f32 v[186:187], v[186:187], v[214:215] neg_lo:[0,1] neg_hi:[0,1]
	v_mov_b32_e32 v200, v208
	v_pk_add_f32 v[170:171], v[206:207], v[170:171] neg_lo:[0,1] neg_hi:[0,1]
	v_mov_b32_e32 v174, v178
	ds_write2_b64 v238, v[220:221], v[184:185] offset1:66
	ds_write2_b64 v238, v[224:225], v[202:203] offset0:132 offset1:198
	ds_write2_b64 v239, v[188:189], v[218:219] offset0:8 offset1:74
	ds_write2_b64 v239, v[200:201], v[174:175] offset0:140 offset1:206
	ds_write2_b64 v240, v[216:217], v[176:177] offset0:16 offset1:82
	ds_write2_b64 v240, v[186:187], v[170:171] offset0:148 offset1:214
	ds_write2_b64 v241, v[180:181], v[212:213] offset0:24 offset1:90
	ds_write2_b64 v241, v[192:193], v[172:173] offset0:156 offset1:222
	v_mov_b32_e32 v32, v22
	v_mov_b32_e32 v33, v31
	v_mov_b32_e32 v31, v23
	ds_write2_b64 v60, v[12:13], v[18:19] offset1:66
	ds_write2_b64 v60, v[16:17], v[38:39] offset0:132 offset1:198
	ds_write2_b64 v65, v[8:9], v[20:21] offset0:8 offset1:74
	ds_write2_b64 v65, v[26:27], v[32:33] offset0:140 offset1:206
	ds_write2_b64 v67, v[2:3], v[10:11] offset0:16 offset1:82
	ds_write2_b64 v67, v[4:5], v[14:15] offset0:148 offset1:214
	ds_write2_b64 v169, v[6:7], v[28:29] offset0:24 offset1:90
	ds_write2_b64 v169, v[24:25], v[30:31] offset0:156 offset1:222
	s_waitcnt lgkmcnt(0)
	s_barrier
	s_waitcnt vmcnt(32)
	v_cmp_ne_u64_e32 vcc, 0, v[36:37]
	s_and_saveexec_b64 s[48:49], vcc
	s_cbranch_execz .LBB0_741
	v_cvt_pk_bf16_f32 v2, v161, v163
	v_cvt_pk_bf16_f32 v3, v162, v165
	v_cvt_pk_bf16_f32 v4, v164, v167
	v_cvt_pk_bf16_f32 v5, v166, v168
	v_lshl_add_u64 v[6:7], v[36:37], 0, s[22:23]
	global_store_dwordx4 v[36:37], v[2:5], off nt
	s_nop 1
	v_cvt_pk_bf16_f32 v2, v120, v122
	v_cvt_pk_bf16_f32 v3, v121, v124
	v_cvt_pk_bf16_f32 v4, v123, v126
	v_cvt_pk_bf16_f32 v5, v125, v127
	s_lshl_b32 s12, s44, 1
	global_store_dwordx4 v[6:7], v[2:5], off nt
	s_nop 1
	v_cvt_pk_bf16_f32 v2, v110, v112
	v_cvt_pk_bf16_f32 v3, v111, v114
	v_cvt_pk_bf16_f32 v4, v113, v116
	v_cvt_pk_bf16_f32 v5, v115, v117
	v_lshl_add_u64 v[8:9], v[36:37], 0, s[12:13]
	global_store_dwordx4 v[8:9], v[2:5], off nt
	s_nop 1
	v_cvt_pk_bf16_f32 v2, v102, v104
	v_cvt_pk_bf16_f32 v3, v103, v106
	v_cvt_pk_bf16_f32 v4, v105, v108
	v_cvt_pk_bf16_f32 v5, v107, v109
	v_lshl_add_u64 v[6:7], v[6:7], 0, s[12:13]
	global_store_dwordx4 v[6:7], v[2:5], off nt
	s_nop 1

; __device__ __forceinline__ KP kparams() { KP q = (KP)__builtin_amdgcn_kernarg_segment_ptr(); asm volatile("" : "+s"(q)); return q; }
; FFT_HD cf2 mk2(float x, float y) { return (cf2){x, y}; }
; FFT_HD void fft_sincos(float frac, float& s, float& c) { s = __builtin_amdgcn_sinf(frac); c = __builtin_amdgcn_cosf(frac); }
; FFT_HD cf2 cmul(cf2 a, cf2 b) { return mk2(a.x * b.x - a.y * b.y, a.x * b.y + a.y * b.x); }
; template <int BANK> __device__ __forceinline__ void bg_issue1(BgState& b, int wg, int NW, int lane) {
;     KP kp = kparams();
;     const float* src; int ldS; bf16_t* dst; int o2;
;     bg_decode(b.st, wg, NW, lane, kp, src, ldS, dst, o2);
;     b.dst[BANK] = dst; b.o2[BANK] = o2;
;     asm volatile("s_nop 6" ::: "memory");
; #pragma unroll
;     for (int i = 0; i < 8; ++i) { const float* p = src + (size_t)i * ldS;
;         asm volatile("global_load_dword %0, %4, off\n\tglobal_load_dword %1, %4, off offset:256\n\tglobal_load_dword %2, %4, off offset:512\n\tglobal_load_dword %3, %4, off offset:768"
;                      : "=&v"(b.r[(BANK * 8 + i) * 4 + 0]), "=&v"(b.r[(BANK * 8 + i) * 4 + 1]), "=&v"(b.r[(BANK * 8 + i) * 4 + 2]), "=&v"(b.r[(BANK * 8 + i) * 4 + 3]) : "v"(p) : "memory"); }
;     b.st += 1;
; }
; FFT_HD void fft_gen_tw(float frac, cf2 (&tw)[16]) {
;     float sn, cs; fft_sincos(frac, sn, cs);
;     tw[1] = mk2(cs, -sn);
;     tw[2] = cmul(tw[1], tw[1]); tw[3] = cmul(tw[2], tw[1]); tw[4] = cmul(tw[2], tw[2]); tw[5] = cmul(tw[4], tw[1]); tw[6] = cmul(tw[4], tw[2]); tw[7] = cmul(tw[4], tw[3]);
;     tw[8] = cmul(tw[4], tw[4]);
; #pragma unroll
;     for (int j = 9; j < 16; ++j) tw[j] = cmul(tw[8], tw[j - 8]);
; }
; template <bool INV, int lS, class ZP> FFT_HD void fft_r16_pass(ZP z, int tid) {
;     ...
; #pragma unroll 1
;         for (int it = 0; it < 2; ++it) {
;             const int w = tid + 512 * it;
;             const int blk = w >> lS, p = w & (S - 1), pb = PADI((blk << (lS + 4)) + p);
;             fft_gen_tw((float)p * inv, tw);
;             cf2 x[16];
; #pragma unroll
;             for (int j = 0; j < 16; ++j) x[j] = z[pb + j * STEP];
.LBB0_751:
	s_nop 6
	global_load_dword v120, v[2:3], off nt
	global_load_dword v110, v[2:3], off offset:256 nt
	global_load_dword v102, v[2:3], off offset:512 nt
	global_load_dword v94, v[2:3], off offset:768 nt
	s_lshl_b32 s12, s48, 2
	v_lshl_add_u64 v[2:3], v[2:3], 0, s[12:13]
	global_load_dword v123, v[2:3], off nt
	global_load_dword v113, v[2:3], off offset:256 nt
	global_load_dword v105, v[2:3], off offset:512 nt
	global_load_dword v97, v[2:3], off offset:768 nt
	v_lshl_add_u64 v[2:3], v[2:3], 0, s[12:13]
	global_load_dword v121, v[2:3], off nt
	global_load_dword v111, v[2:3], off offset:256 nt
	global_load_dword v103, v[2:3], off offset:512 nt
	global_load_dword v95, v[2:3], off offset:768 nt
	v_lshl_add_u64 v[2:3], v[2:3], 0, s[12:13]
	global_load_dword v125, v[2:3], off nt
	global_load_dword v115, v[2:3], off offset:256 nt
	global_load_dword v107, v[2:3], off offset:512 nt
	global_load_dword v99, v[2:3], off offset:768 nt
	v_lshl_add_u64 v[2:3], v[2:3], 0, s[12:13]
	global_load_dword v122, v[2:3], off nt
	global_load_dword v112, v[2:3], off offset:256 nt
	global_load_dword v104, v[2:3], off offset:512 nt
	global_load_dword v96, v[2:3], off offset:768 nt
	v_lshl_add_u64 v[2:3], v[2:3], 0, s[12:13]
	global_load_dword v126, v[2:3], off nt
	global_load_dword v116, v[2:3], off offset:256 nt
	global_load_dword v108, v[2:3], off offset:512 nt
	global_load_dword v100, v[2:3], off offset:768 nt
	v_lshl_add_u64 v[2:3], v[2:3], 0, s[12:13]
	global_load_dword v124, v[2:3], off nt
	global_load_dword v114, v[2:3], off offset:256 nt
	global_load_dword v106, v[2:3], off offset:512 nt
	global_load_dword v98, v[2:3], off offset:768 nt
	v_lshl_add_u64 v[2:3], v[2:3], 0, s[12:13]
	global_load_dword v127, v[2:3], off nt
	global_load_dword v117, v[2:3], off offset:256 nt
	global_load_dword v109, v[2:3], off offset:512 nt
	global_load_dword v101, v[2:3], off offset:768 nt
	s_mov_b32 s12, 0
	s_mov_b64 s[48:49], -1
.LBB0_752:
	v_add_u32_e32 v2, s12, v128
	v_and_b32_e32 v3, 0x3ff, v2
	v_lshlrev_b32_e32 v2, 4, v2
	v_and_or_b32 v60, v2, s81, v3
	v_cvt_f32_u32_e32 v2, v3
	v_ashrrev_i32_e32 v65, 5, v60
	v_lshlrev_b32_e32 v65, 3, v65
	v_and_b32_e32 v65, 0xfffff0f0, v65
	v_mul_f32_e32 v3, 0x38800000, v2
	v_sin_f32_e32 v2, v3
	v_cos_f32_e32 v4, v3
	v_lshlrev_b32_e32 v60, 3, v60
	v_add3_u32 v60, 0, v65, v60
	v_xor_b32_e32 v5, 0x80000000, v2
	v_mov_b32_e32 v3, v4
	v_mov_b32_e32 v6, v2
	v_mov_b32_e32 v7, v5
	v_pk_mul_f32 v[6:7], v[2:3], v[6:7]
	ds_read_b64 v[82:83], v60
	ds_read_b64 v[80:81], v60 offset:8448
	ds_read_b64 v[84:85], v60 offset:16896
	ds_read_b64 v[86:87], v60 offset:25344
	ds_read_b64 v[88:89], v60 offset:33792
	ds_read_b64 v[90:91], v60 offset:42240
	ds_read_b64 v[92:93], v60 offset:50688
	ds_read_b64 v[162:163], v60 offset:59136
	v_pk_fma_f32 v[8:9], v[4:5], v[4:5], v[6:7] op_sel_hi:[0,1,1] neg_lo:[0,0,1] neg_hi:[0,0,1]
	v_pk_fma_f32 v[6:7], v[4:5], v[4:5], v[6:7] op_sel_hi:[0,1,1]
	v_mov_b32_e32 v10, v8
	v_mov_b32_e32 v11, v7
	v_pk_mov_b32 v[12:13], v[6:7], v[8:9] op_sel:[1,0]
	v_mov_b32_e32 v5, v2
	v_pk_mul_f32 v[14:15], v[4:5], v[10:11]
	v_pk_mul_f32 v[16:17], v[2:3], v[10:11]
	v_pk_mul_f32 v[18:19], v[6:7], v[12:13] op_sel:[1,0]
	v_mov_b32_e32 v42, v14
	v_pk_fma_f32 v[20:21], v[8:9], v[10:11], v[18:19] op_sel_hi:[0,1,1] neg_lo:[0,0,1] neg_hi:[0,0,1]
	v_pk_fma_f32 v[18:19], v[8:9], v[10:11], v[18:19] op_sel_hi:[0,1,1]
	v_mov_b32_e32 v43, v17
	v_pk_mov_b32 v[14:15], v[14:15], v[16:17] op_sel:[1,0]
	v_mov_b32_e32 v22, v20
	v_mov_b32_e32 v23, v19
	v_pk_add_f32 v[16:17], v[42:43], v[14:15]
	v_pk_add_f32 v[14:15], v[42:43], v[14:15] neg_lo:[0,1] neg_hi:[0,1]
	s_waitcnt lgkmcnt(5)
	v_pk_mul_f32 v[6:7], v[84:85], v[6:7] op_sel:[1,1] op_sel_hi:[0,1]
	v_pk_mul_f32 v[26:27], v[4:5], v[22:23]
	v_pk_mul_f32 v[28:29], v[2:3], v[22:23]
	v_pk_mul_f32 v[30:31], v[10:11], v[22:23]
	v_pk_mul_f32 v[32:33], v[12:13], v[22:23]
	v_pk_mul_f32 v[36:37], v[22:23], v[22:23]
	v_pk_mul_f32 v[38:39], v[22:23], v[18:19] op_sel:[0,1] op_sel_hi:[1,0]
	v_add_u32_e32 v65, 0x10800, v60
	v_pk_fma_f32 v[180:181], v[84:85], v[8:9], v[6:7] op_sel_hi:[1,0,1]
	v_pk_fma_f32 v[6:7], v[84:85], v[8:9], v[6:7] op_sel_hi:[1,0,1] neg_lo:[0,0,1] neg_hi:[0,0,1]
	s_waitcnt lgkmcnt(4)
	v_pk_mul_f32 v[8:9], v[86:87], v[14:15] op_sel:[1,1] op_sel_hi:[0,1]
	v_mov_b32_e32 v40, v36
	v_mov_b32_e32 v41, v38
	v_pk_mov_b32 v[36:37], v[36:37], v[38:39] op_sel:[1,0]
	v_mov_b32_e32 v42, v16
	v_mov_b32_e32 v43, v15
	v_pk_mov_b32 v[44:45], v[14:15], v[16:17] op_sel:[1,0]
	v_mov_b32_e32 v50, v26
	v_mov_b32_e32 v51, v29
	v_pk_mov_b32 v[26:27], v[26:27], v[28:29] op_sel:[1,0]
	v_mov_b32_e32 v54, v30
	v_mov_b32_e32 v55, v32
	v_mov_b32_e32 v32, v31
	ds_read_b64 v[164:165], v65
	v_add_u32_e32 v67, 0x12900, v60
	v_pk_fma_f32 v[14:15], v[86:87], v[16:17], v[8:9] op_sel_hi:[1,0,1]
	v_pk_fma_f32 v[8:9], v[86:87], v[16:17], v[8:9] op_sel_hi:[1,0,1] neg_lo:[0,0,1] neg_hi:[0,0,1]
	s_waitcnt lgkmcnt(4)
	v_pk_mul_f32 v[16:17], v[88:89], v[18:19] op_sel:[1,1] op_sel_hi:[0,1]
	v_pk_mov_b32 v[24:25], v[18:19], v[20:21] op_sel:[1,0]
	v_pk_add_f32 v[38:39], v[40:41], v[36:37] neg_lo:[0,1] neg_hi:[0,1]
	v_pk_add_f32 v[36:37], v[40:41], v[36:37]
	v_pk_mul_f32 v[46:47], v[22:23], v[42:43]
	v_pk_mul_f32 v[48:49], v[22:23], v[44:45]
	v_pk_add_f32 v[28:29], v[50:51], v[26:27]
	v_pk_add_f32 v[26:27], v[50:51], v[26:27] neg_lo:[0,1] neg_hi:[0,1]
	v_pk_add_f32 v[30:31], v[54:55], v[32:33] neg_lo:[0,1] neg_hi:[0,1]
	v_pk_add_f32 v[32:33], v[54:55], v[32:33]
	ds_read_b64 v[166:167], v67
	v_add_u32_e32 v76, 0x18c00, v60
	v_pk_fma_f32 v[18:19], v[88:89], v[20:21], v[16:17]
	v_pk_fma_f32 v[16:17], v[88:89], v[20:21], v[16:17] op_sel_hi:[1,0,1] neg_lo:[0,0,1] neg_hi:[0,0,1]
	v_mov_b32_e32 v40, v38
	v_mov_b32_e32 v41, v37
	v_mov_b32_e32 v51, v27
	v_pk_mov_b32 v[52:53], v[26:27], v[28:29] op_sel:[1,0]
	v_pk_mov_b32 v[56:57], v[32:33], v[30:31] op_sel:[1,0]
	v_mov_b32_e32 v70, v46
	v_mov_b32_e32 v71, v48
	v_mov_b32_e32 v48, v47
	v_add_u32_e32 v74, 0x14a00, v60
	ds_read_b64 v[172:173], v76
	v_mov_b32_e32 v19, v17
	s_waitcnt lgkmcnt(5)
; FFT_HD cf2 mk2(float x, float y) { return (cf2){x, y}; }
; FFT_HD void fft_sincos(float frac, float& s, float& c) { s = __builtin_amdgcn_sinf(frac); c = __builtin_amdgcn_cosf(frac); }
; FFT_HD cf2 cmul(cf2 a, cf2 b) { return mk2(a.x * b.x - a.y * b.y, a.x * b.y + a.y * b.x); }
; FFT_HD cf2 cmulc(cf2 a, cf2 b) { return mk2(a.x * b.x + a.y * b.y, a.y * b.x - a.x * b.y); }
; FFT_HD cf2 cadd(cf2 a, cf2 b) { return mk2(a.x + b.x, a.y + b.y); }
; template <bool INV> FFT_HD void dft4(cf2& a, cf2& b, cf2& c, cf2& d) {
;     const cf2 s0 = cadd(a, c), s1 = csub(a, c), s2 = cadd(b, d), s3 = csub(b, d);
;     a = cadd(s0, s2); c = csub(s0, s2);
;     const cf2 r = INV ? mk2(-s3.y, s3.x) : mk2(s3.y, -s3.x);
;     b = cadd(s1, r); d = csub(s1, r);
; }
; template <bool INV> FFT_HD void dft16(cf2 (&x)[16]) {
;     const float C1 = 0.9238795325112867f, S1 = 0.3826834323650898f, H = 0.7071067811865476f;
; #pragma unroll
;     for (int b = 0; b < 4; ++b) dft4<INV>(x[b], x[4 + b], x[8 + b], x[12 + b]);
;     const float s = INV ? -1.f : 1.f;
;     x[4 + 1] = cmul(x[4 + 1], mk2(C1, -s * S1)); x[8 + 1] = cmul(x[8 + 1], mk2(H, -s * H));   x[12 + 1] = cmul(x[12 + 1], mk2(S1, -s * C1));
;     x[4 + 2] = cmul(x[4 + 2], mk2(H, -s * H));   x[8 + 2] = cmul(x[8 + 2], mk2(0.f, -s));     x[12 + 2] = cmul(x[12 + 2], mk2(-H, -s * H));
;     x[4 + 3] = cmul(x[4 + 3], mk2(S1, -s * C1)); x[8 + 3] = cmul(x[8 + 3], mk2(-H, -s * H));  x[12 + 3] = cmul(x[12 + 3], mk2(-C1, s * S1));
; #pragma unroll
;     for (int c = 0; c < 4; ++c) dft4<INV>(x[4 * c], x[4 * c + 1], x[4 * c + 2], x[4 * c + 3]);
; #pragma unroll
;     for (int c = 0; c < 4; ++c)
; #pragma unroll
;         for (int d = c + 1; d < 4; ++d) { const cf2 t = x[4 * c + d]; x[4 * c + d] = x[4 * d + c]; x[4 * d + c] = t; }
; }
; FFT_HD void fft_gen_tw(float frac, cf2 (&tw)[16]) {
;     float sn, cs; fft_sincos(frac, sn, cs);
;     tw[1] = mk2(cs, -sn);
;     tw[2] = cmul(tw[1], tw[1]); tw[3] = cmul(tw[2], tw[1]); tw[4] = cmul(tw[2], tw[2]); tw[5] = cmul(tw[4], tw[1]); tw[6] = cmul(tw[4], tw[2]); tw[7] = cmul(tw[4], tw[3]);
;     tw[8] = cmul(tw[4], tw[4]);
; #pragma unroll
;     for (int j = 9; j < 16; ++j) tw[j] = cmul(tw[8], tw[j - 8]);
; }
; template <bool INV, int lS, class ZP> FFT_HD void fft_r16_pass(ZP z, int tid) {
;     ...
;             for (int j = 1; j < 16; ++j) x[j] = cmulc(x[j], tw[j]);
;         }
;         dft16<INV>(x);
	v_pk_mul_f32 v[16:17], v[90:91], v[26:27] op_sel:[1,1] op_sel_hi:[0,1]
	s_waitcnt lgkmcnt(4)
	v_pk_mul_f32 v[26:27], v[92:93], v[32:33] op_sel:[1,1] op_sel_hi:[0,1]
	v_mul_f32_e32 v32, v2, v37
	v_mov_b32_e32 v55, v33
	v_pk_add_f32 v[46:47], v[70:71], v[48:49] neg_lo:[0,1] neg_hi:[0,1]
	v_pk_add_f32 v[48:49], v[70:71], v[48:49]
	ds_read_b64 v[168:169], v74
	v_add_u32_e32 v75, 0x16b00, v60
	v_add_u32_e32 v77, 0x1ad00, v60
	v_pk_fma_f32 v[32:33], v[4:5], v[40:41], v[32:33] op_sel_hi:[1,1,0]
	v_mov_b32_e32 v50, v28
	v_mov_b32_e32 v54, v30
	ds_read_b64 v[170:171], v75
	ds_read_b64 v[174:175], v77
	v_add_u32_e32 v78, 0x1ce00, v60
	v_pk_fma_f32 v[20:21], v[90:91], v[28:29], v[16:17] op_sel_hi:[1,0,1]
	v_pk_fma_f32 v[16:17], v[90:91], v[28:29], v[16:17] op_sel_hi:[1,0,1] neg_lo:[0,0,1] neg_hi:[0,0,1]
	v_pk_fma_f32 v[28:29], v[92:93], v[30:31], v[26:27] op_sel_hi:[1,0,1]
	v_pk_fma_f32 v[30:31], v[92:93], v[30:31], v[26:27] op_sel_hi:[1,0,1] neg_lo:[0,0,1] neg_hi:[0,0,1]
	s_waitcnt lgkmcnt(6)
	v_pk_mul_f32 v[26:27], v[162:163], v[48:49] op_sel:[1,1] op_sel_hi:[0,1]
	v_mov_b32_e32 v33, v4
	v_mul_f32_e32 v4, v4, v37
	v_pk_mul_f32 v[24:25], v[24:25], v[40:41]
	ds_read_b64 v[176:177], v78
	v_pk_fma_f32 v[84:85], v[162:163], v[46:47], v[26:27] op_sel_hi:[1,0,1]
	v_pk_fma_f32 v[86:87], v[162:163], v[46:47], v[26:27] op_sel_hi:[1,0,1] neg_lo:[0,0,1] neg_hi:[0,0,1]
	s_waitcnt lgkmcnt(6)
	v_pk_mul_f32 v[26:27], v[164:165], v[36:37] op_sel:[1,1] op_sel_hi:[0,1]
	v_pk_fma_f32 v[4:5], v[2:3], v[40:41], v[4:5] op_sel_hi:[1,1,0] neg_lo:[1,0,0] neg_hi:[1,0,0]
	v_pk_mul_f32 v[12:13], v[12:13], v[40:41]
	v_pk_mul_f32 v[22:23], v[22:23], v[40:41]
	v_add_u32_e32 v79, 0x1ef00, v60
	v_pk_fma_f32 v[88:89], v[164:165], v[38:39], v[26:27]
	v_pk_fma_f32 v[26:27], v[164:165], v[38:39], v[26:27] op_sel_hi:[1,0,1] neg_lo:[0,0,1] neg_hi:[0,0,1]
	s_waitcnt lgkmcnt(5)
	v_pk_mov_b32 v[38:39], v[166:167], v[80:81] op_sel:[1,0]
	v_mov_b32_e32 v5, v2
	v_pk_add_f32 v[24:25], v[24:25], v[24:25] op_sel:[0,1] op_sel_hi:[0,1]
	v_pk_mul_f32 v[10:11], v[10:11], v[40:41]
	v_pk_mul_f32 v[44:45], v[44:45], v[40:41]
	v_pk_mul_f32 v[52:53], v[40:41], v[52:53]
	ds_read_b64 v[178:179], v79
	v_mov_b32_e32 v89, v27
	v_mov_b32_e32 v26, v166
	v_mov_b32_e32 v27, v81
	v_pk_mul_f32 v[2:3], v[38:39], v[4:5]
	v_pk_add_f32 v[12:13], v[12:13], v[12:13] op_sel:[0,1] op_sel_hi:[0,1]
	v_pk_add_f32 v[22:23], v[22:23], v[22:23] op_sel:[0,1] op_sel_hi:[0,1] neg_lo:[0,1] neg_hi:[0,1]
	s_waitcnt lgkmcnt(5)
	v_pk_mul_f32 v[24:25], v[24:25], v[172:173] op_sel:[0,1] op_sel_hi:[1,0]
	v_pk_mul_f32 v[42:43], v[42:43], v[40:41]
	v_pk_mul_f32 v[50:51], v[40:41], v[50:51]
	v_pk_mul_f32 v[56:57], v[40:41], v[56:57]
	v_pk_fma_f32 v[2:3], v[26:27], v[32:33], v[2:3]
	v_pk_mul_f32 v[4:5], v[26:27], v[4:5]
	v_pk_add_f32 v[10:11], v[10:11], v[10:11] op_sel:[0,1] op_sel_hi:[0,1] neg_lo:[0,1] neg_hi:[0,1]
	s_waitcnt lgkmcnt(4)
	v_pk_mul_f32 v[12:13], v[168:169], v[12:13] op_sel:[1,0] op_sel_hi:[0,1]
	v_pk_add_f32 v[26:27], v[44:45], v[44:45] op_sel:[0,1] op_sel_hi:[0,1]
	v_pk_fma_f32 v[92:93], v[22:23], v[172:173], v[24:25]
	v_pk_fma_f32 v[22:23], v[22:23], v[172:173], v[24:25] neg_lo:[0,0,1] neg_hi:[0,0,1]
	v_pk_add_f32 v[24:25], v[52:53], v[52:53] op_sel:[0,1] op_sel_hi:[0,1]
	v_pk_mul_f32 v[54:55], v[40:41], v[54:55]
	v_mov_b32_e32 v70, v46
	v_pk_mov_b32 v[72:73], v[48:49], v[46:47] op_sel:[1,0]
	v_pk_fma_f32 v[4:5], v[38:39], v[32:33], v[4:5] neg_lo:[0,0,1] neg_hi:[0,0,1]
	v_pk_fma_f32 v[46:47], v[168:169], v[10:11], v[12:13]
	v_pk_fma_f32 v[10:11], v[168:169], v[10:11], v[12:13] neg_lo:[0,0,1] neg_hi:[0,0,1]
	v_pk_add_f32 v[12:13], v[42:43], v[42:43] op_sel:[0,1] op_sel_hi:[0,1] neg_lo:[0,1] neg_hi:[0,1]
	s_waitcnt lgkmcnt(3)
	v_pk_mul_f32 v[26:27], v[170:171], v[26:27] op_sel:[1,0] op_sel_hi:[0,1]
	v_mov_b32_e32 v93, v23
	v_pk_add_f32 v[22:23], v[50:51], v[50:51] op_sel:[0,1] op_sel_hi:[0,1] neg_lo:[0,1] neg_hi:[0,1]
	s_waitcnt lgkmcnt(2)
	v_pk_mul_f32 v[24:25], v[24:25], v[174:175] op_sel:[0,1] op_sel_hi:[1,0]
	v_pk_add_f32 v[32:33], v[56:57], v[56:57] op_sel:[0,1] op_sel_hi:[0,1]
	v_mov_b32_e32 v71, v49
	v_pk_mul_f32 v[72:73], v[40:41], v[72:73]
	v_pk_fma_f32 v[90:91], v[170:171], v[12:13], v[26:27]
	v_pk_fma_f32 v[12:13], v[170:171], v[12:13], v[26:27] neg_lo:[0,0,1] neg_hi:[0,0,1]
	v_pk_fma_f32 v[26:27], v[22:23], v[174:175], v[24:25]
	v_pk_fma_f32 v[22:23], v[22:23], v[174:175], v[24:25] neg_lo:[0,0,1] neg_hi:[0,0,1]
	v_pk_add_f32 v[24:25], v[54:55], v[54:55] op_sel:[0,1] op_sel_hi:[0,1] neg_lo:[0,1] neg_hi:[0,1]
	s_waitcnt lgkmcnt(1)
	v_pk_mul_f32 v[32:33], v[32:33], v[176:177] op_sel:[0,1] op_sel_hi:[1,0]
	v_pk_mul_f32 v[70:71], v[40:41], v[70:71]
	v_pk_fma_f32 v[48:49], v[24:25], v[176:177], v[32:33]
	v_pk_fma_f32 v[50:51], v[24:25], v[176:177], v[32:33] neg_lo:[0,0,1] neg_hi:[0,0,1]
	v_pk_add_f32 v[32:33], v[72:73], v[72:73] op_sel:[0,1] op_sel_hi:[0,1]
	v_mov_b32_e32 v16, v20
	v_mov_b32_e32 v27, v23
	v_pk_add_f32 v[24:25], v[70:71], v[70:71] op_sel:[0,1] op_sel_hi:[0,1] neg_lo:[0,1] neg_hi:[0,1]
	s_waitcnt lgkmcnt(0)
; FFT_HD cf2 mk2(float x, float y) { return (cf2){x, y}; }
; FFT_HD cf2 cmul(cf2 a, cf2 b) { return mk2(a.x * b.x - a.y * b.y, a.x * b.y + a.y * b.x); }
; FFT_HD cf2 cadd(cf2 a, cf2 b) { return mk2(a.x + b.x, a.y + b.y); }
; FFT_HD cf2 csub(cf2 a, cf2 b) { return mk2(a.x - b.x, a.y - b.y); }
; template <bool INV> FFT_HD void dft4(cf2& a, cf2& b, cf2& c, cf2& d) {
;     const cf2 s0 = cadd(a, c), s1 = csub(a, c), s2 = cadd(b, d), s3 = csub(b, d);
;     a = cadd(s0, s2); c = csub(s0, s2);
;     const cf2 r = INV ? mk2(-s3.y, s3.x) : mk2(s3.y, -s3.x);
;     b = cadd(s1, r); d = csub(s1, r);
; }
; template <bool INV> FFT_HD void dft16(cf2 (&x)[16]) {
;     const float C1 = 0.9238795325112867f, S1 = 0.3826834323650898f, H = 0.7071067811865476f;
; #pragma unroll
;     for (int b = 0; b < 4; ++b) dft4<INV>(x[b], x[4 + b], x[8 + b], x[12 + b]);
;     const float s = INV ? -1.f : 1.f;
;     x[4 + 1] = cmul(x[4 + 1], mk2(C1, -s * S1)); x[8 + 1] = cmul(x[8 + 1], mk2(H, -s * H));   x[12 + 1] = cmul(x[12 + 1], mk2(S1, -s * C1));
;     x[4 + 2] = cmul(x[4 + 2], mk2(H, -s * H));   x[8 + 2] = cmul(x[8 + 2], mk2(0.f, -s));     x[12 + 2] = cmul(x[12 + 2], mk2(-H, -s * H));
;     x[4 + 3] = cmul(x[4 + 3], mk2(S1, -s * C1)); x[8 + 3] = cmul(x[8 + 3], mk2(-H, -s * H));  x[12 + 3] = cmul(x[12 + 3], mk2(-C1, s * S1));
; #pragma unroll
;     for (int c = 0; c < 4; ++c) dft4<INV>(x[4 * c], x[4 * c + 1], x[4 * c + 2], x[4 * c + 3]);
; #pragma unroll
;     for (int c = 0; c < 4; ++c)
; #pragma unroll
;         for (int d = c + 1; d < 4; ++d) { const cf2 t = x[4 * c + d]; x[4 * c + d] = x[4 * d + c]; x[4 * d + c] = t; }
; }
	v_pk_mul_f32 v[32:33], v[32:33], v[178:179] op_sel:[0,1] op_sel_hi:[1,0]
	v_mov_b32_e32 v181, v7
	v_mov_b32_e32 v47, v11
	v_pk_fma_f32 v[52:53], v[24:25], v[178:179], v[32:33]
	v_pk_fma_f32 v[54:55], v[24:25], v[178:179], v[32:33] neg_lo:[0,0,1] neg_hi:[0,0,1]
	v_pk_add_f32 v[32:33], v[4:5], v[2:3] op_sel:[1,0] op_sel_hi:[0,1]
	v_pk_add_f32 v[36:37], v[16:17], v[26:27]
	v_mov_b32_e32 v24, v4
	v_mov_b32_e32 v16, v5
	v_pk_mov_b32 v[4:5], v[6:7], v[28:29] op_sel:[1,0]
	v_pk_mov_b32 v[6:7], v[10:11], v[48:49] op_sel:[1,0]
	v_mov_b32_e32 v15, v9
	v_mov_b32_e32 v30, v28
	v_mov_b32_e32 v86, v84
	v_mov_b32_e32 v91, v13
	v_mov_b32_e32 v50, v48
	v_mov_b32_e32 v54, v52
	v_pk_mov_b32 v[20:21], v[2:3], v[20:21] op_sel:[1,0]
	v_mov_b32_e32 v25, v26
	v_pk_add_f32 v[42:43], v[180:181], v[46:47]
	v_pk_add_f32 v[28:29], v[4:5], v[6:7] neg_lo:[0,1] neg_hi:[0,1]
	v_mov_b32_e32 v181, v31
	v_mov_b32_e32 v47, v51
	v_pk_mov_b32 v[6:7], v[8:9], v[84:85] op_sel:[1,0]
	v_pk_mov_b32 v[8:9], v[12:13], v[52:53] op_sel:[1,0]
	v_pk_add_f32 v[38:39], v[82:83], v[88:89]
	v_pk_add_f32 v[40:41], v[18:19], v[92:93]
	v_pk_add_f32 v[24:25], v[20:21], v[24:25] neg_lo:[0,1] neg_hi:[0,1]
	v_mov_b32_e32 v3, v23
	v_pk_add_f32 v[44:45], v[30:31], v[50:51]
	v_pk_add_f32 v[30:31], v[180:181], v[46:47] neg_lo:[0,1] neg_hi:[0,1]
	v_pk_add_f32 v[46:47], v[14:15], v[90:91]
	v_pk_add_f32 v[48:49], v[86:87], v[54:55]
	v_pk_add_f32 v[52:53], v[6:7], v[8:9] neg_lo:[0,1] neg_hi:[0,1]
	v_mov_b32_e32 v15, v87
	v_mov_b32_e32 v91, v55
	v_pk_add_f32 v[56:57], v[38:39], v[40:41]
	v_pk_add_f32 v[26:27], v[16:17], v[2:3] neg_lo:[0,1] neg_hi:[0,1]
	v_pk_add_f32 v[4:5], v[42:43], v[44:45]
	v_pk_add_f32 v[54:55], v[14:15], v[90:91] neg_lo:[0,1] neg_hi:[0,1]
	v_pk_add_f32 v[12:13], v[46:47], v[48:49]
	v_mov_b32_e32 v7, v52
	v_mov_b32_e32 v9, v53
	v_pk_add_f32 v[72:73], v[24:25], v[24:25] op_sel:[0,1] op_sel_hi:[0,1]
	s_mov_b32 s50, s27
	s_mov_b32 s51, s26
	v_pk_add_f32 v[52:53], v[52:53], v[52:53] op_sel:[0,1] op_sel_hi:[0,1]
	v_pk_add_f32 v[38:39], v[38:39], v[40:41] neg_lo:[0,1] neg_hi:[0,1]
	v_pk_add_f32 v[40:41], v[42:43], v[44:45] neg_lo:[0,1] neg_hi:[0,1]
	v_mov_b32_e32 v43, v46
	v_mov_b32_e32 v45, v48
	v_mov_b32_e32 v46, v33
	v_mov_b32_e32 v48, v37
	v_pk_add_f32 v[2:3], v[32:33], v[36:37]
	v_mov_b32_e32 v6, v54
	v_mov_b32_e32 v8, v55
	v_pk_add_f32 v[70:71], v[26:27], v[26:27] op_sel:[0,1] op_sel_hi:[0,1] neg_lo:[0,1] neg_hi:[0,1]
	v_pk_mul_f32 v[72:73], v[72:73], s[50:51]
	v_pk_add_f32 v[54:55], v[54:55], v[54:55] op_sel:[0,1] op_sel_hi:[0,1] neg_lo:[0,1] neg_hi:[0,1]
	v_pk_mul_f32 v[52:53], v[52:53], s[26:27]
	v_mov_b32_e32 v42, v32
	v_mov_b32_e32 v44, v36
	v_pk_add_f32 v[32:33], v[46:47], v[48:49] neg_lo:[0,1] neg_hi:[0,1]
	s_mov_b32 s12, s25
	v_pk_add_f32 v[16:17], v[82:83], v[88:89] neg_lo:[0,1] neg_hi:[0,1]
	v_pk_fma_f32 v[82:83], v[70:71], s[26:27], v[72:73] neg_lo:[0,0,1] neg_hi:[0,0,1]
	v_pk_fma_f32 v[70:71], v[70:71], s[26:27], v[72:73]
	v_pk_fma_f32 v[72:73], v[54:55], s[50:51], v[52:53] neg_lo:[0,0,1] neg_hi:[0,0,1]
	v_pk_fma_f32 v[52:53], v[54:55], s[50:51], v[52:53]
	v_pk_add_f32 v[42:43], v[42:43], v[44:45] neg_lo:[0,1] neg_hi:[0,1]
	v_pk_fma_f32 v[36:37], v[40:41], 0, v[40:41] op_sel:[0,0,1] op_sel_hi:[1,0,0] neg_lo:[0,0,1] neg_hi:[0,0,1]
	v_pk_fma_f32 v[40:41], v[40:41], 0, v[40:41] op_sel:[0,0,1] op_sel_hi:[1,0,0]
	s_mov_b32 s50, s25
	s_mov_b32 s51, s24
	v_pk_mul_f32 v[32:33], v[32:33], s[12:13] op_sel_hi:[1,0]
	v_pk_add_f32 v[22:23], v[6:7], v[8:9]
	v_pk_add_f32 v[20:21], v[6:7], v[8:9] neg_lo:[0,1] neg_hi:[0,1]
	v_mov_b32_e32 v37, v41
	v_pk_fma_f32 v[40:41], v[42:43], s[50:51], v[32:33] neg_lo:[0,0,1] neg_hi:[0,0,1]
	v_pk_fma_f32 v[44:45], v[42:43], s[50:51], v[32:33]
	v_pk_fma_f32 v[32:33], v[42:43], s[12:13], v[32:33] op_sel_hi:[1,0,1] neg_lo:[0,0,1] neg_hi:[0,0,1]
	v_add_f32_e32 v10, v28, v29
	v_mov_b32_e32 v23, v21
	v_mul_f32_e32 v6, 0x3f6c835e, v21
	v_pk_mov_b32 v[46:47], v[40:41], v[44:45] op_sel:[1,0]
	v_mov_b32_e32 v45, v32
	v_mov_b32_e32 v40, v33
	v_sub_f32_e32 v80, v30, v31
	v_mul_f32_e32 v51, 0x3f3504f3, v10
	v_pk_fma_f32 v[10:11], v[22:23], s[14:15], v[6:7] op_sel_hi:[1,1,0] neg_lo:[0,0,1] neg_hi:[0,0,1]
	v_pk_add_f32 v[6:7], v[56:57], v[4:5]
	v_pk_add_f32 v[14:15], v[2:3], v[12:13]
	v_pk_add_f32 v[46:47], v[32:33], v[46:47]
	v_pk_add_f32 v[32:33], v[44:45], v[40:41] neg_lo:[0,1] neg_hi:[0,1]
	v_mov_b32_e32 v40, v30
	v_mov_b32_e32 v41, v26
	v_mov_b32_e32 v26, v31
	v_mov_b32_e32 v30, v28
	v_mov_b32_e32 v31, v24
	v_mov_b32_e32 v24, v29
	v_pk_add_f32 v[8:9], v[6:7], v[14:15]
	v_pk_add_f32 v[6:7], v[6:7], v[14:15] neg_lo:[0,1] neg_hi:[0,1]
	v_pk_add_f32 v[14:15], v[18:19], v[92:93] neg_lo:[0,1] neg_hi:[0,1]
	v_pk_add_f32 v[24:25], v[30:31], v[24:25] neg_lo:[0,1] neg_hi:[0,1]
	s_mov_b32 s52, s25
	s_mov_b32 s53, s27
	v_pk_mov_b32 v[18:19], v[14:15], v[14:15] op_sel:[1,0]
; __device__ __forceinline__ unsigned cvt_pk_bf16(float lo, float hi) { unsigned r; asm volatile("v_cvt_pk_bf16_f32 %0, %1, %2" : "=v"(r) : "v"(lo), "v"(hi)); return r; }
; template <int BANK, int WAITN> __device__ __forceinline__ void bg_finish1(BgState& b) {
;     if (WAITN == 32) asm volatile("s_waitcnt vmcnt(32)" ::: "memory"); else asm volatile("s_waitcnt vmcnt(0)" ::: "memory");
;     asm volatile("" : BG_TIE16(BANK * 32) :: "memory");
;     asm volatile("" : BG_TIE16(BANK * 32 + 16) :: "memory");
;     bf16_t* dst = b.dst[BANK];
;     if (dst != nullptr) {
; #pragma unroll
;         for (int c = 0; c < 4; ++c) { u32x4 w;
;             w.x = cvt_pk_bf16(b.r[(BANK * 8 + 0) * 4 + c], b.r[(BANK * 8 + 1) * 4 + c]); w.y = cvt_pk_bf16(b.r[(BANK * 8 + 2) * 4 + c], b.r[(BANK * 8 + 3) * 4 + c]);
;             w.z = cvt_pk_bf16(b.r[(BANK * 8 + 4) * 4 + c], b.r[(BANK * 8 + 5) * 4 + c]); w.w = cvt_pk_bf16(b.r[(BANK * 8 + 6) * 4 + c], b.r[(BANK * 8 + 7) * 4 + c]);
;             bf16_t* dp = dst + (c & 1) * 512 + (c >> 1) * b.o2[BANK];
;             asm volatile("global_store_dwordx4 %0, %1, off\n\ts_nop 1" :: "v"(dp), "v"(w) : "memory"); }
;     }
; }
; template <bool INV, int lS, class ZP> FFT_HD void fft_r16_pass(ZP z, int tid) {
;     ...
; #pragma unroll
;             for (int j = 0; j < 16; ++j) z[pb + j * STEP] = x[j];
;         }
	v_pk_add_f32 v[26:27], v[40:41], v[26:27]
	s_mov_b32 s50, s24
	s_mov_b32 s51, s26
	v_pk_mul_f32 v[28:29], v[24:25], s[52:53]
	v_mov_b32_e32 v23, v24
	v_mul_f32_e32 v50, 0x3f3504f3, v80
	v_pk_add_f32 v[4:5], v[56:57], v[4:5] neg_lo:[0,1] neg_hi:[0,1]
	v_pk_add_f32 v[56:57], v[16:17], v[14:15] op_sel:[0,1] op_sel_hi:[1,0] neg_lo:[0,1] neg_hi:[0,1]
	v_pk_add_f32 v[14:15], v[16:17], v[14:15] op_sel:[0,1] op_sel_hi:[1,0]
	v_mul_f32_e32 v16, 0x3ec3ef15, v27
	v_mul_f32_e32 v18, 0x3f6c835e, v25
	v_pk_mul_f32 v[22:23], v[22:23], s[40:41]
	v_pk_fma_f32 v[24:25], v[26:27], s[50:51], v[28:29] neg_lo:[0,0,1] neg_hi:[0,0,1]
	v_pk_fma_f32 v[28:29], v[26:27], s[50:51], v[28:29]
	v_pk_mov_b32 v[20:21], v[20:21], v[26:27] op_sel:[1,0]
	s_mov_b32 s50, s27
	s_mov_b32 s51, s25
	v_mov_b32_e32 v57, v15
	v_mov_b32_e32 v83, v71
	v_sub_f32_e32 v50, v50, v51
	v_fmac_f32_e32 v51, 0x3f3504f3, v80
	v_mov_b32_e32 v73, v53
	v_mov_b32_e32 v25, v29
	v_pk_fma_f32 v[20:21], v[20:21], s[50:51], v[22:23]
	v_pk_add_f32 v[16:17], v[16:17], v[18:19] neg_lo:[0,1] neg_hi:[0,1]
	v_mov_b32_e32 v15, v10
	v_pk_add_f32 v[52:53], v[56:57], v[50:51]
	v_pk_add_f32 v[54:55], v[82:83], v[72:73]
	v_pk_add_f32 v[18:19], v[16:17], v[20:21]
	v_pk_add_f32 v[22:23], v[24:25], v[14:15]
	v_mov_b32_e32 v15, v17
	v_mov_b32_e32 v25, v21
	v_pk_mov_b32 v[16:17], v[28:29], v[16:17] op_sel:[1,0]
	v_mov_b32_e32 v11, v20
	v_pk_add_f32 v[12:13], v[2:3], v[12:13] neg_lo:[0,1] neg_hi:[0,1]
	v_pk_add_f32 v[70:71], v[52:53], v[54:55]
	v_pk_add_f32 v[54:55], v[52:53], v[54:55] neg_lo:[0,1] neg_hi:[0,1]
	v_pk_add_f32 v[52:53], v[56:57], v[50:51] neg_lo:[0,1] neg_hi:[0,1]
	v_pk_add_f32 v[56:57], v[82:83], v[72:73] neg_lo:[0,1] neg_hi:[0,1]
	v_pk_add_f32 v[42:43], v[38:39], v[36:37]
	v_pk_add_f32 v[36:37], v[38:39], v[36:37] neg_lo:[0,1] neg_hi:[0,1]
	v_pk_add_f32 v[14:15], v[14:15], v[24:25] neg_lo:[0,1] neg_hi:[0,1]
	v_pk_add_f32 v[10:11], v[16:17], v[10:11] neg_lo:[0,1] neg_hi:[0,1]
	v_pk_add_f32 v[2:3], v[4:5], v[12:13] op_sel:[0,1] op_sel_hi:[1,0] neg_lo:[0,1] neg_hi:[0,1]
	v_pk_add_f32 v[4:5], v[4:5], v[12:13] op_sel:[0,1] op_sel_hi:[1,0]
	v_pk_add_f32 v[50:51], v[52:53], v[56:57] op_sel:[0,1] op_sel_hi:[1,0] neg_lo:[0,1] neg_hi:[0,1]
	v_pk_add_f32 v[52:53], v[52:53], v[56:57] op_sel:[0,1] op_sel_hi:[1,0]
	v_pk_add_f32 v[38:39], v[36:37], v[32:33] neg_lo:[0,1] neg_hi:[0,1]
	v_pk_add_f32 v[32:33], v[36:37], v[32:33]
	v_pk_add_f32 v[16:17], v[14:15], v[10:11] neg_lo:[0,1] neg_hi:[0,1]
	v_pk_add_f32 v[10:11], v[14:15], v[10:11]
	v_mov_b32_e32 v13, v5
	v_mov_b32_e32 v57, v53
	v_mov_b32_e32 v37, v33
	v_pk_add_f32 v[26:27], v[18:19], v[22:23]
	v_mov_b32_e32 v30, v22
	v_mov_b32_e32 v31, v19
	v_mov_b32_e32 v19, v23
	v_mov_b32_e32 v15, v11
	v_mov_b32_e32 v5, v3
	v_mov_b32_e32 v53, v51
	v_mov_b32_e32 v33, v39
	v_mov_b32_e32 v11, v17
	s_movk_i32 s12, 0x200
	s_and_b64 vcc, exec, s[48:49]
	s_mov_b64 s[48:49], 0
	v_mov_b32_e32 v12, v2
	v_mov_b32_e32 v56, v50
	v_pk_add_f32 v[48:49], v[42:43], v[46:47]
	v_pk_add_f32 v[42:43], v[42:43], v[46:47] neg_lo:[0,1] neg_hi:[0,1]
	v_mov_b32_e32 v36, v38
	v_pk_add_f32 v[18:19], v[30:31], v[18:19] neg_lo:[0,1] neg_hi:[0,1]
	v_mov_b32_e32 v14, v16
	ds_write_b64 v60, v[8:9]
	ds_write_b64 v60, v[70:71] offset:8448
	ds_write_b64 v60, v[48:49] offset:16896
	ds_write_b64 v60, v[26:27] offset:25344
	ds_write_b64 v60, v[12:13] offset:33792
	ds_write_b64 v60, v[56:57] offset:42240
	ds_write_b64 v60, v[36:37] offset:50688
	ds_write_b64 v60, v[14:15] offset:59136
	ds_write_b64 v65, v[6:7]
	ds_write_b64 v67, v[54:55]
	ds_write_b64 v74, v[42:43]
	ds_write_b64 v75, v[18:19]
	ds_write_b64 v76, v[4:5]
	ds_write_b64 v77, v[52:53]
	ds_write_b64 v78, v[32:33]
	ds_write_b64 v79, v[10:11]
	s_cbranch_vccnz .LBB0_752
	s_waitcnt lgkmcnt(0)
	s_barrier
	s_waitcnt vmcnt(32)
	v_cmp_ne_u64_e32 vcc, 0, v[34:35]
	s_and_saveexec_b64 s[48:49], vcc
	s_cbranch_execz .LBB0_755
	v_cvt_pk_bf16_f32 v2, v153, v155
	v_cvt_pk_bf16_f32 v3, v154, v157
	v_cvt_pk_bf16_f32 v4, v156, v159
	v_cvt_pk_bf16_f32 v5, v158, v160
	v_lshl_add_u64 v[6:7], v[34:35], 0, s[22:23]
	global_store_dwordx4 v[34:35], v[2:5], off nt
	s_nop 1
	v_cvt_pk_bf16_f32 v2, v145, v147
	v_cvt_pk_bf16_f32 v3, v146, v149
	v_cvt_pk_bf16_f32 v4, v148, v151
	v_cvt_pk_bf16_f32 v5, v150, v152
	s_lshl_b32 s12, s46, 1
	global_store_dwordx4 v[6:7], v[2:5], off nt
	s_nop 1
	v_cvt_pk_bf16_f32 v2, v137, v139
	v_cvt_pk_bf16_f32 v3, v138, v141
	v_cvt_pk_bf16_f32 v4, v140, v143
	v_cvt_pk_bf16_f32 v5, v142, v144
	v_lshl_add_u64 v[8:9], v[34:35], 0, s[12:13]
	global_store_dwordx4 v[8:9], v[2:5], off nt
	s_nop 1
	v_cvt_pk_bf16_f32 v2, v129, v131
	v_cvt_pk_bf16_f32 v3, v130, v133
	v_cvt_pk_bf16_f32 v4, v132, v135
	v_cvt_pk_bf16_f32 v5, v134, v136
	v_lshl_add_u64 v[6:7], v[6:7], 0, s[12:13]
	global_store_dwordx4 v[6:7], v[2:5], off nt
	s_nop 1

; __device__ __forceinline__ unsigned cvt_pk_bf16(float lo, float hi) { unsigned r; asm volatile("v_cvt_pk_bf16_f32 %0, %1, %2" : "=v"(r) : "v"(lo), "v"(hi)); return r; }
; template <int BANK, int WAITN> __device__ __forceinline__ void bg_finish1(BgState& b) {
;     if (WAITN == 32) asm volatile("s_waitcnt vmcnt(32)" ::: "memory"); else asm volatile("s_waitcnt vmcnt(0)" ::: "memory");
;     asm volatile("" : BG_TIE16(BANK * 32) :: "memory");
;     asm volatile("" : BG_TIE16(BANK * 32 + 16) :: "memory");
;     bf16_t* dst = b.dst[BANK];
;     if (dst != nullptr) {
; #pragma unroll
;         for (int c = 0; c < 4; ++c) { u32x4 w;
;             w.x = cvt_pk_bf16(b.r[(BANK * 8 + 0) * 4 + c], b.r[(BANK * 8 + 1) * 4 + c]); w.y = cvt_pk_bf16(b.r[(BANK * 8 + 2) * 4 + c], b.r[(BANK * 8 + 3) * 4 + c]);
;             w.z = cvt_pk_bf16(b.r[(BANK * 8 + 4) * 4 + c], b.r[(BANK * 8 + 5) * 4 + c]); w.w = cvt_pk_bf16(b.r[(BANK * 8 + 6) * 4 + c], b.r[(BANK * 8 + 7) * 4 + c]);
;             bf16_t* dp = dst + (c & 1) * 512 + (c >> 1) * b.o2[BANK];
;             asm volatile("global_store_dwordx4 %0, %1, off\n\ts_nop 1" :: "v"(dp), "v"(w) : "memory"); }
;     }
; }
.LBB0_771:
	s_waitcnt vmcnt(0)
	v_cmp_ne_u64_e32 vcc, 0, v[68:69]
	s_and_saveexec_b64 s[0:1], vcc
	s_cbranch_execz .LBB0_773
	v_cvt_pk_bf16_f32 v2, v120, v123
	v_cvt_pk_bf16_f32 v3, v121, v125
	v_cvt_pk_bf16_f32 v4, v122, v126
	v_cvt_pk_bf16_f32 v5, v124, v127
	v_lshl_add_u64 v[6:7], v[68:69], 0, s[22:23]
	global_store_dwordx4 v[68:69], v[2:5], off nt
	s_nop 1
	v_cvt_pk_bf16_f32 v2, v110, v113
	v_cvt_pk_bf16_f32 v3, v111, v115
	v_cvt_pk_bf16_f32 v4, v112, v116
	v_cvt_pk_bf16_f32 v5, v114, v117
	s_lshl_b32 s12, s44, 1
	global_store_dwordx4 v[6:7], v[2:5], off nt
	s_nop 1
	v_cvt_pk_bf16_f32 v2, v102, v105
	v_cvt_pk_bf16_f32 v3, v103, v107
	v_cvt_pk_bf16_f32 v4, v104, v108
	v_cvt_pk_bf16_f32 v5, v106, v109
	v_lshl_add_u64 v[8:9], v[68:69], 0, s[12:13]
	global_store_dwordx4 v[8:9], v[2:5], off nt
	s_nop 1
	v_cvt_pk_bf16_f32 v2, v94, v97
	v_cvt_pk_bf16_f32 v3, v95, v99
	v_cvt_pk_bf16_f32 v4, v96, v100
	v_cvt_pk_bf16_f32 v5, v98, v101
	v_lshl_add_u64 v[6:7], v[6:7], 0, s[12:13]
	global_store_dwordx4 v[6:7], v[2:5], off nt
	s_nop 1

; __device__ __forceinline__ KP kparams() { KP q = (KP)__builtin_amdgcn_kernarg_segment_ptr(); asm volatile("" : "+s"(q)); return q; }
; #define BG_I(x) bg_issue1<x>(bg, bgwg, bgNW, bglane)
; #define BG_F(y) bg_finish1<y, 32>(bg)
; template <int BANK> __device__ __forceinline__ void bg_issue1(BgState& b, int wg, int NW, int lane) {
;     KP kp = kparams();
;     const float* src; int ldS; bf16_t* dst; int o2;
;     bg_decode(b.st, wg, NW, lane, kp, src, ldS, dst, o2);
;     b.dst[BANK] = dst; b.o2[BANK] = o2;
;     asm volatile("s_nop 6" ::: "memory");
; #pragma unroll
;     for (int i = 0; i < 8; ++i) { const float* p = src + (size_t)i * ldS;
;         asm volatile("global_load_dword %0, %4, off\n\tglobal_load_dword %1, %4, off offset:256\n\tglobal_load_dword %2, %4, off offset:512\n\tglobal_load_dword %3, %4, off offset:768"
;                      : "=&v"(b.r[(BANK * 8 + i) * 4 + 0]), "=&v"(b.r[(BANK * 8 + i) * 4 + 1]), "=&v"(b.r[(BANK * 8 + i) * 4 + 2]), "=&v"(b.r[(BANK * 8 + i) * 4 + 3]) : "v"(p) : "memory"); }
;     b.st += 1;
; }
; __device__ __forceinline__ void hy_fft_phase(LAS unsigned char* lds, int bid, int G, const bf16_t* vgT, bf16_t* zT, const float* a3, const float* wout, const float* skip, float* filt, float4* gspec) {
;     ...
;     { const int nst = (BG_STEPS + bgNW - 1) / bgNW;
;       if (bg.st < nst) { BG_I(0);
; #pragma unroll 1
;         while (bg.st < nst) { BG_I(1); BG_F(0); BG_I(0); BG_F(1); }
;         bg_finish1<0, 0>(bg); } }
.LBB0_786:
	s_nop 6
	global_load_dword v39, v[4:5], off nt
	global_load_dword v31, v[4:5], off offset:256 nt
	global_load_dword v22, v[4:5], off offset:512 nt
	global_load_dword v1, v[4:5], off offset:768 nt
	s_lshl_b32 s2, s2, 2
	s_mov_b32 s3, 0
	v_lshl_add_u64 v[4:5], v[4:5], 0, s[2:3]
	global_load_dword v42, v[4:5], off nt
	global_load_dword v34, v[4:5], off offset:256 nt
	global_load_dword v26, v[4:5], off offset:512 nt
	global_load_dword v16, v[4:5], off offset:768 nt
	v_lshl_add_u64 v[4:5], v[4:5], 0, s[2:3]
	global_load_dword v40, v[4:5], off nt
	global_load_dword v32, v[4:5], off offset:256 nt
	global_load_dword v24, v[4:5], off offset:512 nt
	global_load_dword v7, v[4:5], off offset:768 nt
	v_lshl_add_u64 v[4:5], v[4:5], 0, s[2:3]
	global_load_dword v44, v[4:5], off nt
	global_load_dword v36, v[4:5], off offset:256 nt
	global_load_dword v28, v[4:5], off offset:512 nt
	global_load_dword v18, v[4:5], off offset:768 nt
	v_lshl_add_u64 v[4:5], v[4:5], 0, s[2:3]
	global_load_dword v41, v[4:5], off nt
	global_load_dword v33, v[4:5], off offset:256 nt
	global_load_dword v25, v[4:5], off offset:512 nt
	global_load_dword v9, v[4:5], off offset:768 nt
	v_lshl_add_u64 v[4:5], v[4:5], 0, s[2:3]
	global_load_dword v45, v[4:5], off nt
	global_load_dword v37, v[4:5], off offset:256 nt
	global_load_dword v29, v[4:5], off offset:512 nt
	global_load_dword v19, v[4:5], off offset:768 nt
	v_lshl_add_u64 v[4:5], v[4:5], 0, s[2:3]
	global_load_dword v43, v[4:5], off nt
	global_load_dword v35, v[4:5], off offset:256 nt
	global_load_dword v27, v[4:5], off offset:512 nt
	global_load_dword v17, v[4:5], off offset:768 nt
	v_lshl_add_u64 v[4:5], v[4:5], 0, s[2:3]
	global_load_dword v46, v[4:5], off nt
	global_load_dword v38, v[4:5], off offset:256 nt
	global_load_dword v30, v[4:5], off offset:512 nt
	global_load_dword v20, v[4:5], off offset:768 nt
	s_add_i32 s13, s60, 1
	s_cmp_ge_i32 s13, s12
	s_cbranch_scc1 .LBB0_813
	s_lshl_b32 s1, s17, 8
	s_and_b32 s2, s1, 0x700
	v_or_b32_e32 v6, s2, v58
	s_bfe_u32 s2, s17, 0x10001
	s_and_b32 s1, s1, 0x100
	v_or_b32_e32 v8, s1, v58
	s_lshl_b32 s1, s1, 1
	s_lshl_b32 s4, s2, 7
	s_or_b32 s1, s1, s4
	v_readlane_b32 s4, v254, 4
	v_or_b32_e32 v23, s1, v58
	s_mul_i32 s1, s4, s13
	s_lshl_b32 s14, s1, 3
	s_lshl_b32 s16, s1, 14
	s_add_i32 s1, s60, 2
	s_mul_i32 s1, s4, s1
	v_mov_b32_e32 v5, 0
	v_lshlrev_b32_e32 v21, 3, v6
	s_lshl_b32 s15, s4, 4
	s_lshl_b32 s20, s17, 11
	s_lshl_b32 s21, s4, 15
	s_lshl_b32 s22, s1, 3
	s_lshl_b32 s23, s1, 14
	s_mov_b64 s[4:5], 0x400
	s_lshl_b32 s24, s2, 3
	s_branch .LBB0_789

; __device__ __forceinline__ KP kparams() { KP q = (KP)__builtin_amdgcn_kernarg_segment_ptr(); asm volatile("" : "+s"(q)); return q; }
; __device__ __forceinline__ unsigned cvt_pk_bf16(float lo, float hi) { unsigned r; asm volatile("v_cvt_pk_bf16_f32 %0, %1, %2" : "=v"(r) : "v"(lo), "v"(hi)); return r; }
; template <int BANK> __device__ __forceinline__ void bg_issue1(BgState& b, int wg, int NW, int lane) {
;     KP kp = kparams();
;     const float* src; int ldS; bf16_t* dst; int o2;
;     bg_decode(b.st, wg, NW, lane, kp, src, ldS, dst, o2);
;     b.dst[BANK] = dst; b.o2[BANK] = o2;
;     asm volatile("s_nop 6" ::: "memory");
; #pragma unroll
;     for (int i = 0; i < 8; ++i) { const float* p = src + (size_t)i * ldS;
;         asm volatile("global_load_dword %0, %4, off\n\tglobal_load_dword %1, %4, off offset:256\n\tglobal_load_dword %2, %4, off offset:512\n\tglobal_load_dword %3, %4, off offset:768"
;                      : "=&v"(b.r[(BANK * 8 + i) * 4 + 0]), "=&v"(b.r[(BANK * 8 + i) * 4 + 1]), "=&v"(b.r[(BANK * 8 + i) * 4 + 2]), "=&v"(b.r[(BANK * 8 + i) * 4 + 3]) : "v"(p) : "memory"); }
;     b.st += 1;
; }
; template <int BANK, int WAITN> __device__ __forceinline__ void bg_finish1(BgState& b) {
;     if (WAITN == 32) asm volatile("s_waitcnt vmcnt(32)" ::: "memory"); else asm volatile("s_waitcnt vmcnt(0)" ::: "memory");
;     asm volatile("" : BG_TIE16(BANK * 32) :: "memory");
;     asm volatile("" : BG_TIE16(BANK * 32 + 16) :: "memory");
;     bf16_t* dst = b.dst[BANK];
;     if (dst != nullptr) {
; #pragma unroll
;         for (int c = 0; c < 4; ++c) { u32x4 w;
;             w.x = cvt_pk_bf16(b.r[(BANK * 8 + 0) * 4 + c], b.r[(BANK * 8 + 1) * 4 + c]); w.y = cvt_pk_bf16(b.r[(BANK * 8 + 2) * 4 + c], b.r[(BANK * 8 + 3) * 4 + c]);
;             w.z = cvt_pk_bf16(b.r[(BANK * 8 + 4) * 4 + c], b.r[(BANK * 8 + 5) * 4 + c]); w.w = cvt_pk_bf16(b.r[(BANK * 8 + 6) * 4 + c], b.r[(BANK * 8 + 7) * 4 + c]);
;             bf16_t* dp = dst + (c & 1) * 512 + (c >> 1) * b.o2[BANK];
;             asm volatile("global_store_dwordx4 %0, %1, off\n\ts_nop 1" :: "v"(dp), "v"(w) : "memory"); }
;     }
; }
; __device__ __forceinline__ void hy_fft_phase(LAS unsigned char* lds, int bid, int G, const bf16_t* vgT, bf16_t* zT, const float* a3, const float* wout, const float* skip, float* filt, float4* gspec) {
;     ...
;         while (bg.st < nst) { BG_I(1); BG_F(0); BG_I(0); BG_F(1); }
.LBB0_799:
	s_nop 6
	global_load_dword v72, v[14:15], off nt
	global_load_dword v64, v[14:15], off offset:256 nt
	global_load_dword v55, v[14:15], off offset:512 nt
	global_load_dword v47, v[14:15], off offset:768 nt
	s_lshl_b32 s2, s8, 2
	v_lshl_add_u64 v[14:15], v[14:15], 0, s[2:3]
	global_load_dword v74, v[14:15], off nt
	global_load_dword v66, v[14:15], off offset:256 nt
	global_load_dword v57, v[14:15], off offset:512 nt
	global_load_dword v49, v[14:15], off offset:768 nt
	v_lshl_add_u64 v[14:15], v[14:15], 0, s[2:3]
	global_load_dword v73, v[14:15], off nt
	global_load_dword v65, v[14:15], off offset:256 nt
	global_load_dword v56, v[14:15], off offset:512 nt
	global_load_dword v48, v[14:15], off offset:768 nt
	v_lshl_add_u64 v[14:15], v[14:15], 0, s[2:3]
	global_load_dword v76, v[14:15], off nt
	global_load_dword v68, v[14:15], off offset:256 nt
	global_load_dword v60, v[14:15], off offset:512 nt
	global_load_dword v51, v[14:15], off offset:768 nt
	v_lshl_add_u64 v[14:15], v[14:15], 0, s[2:3]
	global_load_dword v75, v[14:15], off nt
	global_load_dword v67, v[14:15], off offset:256 nt
	global_load_dword v59, v[14:15], off offset:512 nt
	global_load_dword v50, v[14:15], off offset:768 nt
	v_lshl_add_u64 v[14:15], v[14:15], 0, s[2:3]
	global_load_dword v78, v[14:15], off nt
	global_load_dword v70, v[14:15], off offset:256 nt
	global_load_dword v62, v[14:15], off offset:512 nt
	global_load_dword v53, v[14:15], off offset:768 nt
	v_lshl_add_u64 v[14:15], v[14:15], 0, s[2:3]
	global_load_dword v77, v[14:15], off nt
	global_load_dword v69, v[14:15], off offset:256 nt
	global_load_dword v61, v[14:15], off offset:512 nt
	global_load_dword v52, v[14:15], off offset:768 nt
	v_lshl_add_u64 v[14:15], v[14:15], 0, s[2:3]
	global_load_dword v79, v[14:15], off nt
	global_load_dword v71, v[14:15], off offset:256 nt
	global_load_dword v63, v[14:15], off offset:512 nt
	global_load_dword v54, v[14:15], off offset:768 nt
	s_waitcnt vmcnt(32)
	v_cmp_ne_u64_e32 vcc, 0, v[2:3]
	s_and_saveexec_b64 s[8:9], vcc
	s_cbranch_execz .LBB0_801
	s_mov_b32 s1, s3
	s_lshl_b64 s[0:1], s[0:1], 1
	v_cvt_pk_bf16_f32 v80, v39, v42
	v_cvt_pk_bf16_f32 v81, v40, v44
	v_cvt_pk_bf16_f32 v82, v41, v45
	v_cvt_pk_bf16_f32 v83, v43, v46
	s_nop 0
	global_store_dwordx4 v[2:3], v[80:83], off nt
	s_nop 1
	v_cvt_pk_bf16_f32 v40, v31, v34
	v_cvt_pk_bf16_f32 v41, v32, v36
	v_cvt_pk_bf16_f32 v42, v33, v37
	v_lshl_add_u64 v[36:37], v[2:3], 0, s[4:5]
	v_lshl_add_u64 v[2:3], v[2:3], 0, s[0:1]
	v_cvt_pk_bf16_f32 v43, v35, v38
	s_nop 0
	global_store_dwordx4 v[36:37], v[40:43], off nt
	s_nop 1
	v_cvt_pk_bf16_f32 v32, v22, v26
	v_cvt_pk_bf16_f32 v33, v24, v28
	v_cvt_pk_bf16_f32 v34, v25, v29
	v_cvt_pk_bf16_f32 v35, v27, v30
	s_nop 0
	global_store_dwordx4 v[2:3], v[32:35], off nt
	s_nop 1
	v_cvt_pk_bf16_f32 v14, v1, v16
	v_cvt_pk_bf16_f32 v15, v7, v18
	v_cvt_pk_bf16_f32 v16, v9, v19
	v_cvt_pk_bf16_f32 v17, v17, v20
	v_lshl_add_u64 v[2:3], v[36:37], 0, s[0:1]
	global_store_dwordx4 v[2:3], v[14:17], off nt
	s_nop 1

; __device__ __forceinline__ KP kparams() { KP q = (KP)__builtin_amdgcn_kernarg_segment_ptr(); asm volatile("" : "+s"(q)); return q; }
; #define BG_I(x) bg_issue1<x>(bg, bgwg, bgNW, bglane)
; #define BG_F(y) bg_finish1<y, 32>(bg)
; template <int BANK> __device__ __forceinline__ void bg_issue1(BgState& b, int wg, int NW, int lane) {
;     KP kp = kparams();
;     const float* src; int ldS; bf16_t* dst; int o2;
;     bg_decode(b.st, wg, NW, lane, kp, src, ldS, dst, o2);
;     b.dst[BANK] = dst; b.o2[BANK] = o2;
;     asm volatile("s_nop 6" ::: "memory");
; #pragma unroll
;     for (int i = 0; i < 8; ++i) { const float* p = src + (size_t)i * ldS;
;         asm volatile("global_load_dword %0, %4, off\n\tglobal_load_dword %1, %4, off offset:256\n\tglobal_load_dword %2, %4, off offset:512\n\tglobal_load_dword %3, %4, off offset:768"
;                      : "=&v"(b.r[(BANK * 8 + i) * 4 + 0]), "=&v"(b.r[(BANK * 8 + i) * 4 + 1]), "=&v"(b.r[(BANK * 8 + i) * 4 + 2]), "=&v"(b.r[(BANK * 8 + i) * 4 + 3]) : "v"(p) : "memory"); }
;     b.st += 1;
; }
; template <int BANK, int WAITN> __device__ __forceinline__ void bg_finish1(BgState& b) {
;     if (WAITN == 32) asm volatile("s_waitcnt vmcnt(32)" ::: "memory"); else asm volatile("s_waitcnt vmcnt(0)" ::: "memory");
;     asm volatile("" : BG_TIE16(BANK * 32) :: "memory");
;     asm volatile("" : BG_TIE16(BANK * 32 + 16) :: "memory");
;     bf16_t* dst = b.dst[BANK];
;     if (dst != nullptr) {
; #pragma unroll
;         for (int c = 0; c < 4; ++c) { u32x4 w;
;             w.x = cvt_pk_bf16(b.r[(BANK * 8 + 0) * 4 + c], b.r[(BANK * 8 + 1) * 4 + c]); w.y = cvt_pk_bf16(b.r[(BANK * 8 + 2) * 4 + c], b.r[(BANK * 8 + 3) * 4 + c]);
;             w.z = cvt_pk_bf16(b.r[(BANK * 8 + 4) * 4 + c], b.r[(BANK * 8 + 5) * 4 + c]); w.w = cvt_pk_bf16(b.r[(BANK * 8 + 6) * 4 + c], b.r[(BANK * 8 + 7) * 4 + c]);
;             bf16_t* dp = dst + (c & 1) * 512 + (c >> 1) * b.o2[BANK];
;             asm volatile("global_store_dwordx4 %0, %1, off\n\ts_nop 1" :: "v"(dp), "v"(w) : "memory"); }
;     }
; }
; __device__ __forceinline__ void hy_fft_phase(LAS unsigned char* lds, int bid, int G, const bf16_t* vgT, bf16_t* zT, const float* a3, const float* wout, const float* skip, float* filt, float4* gspec) {
;     ...
;         while (bg.st < nst) { BG_I(1); BG_F(0); BG_I(0); BG_F(1); }
;         bg_finish1<0, 0>(bg); } }
.LBB0_811:
	s_nop 6
	global_load_dword v39, v[14:15], off nt
	global_load_dword v31, v[14:15], off offset:256 nt
	global_load_dword v22, v[14:15], off offset:512 nt
	global_load_dword v1, v[14:15], off offset:768 nt
	s_lshl_b32 s2, s8, 2
	v_lshl_add_u64 v[12:13], v[14:15], 0, s[2:3]
	global_load_dword v42, v[12:13], off nt
	global_load_dword v34, v[12:13], off offset:256 nt
	global_load_dword v26, v[12:13], off offset:512 nt
	global_load_dword v16, v[12:13], off offset:768 nt
	v_lshl_add_u64 v[12:13], v[12:13], 0, s[2:3]
	global_load_dword v40, v[12:13], off nt
	global_load_dword v32, v[12:13], off offset:256 nt
	global_load_dword v24, v[12:13], off offset:512 nt
	global_load_dword v7, v[12:13], off offset:768 nt
	v_lshl_add_u64 v[12:13], v[12:13], 0, s[2:3]
	global_load_dword v44, v[12:13], off nt
	global_load_dword v36, v[12:13], off offset:256 nt
	global_load_dword v28, v[12:13], off offset:512 nt
	global_load_dword v18, v[12:13], off offset:768 nt
	v_lshl_add_u64 v[12:13], v[12:13], 0, s[2:3]
	global_load_dword v41, v[12:13], off nt
	global_load_dword v33, v[12:13], off offset:256 nt
	global_load_dword v25, v[12:13], off offset:512 nt
	global_load_dword v9, v[12:13], off offset:768 nt
	v_lshl_add_u64 v[12:13], v[12:13], 0, s[2:3]
	global_load_dword v45, v[12:13], off nt
	global_load_dword v37, v[12:13], off offset:256 nt
	global_load_dword v29, v[12:13], off offset:512 nt
	global_load_dword v19, v[12:13], off offset:768 nt
	v_lshl_add_u64 v[12:13], v[12:13], 0, s[2:3]
	global_load_dword v43, v[12:13], off nt
	global_load_dword v35, v[12:13], off offset:256 nt
	global_load_dword v27, v[12:13], off offset:512 nt
	global_load_dword v17, v[12:13], off offset:768 nt
	v_lshl_add_u64 v[12:13], v[12:13], 0, s[2:3]
	global_load_dword v46, v[12:13], off nt
	global_load_dword v38, v[12:13], off offset:256 nt
	global_load_dword v30, v[12:13], off offset:512 nt
	global_load_dword v20, v[12:13], off offset:768 nt
	s_waitcnt vmcnt(32)
	v_cmp_ne_u64_e32 vcc, 0, v[10:11]
	s_and_saveexec_b64 s[8:9], vcc
	s_cbranch_execz .LBB0_788
	v_cvt_pk_bf16_f32 v12, v72, v74
	v_cvt_pk_bf16_f32 v13, v73, v76
	v_cvt_pk_bf16_f32 v14, v75, v78
	v_cvt_pk_bf16_f32 v15, v77, v79
	s_lshl_b32 s2, s6, 1
	global_store_dwordx4 v[10:11], v[12:15], off nt
	s_nop 1
	v_cvt_pk_bf16_f32 v12, v64, v66
	v_cvt_pk_bf16_f32 v13, v65, v68
	v_cvt_pk_bf16_f32 v14, v67, v70
	v_cvt_pk_bf16_f32 v15, v69, v71
	v_lshl_add_u64 v[64:65], v[10:11], 0, s[4:5]
	global_store_dwordx4 v[64:65], v[12:15], off nt
	s_nop 1
	v_cvt_pk_bf16_f32 v12, v55, v57
	v_cvt_pk_bf16_f32 v13, v56, v60
	v_cvt_pk_bf16_f32 v14, v59, v62
	v_cvt_pk_bf16_f32 v15, v61, v63
	v_lshl_add_u64 v[10:11], v[10:11], 0, s[2:3]
	global_store_dwordx4 v[10:11], v[12:15], off nt
	s_nop 1
	v_cvt_pk_bf16_f32 v10, v47, v49
	v_cvt_pk_bf16_f32 v11, v48, v51
	v_cvt_pk_bf16_f32 v12, v50, v53
	v_cvt_pk_bf16_f32 v13, v52, v54
	v_lshl_add_u64 v[14:15], v[64:65], 0, s[2:3]
	global_store_dwordx4 v[14:15], v[10:13], off nt
	s_nop 1
	s_branch .LBB0_788
.LBB0_813:
	s_waitcnt vmcnt(0)
	v_cmp_ne_u64_e32 vcc, 0, v[2:3]
	s_and_saveexec_b64 s[2:3], vcc
	s_cbranch_execz .LBB0_815
	v_cvt_pk_bf16_f32 v10, v39, v42
	v_cvt_pk_bf16_f32 v11, v40, v44
	v_cvt_pk_bf16_f32 v12, v41, v45
	v_cvt_pk_bf16_f32 v13, v43, v46
	s_mov_b64 s[4:5], 0x400
	s_lshl_b32 s0, s0, 1
	s_mov_b32 s1, 0
	global_store_dwordx4 v[2:3], v[10:13], off nt
	s_nop 1
	v_cvt_pk_bf16_f32 v10, v31, v34
	v_cvt_pk_bf16_f32 v11, v32, v36
	v_cvt_pk_bf16_f32 v12, v33, v37
	v_cvt_pk_bf16_f32 v13, v35, v38
	v_lshl_add_u64 v[14:15], v[2:3], 0, s[4:5]
	v_lshl_add_u64 v[2:3], v[2:3], 0, s[0:1]
	global_store_dwordx4 v[14:15], v[10:13], off nt
	s_nop 1
	v_cvt_pk_bf16_f32 v10, v22, v26
	v_cvt_pk_bf16_f32 v11, v24, v28
	v_cvt_pk_bf16_f32 v12, v25, v29
	v_cvt_pk_bf16_f32 v13, v27, v30
	s_nop 0
	global_store_dwordx4 v[2:3], v[10:13], off nt
	s_nop 1
	v_cvt_pk_bf16_f32 v2, v1, v16
	v_cvt_pk_bf16_f32 v3, v7, v18
	v_cvt_pk_bf16_f32 v4, v9, v19
	v_cvt_pk_bf16_f32 v5, v17, v20
	v_lshl_add_u64 v[6:7], v[14:15], 0, s[0:1]
	global_store_dwordx4 v[6:7], v[2:5], off nt
	s_nop 1
